# K-loop sync edits + m0 save/restore dropped at all LDS-DMA sites + dead zero fills before fp8 packs removed
# speedup vs baseline: 1.0018x; 1.0018x over previous
.LBB0_468:
	v_writelane_b32 v255, s2, 45
	v_readlane_b32 s20, v253, 6
	s_mul_i32 s0, s84, 20
	v_writelane_b32 v255, s3, 46
	v_readlane_b32 s22, v253, 8
	v_readlane_b32 s23, v253, 9
	v_writelane_b32 v255, s0, 47
	s_or_b32 s0, s0, 1
	s_mov_b64 s[2:3], s[22:23]
	s_cmp_le_i32 s2, s0
	s_cselect_b64 s[10:11], -1, 0
	s_cmp_lt_i32 s0, s3
	s_cselect_b64 s[2:3], -1, 0
	s_and_b64 s[2:3], s[10:11], s[2:3]
	s_andn2_b64 vcc, exec, s[2:3]
	v_readlane_b32 s21, v253, 7
	s_cbranch_vccnz .LBB0_491
	v_readlane_b32 s40, v253, 2
	v_readlane_b32 s41, v253, 3
	s_load_dwordx2 s[22:23], s[40:41], 0xf8
	s_lshl_b64 s[2:3], s[16:17], 2
	v_mov_b32_e32 v0, 0x1000
	v_readlane_b32 s0, v253, 12
	v_readlane_b32 s1, v253, 13
	s_waitcnt lgkmcnt(0)
	s_add_u32 s2, s22, s2
	s_addc_u32 s3, s23, s3
	global_load_dword v1, v0, s[2:3] sc1
	global_load_dword v2, v0, s[2:3] offset:4 sc1
	global_load_dwordx2 v[4:5], v0, s[22:23] offset:72 sc1
	v_mbcnt_lo_u32_b32 v0, -1, 0
	v_mbcnt_hi_u32_b32 v0, -1, v0
	s_andn2_b64 vcc, exec, s[0:1]
	v_or_b32_e32 v0, s33, v0
	s_waitcnt vmcnt(0)
	v_readfirstlane_b32 s20, v4
	v_readfirstlane_b32 s21, v5
	v_readfirstlane_b32 s9, v0
	s_cbranch_vccnz .LBB0_491
	v_bfe_i32 v5, v0, 27, 1
	v_lshlrev_b32_e32 v3, 4, v0
	v_lshrrev_b32_e32 v5, 22, v5
	v_add_u32_e32 v5, v3, v5
	v_and_b32_e32 v5, 0xfffffc00, v5
	v_sub_u32_e32 v5, v3, v5
	v_ashrrev_i32_e32 v4, 31, v0
	v_lshrrev_b32_e32 v6, 4, v5
	v_lshrrev_b32_e32 v4, 26, v4
	v_bitop3_b32 v6, v6, v5, 32 bitop3:0x6c
	v_ashrrev_i32_e32 v5, 31, v5
	v_add_u32_e32 v4, v0, v4
	v_lshrrev_b32_e32 v5, 26, v5
	s_add_u32 s2, s22, 0x19900000
	v_ashrrev_i32_e32 v4, 6, v4
	v_add_u32_e32 v5, v6, v5
	s_addc_u32 s3, s23, 0
	s_mul_i32 s0, s84, 0x1100000
	v_lshlrev_b32_e32 v7, 3, v4
	v_ashrrev_i32_e32 v5, 6, v5
	s_add_u32 s0, s22, s0
	v_and_b32_e32 v7, -16, v7
	v_mul_i32_i24_e32 v8, 64, v5
	s_addc_u32 s1, s23, 0
	v_add_u32_e32 v7, v5, v7
	v_sub_u32_e32 v6, v6, v8
	s_add_u32 s13, s0, 0x72f00000
	v_lshlrev_b32_e32 v4, 5, v4
	v_ashrrev_i16_sdwa v6, v242, sext(v6) dst_sel:DWORD dst_unused:UNUSED_PAD src0_sel:DWORD src1_sel:BYTE_0
	v_lshlrev_b32_e32 v8, 1, v7
	v_lshrrev_b32_e32 v9, 2, v7
	v_and_b32_e32 v5, 3, v5
	s_mov_b32 s0, 0x1fffe0
	v_and_b32_e32 v4, 32, v4
	v_bfe_i32 v6, v6, 0, 16
	v_and_b32_e32 v8, 24, v8
	v_and_b32_e32 v9, 4, v9
	v_and_or_b32 v5, v7, s0, v5
	v_or3_b32 v5, v5, v9, v8
	v_add_lshl_u32 v4, v4, v6, 1
	v_add_u32_e32 v3, 0x2000, v3
	v_lshl_add_u32 v165, v7, 11, v4
	v_lshl_add_u32 v170, v5, 11, v4
	v_ashrrev_i32_e32 v4, 31, v3
	v_lshrrev_b32_e32 v4, 22, v4
	v_add_u32_e32 v4, v3, v4
	v_ashrrev_i32_e32 v4, 10, v4
	v_mul_i32_i24_e32 v5, 0x400, v4
	v_sub_u32_e32 v3, v3, v5
	v_lshrrev_b32_e32 v5, 4, v3
	v_bitop3_b32 v3, v5, v3, 32 bitop3:0x6c
	v_ashrrev_i32_e32 v6, 31, v3
	v_lshrrev_b32_e32 v6, 26, v6
	v_lshlrev_b32_e32 v5, 3, v4
	v_add_u32_e32 v6, v3, v6
	v_writelane_b32 v255, s10, 48
	v_and_b32_e32 v5, -16, v5
	v_ashrrev_i32_e32 v7, 6, v6
	v_writelane_b32 v255, s11, 49
	s_addc_u32 s18, s1, 0
	s_ashr_i32 s10, s9, 6
	v_add_u32_e32 v5, v7, v5
	v_and_b32_e32 v6, 0xc0, v6
	v_and_b32_e32 v7, 3, v7
	v_sub_u32_e32 v3, v3, v6
	v_and_or_b32 v7, v5, s0, v7
	s_ashr_i32 s11, s9, 8
	s_lshl_b32 s0, s10, 10
	v_readlane_b32 s16, v254, 57
	v_lshlrev_b32_e32 v4, 5, v4
	v_ashrrev_i16_sdwa v3, v242, sext(v3) dst_sel:DWORD dst_unused:UNUSED_PAD src0_sel:DWORD src1_sel:BYTE_0
	v_lshlrev_b32_e32 v6, 1, v5
	v_lshrrev_b32_e32 v8, 2, v5
	v_readlane_b32 s17, v254, 58
	s_add_u32 s42, s13, s16
	v_and_b32_e32 v4, 32, v4
	v_bfe_i32 v3, v3, 0, 16
	v_and_b32_e32 v6, 24, v6
	v_and_b32_e32 v8, 4, v8
	s_addc_u32 s43, s18, s17
	s_add_i32 s19, s0, 0
	s_load_dwordx4 s[44:47], s[40:41], 0x68
	v_or3_b32 v6, v7, v8, v6
	v_add_lshl_u32 v3, v4, v3, 1
	s_add_i32 s27, s19, 0x10000
	s_mov_b32 m0, s27
	s_nop 0
	global_load_lds_dwordx4 v170, s[42:43]
	s_add_i32 s28, s19, 0x12000
	v_lshl_add_u32 v172, v6, 11, v3
	s_mov_b32 m0, s28
	s_nop 0
	global_load_lds_dwordx4 v172, s[42:43]
	s_add_u32 s16, s42, 0x40000
	s_addc_u32 s17, s43, 0
	s_add_i32 s29, s19, 0x14000
	s_mov_b32 m0, s29
	s_nop 0
	global_load_lds_dwordx4 v170, s[16:17]
	s_add_i32 s34, s19, 0x16000
	s_mov_b32 m0, s34
	s_nop 0
	global_load_lds_dwordx4 v172, s[16:17]
	v_lshl_add_u32 v171, v5, 11, v3
	v_readlane_b32 s0, v254, 61
	v_readlane_b32 s1, v254, 62
	s_add_u32 s76, s2, s0
	s_addc_u32 s77, s3, s1
	s_add_i32 s35, s19, 0x2000
	s_mov_b32 m0, s19
	s_nop 0
	global_load_lds_dwordx4 v165, s[76:77]
	s_add_u32 s30, s76, 0x40000
	s_mov_b32 m0, s35
	s_nop 0
	global_load_lds_dwordx4 v171, s[76:77]
	s_addc_u32 s31, s77, 0
	s_add_i32 s36, s19, 0x4000
	s_add_i32 s37, s19, 0x6000
	v_writelane_b32 v255, s86, 50
	s_mov_b32 m0, s36
	s_nop 0
	global_load_lds_dwordx4 v165, s[30:31]
	s_cmp_eq_u32 s11, 1
	s_cselect_b64 s[0:1], -1, 0
	v_writelane_b32 v255, s87, 51
	v_writelane_b32 v255, s0, 52
	s_cmp_lg_u32 s11, 1
	s_nop 0
	v_writelane_b32 v255, s1, 53
	s_mov_b32 m0, s37
	s_nop 0
	global_load_lds_dwordx4 v171, s[30:31]
	s_cbranch_scc1 .LBB0_472
	s_barrier
.LBB0_472:
	s_flbit_i32_b32 s0, s21
	s_min_u32 s0, s0, 32
	s_lshl_b64 s[20:21], s[20:21], s0
	s_min_u32 s1, s20, 1
	s_or_b32 s1, s21, s1
	v_cvt_f32_u32_e32 v3, s1
	s_sub_i32 s0, 32, s0
	v_fmac_f32_e32 v2, 0x40880000, v1
	v_max_f32_e32 v1, 0xda24260, v2
	v_ldexp_f32 v3, v3, s0
	v_mul_f32_e32 v3, 0x2f800000, v3
	s_mov_b32 s0, 0x4a880000
	v_div_scale_f32 v4, s[20:21], s0, s0, v3
	v_rcp_f32_e32 v5, v4
	v_div_scale_f32 v6, vcc, v3, s0, v3
	s_add_u32 s20, s22, 0x45900000
	v_fma_f32 v7, -v4, v5, 1.0
	v_fmac_f32_e32 v5, v7, v5
	v_mul_f32_e32 v7, v6, v5
	v_fma_f32 v8, -v4, v7, v6
	v_fmac_f32_e32 v7, v8, v5
	v_fma_f32 v4, -v4, v7, v6
	v_div_fmas_f32 v4, v4, v5, v7
	v_div_fixup_f32 v3, v4, s0, v3
	s_mov_b32 s0, 0xf800000
	v_mul_f32_e32 v4, 0x4f800000, v3
	v_cmp_gt_f32_e32 vcc, s0, v3
	s_addc_u32 s21, s23, 0
	s_lshl_b32 s72, s84, 6
	v_cndmask_b32_e32 v3, v3, v4, vcc
	v_sqrt_f32_e32 v4, v3
	s_add_u32 s54, s22, 0x100000
	s_mov_b32 s0, s84
	s_addc_u32 s55, s23, 0
	v_add_u32_e32 v2, -1, v4
	v_fma_f32 v5, -v2, v4, v3
	v_cmp_ge_f32_e64 s[40:41], 0, v5
	v_add_u32_e32 v5, 1, v4
	v_mul_f32_e32 v1, 0x3c010204, v1
	v_cndmask_b32_e64 v2, v4, v2, s[40:41]
	v_fma_f32 v4, -v5, v4, v3
	v_cmp_lt_f32_e64 s[40:41], 0, v4
	v_writelane_b32 v255, s0, 54
	s_add_u32 s56, s22, 0x140000
	v_cndmask_b32_e64 v2, v2, v5, s[40:41]
	v_mul_f32_e32 v4, 0x37800000, v2
	v_cndmask_b32_e32 v2, v2, v4, vcc
	v_cmp_class_f32_e32 vcc, v3, v250
	v_writelane_b32 v255, s1, 55
	s_addc_u32 s57, s23, 0
	v_cndmask_b32_e32 v2, v2, v3, vcc
	v_mul_f32_e32 v2, 0x40880000, v2
	v_max_f32_e32 v2, 0xda24260, v2
	v_mul_f32_e32 v2, 0x3c010204, v2
	v_mul_f32_e32 v158, v1, v2
	s_and_b32 s0, s10, 3
	v_and_b32_e32 v1, 48, v0
	v_lshlrev_b32_e32 v2, 6, v0
	s_movk_i32 s10, 0x3c0
	v_lshlrev_b32_e32 v0, 2, v0
	s_lshl_b32 s1, s11, 13
	v_and_or_b32 v1, v2, s10, v1
	v_and_b32_e32 v0, 32, v0
	s_lshl_b32 s51, s11, 6
	v_bitop3_b32 v2, v1, s1, v0 bitop3:0xde
	s_lshl_b32 s65, s0, 5
	s_lshl_b32 s1, s0, 12
	s_add_u32 s10, s42, 0x80
	v_bitop3_b32 v0, v1, s1, v0 bitop3:0xde
	s_waitcnt vmcnt(2)
	s_barrier
	s_addc_u32 s11, s43, 0
	s_add_i32 s66, s19, 0x18000
	s_mov_b32 m0, s66
	s_nop 0
	global_load_lds_dwordx4 v170, s[10:11]
	s_add_i32 s67, s19, 0x1a000
	s_mov_b32 m0, s67
	s_nop 0
	global_load_lds_dwordx4 v172, s[10:11]
	s_add_u32 s10, s76, 0x80
	s_addc_u32 s11, s77, 0
	s_add_i32 s68, s19, 0x8000
	s_mov_b32 m0, s68
	s_nop 0
	global_load_lds_dwordx4 v165, s[10:11]
	s_add_i32 s69, s19, 0xa000
	s_mov_b32 m0, s69
	s_nop 0
	global_load_lds_dwordx4 v171, s[10:11]
	s_add_u32 s10, s42, 0x40080
	s_addc_u32 s11, s43, 0
	s_add_i32 s71, s19, 0x1c000
	s_mov_b32 m0, s71
	s_nop 0
	global_load_lds_dwordx4 v170, s[10:11]
	s_add_i32 s88, s19, 0x1e000
	s_mov_b32 m0, s88
	s_nop 0
	global_load_lds_dwordx4 v172, s[10:11]
	s_add_i32 s89, s19, 0xc000
	s_waitcnt vmcnt(6)
	s_cmpk_lt_u32 s9, 0x100
	s_cselect_b64 s[58:59], -1, 0
	s_lshl_b32 s90, s0, 6
	v_readlane_b32 s0, v254, 59
	v_cmp_neq_f32_e64 s[40:41], 1.0, v158
	v_mov_b32_e32 v160, v158
	v_mov_b32_e32 v161, v158
	s_mov_b32 s91, 0
	v_add_u32_e32 v173, 0, v0
	v_add_u32_e32 v174, 0, v2
	s_lshl_b64 s[60:61], s[72:73], 2
	v_readlane_b32 s30, v254, 56
	s_mov_b32 s31, s0
	s_barrier
	v_readlane_b32 s1, v254, 60
	s_branch .LBB0_475

.LBB0_478:
	s_cmp_gt_u32 s92, 13
	s_cselect_b64 s[80:81], -1, 0
	s_and_b64 vcc, s[80:81], exec
	s_cselect_b32 s0, -14, 2
	s_add_i32 s80, s0, s92
	s_ashr_i32 s81, s80, 31
	s_lshl_b64 s[80:81], s[80:81], 7
	s_add_u32 s0, s76, s80
	s_addc_u32 s1, s77, s81
	s_add_u32 s82, s42, s80
	s_addc_u32 s83, s43, s81
	s_cmp_gt_u32 s92, 12
	s_cselect_b32 s80, -13, 3
	s_add_i32 s80, s80, s92
	s_ashr_i32 s81, s80, 31
	s_lshl_b64 s[80:81], s[80:81], 7
	s_add_u32 s94, s76, s80
	s_addc_u32 s50, s77, s81
	s_add_u32 s16, s42, s80
	s_addc_u32 s17, s43, s81
	s_cmp_eq_u32 s92, 14
	s_cselect_b32 s84, s70, s0
	s_mov_b32 s0, s92
	v_add_u32_e32 v140, 0x10000, v173
	v_add_u32_e32 v156, 0x14000, v173
	ds_read_b128 v[128:131], v140
	ds_read_b128 v[132:135], v140 offset:1024
	ds_read_b128 v[136:139], v140 offset:2048
	ds_read_b128 v[140:143], v140 offset:3072
	ds_read_b128 v[144:147], v156
	ds_read_b128 v[148:151], v156 offset:1024
	ds_read_b128 v[152:155], v156 offset:2048
	ds_read_b128 v[166:169], v156 offset:3072
	s_cselect_b32 s85, s63, s1
	s_cselect_b32 s87, s72, s83
	s_cselect_b32 s86, s75, s82
	s_cselect_b32 s81, s10, s50
	s_cselect_b32 s80, s9, s94
	s_cselect_b32 s83, s12, s17
	s_cselect_b32 s82, s11, s16
	ds_read_b128 v[176:179], v174
	ds_read_b128 v[180:183], v174 offset:1024
	ds_read_b128 v[184:187], v174 offset:2048
	ds_read_b128 v[190:193], v174 offset:3072
	ds_read_b128 v[194:197], v174 offset:4096
	ds_read_b128 v[198:201], v174 offset:5120
	ds_read_b128 v[202:205], v174 offset:6144
	ds_read_b128 v[206:209], v174 offset:7168
	s_add_u32 s0, s78, 0x40080
	s_addc_u32 s1, s79, 0
	s_mov_b32 m0, s89
	s_nop 0
	global_load_lds_dwordx4 v165, s[0:1]
	s_add_i32 s16, s19, 0xe000
	s_mov_b32 m0, s16
	s_nop 0
	global_load_lds_dwordx4 v171, s[0:1]
	s_setprio 1
	s_waitcnt vmcnt(8)
	s_waitcnt lgkmcnt(0)
	s_barrier
	v_mfma_i32_16x16x64_i8 v[124:127], v[128:131], v[176:179], v[124:127]
	v_mfma_i32_16x16x64_i8 v[120:123], v[136:139], v[176:179], v[120:123]
	v_mfma_i32_16x16x64_i8 v[116:119], v[128:131], v[184:187], v[116:119]
	v_mfma_i32_16x16x64_i8 v[108:111], v[136:139], v[184:187], v[108:111]
	v_mfma_i32_16x16x64_i8 v[100:103], v[128:131], v[194:197], v[100:103]
	v_mfma_i32_16x16x64_i8 v[92:95], v[136:139], v[194:197], v[92:95]
	v_mfma_i32_16x16x64_i8 v[84:87], v[128:131], v[202:205], v[84:87]
	v_mfma_i32_16x16x64_i8 v[76:79], v[136:139], v[202:205], v[76:79]
	v_mfma_i32_16x16x64_i8 v[124:127], v[132:135], v[180:183], v[124:127]
	v_mfma_i32_16x16x64_i8 v[120:123], v[140:143], v[180:183], v[120:123]
	v_mfma_i32_16x16x64_i8 v[116:119], v[132:135], v[190:193], v[116:119]
	v_mfma_i32_16x16x64_i8 v[108:111], v[140:143], v[190:193], v[108:111]
	v_mfma_i32_16x16x64_i8 v[100:103], v[132:135], v[198:201], v[100:103]
	v_mfma_i32_16x16x64_i8 v[92:95], v[140:143], v[198:201], v[92:95]
	v_mfma_i32_16x16x64_i8 v[84:87], v[132:135], v[206:209], v[84:87]
	v_mfma_i32_16x16x64_i8 v[76:79], v[140:143], v[206:209], v[76:79]
	v_mfma_i32_16x16x64_i8 v[112:115], v[144:147], v[176:179], v[112:115]
	v_mfma_i32_16x16x64_i8 v[104:107], v[152:155], v[176:179], v[104:107]
	v_mfma_i32_16x16x64_i8 v[96:99], v[144:147], v[184:187], v[96:99]
	v_mfma_i32_16x16x64_i8 v[88:91], v[152:155], v[184:187], v[88:91]
	v_mfma_i32_16x16x64_i8 v[80:83], v[144:147], v[194:197], v[80:83]
	v_mfma_i32_16x16x64_i8 v[72:75], v[152:155], v[194:197], v[72:75]
	v_mfma_i32_16x16x64_i8 v[68:71], v[144:147], v[202:205], v[68:71]
	v_mfma_i32_16x16x64_i8 v[64:67], v[152:155], v[202:205], v[64:67]
	v_mfma_i32_16x16x64_i8 v[112:115], v[148:151], v[180:183], v[112:115]
	v_mfma_i32_16x16x64_i8 v[104:107], v[166:169], v[180:183], v[104:107]
	v_mfma_i32_16x16x64_i8 v[96:99], v[148:151], v[190:193], v[96:99]
	v_mfma_i32_16x16x64_i8 v[88:91], v[166:169], v[190:193], v[88:91]
	v_mfma_i32_16x16x64_i8 v[80:83], v[148:151], v[198:201], v[80:83]
	v_mfma_i32_16x16x64_i8 v[72:75], v[166:169], v[198:201], v[72:75]
	v_mfma_i32_16x16x64_i8 v[68:71], v[148:151], v[206:209], v[68:71]
	v_mfma_i32_16x16x64_i8 v[64:67], v[166:169], v[206:209], v[64:67]
	s_barrier
	s_setprio 0
	ds_read_b128 v[176:179], v174 offset:16384
	ds_read_b128 v[180:183], v174 offset:17408
	ds_read_b128 v[184:187], v174 offset:18432
	ds_read_b128 v[190:193], v174 offset:19456
	ds_read_b128 v[194:197], v174 offset:20480
	ds_read_b128 v[198:201], v174 offset:21504
	ds_read_b128 v[202:205], v174 offset:22528
	ds_read_b128 v[206:209], v174 offset:23552
	s_mov_b32 m0, s27
	s_nop 0
	global_load_lds_dwordx4 v170, s[86:87]
	s_nop 0
	s_mov_b32 m0, s28
	s_nop 0
	global_load_lds_dwordx4 v172, s[86:87]
	s_add_u32 s0, s86, 0x40000
	s_addc_u32 s1, s87, 0
	s_mov_b32 m0, s29
	s_nop 0
	global_load_lds_dwordx4 v170, s[0:1]
	s_nop 0
	s_mov_b32 m0, s34
	s_nop 0
	global_load_lds_dwordx4 v172, s[0:1]
	s_mov_b32 m0, s19
	s_nop 0
	global_load_lds_dwordx4 v165, s[84:85]
	s_nop 0
	s_mov_b32 m0, s35
	s_nop 0
	global_load_lds_dwordx4 v171, s[84:85]
	s_setprio 1
	s_waitcnt vmcnt(8)
	s_waitcnt lgkmcnt(0)
	s_barrier
	v_mfma_i32_16x16x64_i8 v[60:63], v[128:131], v[176:179], v[60:63]
	v_mfma_i32_16x16x64_i8 v[56:59], v[136:139], v[176:179], v[56:59]
	v_mfma_i32_16x16x64_i8 v[52:55], v[128:131], v[184:187], v[52:55]
	v_mfma_i32_16x16x64_i8 v[44:47], v[136:139], v[184:187], v[44:47]
	v_mfma_i32_16x16x64_i8 v[36:39], v[128:131], v[194:197], v[36:39]
	v_mfma_i32_16x16x64_i8 v[28:31], v[136:139], v[194:197], v[28:31]
	v_mfma_i32_16x16x64_i8 v[20:23], v[128:131], v[202:205], v[20:23]
	v_mfma_i32_16x16x64_i8 v[12:15], v[136:139], v[202:205], v[12:15]
	v_mfma_i32_16x16x64_i8 v[60:63], v[132:135], v[180:183], v[60:63]
	v_mfma_i32_16x16x64_i8 v[56:59], v[140:143], v[180:183], v[56:59]
	v_mfma_i32_16x16x64_i8 v[52:55], v[132:135], v[190:193], v[52:55]
	v_mfma_i32_16x16x64_i8 v[44:47], v[140:143], v[190:193], v[44:47]
	v_mfma_i32_16x16x64_i8 v[36:39], v[132:135], v[198:201], v[36:39]
	v_mfma_i32_16x16x64_i8 v[28:31], v[140:143], v[198:201], v[28:31]
	v_mfma_i32_16x16x64_i8 v[20:23], v[132:135], v[206:209], v[20:23]
	v_mfma_i32_16x16x64_i8 v[12:15], v[140:143], v[206:209], v[12:15]
	v_mfma_i32_16x16x64_i8 v[48:51], v[144:147], v[176:179], v[48:51]
	v_mfma_i32_16x16x64_i8 v[40:43], v[152:155], v[176:179], v[40:43]
	v_mfma_i32_16x16x64_i8 v[32:35], v[144:147], v[184:187], v[32:35]
	v_mfma_i32_16x16x64_i8 v[24:27], v[152:155], v[184:187], v[24:27]
	v_mfma_i32_16x16x64_i8 v[16:19], v[144:147], v[194:197], v[16:19]
	v_mfma_i32_16x16x64_i8 v[8:11], v[152:155], v[194:197], v[8:11]
	v_mfma_i32_16x16x64_i8 v[4:7], v[144:147], v[202:205], v[4:7]
	v_mfma_i32_16x16x64_i8 v[0:3], v[152:155], v[202:205], v[0:3]
	v_mfma_i32_16x16x64_i8 v[48:51], v[148:151], v[180:183], v[48:51]
	v_mfma_i32_16x16x64_i8 v[40:43], v[166:169], v[180:183], v[40:43]
	v_mfma_i32_16x16x64_i8 v[32:35], v[148:151], v[190:193], v[32:35]
	v_mfma_i32_16x16x64_i8 v[24:27], v[166:169], v[190:193], v[24:27]
	v_mfma_i32_16x16x64_i8 v[16:19], v[148:151], v[198:201], v[16:19]
	v_mfma_i32_16x16x64_i8 v[8:11], v[166:169], v[198:201], v[8:11]
	v_mfma_i32_16x16x64_i8 v[4:7], v[148:151], v[206:209], v[4:7]
	v_mfma_i32_16x16x64_i8 v[0:3], v[166:169], v[206:209], v[0:3]
	s_barrier
	s_setprio 0
	v_add_u32_e32 v140, 0x18000, v173
	v_add_u32_e32 v156, 0x1c000, v173
	ds_read_b128 v[128:131], v140
	ds_read_b128 v[132:135], v140 offset:1024
	ds_read_b128 v[136:139], v140 offset:2048
	ds_read_b128 v[140:143], v140 offset:3072
	ds_read_b128 v[144:147], v156
	ds_read_b128 v[148:151], v156 offset:1024
	ds_read_b128 v[152:155], v156 offset:2048
	ds_read_b128 v[166:169], v156 offset:3072
	ds_read_b128 v[176:179], v174 offset:32768
	ds_read_b128 v[180:183], v174 offset:33792
	ds_read_b128 v[184:187], v174 offset:34816
	ds_read_b128 v[190:193], v174 offset:35840
	ds_read_b128 v[194:197], v174 offset:36864
	ds_read_b128 v[198:201], v174 offset:37888
	ds_read_b128 v[202:205], v174 offset:38912
	ds_read_b128 v[206:209], v174 offset:39936
	s_add_u32 s0, s84, 0x40000
	s_addc_u32 s1, s85, 0
	s_mov_b32 m0, s36
	s_nop 0
	global_load_lds_dwordx4 v165, s[0:1]
	s_nop 0
	s_mov_b32 m0, s37
	s_nop 0
	global_load_lds_dwordx4 v171, s[0:1]
	s_setprio 1
	s_waitcnt vmcnt(8)
	s_waitcnt lgkmcnt(0)
	s_barrier
	v_mfma_i32_16x16x64_i8 v[124:127], v[128:131], v[176:179], v[124:127]
	v_mfma_i32_16x16x64_i8 v[120:123], v[136:139], v[176:179], v[120:123]
	v_mfma_i32_16x16x64_i8 v[116:119], v[128:131], v[184:187], v[116:119]
	v_mfma_i32_16x16x64_i8 v[108:111], v[136:139], v[184:187], v[108:111]
	v_mfma_i32_16x16x64_i8 v[100:103], v[128:131], v[194:197], v[100:103]
	v_mfma_i32_16x16x64_i8 v[92:95], v[136:139], v[194:197], v[92:95]
	v_mfma_i32_16x16x64_i8 v[84:87], v[128:131], v[202:205], v[84:87]
	v_mfma_i32_16x16x64_i8 v[76:79], v[136:139], v[202:205], v[76:79]
	v_mfma_i32_16x16x64_i8 v[124:127], v[132:135], v[180:183], v[124:127]
	v_mfma_i32_16x16x64_i8 v[120:123], v[140:143], v[180:183], v[120:123]
	v_mfma_i32_16x16x64_i8 v[116:119], v[132:135], v[190:193], v[116:119]
	v_mfma_i32_16x16x64_i8 v[108:111], v[140:143], v[190:193], v[108:111]
	v_mfma_i32_16x16x64_i8 v[100:103], v[132:135], v[198:201], v[100:103]
	v_mfma_i32_16x16x64_i8 v[92:95], v[140:143], v[198:201], v[92:95]
	v_mfma_i32_16x16x64_i8 v[84:87], v[132:135], v[206:209], v[84:87]
	v_mfma_i32_16x16x64_i8 v[76:79], v[140:143], v[206:209], v[76:79]
	v_mfma_i32_16x16x64_i8 v[112:115], v[144:147], v[176:179], v[112:115]
	v_mfma_i32_16x16x64_i8 v[104:107], v[152:155], v[176:179], v[104:107]
	v_mfma_i32_16x16x64_i8 v[96:99], v[144:147], v[184:187], v[96:99]
	v_mfma_i32_16x16x64_i8 v[88:91], v[152:155], v[184:187], v[88:91]
	v_mfma_i32_16x16x64_i8 v[80:83], v[144:147], v[194:197], v[80:83]
	v_mfma_i32_16x16x64_i8 v[72:75], v[152:155], v[194:197], v[72:75]
	v_mfma_i32_16x16x64_i8 v[68:71], v[144:147], v[202:205], v[68:71]
	v_mfma_i32_16x16x64_i8 v[64:67], v[152:155], v[202:205], v[64:67]
	v_mfma_i32_16x16x64_i8 v[112:115], v[148:151], v[180:183], v[112:115]
	v_mfma_i32_16x16x64_i8 v[104:107], v[166:169], v[180:183], v[104:107]
	v_mfma_i32_16x16x64_i8 v[96:99], v[148:151], v[190:193], v[96:99]
	v_mfma_i32_16x16x64_i8 v[88:91], v[166:169], v[190:193], v[88:91]
	v_mfma_i32_16x16x64_i8 v[80:83], v[148:151], v[198:201], v[80:83]
	v_mfma_i32_16x16x64_i8 v[72:75], v[166:169], v[198:201], v[72:75]
	v_mfma_i32_16x16x64_i8 v[68:71], v[148:151], v[206:209], v[68:71]
	v_mfma_i32_16x16x64_i8 v[64:67], v[166:169], v[206:209], v[64:67]
	s_barrier
	s_setprio 0
	ds_read_b128 v[176:179], v174 offset:49152
	ds_read_b128 v[180:183], v174 offset:50176
	ds_read_b128 v[184:187], v174 offset:51200
	ds_read_b128 v[190:193], v174 offset:52224
	ds_read_b128 v[194:197], v174 offset:53248
	ds_read_b128 v[198:201], v174 offset:54272
	ds_read_b128 v[202:205], v174 offset:55296
	ds_read_b128 v[206:209], v174 offset:56320
	s_mov_b32 m0, s66
	s_nop 0
	global_load_lds_dwordx4 v170, s[82:83]
	s_nop 0
	s_mov_b32 m0, s67
	s_nop 0
	global_load_lds_dwordx4 v172, s[82:83]
	s_add_u32 s0, s82, 0x40000
	s_addc_u32 s1, s83, 0
	s_mov_b32 m0, s71
	s_nop 0
	global_load_lds_dwordx4 v170, s[0:1]
	s_nop 0
	s_mov_b32 m0, s88
	s_nop 0
	global_load_lds_dwordx4 v172, s[0:1]
	s_mov_b32 m0, s68
	s_nop 0
	global_load_lds_dwordx4 v165, s[80:81]
	s_nop 0
	s_mov_b32 m0, s69
	s_nop 0
	global_load_lds_dwordx4 v171, s[80:81]
	s_setprio 1
	s_waitcnt vmcnt(8)
	s_waitcnt lgkmcnt(0)
	s_barrier
	v_mfma_i32_16x16x64_i8 v[60:63], v[128:131], v[176:179], v[60:63]
	v_mfma_i32_16x16x64_i8 v[56:59], v[136:139], v[176:179], v[56:59]
	v_mfma_i32_16x16x64_i8 v[52:55], v[128:131], v[184:187], v[52:55]
	v_mfma_i32_16x16x64_i8 v[44:47], v[136:139], v[184:187], v[44:47]
	v_mfma_i32_16x16x64_i8 v[36:39], v[128:131], v[194:197], v[36:39]
	v_mfma_i32_16x16x64_i8 v[28:31], v[136:139], v[194:197], v[28:31]
	v_mfma_i32_16x16x64_i8 v[20:23], v[128:131], v[202:205], v[20:23]
	v_mfma_i32_16x16x64_i8 v[12:15], v[136:139], v[202:205], v[12:15]
	v_mfma_i32_16x16x64_i8 v[60:63], v[132:135], v[180:183], v[60:63]
	v_mfma_i32_16x16x64_i8 v[56:59], v[140:143], v[180:183], v[56:59]
	v_mfma_i32_16x16x64_i8 v[52:55], v[132:135], v[190:193], v[52:55]
	v_mfma_i32_16x16x64_i8 v[44:47], v[140:143], v[190:193], v[44:47]
	v_mfma_i32_16x16x64_i8 v[36:39], v[132:135], v[198:201], v[36:39]
	v_mfma_i32_16x16x64_i8 v[28:31], v[140:143], v[198:201], v[28:31]
	v_mfma_i32_16x16x64_i8 v[20:23], v[132:135], v[206:209], v[20:23]
	v_mfma_i32_16x16x64_i8 v[12:15], v[140:143], v[206:209], v[12:15]
	v_mfma_i32_16x16x64_i8 v[48:51], v[144:147], v[176:179], v[48:51]
	v_mfma_i32_16x16x64_i8 v[40:43], v[152:155], v[176:179], v[40:43]
	v_mfma_i32_16x16x64_i8 v[32:35], v[144:147], v[184:187], v[32:35]
	v_mfma_i32_16x16x64_i8 v[24:27], v[152:155], v[184:187], v[24:27]
	v_mfma_i32_16x16x64_i8 v[16:19], v[144:147], v[194:197], v[16:19]
	v_mfma_i32_16x16x64_i8 v[8:11], v[152:155], v[194:197], v[8:11]
	v_mfma_i32_16x16x64_i8 v[4:7], v[144:147], v[202:205], v[4:7]
	v_mfma_i32_16x16x64_i8 v[0:3], v[152:155], v[202:205], v[0:3]
	v_mfma_i32_16x16x64_i8 v[48:51], v[148:151], v[180:183], v[48:51]
	v_mfma_i32_16x16x64_i8 v[40:43], v[166:169], v[180:183], v[40:43]
	v_mfma_i32_16x16x64_i8 v[32:35], v[148:151], v[190:193], v[32:35]
	v_mfma_i32_16x16x64_i8 v[24:27], v[166:169], v[190:193], v[24:27]
	v_mfma_i32_16x16x64_i8 v[16:19], v[148:151], v[198:201], v[16:19]
	v_mfma_i32_16x16x64_i8 v[8:11], v[166:169], v[198:201], v[8:11]
	v_mfma_i32_16x16x64_i8 v[4:7], v[148:151], v[206:209], v[4:7]
	v_mfma_i32_16x16x64_i8 v[0:3], v[166:169], v[206:209], v[0:3]
	s_barrier
	s_setprio 0
	s_add_i32 s92, s92, 2
	s_add_u32 s78, s78, 0x100
	s_addc_u32 s79, s79, 0
	s_cbranch_vccz .LBB0_478
	s_and_b64 vcc, exec, s[58:59]
	s_cbranch_vccz .LBB0_481
	s_barrier

.LBB0_619:
	v_mbcnt_lo_u32_b32 v0, -1, 0
	v_mbcnt_hi_u32_b32 v0, -1, v0
	s_lshl_b32 s9, s66, 8
	v_or_b32_e32 v82, s33, v0
	v_mov_b32_e32 v81, v189
	v_readfirstlane_b32 s12, v82
	s_ashr_i32 s67, s12, 6
	s_add_u32 s9, s20, s9
	s_addc_u32 s10, s21, 0
	s_lshl_b32 s11, s67, 5
	s_ashr_i32 s42, s11, 31
	s_add_u32 s9, s9, s11
	s_addc_u32 s10, s10, s42
	s_mulk_i32 s10, 0x4400
	s_mul_hi_u32 s11, s9, 0x4400
	s_add_i32 s11, s11, s10
	s_mulk_i32 s9, 0x4400
	v_and_b32_e32 v192, 63, v82
	s_add_u32 s54, s51, s9
	s_addc_u32 s55, s65, s11
	v_mul_u32_u24_e32 v0, 0x2200, v192
	s_lshl_b32 s10, s67, 3
	v_lshlrev_b32_e32 v188, 1, v0
	s_ashr_i32 s11, s10, 31
	v_lshl_add_u64 v[0:1], s[22:23], 0, v[188:189]
	s_lshl_b64 s[56:57], s[10:11], 1
	v_lshl_add_u64 v[180:181], v[0:1], 0, s[56:57]
	s_lshl_b32 s10, s67, 4
	v_bfe_u32 v0, v82, 2, 4
	v_and_or_b32 v0, s10, 48, v0
	s_ashr_i32 s10, s12, 3
	s_andn2_b32 s10, s10, 31
	s_ashr_i32 s11, s10, 31
	s_and_b32 s9, s12, 0x3fffffc0
	v_mul_u32_u24_e32 v0, 0x2200, v0
	s_lshl_b64 s[58:59], s[10:11], 1
	s_lshl_b32 s10, s67, 10
	v_lshlrev_b32_e32 v80, 1, v0
	v_lshlrev_b32_e32 v193, 3, v82
	s_cmp_lg_u32 0, -1
	v_lshl_add_u64 v[0:1], s[44:45], 0, v[80:81]
	v_and_b32_e32 v196, 24, v193
	s_cselect_b32 s11, 0, 0
	v_lshl_add_u64 v[0:1], v[0:1], 0, s[58:59]
	s_waitcnt vmcnt(1)
	v_lshlrev_b32_e32 v2, 1, v196
	s_waitcnt vmcnt(0)
	v_mov_b32_e32 v3, v189
	s_add_i32 s69, s10, s11
	s_mov_b32 m0, s69
	s_nop 0
	global_load_lds_dwordx4 v[180:181], off
	v_and_b32_e32 v194, 31, v82
	v_bfe_u32 v195, v82, 5, 1
	v_lshl_add_u64 v[182:183], v[0:1], 0, v[2:3]
	s_add_i32 s70, s69, 0x6000
	s_mov_b32 m0, s70
	s_nop 0
	global_load_lds_dwordx4 v[182:183], off
	v_lshl_add_u64 v[0:1], v[180:181], 0, s[4:5]
	s_add_i32 s10, s69, 0x2000
	s_mov_b32 m0, s10
	s_nop 0
	global_load_lds_dwordx4 v[0:1], off
	v_mul_u32_u24_e32 v0, 0x2200, v194
	v_lshlrev_b32_e32 v199, 4, v195
	v_lshl_or_b32 v8, v0, 1, v199
	global_load_dwordx4 v[140:143], v8, s[54:55]
	global_load_dwordx4 v[136:139], v8, s[54:55] offset:32
	global_load_dwordx4 v[128:131], v8, s[54:55] offset:64
	global_load_dwordx4 v[120:123], v8, s[54:55] offset:96
	v_mov_b32_e32 v0, v189
	v_mov_b32_e32 v1, v189
	v_mov_b32_e32 v2, v189
	v_mov_b32_e32 v4, v189
	v_mov_b32_e32 v5, v189
	v_mov_b32_e32 v6, v189
	v_mov_b32_e32 v7, v189
	v_mov_b32_e32 v8, v189
	v_mov_b32_e32 v9, v189
	v_mov_b32_e32 v10, v189
	v_mov_b32_e32 v11, v189
	v_mov_b32_e32 v12, v189
	v_mov_b32_e32 v13, v189
	v_mov_b32_e32 v14, v189
	v_mov_b32_e32 v15, v189
	v_lshlrev_b32_e32 v16, 10, v195
	v_lshlrev_b32_e32 v17, 4, v194
	v_add3_u32 v202, 0, v16, v17
	v_lshl_add_u64 v[16:17], v[180:181], 0, s[38:39]
	s_add_i32 s10, s69, 0x4000
	s_mov_b32 m0, s10
	s_nop 0
	global_load_lds_dwordx4 v[16:17], off
	s_waitcnt vmcnt(3) lgkmcnt(0)
	s_barrier
	ds_read_b128 v[32:35], v202
	ds_read_b128 v[36:39], v202 offset:512
	s_lshl_b32 s9, s9, 2
	s_add_i32 s68, s9, 0
	v_lshl_add_u64 v[184:185], s[56:57], 0, v[188:189]
	v_mov_b32_e32 v188, 0
	s_mov_b32 s60, -1
	s_movk_i32 s62, 0x2000
	s_movk_i32 s61, 0x4000
	v_cmp_gt_u32_e64 s[42:43], 32, v192
	v_lshl_add_u32 v200, v194, 2, s68
	v_lshl_add_u64 v[186:187], s[46:47], 0, v[184:185]
	s_waitcnt vmcnt(3) lgkmcnt(1)
	v_mfma_f32_32x32x16_bf16 v[16:31], v[32:35], v[140:143], v[0:15]
	s_waitcnt lgkmcnt(0)
	v_mfma_f32_32x32x16_bf16 v[0:15], v[36:39], v[140:143], v[0:15]
	ds_read_b128 v[32:35], v202 offset:2048
	ds_read_b128 v[36:39], v202 offset:2560
	s_waitcnt vmcnt(2) lgkmcnt(1)
	v_mfma_f32_32x32x16_bf16 v[16:31], v[32:35], v[136:139], v[16:31]
	s_waitcnt lgkmcnt(0)
	v_mfma_f32_32x32x16_bf16 v[0:15], v[36:39], v[136:139], v[0:15]
	ds_read_b128 v[32:35], v202 offset:4096
	ds_read_b128 v[36:39], v202 offset:4608
	s_waitcnt vmcnt(1) lgkmcnt(1)
	v_mfma_f32_32x32x16_bf16 v[16:31], v[32:35], v[128:131], v[16:31]
	ds_read_b128 v[32:35], v202 offset:6144
	s_waitcnt lgkmcnt(1)
	v_mfma_f32_32x32x16_bf16 v[0:15], v[36:39], v[128:131], v[0:15]
	ds_read_b128 v[36:39], v202 offset:6656
	s_waitcnt vmcnt(0) lgkmcnt(1)
	v_mfma_f32_32x32x16_bf16 v[16:31], v[32:35], v[120:123], v[16:31]
	v_lshlrev_b32_e32 v32, 1, v82
	v_lshlrev_b32_e32 v33, 4, v82
	v_and_b32_e32 v197, 32, v32
	v_and_b32_e32 v32, 0xc0, v33
	v_lshl_or_b32 v198, v195, 8, v32
	v_add_u32_e32 v83, 0, v197
	v_add3_u32 v203, v83, v196, v198
	s_waitcnt lgkmcnt(0)
	v_mfma_f32_32x32x16_bf16 v[0:15], v[36:39], v[120:123], v[0:15]
	s_nop 15
	s_nop 7
	s_nop 0
	v_max3_f32 v32, v16, v17, v0
	v_max3_f32 v33, v18, v19, v1
	s_nop 0
	v_max3_f32 v32, v32, v2, v3
	v_max3_f32 v33, v33, v22, v23
	s_nop 0
	v_max3_f32 v32, v32, v20, v21
	v_max3_f32 v33, v33, v6, v7
	s_nop 0
	v_max3_f32 v32, v32, v4, v5
	v_max3_f32 v33, v33, v26, v27
	s_nop 0
	v_max3_f32 v32, v32, v24, v25
	v_max3_f32 v33, v33, v10, v11
	s_nop 0
	v_max3_f32 v32, v32, v8, v9
	v_max3_f32 v33, v33, v30, v31
	s_nop 0
	v_max3_f32 v32, v32, v28, v29
	v_max3_f32 v33, v33, v14, v15
	s_nop 0
	v_max3_f32 v32, v32, v12, v13
	s_nop 0
	v_max_f32_e32 v32, v32, v33
	s_nop 0
	v_mov_b32_e32 v33, v32
	s_nop 1
	v_permlane32_swap_b32_e32 v32, v33
	v_max_f32_e32 v32, v32, v33
	s_nop 0
	v_add_f32_e32 v201, v189, v32
	v_sub_f32_e32 v16, v16, v32
	v_sub_f32_e32 v0, v0, v32
	v_sub_f32_e32 v17, v17, v32
	v_sub_f32_e32 v1, v1, v32
	v_sub_f32_e32 v18, v18, v32
	v_sub_f32_e32 v2, v2, v32
	v_sub_f32_e32 v19, v19, v32
	v_sub_f32_e32 v3, v3, v32
	v_sub_f32_e32 v20, v20, v32
	v_sub_f32_e32 v4, v4, v32
	v_sub_f32_e32 v21, v21, v32
	v_sub_f32_e32 v5, v5, v32
	v_sub_f32_e32 v22, v22, v32
	v_sub_f32_e32 v6, v6, v32
	v_sub_f32_e32 v23, v23, v32
	v_sub_f32_e32 v7, v7, v32
	v_sub_f32_e32 v24, v24, v32
	v_sub_f32_e32 v8, v8, v32
	v_sub_f32_e32 v25, v25, v32
	v_sub_f32_e32 v9, v9, v32
	v_sub_f32_e32 v26, v26, v32
	v_sub_f32_e32 v10, v10, v32
	v_sub_f32_e32 v27, v27, v32
	v_sub_f32_e32 v11, v11, v32
	v_sub_f32_e32 v28, v28, v32
	v_sub_f32_e32 v12, v12, v32
	v_sub_f32_e32 v29, v29, v32
	v_sub_f32_e32 v13, v13, v32
	v_sub_f32_e32 v30, v30, v32
	v_sub_f32_e32 v14, v14, v32
	v_sub_f32_e32 v31, v31, v32
	v_sub_f32_e32 v15, v15, v32
	s_nop 0
	v_xor_b32_e32 v32, 0x80000000, v201
	v_mov_b32_e32 v33, v32
	v_mov_b32_e32 v34, v32
	v_mov_b32_e32 v35, v32
	v_mov_b32_e32 v36, v32
	v_mov_b32_e32 v37, v32
	v_mov_b32_e32 v38, v32
	v_mov_b32_e32 v39, v32
	v_mov_b32_e32 v40, v32
	v_mov_b32_e32 v41, v32
	v_mov_b32_e32 v42, v32
	v_mov_b32_e32 v43, v32
	v_mov_b32_e32 v44, v32
	v_mov_b32_e32 v45, v32
	v_mov_b32_e32 v46, v32
	v_mov_b32_e32 v47, v32
	s_waitcnt vmcnt(0) lgkmcnt(0)
	s_barrier
	v_exp_f32_e32 v48, v0
	v_exp_f32_e32 v49, v1
	v_lshl_add_u64 v[0:1], v[180:181], 0, s[14:15]
	s_mov_b32 m0, s69
	s_nop 0
	global_load_lds_dwordx4 v[0:1], off
	v_lshl_add_u64 v[0:1], v[182:183], 0, s[4:5]
	s_add_i32 s9, s69, 0x8000
	s_mov_b32 m0, s9
	s_nop 0
	global_load_lds_dwordx4 v[0:1], off
	ds_read_b128 v[172:175], v202 offset:8192
	ds_read_b128 v[168:171], v202 offset:8704
	ds_read_b128 v[164:167], v202 offset:10240
	ds_read_b128 v[160:163], v202 offset:10752
	ds_read_b128 v[156:159], v202 offset:12288
	ds_read_b128 v[152:155], v202 offset:12800
	ds_read_b128 v[148:151], v202 offset:14336
	ds_read_b128 v[144:147], v202 offset:14848
	v_exp_f32_e32 v64, v16
	v_exp_f32_e32 v65, v17
	v_exp_f32_e32 v66, v18
	v_exp_f32_e32 v67, v19
	v_exp_f32_e32 v68, v20
	v_exp_f32_e32 v69, v21
	v_exp_f32_e32 v70, v22
	v_exp_f32_e32 v71, v23
	v_exp_f32_e32 v72, v24
	v_exp_f32_e32 v73, v25
	v_exp_f32_e32 v74, v26
	v_exp_f32_e32 v75, v27
	v_exp_f32_e32 v76, v28
	v_exp_f32_e32 v77, v29
	v_exp_f32_e32 v78, v30
	v_exp_f32_e32 v79, v31
	v_exp_f32_e32 v50, v2
	v_exp_f32_e32 v51, v3
	v_exp_f32_e32 v52, v4
	v_exp_f32_e32 v53, v5
	v_exp_f32_e32 v54, v6
	v_exp_f32_e32 v55, v7
	v_exp_f32_e32 v56, v8
	v_exp_f32_e32 v57, v9
	v_exp_f32_e32 v58, v10
	v_exp_f32_e32 v59, v11
	v_exp_f32_e32 v60, v12
	v_exp_f32_e32 v61, v13
	v_exp_f32_e32 v62, v14
	v_exp_f32_e32 v63, v15
	v_and_b32_e32 v0, 3, v82
	s_waitcnt vmcnt(2) lgkmcnt(0)
	s_barrier
	v_lshl_or_b32 v0, v0, 4, s58
	v_mov_b32_e32 v1, s59
	v_lshl_add_u64 v[0:1], v[0:1], 0, v[80:81]
	v_lshl_add_u64 v[190:191], s[48:49], 0, v[0:1]
	s_mov_b32 s10, 0
	v_mov_b32_e32 v0, 0
	v_mov_b32_e32 v1, v188
	v_mov_b32_e32 v2, v188
	v_mov_b32_e32 v3, v188
	v_mov_b32_e32 v4, v188
	v_mov_b32_e32 v5, v188
	v_mov_b32_e32 v6, v188
	v_mov_b32_e32 v7, v188
	v_mov_b32_e32 v8, v188
	v_mov_b32_e32 v9, v188
	v_mov_b32_e32 v10, v188
	v_mov_b32_e32 v11, v188
	v_mov_b32_e32 v12, v188
	v_mov_b32_e32 v13, v188
	v_mov_b32_e32 v14, v188
	v_mov_b32_e32 v15, v188
	v_mov_b32_e32 v16, 0
	v_mov_b32_e32 v17, v188
	v_mov_b32_e32 v18, v188
	v_mov_b32_e32 v19, v188
	v_mov_b32_e32 v20, v188
	v_mov_b32_e32 v21, v188
	v_mov_b32_e32 v22, v188
	v_mov_b32_e32 v23, v188
	v_mov_b32_e32 v24, v188
	v_mov_b32_e32 v25, v188
	v_mov_b32_e32 v26, v188
	v_mov_b32_e32 v27, v188
	v_mov_b32_e32 v28, v188
	v_mov_b32_e32 v29, v188
	v_mov_b32_e32 v30, v188
	v_mov_b32_e32 v31, v188
.LBB0_620:
	v_add_u32_e32 v204, s10, v203
	ds_read_b64_tr_b16 v[176:177], v204 offset:24576
	ds_read_b64_tr_b16 v[178:179], v204 offset:25088
	s_waitcnt lgkmcnt(9)
	v_mfma_f32_32x32x16_bf16 v[96:111], v[172:175], v[140:143], v[32:47]
	v_add_f32_e32 v80, v64, v65
	v_add_f32_e32 v80, v66, v80
	v_add_f32_e32 v80, v67, v80
	v_add_f32_e32 v80, v68, v80
	v_add_f32_e32 v80, v69, v80
	v_cvt_pk_bf16_f32 v132, v64, v65
	v_cvt_pk_bf16_f32 v133, v66, v67
	ds_read_b64_tr_b16 v[172:173], v204 offset:28672
	ds_read_b64_tr_b16 v[174:175], v204 offset:29184
	v_add_f32_e32 v64, v70, v80
	s_waitcnt lgkmcnt(10)
	v_mfma_f32_32x32x16_bf16 v[80:95], v[168:171], v[140:143], v[32:47]
	v_add_f32_e32 v64, v71, v64
	v_add_f32_e32 v64, v72, v64
	v_add_f32_e32 v112, v73, v64
	v_cvt_pk_bf16_f32 v134, v68, v69
	v_cvt_pk_bf16_f32 v135, v70, v71
	ds_read_b64_tr_b16 v[64:65], v204 offset:25600
	ds_read_b64_tr_b16 v[66:67], v204 offset:26112
	s_waitcnt lgkmcnt(11)
	v_mfma_f32_32x32x16_bf16 v[96:111], v[164:167], v[136:139], v[96:111]
	v_add_f32_e32 v68, v74, v112
	v_add_f32_e32 v68, v75, v68
	v_add_f32_e32 v68, v76, v68
	v_add_f32_e32 v112, v77, v68
	v_cvt_pk_bf16_f32 v124, v72, v73
	v_cvt_pk_bf16_f32 v125, v74, v75
	ds_read_b64_tr_b16 v[68:69], v204 offset:29696
	ds_read_b64_tr_b16 v[70:71], v204 offset:30208
	s_waitcnt lgkmcnt(12)
	v_mfma_f32_32x32x16_bf16 v[80:95], v[160:163], v[136:139], v[80:95]
	v_add_f32_e32 v72, v78, v112
	v_add_f32_e32 v72, v79, v72
	v_add_f32_e32 v72, v48, v72
	v_add_f32_e32 v112, v49, v72
	v_cvt_pk_bf16_f32 v126, v76, v77
	v_cvt_pk_bf16_f32 v127, v78, v79
	ds_read_b64_tr_b16 v[72:73], v204 offset:26624
	ds_read_b64_tr_b16 v[74:75], v204 offset:27136
	s_waitcnt lgkmcnt(13)
	v_mfma_f32_32x32x16_bf16 v[96:111], v[156:159], v[128:131], v[96:111]
	v_add_f32_e32 v76, v50, v112
	v_add_f32_e32 v76, v51, v76
	v_add_f32_e32 v76, v52, v76
	v_add_f32_e32 v76, v53, v76
	v_cvt_pk_bf16_f32 v116, v48, v49
	v_cvt_pk_bf16_f32 v117, v50, v51
	ds_read_b64_tr_b16 v[48:49], v204 offset:30720
	ds_read_b64_tr_b16 v[50:51], v204 offset:31232
	s_waitcnt lgkmcnt(14)
	v_mfma_f32_32x32x16_bf16 v[80:95], v[152:155], v[128:131], v[80:95]
	v_add_f32_e32 v76, v54, v76
	v_add_f32_e32 v76, v55, v76
	v_add_f32_e32 v76, v56, v76
	v_add_f32_e32 v76, v57, v76
	v_cvt_pk_bf16_f32 v118, v52, v53
	v_cvt_pk_bf16_f32 v119, v54, v55
	ds_read_b64_tr_b16 v[52:53], v204 offset:27648
	ds_read_b64_tr_b16 v[54:55], v204 offset:28160
	s_waitcnt lgkmcnt(14)
	v_mfma_f32_32x32x16_bf16 v[96:111], v[148:151], v[120:123], v[96:111]
	v_add_f32_e32 v76, v58, v76
	v_add_f32_e32 v76, v59, v76
	v_add_f32_e32 v76, v60, v76
	v_add_f32_e32 v76, v61, v76
	v_cvt_pk_bf16_f32 v112, v56, v57
	v_cvt_pk_bf16_f32 v113, v58, v59
	ds_read_b64_tr_b16 v[56:57], v204 offset:31744
	ds_read_b64_tr_b16 v[58:59], v204 offset:32256
	v_mfma_f32_32x32x16_bf16 v[80:95], v[144:147], v[120:123], v[80:95]
	v_add_f32_e32 v76, v62, v76
	v_add_f32_e32 v76, v63, v76
	v_add_f32_e32 v76, 0, v76
	v_cvt_pk_bf16_f32 v114, v60, v61
	v_cvt_pk_bf16_f32 v115, v62, v63
	v_lshl_add_u64 v[60:61], v[186:187], 0, s[14:15]
	s_add_i32 s9, s62, s69
	s_mov_b32 m0, s9
	s_nop 0
	global_load_lds_dwordx4 v[60:61], off
	v_lshl_add_u64 v[60:61], v[190:191], 0, s[4:5]
	s_add_i32 s9, s61, s70
	s_mov_b32 m0, s9
	s_nop 0
	global_load_lds_dwordx4 v[60:61], off
	v_max_f32_e32 v60, v97, v97
	v_max_f32_e32 v61, v96, v96
	v_max_f32_e32 v60, v61, v60
	v_max3_f32 v61, v98, v99, v81
	v_max3_f32 v60, v60, v80, v82
	v_max3_f32 v60, v60, v83, v100
	v_max3_f32 v61, v61, v102, v103
	v_max3_f32 v60, v60, v101, v84
	v_max3_f32 v61, v61, v86, v87
	v_max3_f32 v60, v60, v85, v104
	v_max3_f32 v61, v61, v106, v107
	v_max3_f32 v60, v60, v105, v88
	v_max3_f32 v61, v61, v90, v91
	v_max3_f32 v60, v60, v89, v108
	v_max3_f32 v61, v61, v110, v111
	v_max3_f32 v60, v60, v109, v92
	v_max3_f32 v61, v61, v94, v95
	v_max3_f32 v60, v60, v93, v61
	v_mov_b32_e32 v61, v60
	s_nop 1
	v_permlane32_swap_b32_e32 v60, v61
	v_max_f32_e32 v61, v61, v61
	v_max_f32_e32 v60, v60, v60
	v_max_f32_e32 v60, v60, v61
	v_cmp_lt_f32_e32 vcc, s97, v60
	s_cmp_lg_u64 vcc, 0
	v_add_f32_e32 v188, v188, v76
	s_cselect_b64 s[56:57], -1, 0
	s_cbranch_vccnz .LBB0_628

.LBB0_623:
	s_add_i32 s9, s61, 0x2000
	s_cmpk_lg_i32 s61, 0x4000
	s_cselect_b32 s9, s9, 0
	v_add_u32_e32 v204, s62, v203
	ds_read_b64_tr_b16 v[148:149], v204 offset:24576
	ds_read_b64_tr_b16 v[150:151], v204 offset:25088
	s_waitcnt lgkmcnt(9)
	v_mfma_f32_32x32x16_bf16 v[64:79], v[60:63], v[140:143], v[32:47]
	v_add_f32_e32 v48, v96, v97
	v_add_f32_e32 v48, v98, v48
	v_add_f32_e32 v48, v99, v48
	v_add_f32_e32 v48, v100, v48
	v_add_f32_e32 v48, v101, v48
	v_cvt_pk_bf16_f32 v132, v96, v97
	v_cvt_pk_bf16_f32 v133, v98, v99
	ds_read_b64_tr_b16 v[144:145], v204 offset:28672
	ds_read_b64_tr_b16 v[146:147], v204 offset:29184
	v_add_f32_e32 v48, v102, v48
	v_add_f32_e32 v48, v103, v48
	v_add_f32_e32 v48, v104, v48
	v_add_f32_e32 v112, v105, v48
	s_waitcnt lgkmcnt(10)
	v_mfma_f32_32x32x16_bf16 v[48:63], v[172:175], v[140:143], v[32:47]
	v_cvt_pk_bf16_f32 v134, v100, v101
	v_cvt_pk_bf16_f32 v135, v102, v103
	ds_read_b64_tr_b16 v[96:97], v204 offset:25600
	ds_read_b64_tr_b16 v[98:99], v204 offset:26112
	s_waitcnt lgkmcnt(11)
	v_mfma_f32_32x32x16_bf16 v[64:79], v[176:179], v[136:139], v[64:79]
	v_add_f32_e32 v100, v106, v112
	v_add_f32_e32 v100, v107, v100
	v_add_f32_e32 v100, v108, v100
	v_add_f32_e32 v112, v109, v100
	v_cvt_pk_bf16_f32 v124, v104, v105
	v_cvt_pk_bf16_f32 v125, v106, v107
	ds_read_b64_tr_b16 v[100:101], v204 offset:29696
	ds_read_b64_tr_b16 v[102:103], v204 offset:30208
	s_waitcnt lgkmcnt(12)
	v_mfma_f32_32x32x16_bf16 v[48:63], v[168:171], v[136:139], v[48:63]
	v_add_f32_e32 v104, v110, v112
	v_add_f32_e32 v104, v111, v104
	v_add_f32_e32 v104, v80, v104
	v_add_f32_e32 v112, v81, v104
	v_cvt_pk_bf16_f32 v126, v108, v109
	v_cvt_pk_bf16_f32 v127, v110, v111
	ds_read_b64_tr_b16 v[104:105], v204 offset:26624
	ds_read_b64_tr_b16 v[106:107], v204 offset:27136
	s_waitcnt lgkmcnt(13)
	v_mfma_f32_32x32x16_bf16 v[64:79], v[164:167], v[128:131], v[64:79]
	v_add_f32_e32 v108, v82, v112
	v_add_f32_e32 v108, v83, v108
	v_add_f32_e32 v108, v84, v108
	v_add_f32_e32 v108, v85, v108
	v_cvt_pk_bf16_f32 v116, v80, v81
	v_cvt_pk_bf16_f32 v117, v82, v83
	ds_read_b64_tr_b16 v[80:81], v204 offset:30720
	ds_read_b64_tr_b16 v[82:83], v204 offset:31232
	s_waitcnt lgkmcnt(14)
	v_mfma_f32_32x32x16_bf16 v[48:63], v[160:163], v[128:131], v[48:63]
	v_add_f32_e32 v108, v86, v108
	v_add_f32_e32 v108, v87, v108
	v_add_f32_e32 v108, v88, v108
	v_add_f32_e32 v108, v89, v108
	v_cvt_pk_bf16_f32 v118, v84, v85
	v_cvt_pk_bf16_f32 v119, v86, v87
	ds_read_b64_tr_b16 v[84:85], v204 offset:27648
	ds_read_b64_tr_b16 v[86:87], v204 offset:28160
	s_waitcnt lgkmcnt(14)
	v_mfma_f32_32x32x16_bf16 v[64:79], v[156:159], v[120:123], v[64:79]
	v_add_f32_e32 v108, v90, v108
	v_add_f32_e32 v108, v91, v108
	v_add_f32_e32 v108, v92, v108
	v_add_f32_e32 v108, v93, v108
	v_cvt_pk_bf16_f32 v112, v88, v89
	v_cvt_pk_bf16_f32 v113, v90, v91
	ds_read_b64_tr_b16 v[88:89], v204 offset:31744
	ds_read_b64_tr_b16 v[90:91], v204 offset:32256
	v_mfma_f32_32x32x16_bf16 v[48:63], v[152:155], v[120:123], v[48:63]
	v_add_f32_e32 v108, v94, v108
	v_add_f32_e32 v108, v95, v108
	v_add_f32_e32 v108, 0, v108
	v_cvt_pk_bf16_f32 v114, v92, v93
	v_cvt_pk_bf16_f32 v115, v94, v95
	v_lshl_add_u64 v[92:93], v[186:187], 0, s[24:25]
	s_add_i32 s10, s61, s69
	s_mov_b32 m0, s10
	s_nop 0
	global_load_lds_dwordx4 v[92:93], off
	v_max_f32_e32 v92, v65, v65
	v_max_f32_e32 v93, v64, v64
	v_max_f32_e32 v92, v93, v92
	s_nop 1
	v_max3_f32 v93, v66, v67, v49
	v_max3_f32 v92, v92, v48, v50
	v_max3_f32 v92, v92, v51, v68
	v_max3_f32 v93, v93, v70, v71
	v_max3_f32 v92, v92, v69, v52
	v_max3_f32 v93, v93, v54, v55
	v_max3_f32 v92, v92, v53, v72
	v_max3_f32 v93, v93, v74, v75
	v_max3_f32 v92, v92, v73, v56
	v_max3_f32 v93, v93, v58, v59
	v_max3_f32 v92, v92, v57, v76
	v_max3_f32 v93, v93, v78, v79
	v_max3_f32 v92, v92, v77, v60
	v_max3_f32 v93, v93, v62, v63
	v_max3_f32 v92, v92, v61, v93
	v_mov_b32_e32 v93, v92
	s_nop 1
	v_permlane32_swap_b32_e32 v92, v93
	v_max_f32_e32 v93, v93, v93
	v_max_f32_e32 v92, v92, v92
	v_max_f32_e32 v92, v92, v93
	v_lshl_add_u64 v[190:191], v[190:191], 0, s[38:39]
	s_add_i32 s10, s9, s70
	s_mov_b32 m0, s10
	s_nop 0
	global_load_lds_dwordx4 v[190:191], off
	v_cmp_lt_f32_e32 vcc, s97, v92
	s_cmp_lg_u64 vcc, 0
	v_add_f32_e32 v188, v188, v108
	s_cselect_b64 s[56:57], -1, 0
	s_cbranch_vccnz .LBB0_631

.LBB0_635:
	v_add_u32_e32 v186, s9, v203
	ds_read_b64_tr_b16 v[176:177], v186 offset:24576
	ds_read_b64_tr_b16 v[178:179], v186 offset:25088
	s_waitcnt lgkmcnt(9)
	v_mfma_f32_32x32x16_bf16 v[96:111], v[172:175], v[140:143], v[32:47]
	v_add_f32_e32 v80, v64, v65
	v_add_f32_e32 v80, v66, v80
	v_add_f32_e32 v80, v67, v80
	v_add_f32_e32 v80, v68, v80
	v_add_f32_e32 v80, v69, v80
	v_cvt_pk_bf16_f32 v132, v64, v65
	v_cvt_pk_bf16_f32 v133, v66, v67
	ds_read_b64_tr_b16 v[172:173], v186 offset:28672
	ds_read_b64_tr_b16 v[174:175], v186 offset:29184
	v_add_f32_e32 v64, v70, v80
	s_waitcnt lgkmcnt(10)
	v_mfma_f32_32x32x16_bf16 v[80:95], v[168:171], v[140:143], v[32:47]
	v_add_f32_e32 v64, v71, v64
	v_add_f32_e32 v64, v72, v64
	v_add_f32_e32 v112, v73, v64
	v_cvt_pk_bf16_f32 v134, v68, v69
	v_cvt_pk_bf16_f32 v135, v70, v71
	ds_read_b64_tr_b16 v[64:65], v186 offset:25600
	ds_read_b64_tr_b16 v[66:67], v186 offset:26112
	s_waitcnt lgkmcnt(11)
	v_mfma_f32_32x32x16_bf16 v[96:111], v[164:167], v[136:139], v[96:111]
	v_add_f32_e32 v68, v74, v112
	v_add_f32_e32 v68, v75, v68
	v_add_f32_e32 v68, v76, v68
	v_add_f32_e32 v112, v77, v68
	v_cvt_pk_bf16_f32 v124, v72, v73
	v_cvt_pk_bf16_f32 v125, v74, v75
	ds_read_b64_tr_b16 v[68:69], v186 offset:29696
	ds_read_b64_tr_b16 v[70:71], v186 offset:30208
	s_waitcnt lgkmcnt(12)
	v_mfma_f32_32x32x16_bf16 v[80:95], v[160:163], v[136:139], v[80:95]
	v_add_f32_e32 v72, v78, v112
	v_add_f32_e32 v72, v79, v72
	v_add_f32_e32 v72, v48, v72
	v_add_f32_e32 v112, v49, v72
	v_cvt_pk_bf16_f32 v126, v76, v77
	v_cvt_pk_bf16_f32 v127, v78, v79
	ds_read_b64_tr_b16 v[72:73], v186 offset:26624
	ds_read_b64_tr_b16 v[74:75], v186 offset:27136
	s_waitcnt lgkmcnt(13)
	v_mfma_f32_32x32x16_bf16 v[96:111], v[156:159], v[128:131], v[96:111]
	v_add_f32_e32 v76, v50, v112
	v_add_f32_e32 v76, v51, v76
	v_add_f32_e32 v76, v52, v76
	v_add_f32_e32 v76, v53, v76
	v_cvt_pk_bf16_f32 v116, v48, v49
	v_cvt_pk_bf16_f32 v117, v50, v51
	ds_read_b64_tr_b16 v[48:49], v186 offset:30720
	ds_read_b64_tr_b16 v[50:51], v186 offset:31232
	s_waitcnt lgkmcnt(14)
	v_mfma_f32_32x32x16_bf16 v[80:95], v[152:155], v[128:131], v[80:95]
	v_add_f32_e32 v76, v54, v76
	v_add_f32_e32 v76, v55, v76
	v_add_f32_e32 v76, v56, v76
	v_add_f32_e32 v76, v57, v76
	v_cvt_pk_bf16_f32 v118, v52, v53
	v_cvt_pk_bf16_f32 v119, v54, v55
	ds_read_b64_tr_b16 v[52:53], v186 offset:27648
	ds_read_b64_tr_b16 v[54:55], v186 offset:28160
	s_waitcnt lgkmcnt(14)
	v_mfma_f32_32x32x16_bf16 v[96:111], v[148:151], v[120:123], v[96:111]
	v_add_f32_e32 v76, v58, v76
	v_add_f32_e32 v76, v59, v76
	v_add_f32_e32 v76, v60, v76
	v_add_f32_e32 v76, v61, v76
	v_cvt_pk_bf16_f32 v112, v56, v57
	v_cvt_pk_bf16_f32 v113, v58, v59
	ds_read_b64_tr_b16 v[56:57], v186 offset:31744
	ds_read_b64_tr_b16 v[58:59], v186 offset:32256
	v_mfma_f32_32x32x16_bf16 v[80:95], v[144:147], v[120:123], v[80:95]
	v_add_f32_e32 v76, v62, v76
	v_add_f32_e32 v76, v63, v76
	v_add_f32_e32 v76, 0, v76
	v_cvt_pk_bf16_f32 v114, v60, v61
	v_cvt_pk_bf16_f32 v115, v62, v63
	s_cmp_gt_u32 s71, 28
	s_cselect_b64 s[58:59], -1, 0
	s_and_b64 vcc, exec, s[58:59]
	s_mov_b64 s[60:61], s[56:57]
	s_cbranch_vccnz .LBB0_637
	s_add_i32 s9, s77, s69
	v_lshl_add_u64 v[60:61], v[184:185], 0, s[14:15]
	s_mov_b32 m0, s9
	s_nop 0
	global_load_lds_dwordx4 v[60:61], off
	s_mul_i32 s72, s71, 0x88000
	s_mov_b64 s[60:61], s[72:73]
.LBB0_637:
	v_lshl_add_u64 v[186:187], s[60:61], 1, v[182:183]
	v_lshl_add_u64 v[60:61], v[186:187], 0, s[4:5]
	s_add_i32 s9, s76, s70
	s_mov_b32 m0, s9
	s_nop 0
	global_load_lds_dwordx4 v[60:61], off
	v_max_f32_e32 v60, v97, v97
	v_max_f32_e32 v61, v96, v96
	v_max_f32_e32 v60, v61, v60
	v_max3_f32 v61, v98, v99, v81
	v_max3_f32 v60, v60, v80, v82
	v_max3_f32 v60, v60, v83, v100
	v_max3_f32 v61, v61, v102, v103
	v_max3_f32 v60, v60, v101, v84
	v_max3_f32 v61, v61, v86, v87
	v_max3_f32 v60, v60, v85, v104
	v_max3_f32 v61, v61, v106, v107
	v_max3_f32 v60, v60, v105, v88
	v_max3_f32 v61, v61, v90, v91
	v_max3_f32 v60, v60, v89, v108
	v_max3_f32 v61, v61, v110, v111
	v_max3_f32 v60, v60, v109, v92
	v_max3_f32 v61, v61, v94, v95
	v_max3_f32 v60, v60, v93, v61
	v_mov_b32_e32 v61, v60
	s_nop 1
	v_permlane32_swap_b32_e32 v60, v61
	v_max_f32_e32 v61, v61, v61
	v_max_f32_e32 v60, v60, v60
	v_max_f32_e32 v60, v60, v61
	v_cmp_lt_f32_e32 vcc, s97, v60
	s_cmp_lg_u64 vcc, 0
	v_add_f32_e32 v188, v188, v76
	s_cselect_b64 s[62:63], -1, 0
	s_cbranch_vccnz .LBB0_655

.LBB0_642:
	v_add_u32_e32 v190, s77, v203
	ds_read_b64_tr_b16 v[148:149], v190 offset:24576
	ds_read_b64_tr_b16 v[150:151], v190 offset:25088
	s_waitcnt lgkmcnt(9)
	v_mfma_f32_32x32x16_bf16 v[64:79], v[60:63], v[140:143], v[32:47]
	v_add_f32_e32 v48, v96, v97
	v_add_f32_e32 v48, v98, v48
	v_add_f32_e32 v48, v99, v48
	v_add_f32_e32 v48, v100, v48
	v_add_f32_e32 v48, v101, v48
	v_cvt_pk_bf16_f32 v132, v96, v97
	v_cvt_pk_bf16_f32 v133, v98, v99
	ds_read_b64_tr_b16 v[144:145], v190 offset:28672
	ds_read_b64_tr_b16 v[146:147], v190 offset:29184
	v_add_f32_e32 v48, v102, v48
	v_add_f32_e32 v48, v103, v48
	v_add_f32_e32 v48, v104, v48
	v_add_f32_e32 v112, v105, v48
	s_waitcnt lgkmcnt(10)
	v_mfma_f32_32x32x16_bf16 v[48:63], v[172:175], v[140:143], v[32:47]
	v_cvt_pk_bf16_f32 v134, v100, v101
	v_cvt_pk_bf16_f32 v135, v102, v103
	ds_read_b64_tr_b16 v[96:97], v190 offset:25600
	ds_read_b64_tr_b16 v[98:99], v190 offset:26112
	s_waitcnt lgkmcnt(11)
	v_mfma_f32_32x32x16_bf16 v[64:79], v[176:179], v[136:139], v[64:79]
	v_add_f32_e32 v100, v106, v112
	v_add_f32_e32 v100, v107, v100
	v_add_f32_e32 v100, v108, v100
	v_add_f32_e32 v112, v109, v100
	v_cvt_pk_bf16_f32 v124, v104, v105
	v_cvt_pk_bf16_f32 v125, v106, v107
	ds_read_b64_tr_b16 v[100:101], v190 offset:29696
	ds_read_b64_tr_b16 v[102:103], v190 offset:30208
	s_waitcnt lgkmcnt(12)
	v_mfma_f32_32x32x16_bf16 v[48:63], v[168:171], v[136:139], v[48:63]
	v_add_f32_e32 v104, v110, v112
	v_add_f32_e32 v104, v111, v104
	v_add_f32_e32 v104, v80, v104
	v_add_f32_e32 v112, v81, v104
	v_cvt_pk_bf16_f32 v126, v108, v109
	v_cvt_pk_bf16_f32 v127, v110, v111
	ds_read_b64_tr_b16 v[104:105], v190 offset:26624
	ds_read_b64_tr_b16 v[106:107], v190 offset:27136
	s_waitcnt lgkmcnt(13)
	v_mfma_f32_32x32x16_bf16 v[64:79], v[164:167], v[128:131], v[64:79]
	v_add_f32_e32 v108, v82, v112
	v_add_f32_e32 v108, v83, v108
	v_add_f32_e32 v108, v84, v108
	v_add_f32_e32 v108, v85, v108
	v_cvt_pk_bf16_f32 v116, v80, v81
	v_cvt_pk_bf16_f32 v117, v82, v83
	ds_read_b64_tr_b16 v[80:81], v190 offset:30720
	ds_read_b64_tr_b16 v[82:83], v190 offset:31232
	s_waitcnt lgkmcnt(14)
	v_mfma_f32_32x32x16_bf16 v[48:63], v[160:163], v[128:131], v[48:63]
	v_add_f32_e32 v108, v86, v108
	v_add_f32_e32 v108, v87, v108
	v_add_f32_e32 v108, v88, v108
	v_add_f32_e32 v108, v89, v108
	v_cvt_pk_bf16_f32 v118, v84, v85
	v_cvt_pk_bf16_f32 v119, v86, v87
	ds_read_b64_tr_b16 v[84:85], v190 offset:27648
	ds_read_b64_tr_b16 v[86:87], v190 offset:28160
	s_waitcnt lgkmcnt(14)
	v_mfma_f32_32x32x16_bf16 v[64:79], v[156:159], v[120:123], v[64:79]
	v_add_f32_e32 v108, v90, v108
	v_add_f32_e32 v108, v91, v108
	v_add_f32_e32 v108, v92, v108
	v_add_f32_e32 v108, v93, v108
	v_cvt_pk_bf16_f32 v112, v88, v89
	v_cvt_pk_bf16_f32 v113, v90, v91
	ds_read_b64_tr_b16 v[88:89], v190 offset:31744
	ds_read_b64_tr_b16 v[90:91], v190 offset:32256
	v_mfma_f32_32x32x16_bf16 v[48:63], v[152:155], v[120:123], v[48:63]
	v_add_f32_e32 v108, v94, v108
	v_add_f32_e32 v108, v95, v108
	v_add_f32_e32 v108, 0, v108
	v_cvt_pk_bf16_f32 v114, v92, v93
	v_cvt_pk_bf16_f32 v115, v94, v95
	s_cmp_gt_u32 s71, 27
	s_cselect_b64 s[62:63], -1, 0
	s_and_b64 vcc, exec, s[62:63]
	s_cbranch_vccnz .LBB0_644
	v_lshl_add_u64 v[92:93], s[60:61], 1, v[180:181]
	s_add_i32 s9, s76, s69
	v_lshl_add_u64 v[92:93], v[92:93], 0, s[24:25]
	s_mov_b32 m0, s9
	s_nop 0
	global_load_lds_dwordx4 v[92:93], off
.LBB0_644:
	s_add_i32 s9, s76, 0x2000
	s_cmpk_lg_i32 s76, 0x4000
	s_cselect_b32 s77, s9, 0
	v_lshl_add_u64 v[92:93], v[186:187], 0, s[38:39]
	s_add_i32 s9, s77, s70
	s_mov_b32 m0, s9
	s_nop 0
	global_load_lds_dwordx4 v[92:93], off
	v_max_f32_e32 v92, v65, v65
	v_max_f32_e32 v93, v64, v64
	v_max_f32_e32 v92, v93, v92
	v_max3_f32 v93, v66, v67, v49
	v_max3_f32 v92, v92, v48, v50
	v_max3_f32 v92, v92, v51, v68
	v_max3_f32 v93, v93, v70, v71
	v_max3_f32 v92, v92, v69, v52
	v_max3_f32 v93, v93, v54, v55
	v_max3_f32 v92, v92, v53, v72
	v_max3_f32 v93, v93, v74, v75
	v_max3_f32 v92, v92, v73, v56
	v_max3_f32 v93, v93, v58, v59
	v_max3_f32 v92, v92, v57, v76
	v_max3_f32 v93, v93, v78, v79
	v_max3_f32 v92, v92, v77, v60
	v_max3_f32 v93, v93, v62, v63
	v_max3_f32 v92, v92, v61, v93
	v_mov_b32_e32 v93, v92
	s_nop 1
	v_permlane32_swap_b32_e32 v92, v93
	v_max_f32_e32 v93, v93, v93
	v_max_f32_e32 v92, v92, v92
	v_max_f32_e32 v92, v92, v93
	v_cmp_lt_f32_e32 vcc, s97, v92
	s_cmp_lg_u64 vcc, 0
	v_add_f32_e32 v188, v188, v108
	s_cselect_b64 s[60:61], -1, 0
	s_cbranch_vccnz .LBB0_658

.LBB0_805:
	v_readlane_b32 s16, v253, 6
	v_readlane_b32 s18, v253, 8
	s_cmp_le_i32 s18, s2
	s_cselect_b64 s[10:11], -1, 0
	s_and_b64 s[0:1], s[10:11], s[20:21]
	s_andn2_b64 vcc, exec, s[0:1]
	v_readlane_b32 s17, v253, 7
	v_readlane_b32 s19, v253, 9
	s_cbranch_vccnz .LBB0_862
	v_readlane_b32 s0, v253, 2
	v_readlane_b32 s1, v253, 3
	s_load_dwordx2 s[40:41], s[0:1], 0xf8
	v_mbcnt_lo_u32_b32 v0, -1, 0
	v_mbcnt_hi_u32_b32 v0, -1, v0
	s_mov_b32 s85, s73
	v_or_b32_e32 v0, s33, v0
	s_waitcnt lgkmcnt(0)
	s_add_u32 s2, s40, 0x67900000
	s_waitcnt vmcnt(0)
	v_bfe_i32 v3, v0, 27, 1
	v_lshlrev_b32_e32 v1, 4, v0
	v_lshrrev_b32_e32 v3, 22, v3
	v_add_u32_e32 v3, v1, v3
	v_and_b32_e32 v3, 0xfffffc00, v3
	v_sub_u32_e32 v3, v1, v3
	v_ashrrev_i32_e32 v2, 31, v0
	v_lshrrev_b32_e32 v4, 4, v3
	v_lshrrev_b32_e32 v2, 26, v2
	v_bitop3_b32 v4, v4, v3, 32 bitop3:0x6c
	v_ashrrev_i32_e32 v3, 31, v3
	v_add_u32_e32 v2, v0, v2
	v_lshrrev_b32_e32 v3, 26, v3
	v_ashrrev_i32_e32 v2, 6, v2
	v_add_u32_e32 v3, v4, v3
	s_addc_u32 s3, s41, 0
	s_lshl_b64 s[0:1], s[84:85], 22
	v_lshlrev_b32_e32 v5, 3, v2
	v_ashrrev_i32_e32 v3, 6, v3
	s_add_u32 s0, s40, s0
	v_and_b32_e32 v5, -16, v5
	v_mul_i32_i24_e32 v6, 64, v3
	s_addc_u32 s1, s41, s1
	v_add_u32_e32 v5, v3, v5
	v_sub_u32_e32 v4, v4, v6
	s_add_u32 s13, s0, 0x5700000
	v_lshlrev_b32_e32 v2, 5, v2
	v_ashrrev_i16_sdwa v4, v242, sext(v4) dst_sel:DWORD dst_unused:UNUSED_PAD src0_sel:DWORD src1_sel:BYTE_0
	v_lshlrev_b32_e32 v6, 1, v5
	v_lshrrev_b32_e32 v7, 2, v5
	v_and_b32_e32 v3, 3, v3
	s_mov_b32 s0, 0x1fffe0
	v_and_b32_e32 v2, 32, v2
	v_bfe_i32 v4, v4, 0, 16
	v_and_b32_e32 v6, 24, v6
	v_and_b32_e32 v7, 4, v7
	v_and_or_b32 v3, v5, s0, v3
	v_or3_b32 v3, v3, v7, v6
	v_add_lshl_u32 v2, v2, v4, 1
	v_add_u32_e32 v1, 0x2000, v1
	v_lshl_add_u32 v132, v5, 11, v2
	v_lshl_add_u32 v133, v3, 11, v2
	v_ashrrev_i32_e32 v2, 31, v1
	v_lshrrev_b32_e32 v2, 22, v2
	v_add_u32_e32 v2, v1, v2
	v_ashrrev_i32_e32 v2, 10, v2
	v_mul_i32_i24_e32 v3, 0x400, v2
	v_sub_u32_e32 v1, v1, v3
	v_lshrrev_b32_e32 v3, 4, v1
	v_bitop3_b32 v1, v3, v1, 32 bitop3:0x6c
	v_ashrrev_i32_e32 v4, 31, v1
	v_lshrrev_b32_e32 v4, 26, v4
	v_lshlrev_b32_e32 v3, 3, v2
	v_add_u32_e32 v4, v1, v4
	v_writelane_b32 v255, s10, 52
	v_readfirstlane_b32 s9, v0
	v_and_b32_e32 v3, -16, v3
	v_ashrrev_i32_e32 v5, 6, v4
	v_writelane_b32 v255, s11, 53
	s_addc_u32 s18, s1, 0
	v_add_u32_e32 v3, v5, v3
	v_and_b32_e32 v4, 0xc0, v4
	v_and_b32_e32 v5, 3, v5
	s_ashr_i32 s11, s9, 6
	s_ashr_i32 s10, s9, 8
	v_sub_u32_e32 v1, v1, v4
	v_and_or_b32 v5, v3, s0, v5
	s_lshl_b32 s0, s11, 10
	v_readlane_b32 s16, v254, 37
	v_lshlrev_b32_e32 v2, 5, v2
	v_ashrrev_i16_sdwa v1, v242, sext(v1) dst_sel:DWORD dst_unused:UNUSED_PAD src0_sel:DWORD src1_sel:BYTE_0
	v_lshlrev_b32_e32 v4, 1, v3
	v_lshrrev_b32_e32 v6, 2, v3
	v_readlane_b32 s17, v254, 38
	s_add_u32 s52, s13, s16
	v_and_b32_e32 v2, 32, v2
	v_bfe_i32 v1, v1, 0, 16
	v_and_b32_e32 v4, 24, v4
	v_and_b32_e32 v6, 4, v6
	s_addc_u32 s53, s18, s17
	s_add_i32 s19, s0, 0
	v_or3_b32 v4, v5, v6, v4
	v_add_lshl_u32 v1, v2, v1, 1
	s_add_i32 s28, s19, 0x10000
	s_mov_b32 m0, s28
	s_nop 0
	global_load_lds_dwordx4 v133, s[52:53]
	v_lshl_add_u32 v135, v4, 11, v1
	s_add_i32 s29, s19, 0x12000
	s_mov_b32 m0, s29
	s_nop 0
	global_load_lds_dwordx4 v135, s[52:53]
	s_add_u32 s0, s52, 0x40000
	s_addc_u32 s1, s53, 0
	s_add_i32 s30, s19, 0x14000
	s_mov_b32 m0, s30
	s_nop 0
	global_load_lds_dwordx4 v133, s[0:1]
	s_add_i32 s31, s19, 0x16000
	s_mov_b32 m0, s31
	s_nop 0
	global_load_lds_dwordx4 v135, s[0:1]
	v_readlane_b32 s0, v254, 36
	s_add_u32 s54, s2, s0
	s_addc_u32 s55, s3, 0
	s_mov_b32 m0, s19
	s_nop 0
	global_load_lds_dwordx4 v132, s[54:55]
	v_lshl_add_u32 v134, v3, 11, v1
	s_add_i32 s34, s19, 0x2000
	s_mov_b32 m0, s34
	s_nop 0
	global_load_lds_dwordx4 v134, s[54:55]
	s_add_u32 s0, s54, 0x40000
	s_addc_u32 s1, s55, 0
	s_add_i32 s35, s19, 0x4000
	s_mov_b32 m0, s35
	s_nop 0
	global_load_lds_dwordx4 v132, s[0:1]
	s_add_i32 s36, s19, 0x6000
	s_mov_b32 m0, s36
	s_nop 0
	global_load_lds_dwordx4 v134, s[0:1]
	s_cmp_eq_u32 s10, 1
	s_cselect_b64 s[0:1], -1, 0
	s_cmp_lg_u32 s10, 1
	s_cbranch_scc1 .LBB0_808
	s_barrier
.LBB0_808:
	s_lshl_b64 s[20:21], s[84:85], 21
	s_add_u32 s22, s40, 0x45900000
	s_addc_u32 s23, s41, 0
	s_add_u32 s40, s40, 0x45902400
	v_and_b32_e32 v1, 48, v0
	v_lshlrev_b32_e32 v2, 6, v0
	s_movk_i32 s12, 0x3c0
	v_lshlrev_b32_e32 v0, 2, v0
	s_addc_u32 s41, s41, 0
	s_lshl_b32 s37, s10, 6
	s_lshl_b32 s10, s10, 13
	v_and_or_b32 v1, v2, s12, v1
	v_and_b32_e32 v0, 32, v0
	v_bitop3_b32 v2, v1, s10, v0 bitop3:0xde
	s_lshl_b32 s10, s11, 5
	s_and_b32 s65, s10, 0x60
	s_lshl_b32 s10, s65, 7
	v_bitop3_b32 v0, s10, v1, v0 bitop3:0xf6
	s_add_u32 s10, s52, 0x80
	s_waitcnt vmcnt(2)
	s_barrier
	s_addc_u32 s11, s53, 0
	s_add_i32 s66, s19, 0x18000
	s_mov_b32 m0, s66
	s_nop 0
	global_load_lds_dwordx4 v133, s[10:11]
	s_add_i32 s67, s19, 0x1a000
	s_mov_b32 m0, s67
	s_nop 0
	global_load_lds_dwordx4 v135, s[10:11]
	s_add_u32 s10, s54, 0x80
	s_addc_u32 s11, s55, 0
	s_add_i32 s68, s19, 0x8000
	s_mov_b32 m0, s68
	s_nop 0
	global_load_lds_dwordx4 v132, s[10:11]
	s_add_i32 s69, s19, 0xa000
	s_mov_b32 m0, s69
	s_nop 0
	global_load_lds_dwordx4 v134, s[10:11]
	s_add_u32 s10, s52, 0x40080
	s_addc_u32 s11, s53, 0
	s_add_i32 s70, s19, 0x1c000
	s_mov_b32 m0, s70
	s_nop 0
	global_load_lds_dwordx4 v133, s[10:11]
	s_add_i32 s71, s19, 0x1e000
	s_mov_b32 m0, s71
	s_nop 0
	global_load_lds_dwordx4 v135, s[10:11]
	s_waitcnt vmcnt(6)
	s_add_i32 s72, s19, 0xc000
	s_cmpk_lt_u32 s9, 0x100
	s_mov_b32 s77, 0
	s_cselect_b64 s[42:43], -1, 0
	v_add_u32_e32 v136, 0, v0
	v_add_u32_e32 v137, 0, v2
	v_readlane_b32 s9, v253, 10
	s_barrier
	s_branch .LBB0_811

.LBB0_816:
	s_cmp_gt_u32 s81, 13
	s_cselect_b64 s[58:59], -1, 0
	s_and_b64 vcc, s[58:59], exec
	s_cselect_b32 s16, -14, 2
	s_add_i32 s58, s16, s81
	s_ashr_i32 s59, s58, 31
	s_lshl_b64 s[58:59], s[58:59], 7
	s_add_u32 s16, s54, s58
	s_addc_u32 s17, s55, s59
	s_add_u32 s50, s52, s58
	s_addc_u32 s51, s53, s59
	s_cmp_gt_u32 s81, 12
	s_cselect_b32 s58, -13, 3
	s_add_i32 s58, s58, s81
	s_ashr_i32 s59, s58, 31
	s_lshl_b64 s[58:59], s[58:59], 7
	s_add_u32 s60, s54, s58
	s_addc_u32 s61, s55, s59
	s_add_u32 s82, s52, s58
	s_addc_u32 s83, s53, s59
	s_cmp_eq_u32 s81, 14
	s_cselect_b32 s62, s11, s16
	s_mov_b32 s16, s81
	v_add_u32_e32 v146, 0x10000, v136
	v_add_u32_e32 v162, 0x14000, v136
	ds_read_b128 v[128:131], v146
	ds_read_b128 v[138:141], v146 offset:1024
	ds_read_b128 v[142:145], v146 offset:2048
	ds_read_b128 v[146:149], v146 offset:3072
	ds_read_b128 v[150:153], v162
	ds_read_b128 v[154:157], v162 offset:1024
	ds_read_b128 v[158:161], v162 offset:2048
	ds_read_b128 v[162:165], v162 offset:3072
	s_cselect_b32 s63, s10, s17
	s_cselect_b32 s75, s12, s51
	s_cselect_b32 s74, s27, s50
	s_cselect_b32 s59, s78, s61
	s_cselect_b32 s58, s45, s60
	s_cselect_b32 s61, s80, s83
	s_cselect_b32 s60, s79, s82
	ds_read_b128 v[166:169], v137
	ds_read_b128 v[170:173], v137 offset:1024
	ds_read_b128 v[174:177], v137 offset:2048
	ds_read_b128 v[178:181], v137 offset:3072
	ds_read_b128 v[182:185], v137 offset:4096
	ds_read_b128 v[190:193], v137 offset:5120
	ds_read_b128 v[194:197], v137 offset:6144
	ds_read_b128 v[198:201], v137 offset:7168
	s_add_u32 s82, s56, 0x40080
	s_addc_u32 s83, s57, 0
	s_mov_b32 m0, s72
	s_nop 0
	global_load_lds_dwordx4 v132, s[82:83]
	s_add_i32 s16, s19, 0xe000
	s_mov_b32 m0, s16
	s_nop 0
	global_load_lds_dwordx4 v134, s[82:83]
	s_setprio 1
	s_waitcnt vmcnt(8)
	s_waitcnt lgkmcnt(0)
	s_barrier
	v_mfma_f32_16x16x32_bf16 v[124:127], v[128:131], v[166:169], v[124:127]
	v_mfma_f32_16x16x32_bf16 v[120:123], v[142:145], v[166:169], v[120:123]
	v_mfma_f32_16x16x32_bf16 v[108:111], v[128:131], v[174:177], v[108:111]
	v_mfma_f32_16x16x32_bf16 v[104:107], v[142:145], v[174:177], v[104:107]
	v_mfma_f32_16x16x32_bf16 v[92:95], v[128:131], v[182:185], v[92:95]
	v_mfma_f32_16x16x32_bf16 v[88:91], v[142:145], v[182:185], v[88:91]
	v_mfma_f32_16x16x32_bf16 v[76:79], v[128:131], v[194:197], v[76:79]
	v_mfma_f32_16x16x32_bf16 v[72:75], v[142:145], v[194:197], v[72:75]
	v_mfma_f32_16x16x32_bf16 v[124:127], v[138:141], v[170:173], v[124:127]
	v_mfma_f32_16x16x32_bf16 v[120:123], v[146:149], v[170:173], v[120:123]
	v_mfma_f32_16x16x32_bf16 v[108:111], v[138:141], v[178:181], v[108:111]
	v_mfma_f32_16x16x32_bf16 v[104:107], v[146:149], v[178:181], v[104:107]
	v_mfma_f32_16x16x32_bf16 v[92:95], v[138:141], v[190:193], v[92:95]
	v_mfma_f32_16x16x32_bf16 v[88:91], v[146:149], v[190:193], v[88:91]
	v_mfma_f32_16x16x32_bf16 v[76:79], v[138:141], v[198:201], v[76:79]
	v_mfma_f32_16x16x32_bf16 v[72:75], v[146:149], v[198:201], v[72:75]
	v_mfma_f32_16x16x32_bf16 v[116:119], v[150:153], v[166:169], v[116:119]
	v_mfma_f32_16x16x32_bf16 v[112:115], v[158:161], v[166:169], v[112:115]
	v_mfma_f32_16x16x32_bf16 v[100:103], v[150:153], v[174:177], v[100:103]
	v_mfma_f32_16x16x32_bf16 v[96:99], v[158:161], v[174:177], v[96:99]
	v_mfma_f32_16x16x32_bf16 v[84:87], v[150:153], v[182:185], v[84:87]
	v_mfma_f32_16x16x32_bf16 v[80:83], v[158:161], v[182:185], v[80:83]
	v_mfma_f32_16x16x32_bf16 v[68:71], v[150:153], v[194:197], v[68:71]
	v_mfma_f32_16x16x32_bf16 v[64:67], v[158:161], v[194:197], v[64:67]
	v_mfma_f32_16x16x32_bf16 v[116:119], v[154:157], v[170:173], v[116:119]
	v_mfma_f32_16x16x32_bf16 v[112:115], v[162:165], v[170:173], v[112:115]
	v_mfma_f32_16x16x32_bf16 v[100:103], v[154:157], v[178:181], v[100:103]
	v_mfma_f32_16x16x32_bf16 v[96:99], v[162:165], v[178:181], v[96:99]
	v_mfma_f32_16x16x32_bf16 v[84:87], v[154:157], v[190:193], v[84:87]
	v_mfma_f32_16x16x32_bf16 v[80:83], v[162:165], v[190:193], v[80:83]
	v_mfma_f32_16x16x32_bf16 v[68:71], v[154:157], v[198:201], v[68:71]
	v_mfma_f32_16x16x32_bf16 v[64:67], v[162:165], v[198:201], v[64:67]
	s_barrier
	s_setprio 0
	ds_read_b128 v[166:169], v137 offset:16384
	ds_read_b128 v[170:173], v137 offset:17408
	ds_read_b128 v[174:177], v137 offset:18432
	ds_read_b128 v[178:181], v137 offset:19456
	ds_read_b128 v[182:185], v137 offset:20480
	ds_read_b128 v[190:193], v137 offset:21504
	ds_read_b128 v[194:197], v137 offset:22528
	ds_read_b128 v[198:201], v137 offset:23552
	s_mov_b32 m0, s28
	s_nop 0
	global_load_lds_dwordx4 v133, s[74:75]
	s_nop 0
	s_mov_b32 m0, s29
	s_nop 0
	global_load_lds_dwordx4 v135, s[74:75]
	s_add_u32 s74, s74, 0x40000
	s_addc_u32 s75, s75, 0
	s_mov_b32 m0, s30
	s_nop 0
	global_load_lds_dwordx4 v133, s[74:75]
	s_nop 0
	s_mov_b32 m0, s31
	s_nop 0
	global_load_lds_dwordx4 v135, s[74:75]
	s_nop 0
	s_mov_b32 m0, s19
	s_nop 0
	global_load_lds_dwordx4 v132, s[62:63]
	s_nop 0
	s_mov_b32 m0, s34
	s_nop 0
	global_load_lds_dwordx4 v134, s[62:63]
	s_setprio 1
	s_waitcnt vmcnt(8)
	s_waitcnt lgkmcnt(0)
	s_barrier
	v_mfma_f32_16x16x32_bf16 v[60:63], v[128:131], v[166:169], v[60:63]
	v_mfma_f32_16x16x32_bf16 v[56:59], v[142:145], v[166:169], v[56:59]
	v_mfma_f32_16x16x32_bf16 v[44:47], v[128:131], v[174:177], v[44:47]
	v_mfma_f32_16x16x32_bf16 v[40:43], v[142:145], v[174:177], v[40:43]
	v_mfma_f32_16x16x32_bf16 v[28:31], v[128:131], v[182:185], v[28:31]
	v_mfma_f32_16x16x32_bf16 v[24:27], v[142:145], v[182:185], v[24:27]
	v_mfma_f32_16x16x32_bf16 v[12:15], v[128:131], v[194:197], v[12:15]
	v_mfma_f32_16x16x32_bf16 v[8:11], v[142:145], v[194:197], v[8:11]
	v_mfma_f32_16x16x32_bf16 v[60:63], v[138:141], v[170:173], v[60:63]
	v_mfma_f32_16x16x32_bf16 v[56:59], v[146:149], v[170:173], v[56:59]
	v_mfma_f32_16x16x32_bf16 v[44:47], v[138:141], v[178:181], v[44:47]
	v_mfma_f32_16x16x32_bf16 v[40:43], v[146:149], v[178:181], v[40:43]
	v_mfma_f32_16x16x32_bf16 v[28:31], v[138:141], v[190:193], v[28:31]
	v_mfma_f32_16x16x32_bf16 v[24:27], v[146:149], v[190:193], v[24:27]
	v_mfma_f32_16x16x32_bf16 v[12:15], v[138:141], v[198:201], v[12:15]
	v_mfma_f32_16x16x32_bf16 v[8:11], v[146:149], v[198:201], v[8:11]
	v_mfma_f32_16x16x32_bf16 v[52:55], v[150:153], v[166:169], v[52:55]
	v_mfma_f32_16x16x32_bf16 v[48:51], v[158:161], v[166:169], v[48:51]
	v_mfma_f32_16x16x32_bf16 v[36:39], v[150:153], v[174:177], v[36:39]
	v_mfma_f32_16x16x32_bf16 v[32:35], v[158:161], v[174:177], v[32:35]
	v_mfma_f32_16x16x32_bf16 v[20:23], v[150:153], v[182:185], v[20:23]
	v_mfma_f32_16x16x32_bf16 v[16:19], v[158:161], v[182:185], v[16:19]
	v_mfma_f32_16x16x32_bf16 v[4:7], v[150:153], v[194:197], v[4:7]
	v_mfma_f32_16x16x32_bf16 v[0:3], v[158:161], v[194:197], v[0:3]
	v_mfma_f32_16x16x32_bf16 v[52:55], v[154:157], v[170:173], v[52:55]
	v_mfma_f32_16x16x32_bf16 v[48:51], v[162:165], v[170:173], v[48:51]
	v_mfma_f32_16x16x32_bf16 v[36:39], v[154:157], v[178:181], v[36:39]
	v_mfma_f32_16x16x32_bf16 v[32:35], v[162:165], v[178:181], v[32:35]
	v_mfma_f32_16x16x32_bf16 v[20:23], v[154:157], v[190:193], v[20:23]
	v_mfma_f32_16x16x32_bf16 v[16:19], v[162:165], v[190:193], v[16:19]
	v_mfma_f32_16x16x32_bf16 v[4:7], v[154:157], v[198:201], v[4:7]
	v_mfma_f32_16x16x32_bf16 v[0:3], v[162:165], v[198:201], v[0:3]
	s_barrier
	s_setprio 0
	v_add_u32_e32 v146, 0x18000, v136
	v_add_u32_e32 v162, 0x1c000, v136
	ds_read_b128 v[128:131], v146
	ds_read_b128 v[138:141], v146 offset:1024
	ds_read_b128 v[142:145], v146 offset:2048
	ds_read_b128 v[146:149], v146 offset:3072
	ds_read_b128 v[150:153], v162
	ds_read_b128 v[154:157], v162 offset:1024
	ds_read_b128 v[158:161], v162 offset:2048
	ds_read_b128 v[162:165], v162 offset:3072
	ds_read_b128 v[166:169], v137 offset:32768
	ds_read_b128 v[170:173], v137 offset:33792
	ds_read_b128 v[174:177], v137 offset:34816
	ds_read_b128 v[178:181], v137 offset:35840
	ds_read_b128 v[182:185], v137 offset:36864
	ds_read_b128 v[190:193], v137 offset:37888
	ds_read_b128 v[194:197], v137 offset:38912
	ds_read_b128 v[198:201], v137 offset:39936
	s_add_u32 s62, s62, 0x40000
	s_addc_u32 s63, s63, 0
	s_mov_b32 m0, s35
	s_nop 0
	global_load_lds_dwordx4 v132, s[62:63]
	s_nop 0
	s_mov_b32 m0, s36
	s_nop 0
	global_load_lds_dwordx4 v134, s[62:63]
	s_setprio 1
	s_waitcnt vmcnt(8)
	s_waitcnt lgkmcnt(0)
	s_barrier
	v_mfma_f32_16x16x32_bf16 v[124:127], v[128:131], v[166:169], v[124:127]
	v_mfma_f32_16x16x32_bf16 v[120:123], v[142:145], v[166:169], v[120:123]
	v_mfma_f32_16x16x32_bf16 v[108:111], v[128:131], v[174:177], v[108:111]
	v_mfma_f32_16x16x32_bf16 v[104:107], v[142:145], v[174:177], v[104:107]
	v_mfma_f32_16x16x32_bf16 v[92:95], v[128:131], v[182:185], v[92:95]
	v_mfma_f32_16x16x32_bf16 v[88:91], v[142:145], v[182:185], v[88:91]
	v_mfma_f32_16x16x32_bf16 v[76:79], v[128:131], v[194:197], v[76:79]
	v_mfma_f32_16x16x32_bf16 v[72:75], v[142:145], v[194:197], v[72:75]
	v_mfma_f32_16x16x32_bf16 v[124:127], v[138:141], v[170:173], v[124:127]
	v_mfma_f32_16x16x32_bf16 v[120:123], v[146:149], v[170:173], v[120:123]
	v_mfma_f32_16x16x32_bf16 v[108:111], v[138:141], v[178:181], v[108:111]
	v_mfma_f32_16x16x32_bf16 v[104:107], v[146:149], v[178:181], v[104:107]
	v_mfma_f32_16x16x32_bf16 v[92:95], v[138:141], v[190:193], v[92:95]
	v_mfma_f32_16x16x32_bf16 v[88:91], v[146:149], v[190:193], v[88:91]
	v_mfma_f32_16x16x32_bf16 v[76:79], v[138:141], v[198:201], v[76:79]
	v_mfma_f32_16x16x32_bf16 v[72:75], v[146:149], v[198:201], v[72:75]
	v_mfma_f32_16x16x32_bf16 v[116:119], v[150:153], v[166:169], v[116:119]
	v_mfma_f32_16x16x32_bf16 v[112:115], v[158:161], v[166:169], v[112:115]
	v_mfma_f32_16x16x32_bf16 v[100:103], v[150:153], v[174:177], v[100:103]
	v_mfma_f32_16x16x32_bf16 v[96:99], v[158:161], v[174:177], v[96:99]
	v_mfma_f32_16x16x32_bf16 v[84:87], v[150:153], v[182:185], v[84:87]
	v_mfma_f32_16x16x32_bf16 v[80:83], v[158:161], v[182:185], v[80:83]
	v_mfma_f32_16x16x32_bf16 v[68:71], v[150:153], v[194:197], v[68:71]
	v_mfma_f32_16x16x32_bf16 v[64:67], v[158:161], v[194:197], v[64:67]
	v_mfma_f32_16x16x32_bf16 v[116:119], v[154:157], v[170:173], v[116:119]
	v_mfma_f32_16x16x32_bf16 v[112:115], v[162:165], v[170:173], v[112:115]
	v_mfma_f32_16x16x32_bf16 v[100:103], v[154:157], v[178:181], v[100:103]
	v_mfma_f32_16x16x32_bf16 v[96:99], v[162:165], v[178:181], v[96:99]
	v_mfma_f32_16x16x32_bf16 v[84:87], v[154:157], v[190:193], v[84:87]
	v_mfma_f32_16x16x32_bf16 v[80:83], v[162:165], v[190:193], v[80:83]
	v_mfma_f32_16x16x32_bf16 v[68:71], v[154:157], v[198:201], v[68:71]
	v_mfma_f32_16x16x32_bf16 v[64:67], v[162:165], v[198:201], v[64:67]
	s_barrier
	s_setprio 0
	ds_read_b128 v[166:169], v137 offset:49152
	ds_read_b128 v[170:173], v137 offset:50176
	ds_read_b128 v[174:177], v137 offset:51200
	ds_read_b128 v[178:181], v137 offset:52224
	ds_read_b128 v[182:185], v137 offset:53248
	ds_read_b128 v[190:193], v137 offset:54272
	ds_read_b128 v[194:197], v137 offset:55296
	ds_read_b128 v[198:201], v137 offset:56320
	s_mov_b32 m0, s66
	s_nop 0
	global_load_lds_dwordx4 v133, s[60:61]
	s_nop 0
	s_mov_b32 m0, s67
	s_nop 0
	global_load_lds_dwordx4 v135, s[60:61]
	s_add_u32 s60, s60, 0x40000
	s_addc_u32 s61, s61, 0
	s_mov_b32 m0, s70
	s_nop 0
	global_load_lds_dwordx4 v133, s[60:61]
	s_nop 0
	s_mov_b32 m0, s71
	s_nop 0
	global_load_lds_dwordx4 v135, s[60:61]
	s_nop 0
	s_mov_b32 m0, s68
	s_nop 0
	global_load_lds_dwordx4 v132, s[58:59]
	s_nop 0
	s_mov_b32 m0, s69
	s_nop 0
	global_load_lds_dwordx4 v134, s[58:59]
	s_setprio 1
	s_waitcnt vmcnt(8)
	s_waitcnt lgkmcnt(0)
	s_barrier
	v_mfma_f32_16x16x32_bf16 v[60:63], v[128:131], v[166:169], v[60:63]
	v_mfma_f32_16x16x32_bf16 v[56:59], v[142:145], v[166:169], v[56:59]
	v_mfma_f32_16x16x32_bf16 v[44:47], v[128:131], v[174:177], v[44:47]
	v_mfma_f32_16x16x32_bf16 v[40:43], v[142:145], v[174:177], v[40:43]
	v_mfma_f32_16x16x32_bf16 v[28:31], v[128:131], v[182:185], v[28:31]
	v_mfma_f32_16x16x32_bf16 v[24:27], v[142:145], v[182:185], v[24:27]
	v_mfma_f32_16x16x32_bf16 v[12:15], v[128:131], v[194:197], v[12:15]
	v_mfma_f32_16x16x32_bf16 v[8:11], v[142:145], v[194:197], v[8:11]
	v_mfma_f32_16x16x32_bf16 v[60:63], v[138:141], v[170:173], v[60:63]
	v_mfma_f32_16x16x32_bf16 v[56:59], v[146:149], v[170:173], v[56:59]
	v_mfma_f32_16x16x32_bf16 v[44:47], v[138:141], v[178:181], v[44:47]
	v_mfma_f32_16x16x32_bf16 v[40:43], v[146:149], v[178:181], v[40:43]
	v_mfma_f32_16x16x32_bf16 v[28:31], v[138:141], v[190:193], v[28:31]
	v_mfma_f32_16x16x32_bf16 v[24:27], v[146:149], v[190:193], v[24:27]
	v_mfma_f32_16x16x32_bf16 v[12:15], v[138:141], v[198:201], v[12:15]
	v_mfma_f32_16x16x32_bf16 v[8:11], v[146:149], v[198:201], v[8:11]
	v_mfma_f32_16x16x32_bf16 v[52:55], v[150:153], v[166:169], v[52:55]
	v_mfma_f32_16x16x32_bf16 v[48:51], v[158:161], v[166:169], v[48:51]
	v_mfma_f32_16x16x32_bf16 v[36:39], v[150:153], v[174:177], v[36:39]
	v_mfma_f32_16x16x32_bf16 v[32:35], v[158:161], v[174:177], v[32:35]
	v_mfma_f32_16x16x32_bf16 v[20:23], v[150:153], v[182:185], v[20:23]
	v_mfma_f32_16x16x32_bf16 v[16:19], v[158:161], v[182:185], v[16:19]
	v_mfma_f32_16x16x32_bf16 v[4:7], v[150:153], v[194:197], v[4:7]
	v_mfma_f32_16x16x32_bf16 v[0:3], v[158:161], v[194:197], v[0:3]
	v_mfma_f32_16x16x32_bf16 v[52:55], v[154:157], v[170:173], v[52:55]
	v_mfma_f32_16x16x32_bf16 v[48:51], v[162:165], v[170:173], v[48:51]
	v_mfma_f32_16x16x32_bf16 v[36:39], v[154:157], v[178:181], v[36:39]
	v_mfma_f32_16x16x32_bf16 v[32:35], v[162:165], v[178:181], v[32:35]
	v_mfma_f32_16x16x32_bf16 v[20:23], v[154:157], v[190:193], v[20:23]
	v_mfma_f32_16x16x32_bf16 v[16:19], v[162:165], v[190:193], v[16:19]
	v_mfma_f32_16x16x32_bf16 v[4:7], v[154:157], v[198:201], v[4:7]
	v_mfma_f32_16x16x32_bf16 v[0:3], v[162:165], v[198:201], v[0:3]
	s_barrier
	s_setprio 0
	s_add_i32 s81, s81, 2
	s_add_u32 s56, s56, 0x100
	s_addc_u32 s57, s57, 0
	s_cbranch_vccz .LBB0_816
	s_and_b64 vcc, exec, s[42:43]
	s_cbranch_vccz .LBB0_819
	s_barrier

.LBB0_822:
	v_readlane_b32 s0, v253, 2
	v_readlane_b32 s1, v253, 3
	s_waitcnt vmcnt(0)
	s_barrier
	s_waitcnt vmcnt(0)
	s_barrier
	s_load_dwordx2 s[0:1], s[0:1], 0xf8
	v_mbcnt_lo_u32_b32 v0, -1, 0
	v_mbcnt_hi_u32_b32 v0, -1, v0
	v_readlane_b32 s16, v254, 37
	v_or_b32_e32 v0, s33, v0
	s_waitcnt lgkmcnt(0)
	s_add_u32 s2, s0, 0x45901800
	v_bfe_i32 v3, v0, 27, 1
	v_lshlrev_b32_e32 v1, 4, v0
	v_lshrrev_b32_e32 v3, 22, v3
	v_add_u32_e32 v3, v1, v3
	v_and_b32_e32 v3, 0xfffffc00, v3
	v_sub_u32_e32 v3, v1, v3
	v_ashrrev_i32_e32 v2, 31, v0
	v_lshrrev_b32_e32 v4, 4, v3
	v_lshrrev_b32_e32 v2, 26, v2
	v_bitop3_b32 v4, v4, v3, 32 bitop3:0x6c
	v_ashrrev_i32_e32 v3, 31, v3
	v_add_u32_e32 v2, v0, v2
	v_lshrrev_b32_e32 v3, 26, v3
	v_ashrrev_i32_e32 v2, 6, v2
	v_add_u32_e32 v3, v4, v3
	v_lshlrev_b32_e32 v5, 3, v2
	v_ashrrev_i32_e32 v3, 6, v3
	s_addc_u32 s3, s1, 0
	s_lshl_b64 s[10:11], s[20:21], 1
	v_and_b32_e32 v5, -16, v5
	v_mul_i32_i24_e32 v6, 64, v3
	s_add_u32 s9, s0, s10
	v_add_u32_e32 v5, v3, v5
	v_sub_u32_e32 v4, v4, v6
	s_addc_u32 s10, s1, s11
	v_lshlrev_b32_e32 v2, 5, v2
	v_ashrrev_i16_sdwa v4, v242, sext(v4) dst_sel:DWORD dst_unused:UNUSED_PAD src0_sel:DWORD src1_sel:BYTE_0
	v_lshlrev_b32_e32 v6, 1, v5
	v_lshrrev_b32_e32 v7, 2, v5
	v_and_b32_e32 v3, 3, v3
	s_mov_b32 s11, 0x1fffe0
	v_and_b32_e32 v2, 32, v2
	v_bfe_i32 v4, v4, 0, 16
	v_and_b32_e32 v6, 24, v6
	v_and_b32_e32 v7, 4, v7
	v_and_or_b32 v3, v5, s11, v3
	v_or3_b32 v3, v3, v7, v6
	v_add_lshl_u32 v2, v2, v4, 1
	v_add_u32_e32 v1, 0x2000, v1
	v_mad_u64_u32 v[190:191], s[20:21], v5, s93, v[2:3]
	v_lshl_add_u32 v188, v3, 11, v2
	v_ashrrev_i32_e32 v2, 31, v1
	v_lshrrev_b32_e32 v2, 22, v2
	v_add_u32_e32 v2, v1, v2
	v_ashrrev_i32_e32 v2, 10, v2
	v_mul_i32_i24_e32 v3, 0x400, v2
	v_sub_u32_e32 v1, v1, v3
	v_lshrrev_b32_e32 v3, 4, v1
	v_bitop3_b32 v1, v3, v1, 32 bitop3:0x6c
	v_ashrrev_i32_e32 v4, 31, v1
	v_lshrrev_b32_e32 v4, 26, v4
	v_lshlrev_b32_e32 v3, 3, v2
	v_add_u32_e32 v4, v1, v4
	s_add_u32 s13, s9, 0x5f00000
	v_readfirstlane_b32 s9, v0
	v_and_b32_e32 v3, -16, v3
	v_ashrrev_i32_e32 v5, 6, v4
	v_and_b32_e32 v4, 0xc0, v4
	s_addc_u32 s18, s10, 0
	s_ashr_i32 s10, s9, 6
	v_add_u32_e32 v3, v5, v3
	v_sub_u32_e32 v1, v1, v4
	v_and_b32_e32 v5, 3, v5
	v_lshlrev_b32_e32 v2, 5, v2
	v_ashrrev_i16_sdwa v1, v242, sext(v1) dst_sel:DWORD dst_unused:UNUSED_PAD src0_sel:DWORD src1_sel:BYTE_0
	v_and_or_b32 v5, v3, s11, v5
	s_ashr_i32 s11, s9, 8
	s_lshl_b32 s19, s10, 10
	v_and_b32_e32 v2, 32, v2
	v_bfe_i32 v1, v1, 0, 16
	v_lshlrev_b32_e32 v4, 1, v3
	v_lshrrev_b32_e32 v6, 2, v3
	v_readlane_b32 s17, v254, 38
	s_add_u32 s40, s13, s16
	v_and_b32_e32 v4, 24, v4
	v_and_b32_e32 v6, 4, v6
	v_add_lshl_u32 v2, v2, v1, 1
	s_addc_u32 s41, s18, s17
	s_add_i32 s19, s19, 0
	v_or3_b32 v4, v5, v6, v4
	v_mad_u64_u32 v[192:193], s[20:21], v3, s93, v[2:3]
	s_add_i32 s28, s19, 0x10000
	s_mov_b32 m0, s28
	s_nop 0
	global_load_lds_dwordx4 v188, s[40:41]
	s_add_i32 s29, s19, 0x12000
	v_lshl_add_u32 v191, v4, 11, v2
	s_mov_b32 m0, s29
	s_nop 0
	global_load_lds_dwordx4 v191, s[40:41]
	s_add_u32 s20, s40, 0x40000
	s_addc_u32 s21, s41, 0
	s_add_i32 s34, s19, 0x14000
	s_mov_b32 m0, s34
	s_nop 0
	global_load_lds_dwordx4 v188, s[20:21]
	s_add_i32 s35, s19, 0x16000
	s_mov_b32 m0, s35
	s_nop 0
	global_load_lds_dwordx4 v191, s[20:21]
	v_writelane_b32 v255, s86, 50
	v_readlane_b32 s12, v253, 10
	s_mul_i32 s12, s12, 0x440000
	s_add_u32 s42, s2, s12
	s_addc_u32 s43, s3, 0
	s_mov_b32 m0, s19
	s_nop 0
	global_load_lds_dwordx4 v190, s[42:43]
	s_add_i32 s36, s19, 0x2000
	s_mov_b32 m0, s36
	s_nop 0
	global_load_lds_dwordx4 v192, s[42:43]
	s_add_u32 s20, s42, 0x220000
	s_addc_u32 s21, s43, 0
	s_add_i32 s37, s19, 0x4000
	s_mov_b32 m0, s37
	s_nop 0
	global_load_lds_dwordx4 v190, s[20:21]
	s_add_i32 s65, s19, 0x6000
	s_mov_b32 m0, s65
	s_nop 0
	global_load_lds_dwordx4 v192, s[20:21]
	s_cmp_eq_u32 s11, 1
	v_writelane_b32 v255, s87, 51
	s_cselect_b64 s[20:21], -1, 0
	s_cmp_lg_u32 s11, 1
	s_cbranch_scc1 .LBB0_824
	s_barrier
.LBB0_824:
	s_add_u32 s22, s0, 0x45900000
	s_addc_u32 s23, s1, 0
	s_add_u32 s44, s0, 0x45903400
	s_addc_u32 s45, s1, 0
	s_add_u32 s46, s0, 0x1300000
	s_addc_u32 s47, s1, 0
	s_add_u32 s48, s0, 0x1ec00000
	s_addc_u32 s49, s1, 0
	s_lshl_b64 s[30:31], s[84:85], 20
	s_add_u32 s12, s0, s30
	s_addc_u32 s16, s1, s31
	s_add_u32 s52, s12, 0x1e800000
	s_addc_u32 s53, s16, 0
	s_mov_b32 s12, s84
	s_lshl_b32 s72, s84, 13
	v_writelane_b32 v255, s12, 54
	s_lshl_b64 s[30:31], s[72:73], 2
	v_and_b32_e32 v1, 48, v0
	v_writelane_b32 v255, s13, 55
	s_add_u32 s12, s0, s30
	s_addc_u32 s16, s1, s31
	s_add_u32 s31, s12, 0x28000
	s_addc_u32 s51, s16, 0
	v_lshlrev_b32_e32 v2, 6, v0
	s_movk_i32 s16, 0x3c0
	v_lshlrev_b32_e32 v0, 2, v0
	s_and_b32 s12, s10, 3
	s_lshl_b32 s66, s11, 6
	s_lshl_b32 s11, s11, 13
	v_and_or_b32 v1, v2, s16, v1
	v_and_b32_e32 v0, 32, v0
	v_bitop3_b32 v2, v1, s11, v0 bitop3:0xde
	s_lshl_b32 s67, s12, 5
	s_lshl_b32 s11, s12, 12
	s_add_u32 s54, s40, 0x80
	v_bitop3_b32 v0, v1, s11, v0 bitop3:0xde
	s_waitcnt vmcnt(2)
	s_barrier
	s_addc_u32 s55, s41, 0
	s_add_i32 s68, s19, 0x18000
	s_mov_b32 m0, s68
	s_nop 0
	global_load_lds_dwordx4 v188, s[54:55]
	s_add_i32 s30, s19, 0x1a000
	s_mov_b32 m0, s30
	s_nop 0
	global_load_lds_dwordx4 v191, s[54:55]
	s_add_u32 s54, s42, 0x80
	s_addc_u32 s55, s43, 0
	s_add_i32 s69, s19, 0x8000
	s_mov_b32 m0, s69
	s_nop 0
	global_load_lds_dwordx4 v190, s[54:55]
	s_add_i32 s70, s19, 0xa000
	s_mov_b32 m0, s70
	s_nop 0
	global_load_lds_dwordx4 v192, s[54:55]
	s_add_u32 s54, s40, 0x40080
	s_addc_u32 s55, s41, 0
	s_add_i32 s71, s19, 0x1c000
	s_mov_b32 m0, s71
	s_nop 0
	global_load_lds_dwordx4 v188, s[54:55]
	s_add_i32 s72, s19, 0x1e000
	s_mov_b32 m0, s72
	s_nop 0
	global_load_lds_dwordx4 v191, s[54:55]
	s_lshl_b32 s11, s12, 2
	s_add_i32 s83, s11, 0
	s_add_i32 s82, s19, 0xc000
	s_add_i32 s83, s83, 0x20000
	s_cmpk_lt_u32 s9, 0x100
	s_waitcnt vmcnt(6)
	s_cselect_b64 s[54:55], -1, 0
	s_lshl_b32 s84, s10, 5
	s_cmp_lt_u32 s9, 64
	s_mov_b32 s87, 0
	s_cselect_b64 s[56:57], -1, 0
	v_add_u32_e32 v193, 0, v0
	v_add_u32_e32 v194, 0, v2
	v_readlane_b32 s88, v253, 10
	s_barrier
	s_branch .LBB0_827

.LBB0_832:
	s_cmp_gt_u32 s90, 13
	s_cselect_b64 s[74:75], -1, 0
	s_and_b64 vcc, s[74:75], exec
	s_cselect_b32 s16, -14, 2
	s_add_i32 s74, s16, s90
	s_ashr_i32 s75, s74, 31
	s_lshl_b64 s[74:75], s[74:75], 7
	s_add_u32 s16, s42, s74
	s_addc_u32 s17, s43, s75
	s_add_u32 s50, s40, s74
	s_addc_u32 s76, s41, s75
	s_cmp_gt_u32 s90, 12
	s_cselect_b32 s74, -13, 3
	s_add_i32 s74, s74, s90
	s_ashr_i32 s75, s74, 31
	s_lshl_b64 s[74:75], s[74:75], 7
	s_add_u32 s77, s42, s74
	s_addc_u32 s91, s43, s75
	s_add_u32 s92, s40, s74
	s_addc_u32 s94, s41, s75
	s_cmp_eq_u32 s90, 14
	s_cselect_b32 s78, s58, s16
	s_mov_b32 s16, s90
	v_add_u32_e32 v108, 0x10000, v193
	v_add_u32_e32 v140, 0x14000, v193
	ds_read_b128 v[88:91], v108
	ds_read_b128 v[92:95], v108 offset:1024
	ds_read_b128 v[104:107], v108 offset:2048
	ds_read_b128 v[108:111], v108 offset:3072
	ds_read_b128 v[120:123], v140
	ds_read_b128 v[124:127], v140 offset:1024
	ds_read_b128 v[136:139], v140 offset:2048
	ds_read_b128 v[140:143], v140 offset:3072
	s_cselect_b32 s79, s59, s17
	s_cselect_b32 s81, s9, s76
	s_cselect_b32 s80, s10, s50
	s_cselect_b32 s75, s12, s91
	s_cselect_b32 s74, s11, s77
	s_cselect_b32 s77, s89, s94
	s_cselect_b32 s76, s27, s92
	ds_read_b128 v[152:155], v194
	ds_read_b128 v[156:159], v194 offset:1024
	ds_read_b128 v[168:171], v194 offset:2048
	ds_read_b128 v[172:175], v194 offset:3072
	ds_read_b128 v[176:179], v194 offset:4096
	ds_read_b128 v[180:183], v194 offset:5120
	ds_read_b128 v[184:187], v194 offset:6144
	ds_read_b128 v[196:199], v194 offset:7168
	s_add_u32 s16, s62, 0x220080
	s_addc_u32 s17, s63, 0
	s_mov_b32 m0, s82
	s_nop 0
	global_load_lds_dwordx4 v190, s[16:17]
	s_add_i32 s50, s19, 0xe000
	s_mov_b32 m0, s50
	s_nop 0
	global_load_lds_dwordx4 v192, s[16:17]
	s_setprio 1
	s_waitcnt vmcnt(8)
	s_waitcnt lgkmcnt(0)
	s_barrier
	v_mfma_f32_16x16x32_bf16 v[164:167], v[88:91], v[152:155], v[164:167]
	v_mfma_f32_16x16x32_bf16 v[160:163], v[104:107], v[152:155], v[160:163]
	v_mfma_f32_16x16x32_bf16 v[132:135], v[88:91], v[168:171], v[132:135]
	v_mfma_f32_16x16x32_bf16 v[128:131], v[104:107], v[168:171], v[128:131]
	v_mfma_f32_16x16x32_bf16 v[100:103], v[88:91], v[176:179], v[100:103]
	v_mfma_f32_16x16x32_bf16 v[96:99], v[104:107], v[176:179], v[96:99]
	v_mfma_f32_16x16x32_bf16 v[76:79], v[88:91], v[184:187], v[76:79]
	v_mfma_f32_16x16x32_bf16 v[72:75], v[104:107], v[184:187], v[72:75]
	v_mfma_f32_16x16x32_bf16 v[164:167], v[92:95], v[156:159], v[164:167]
	v_mfma_f32_16x16x32_bf16 v[160:163], v[108:111], v[156:159], v[160:163]
	v_mfma_f32_16x16x32_bf16 v[132:135], v[92:95], v[172:175], v[132:135]
	v_mfma_f32_16x16x32_bf16 v[128:131], v[108:111], v[172:175], v[128:131]
	v_mfma_f32_16x16x32_bf16 v[100:103], v[92:95], v[180:183], v[100:103]
	v_mfma_f32_16x16x32_bf16 v[96:99], v[108:111], v[180:183], v[96:99]
	v_mfma_f32_16x16x32_bf16 v[76:79], v[92:95], v[196:199], v[76:79]
	v_mfma_f32_16x16x32_bf16 v[72:75], v[108:111], v[196:199], v[72:75]
	v_mfma_f32_16x16x32_bf16 v[148:151], v[120:123], v[152:155], v[148:151]
	v_mfma_f32_16x16x32_bf16 v[144:147], v[136:139], v[152:155], v[144:147]
	v_mfma_f32_16x16x32_bf16 v[116:119], v[120:123], v[168:171], v[116:119]
	v_mfma_f32_16x16x32_bf16 v[112:115], v[136:139], v[168:171], v[112:115]
	v_mfma_f32_16x16x32_bf16 v[84:87], v[120:123], v[176:179], v[84:87]
	v_mfma_f32_16x16x32_bf16 v[80:83], v[136:139], v[176:179], v[80:83]
	v_mfma_f32_16x16x32_bf16 v[68:71], v[120:123], v[184:187], v[68:71]
	v_mfma_f32_16x16x32_bf16 v[64:67], v[136:139], v[184:187], v[64:67]
	v_mfma_f32_16x16x32_bf16 v[148:151], v[124:127], v[156:159], v[148:151]
	v_mfma_f32_16x16x32_bf16 v[144:147], v[140:143], v[156:159], v[144:147]
	v_mfma_f32_16x16x32_bf16 v[116:119], v[124:127], v[172:175], v[116:119]
	v_mfma_f32_16x16x32_bf16 v[112:115], v[140:143], v[172:175], v[112:115]
	v_mfma_f32_16x16x32_bf16 v[84:87], v[124:127], v[180:183], v[84:87]
	v_mfma_f32_16x16x32_bf16 v[80:83], v[140:143], v[180:183], v[80:83]
	v_mfma_f32_16x16x32_bf16 v[68:71], v[124:127], v[196:199], v[68:71]
	v_mfma_f32_16x16x32_bf16 v[64:67], v[140:143], v[196:199], v[64:67]
	s_barrier
	s_setprio 0
	ds_read_b128 v[152:155], v194 offset:16384
	ds_read_b128 v[156:159], v194 offset:17408
	ds_read_b128 v[168:171], v194 offset:18432
	ds_read_b128 v[172:175], v194 offset:19456
	ds_read_b128 v[176:179], v194 offset:20480
	ds_read_b128 v[180:183], v194 offset:21504
	ds_read_b128 v[184:187], v194 offset:22528
	ds_read_b128 v[196:199], v194 offset:23552
	s_mov_b32 m0, s28
	s_nop 0
	global_load_lds_dwordx4 v188, s[80:81]
	s_nop 0
	s_mov_b32 m0, s29
	s_nop 0
	global_load_lds_dwordx4 v191, s[80:81]
	s_add_u32 s16, s80, 0x40000
	s_addc_u32 s17, s81, 0
	s_mov_b32 m0, s34
	s_nop 0
	global_load_lds_dwordx4 v188, s[16:17]
	s_nop 0
	s_mov_b32 m0, s35
	s_nop 0
	global_load_lds_dwordx4 v191, s[16:17]
	s_mov_b32 m0, s19
	s_nop 0
	global_load_lds_dwordx4 v190, s[78:79]
	s_nop 0
	s_mov_b32 m0, s36
	s_nop 0
	global_load_lds_dwordx4 v192, s[78:79]
	s_setprio 1
	s_waitcnt vmcnt(8)
	s_waitcnt lgkmcnt(0)
	s_barrier
	v_mfma_f32_16x16x32_bf16 v[60:63], v[88:91], v[152:155], v[60:63]
	v_mfma_f32_16x16x32_bf16 v[56:59], v[104:107], v[152:155], v[56:59]
	v_mfma_f32_16x16x32_bf16 v[44:47], v[88:91], v[168:171], v[44:47]
	v_mfma_f32_16x16x32_bf16 v[40:43], v[104:107], v[168:171], v[40:43]
	v_mfma_f32_16x16x32_bf16 v[28:31], v[88:91], v[176:179], v[28:31]
	v_mfma_f32_16x16x32_bf16 v[24:27], v[104:107], v[176:179], v[24:27]
	v_mfma_f32_16x16x32_bf16 v[12:15], v[88:91], v[184:187], v[12:15]
	v_mfma_f32_16x16x32_bf16 v[8:11], v[104:107], v[184:187], v[8:11]
	v_mfma_f32_16x16x32_bf16 v[60:63], v[92:95], v[156:159], v[60:63]
	v_mfma_f32_16x16x32_bf16 v[56:59], v[108:111], v[156:159], v[56:59]
	v_mfma_f32_16x16x32_bf16 v[44:47], v[92:95], v[172:175], v[44:47]
	v_mfma_f32_16x16x32_bf16 v[40:43], v[108:111], v[172:175], v[40:43]
	v_mfma_f32_16x16x32_bf16 v[28:31], v[92:95], v[180:183], v[28:31]
	v_mfma_f32_16x16x32_bf16 v[24:27], v[108:111], v[180:183], v[24:27]
	v_mfma_f32_16x16x32_bf16 v[12:15], v[92:95], v[196:199], v[12:15]
	v_mfma_f32_16x16x32_bf16 v[8:11], v[108:111], v[196:199], v[8:11]
	v_mfma_f32_16x16x32_bf16 v[52:55], v[120:123], v[152:155], v[52:55]
	v_mfma_f32_16x16x32_bf16 v[48:51], v[136:139], v[152:155], v[48:51]
	v_mfma_f32_16x16x32_bf16 v[36:39], v[120:123], v[168:171], v[36:39]
	v_mfma_f32_16x16x32_bf16 v[32:35], v[136:139], v[168:171], v[32:35]
	v_mfma_f32_16x16x32_bf16 v[20:23], v[120:123], v[176:179], v[20:23]
	v_mfma_f32_16x16x32_bf16 v[16:19], v[136:139], v[176:179], v[16:19]
	v_mfma_f32_16x16x32_bf16 v[4:7], v[120:123], v[184:187], v[4:7]
	v_mfma_f32_16x16x32_bf16 v[0:3], v[136:139], v[184:187], v[0:3]
	v_mfma_f32_16x16x32_bf16 v[52:55], v[124:127], v[156:159], v[52:55]
	v_mfma_f32_16x16x32_bf16 v[48:51], v[140:143], v[156:159], v[48:51]
	v_mfma_f32_16x16x32_bf16 v[36:39], v[124:127], v[172:175], v[36:39]
	v_mfma_f32_16x16x32_bf16 v[32:35], v[140:143], v[172:175], v[32:35]
	v_mfma_f32_16x16x32_bf16 v[20:23], v[124:127], v[180:183], v[20:23]
	v_mfma_f32_16x16x32_bf16 v[16:19], v[140:143], v[180:183], v[16:19]
	v_mfma_f32_16x16x32_bf16 v[4:7], v[124:127], v[196:199], v[4:7]
	v_mfma_f32_16x16x32_bf16 v[0:3], v[140:143], v[196:199], v[0:3]
	s_barrier
	s_setprio 0
	v_add_u32_e32 v108, 0x18000, v193
	v_add_u32_e32 v140, 0x1c000, v193
	ds_read_b128 v[88:91], v108
	ds_read_b128 v[92:95], v108 offset:1024
	ds_read_b128 v[104:107], v108 offset:2048
	ds_read_b128 v[108:111], v108 offset:3072
	ds_read_b128 v[120:123], v140
	ds_read_b128 v[124:127], v140 offset:1024
	ds_read_b128 v[136:139], v140 offset:2048
	ds_read_b128 v[140:143], v140 offset:3072
	ds_read_b128 v[152:155], v194 offset:32768
	ds_read_b128 v[156:159], v194 offset:33792
	ds_read_b128 v[168:171], v194 offset:34816
	ds_read_b128 v[172:175], v194 offset:35840
	ds_read_b128 v[176:179], v194 offset:36864
	ds_read_b128 v[180:183], v194 offset:37888
	ds_read_b128 v[184:187], v194 offset:38912
	ds_read_b128 v[196:199], v194 offset:39936
	s_add_u32 s16, s78, 0x220000
	s_addc_u32 s17, s79, 0
	s_mov_b32 m0, s37
	s_nop 0
	global_load_lds_dwordx4 v190, s[16:17]
	s_nop 0
	s_mov_b32 m0, s65
	s_nop 0
	global_load_lds_dwordx4 v192, s[16:17]
	s_setprio 1
	s_waitcnt vmcnt(8)
	s_waitcnt lgkmcnt(0)
	s_barrier
	v_mfma_f32_16x16x32_bf16 v[164:167], v[88:91], v[152:155], v[164:167]
	v_mfma_f32_16x16x32_bf16 v[160:163], v[104:107], v[152:155], v[160:163]
	v_mfma_f32_16x16x32_bf16 v[132:135], v[88:91], v[168:171], v[132:135]
	v_mfma_f32_16x16x32_bf16 v[128:131], v[104:107], v[168:171], v[128:131]
	v_mfma_f32_16x16x32_bf16 v[100:103], v[88:91], v[176:179], v[100:103]
	v_mfma_f32_16x16x32_bf16 v[96:99], v[104:107], v[176:179], v[96:99]
	v_mfma_f32_16x16x32_bf16 v[76:79], v[88:91], v[184:187], v[76:79]
	v_mfma_f32_16x16x32_bf16 v[72:75], v[104:107], v[184:187], v[72:75]
	v_mfma_f32_16x16x32_bf16 v[164:167], v[92:95], v[156:159], v[164:167]
	v_mfma_f32_16x16x32_bf16 v[160:163], v[108:111], v[156:159], v[160:163]
	v_mfma_f32_16x16x32_bf16 v[132:135], v[92:95], v[172:175], v[132:135]
	v_mfma_f32_16x16x32_bf16 v[128:131], v[108:111], v[172:175], v[128:131]
	v_mfma_f32_16x16x32_bf16 v[100:103], v[92:95], v[180:183], v[100:103]
	v_mfma_f32_16x16x32_bf16 v[96:99], v[108:111], v[180:183], v[96:99]
	v_mfma_f32_16x16x32_bf16 v[76:79], v[92:95], v[196:199], v[76:79]
	v_mfma_f32_16x16x32_bf16 v[72:75], v[108:111], v[196:199], v[72:75]
	v_mfma_f32_16x16x32_bf16 v[148:151], v[120:123], v[152:155], v[148:151]
	v_mfma_f32_16x16x32_bf16 v[144:147], v[136:139], v[152:155], v[144:147]
	v_mfma_f32_16x16x32_bf16 v[116:119], v[120:123], v[168:171], v[116:119]
	v_mfma_f32_16x16x32_bf16 v[112:115], v[136:139], v[168:171], v[112:115]
	v_mfma_f32_16x16x32_bf16 v[84:87], v[120:123], v[176:179], v[84:87]
	v_mfma_f32_16x16x32_bf16 v[80:83], v[136:139], v[176:179], v[80:83]
	v_mfma_f32_16x16x32_bf16 v[68:71], v[120:123], v[184:187], v[68:71]
	v_mfma_f32_16x16x32_bf16 v[64:67], v[136:139], v[184:187], v[64:67]
	v_mfma_f32_16x16x32_bf16 v[148:151], v[124:127], v[156:159], v[148:151]
	v_mfma_f32_16x16x32_bf16 v[144:147], v[140:143], v[156:159], v[144:147]
	v_mfma_f32_16x16x32_bf16 v[116:119], v[124:127], v[172:175], v[116:119]
	v_mfma_f32_16x16x32_bf16 v[112:115], v[140:143], v[172:175], v[112:115]
	v_mfma_f32_16x16x32_bf16 v[84:87], v[124:127], v[180:183], v[84:87]
	v_mfma_f32_16x16x32_bf16 v[80:83], v[140:143], v[180:183], v[80:83]
	v_mfma_f32_16x16x32_bf16 v[68:71], v[124:127], v[196:199], v[68:71]
	v_mfma_f32_16x16x32_bf16 v[64:67], v[140:143], v[196:199], v[64:67]
	s_barrier
	s_setprio 0
	ds_read_b128 v[152:155], v194 offset:49152
	ds_read_b128 v[156:159], v194 offset:50176
	ds_read_b128 v[168:171], v194 offset:51200
	ds_read_b128 v[172:175], v194 offset:52224
	ds_read_b128 v[176:179], v194 offset:53248
	ds_read_b128 v[180:183], v194 offset:54272
	ds_read_b128 v[184:187], v194 offset:55296
	ds_read_b128 v[196:199], v194 offset:56320
	s_mov_b32 m0, s68
	s_nop 0
	global_load_lds_dwordx4 v188, s[76:77]
	s_nop 0
	s_mov_b32 m0, s30
	s_nop 0
	global_load_lds_dwordx4 v191, s[76:77]
	s_add_u32 s16, s76, 0x40000
	s_addc_u32 s17, s77, 0
	s_mov_b32 m0, s71
	s_nop 0
	global_load_lds_dwordx4 v188, s[16:17]
	s_nop 0
	s_mov_b32 m0, s72
	s_nop 0
	global_load_lds_dwordx4 v191, s[16:17]
	s_mov_b32 m0, s69
	s_nop 0
	global_load_lds_dwordx4 v190, s[74:75]
	s_nop 0
	s_mov_b32 m0, s70
	s_nop 0
	global_load_lds_dwordx4 v192, s[74:75]
	s_setprio 1
	s_waitcnt vmcnt(8)
	s_waitcnt lgkmcnt(0)
	s_barrier
	v_mfma_f32_16x16x32_bf16 v[60:63], v[88:91], v[152:155], v[60:63]
	v_mfma_f32_16x16x32_bf16 v[56:59], v[104:107], v[152:155], v[56:59]
	v_mfma_f32_16x16x32_bf16 v[44:47], v[88:91], v[168:171], v[44:47]
	v_mfma_f32_16x16x32_bf16 v[40:43], v[104:107], v[168:171], v[40:43]
	v_mfma_f32_16x16x32_bf16 v[28:31], v[88:91], v[176:179], v[28:31]
	v_mfma_f32_16x16x32_bf16 v[24:27], v[104:107], v[176:179], v[24:27]
	v_mfma_f32_16x16x32_bf16 v[12:15], v[88:91], v[184:187], v[12:15]
	v_mfma_f32_16x16x32_bf16 v[8:11], v[104:107], v[184:187], v[8:11]
	v_mfma_f32_16x16x32_bf16 v[60:63], v[92:95], v[156:159], v[60:63]
	v_mfma_f32_16x16x32_bf16 v[56:59], v[108:111], v[156:159], v[56:59]
	v_mfma_f32_16x16x32_bf16 v[44:47], v[92:95], v[172:175], v[44:47]
	v_mfma_f32_16x16x32_bf16 v[40:43], v[108:111], v[172:175], v[40:43]
	v_mfma_f32_16x16x32_bf16 v[28:31], v[92:95], v[180:183], v[28:31]
	v_mfma_f32_16x16x32_bf16 v[24:27], v[108:111], v[180:183], v[24:27]
	v_mfma_f32_16x16x32_bf16 v[12:15], v[92:95], v[196:199], v[12:15]
	v_mfma_f32_16x16x32_bf16 v[8:11], v[108:111], v[196:199], v[8:11]
	v_mfma_f32_16x16x32_bf16 v[52:55], v[120:123], v[152:155], v[52:55]
	v_mfma_f32_16x16x32_bf16 v[48:51], v[136:139], v[152:155], v[48:51]
	v_mfma_f32_16x16x32_bf16 v[36:39], v[120:123], v[168:171], v[36:39]
	v_mfma_f32_16x16x32_bf16 v[32:35], v[136:139], v[168:171], v[32:35]
	v_mfma_f32_16x16x32_bf16 v[20:23], v[120:123], v[176:179], v[20:23]
	v_mfma_f32_16x16x32_bf16 v[16:19], v[136:139], v[176:179], v[16:19]
	v_mfma_f32_16x16x32_bf16 v[4:7], v[120:123], v[184:187], v[4:7]
	v_mfma_f32_16x16x32_bf16 v[0:3], v[136:139], v[184:187], v[0:3]
	v_mfma_f32_16x16x32_bf16 v[52:55], v[124:127], v[156:159], v[52:55]
	v_mfma_f32_16x16x32_bf16 v[48:51], v[140:143], v[156:159], v[48:51]
	v_mfma_f32_16x16x32_bf16 v[36:39], v[124:127], v[172:175], v[36:39]
	v_mfma_f32_16x16x32_bf16 v[32:35], v[140:143], v[172:175], v[32:35]
	v_mfma_f32_16x16x32_bf16 v[20:23], v[124:127], v[180:183], v[20:23]
	v_mfma_f32_16x16x32_bf16 v[16:19], v[140:143], v[180:183], v[16:19]
	v_mfma_f32_16x16x32_bf16 v[4:7], v[124:127], v[196:199], v[4:7]
	v_mfma_f32_16x16x32_bf16 v[0:3], v[140:143], v[196:199], v[0:3]
	s_barrier
	s_setprio 0
	s_add_i32 s90, s90, 2
	s_add_u32 s62, s62, 0x100
	s_addc_u32 s63, s63, 0
	s_cbranch_vccz .LBB0_832
	s_and_b64 vcc, exec, s[54:55]
	s_cbranch_vccz .LBB0_835
	s_barrier

.LBB0_918:
	v_readlane_b32 s16, v253, 6
	v_readlane_b32 s18, v253, 8
	s_cmp_le_i32 s18, s2
	s_cselect_b64 s[10:11], -1, 0
	s_and_b64 s[0:1], s[10:11], s[0:1]
	s_andn2_b64 vcc, exec, s[0:1]
	v_readlane_b32 s17, v253, 7
	v_readlane_b32 s19, v253, 9
	s_cbranch_vccnz .LBB0_1038
	v_readlane_b32 s0, v253, 2
	v_readlane_b32 s1, v253, 3
	s_load_dwordx2 s[46:47], s[0:1], 0xf8
	s_mov_b32 s54, 0x3fb504f3
	s_waitcnt vmcnt(1)
	v_mov_b32_e32 v2, 0x1000
	s_load_dwordx4 s[40:43], s[0:1], 0x90
	s_waitcnt lgkmcnt(0)
	global_load_dwordx2 v[0:1], v2, s[46:47] offset:88 sc1
	s_add_u32 s20, s46, 0x1300000
	s_addc_u32 s21, s47, 0
	s_lshl_b32 s9, s84, 22
	s_add_u32 s2, s46, s9
	v_writelane_b32 v255, s10, 56
	s_addc_u32 s3, s47, 0
	v_readlane_b32 s12, v254, 37
	v_writelane_b32 v255, s11, 57
	s_add_u32 s11, s2, 0x6700000
	s_addc_u32 s3, s3, 0
	s_lshl_b64 s[0:1], s[86:87], 2
	s_add_u32 s0, s46, s0
	s_addc_u32 s1, s47, s1
	s_mov_b32 s2, 0x1fffe0
	v_readlane_b32 s13, v254, 38
	v_writelane_b32 v255, s11, 50
	v_writelane_b32 v255, s3, 48
	v_writelane_b32 v255, s20, 52
	v_writelane_b32 v255, s21, 54
	s_waitcnt vmcnt(0)
	v_readfirstlane_b32 s23, v1
	global_load_dword v1, v2, s[0:1] sc1
	s_nop 0
	global_load_dword v2, v2, s[0:1] offset:4 sc1
	v_readfirstlane_b32 s22, v0
	v_mbcnt_lo_u32_b32 v0, -1, 0
	v_mbcnt_hi_u32_b32 v0, -1, v0
	s_nop 0
	v_or_b32_e32 v0, s33, v0
	s_nop 0
	v_bfe_i32 v5, v0, 27, 1
	v_lshlrev_b32_e32 v3, 4, v0
	v_lshrrev_b32_e32 v5, 22, v5
	v_add_u32_e32 v5, v3, v5
	v_and_b32_e32 v5, 0xfffffc00, v5
	v_sub_u32_e32 v5, v3, v5
	v_ashrrev_i32_e32 v4, 31, v0
	v_lshrrev_b32_e32 v6, 4, v5
	v_lshrrev_b32_e32 v4, 26, v4
	v_bitop3_b32 v6, v6, v5, 32 bitop3:0x6c
	v_ashrrev_i32_e32 v5, 31, v5
	v_add_u32_e32 v4, v0, v4
	v_lshrrev_b32_e32 v5, 26, v5
	v_ashrrev_i32_e32 v4, 6, v4
	v_add_u32_e32 v5, v6, v5
	v_lshlrev_b32_e32 v7, 3, v4
	v_ashrrev_i32_e32 v5, 6, v5
	v_and_b32_e32 v7, -16, v7
	v_mul_i32_i24_e32 v8, 64, v5
	v_add_u32_e32 v7, v5, v7
	v_sub_u32_e32 v6, v6, v8
	v_lshlrev_b32_e32 v4, 5, v4
	v_ashrrev_i16_sdwa v6, v242, sext(v6) dst_sel:DWORD dst_unused:UNUSED_PAD src0_sel:DWORD src1_sel:BYTE_0
	v_lshlrev_b32_e32 v8, 1, v7
	v_lshrrev_b32_e32 v9, 2, v7
	v_and_b32_e32 v5, 3, v5
	v_and_b32_e32 v4, 32, v4
	v_bfe_i32 v6, v6, 0, 16
	v_and_b32_e32 v8, 24, v8
	v_and_b32_e32 v9, 4, v9
	v_and_or_b32 v5, v7, s2, v5
	v_or3_b32 v5, v5, v9, v8
	v_add_lshl_u32 v4, v4, v6, 1
	v_add_u32_e32 v3, 0x2000, v3
	v_lshl_add_u32 v184, v7, 11, v4
	v_lshl_add_u32 v185, v5, 11, v4
	v_ashrrev_i32_e32 v4, 31, v3
	v_lshrrev_b32_e32 v4, 22, v4
	v_add_u32_e32 v4, v3, v4
	v_ashrrev_i32_e32 v4, 10, v4
	v_mul_i32_i24_e32 v5, 0x400, v4
	v_sub_u32_e32 v3, v3, v5
	v_lshrrev_b32_e32 v5, 4, v3
	v_bitop3_b32 v3, v5, v3, 32 bitop3:0x6c
	v_ashrrev_i32_e32 v6, 31, v3
	v_lshrrev_b32_e32 v6, 26, v6
	v_lshlrev_b32_e32 v5, 3, v4
	v_add_u32_e32 v6, v3, v6
	v_readfirstlane_b32 s0, v0
	v_and_b32_e32 v5, -16, v5
	v_ashrrev_i32_e32 v7, 6, v6
	s_ashr_i32 s1, s0, 6
	v_add_u32_e32 v5, v7, v5
	v_and_b32_e32 v6, 0xc0, v6
	v_and_b32_e32 v7, 3, v7
	v_sub_u32_e32 v3, v3, v6
	v_and_or_b32 v7, v5, s2, v7
	s_ashr_i32 s10, s0, 8
	s_lshl_b32 s2, s1, 10
	v_lshlrev_b32_e32 v4, 5, v4
	v_ashrrev_i16_sdwa v3, v242, sext(v3) dst_sel:DWORD dst_unused:UNUSED_PAD src0_sel:DWORD src1_sel:BYTE_0
	v_lshlrev_b32_e32 v6, 1, v5
	v_lshrrev_b32_e32 v8, 2, v5
	s_add_u32 s44, s11, s12
	v_and_b32_e32 v4, 32, v4
	v_bfe_i32 v3, v3, 0, 16
	v_and_b32_e32 v6, 24, v6
	v_and_b32_e32 v8, 4, v8
	s_addc_u32 s45, s3, s13
	s_add_i32 s2, s2, 0
	v_or3_b32 v6, v7, v8, v6
	v_add_lshl_u32 v3, v4, v3, 1
	s_add_i32 s3, s2, 0x10000
	s_mov_b32 m0, s3
	s_nop 0
	global_load_lds_dwordx4 v185, s[44:45]
	s_add_i32 s18, s2, 0x12000
	v_lshl_add_u32 v187, v6, 11, v3
	s_mov_b32 m0, s18
	s_nop 0
	global_load_lds_dwordx4 v187, s[44:45]
	s_add_u32 s16, s44, 0x40000
	s_addc_u32 s17, s45, 0
	s_add_i32 s19, s2, 0x14000
	s_mov_b32 m0, s19
	s_nop 0
	global_load_lds_dwordx4 v185, s[16:17]
	s_add_i32 s28, s2, 0x16000
	s_mov_b32 m0, s28
	s_nop 0
	global_load_lds_dwordx4 v187, s[16:17]
	v_lshl_add_u32 v186, v5, 11, v3
	v_readlane_b32 s11, v254, 36
	s_add_u32 s76, s20, s11
	s_addc_u32 s77, s21, 0
	s_add_i32 s29, s2, 0x2000
	s_mov_b32 m0, s2
	s_nop 0
	global_load_lds_dwordx4 v184, s[76:77]
	s_add_u32 s16, s76, 0x40000
	s_mov_b32 m0, s29
	s_nop 0
	global_load_lds_dwordx4 v186, s[76:77]
	s_addc_u32 s17, s77, 0
	s_add_i32 s34, s2, 0x4000
	s_add_i32 s36, s2, 0x6000
	s_mov_b32 m0, s34
	s_nop 0
	global_load_lds_dwordx4 v184, s[16:17]
	s_cmp_eq_u32 s10, 1
	s_mov_b32 m0, s36
	s_nop 0
	global_load_lds_dwordx4 v186, s[16:17]
	s_cselect_b64 s[12:13], -1, 0
	v_writelane_b32 v255, s12, 58
	s_cmp_lg_u32 s10, 1
	s_nop 0
	v_writelane_b32 v255, s13, 59
	s_cbranch_scc1 .LBB0_921
	s_barrier
.LBB0_921:
	s_add_u32 s20, s46, 0x35900000
	s_addc_u32 s21, s47, 0
	s_add_u32 s52, s46, 0x3d900000
	s_addc_u32 s53, s47, 0
	s_add_u32 s56, s46, 0x19900000
	s_addc_u32 s57, s47, 0
	s_lshl_b32 s72, s84, 11
	s_lshl_b64 s[16:17], s[72:73], 2
	s_add_u32 s58, s40, s16
	s_addc_u32 s59, s41, s17
	s_add_u32 s60, s42, s16
	s_flbit_i32_b32 s11, s23
	s_addc_u32 s61, s43, s17
	s_min_u32 s11, s11, 32
	s_lshl_b64 s[16:17], s[22:23], s11
	s_min_u32 s12, s16, 1
	s_or_b32 s12, s17, s12
	v_cvt_f32_u32_e32 v3, s12
	s_sub_i32 s11, 32, s11
	s_waitcnt vmcnt(0)
	v_fmac_f32_e32 v2, 0x40880000, v1
	v_max_f32_e32 v1, 0xda24260, v2
	v_ldexp_f32 v3, v3, s11
	v_mul_f32_e32 v3, 0x2f800000, v3
	v_mul_f32_e32 v3, 0x35800000, v3
	s_mov_b32 s11, 0xf800000
	v_mul_f32_e32 v4, 0x4f800000, v3
	v_cmp_gt_f32_e32 vcc, s11, v3
	s_mov_b32 s12, 0x42fe0000
	v_div_scale_f32 v2, s[22:23], v1, v1, s12
	v_cndmask_b32_e32 v3, v3, v4, vcc
	v_sqrt_f32_e32 v4, v3
	s_add_u32 s9, s46, s9
	s_addc_u32 s11, s47, 0
	s_add_u32 s48, s9, 0x1e000000
	v_add_u32_e32 v5, -1, v4
	v_fma_f32 v6, -v5, v4, v3
	v_cmp_ge_f32_e64 s[40:41], 0, v6
	v_add_u32_e32 v6, 1, v4
	s_addc_u32 s49, s11, 0
	v_cndmask_b32_e64 v5, v4, v5, s[40:41]
	v_fma_f32 v4, -v6, v4, v3
	v_cmp_lt_f32_e64 s[40:41], 0, v4
	s_lshl_b32 s72, s84, 14
	s_lshl_b64 s[16:17], s[72:73], 2
	v_cndmask_b32_e64 v4, v5, v6, s[40:41]
	v_mul_f32_e32 v5, 0x37800000, v4
	v_cndmask_b32_e32 v4, v4, v5, vcc
	v_cmp_class_f32_e32 vcc, v3, v250
	s_add_u32 s9, s46, s16
	s_addc_u32 s11, s47, s17
	v_cndmask_b32_e32 v3, v4, v3, vcc
	v_mul_f32_e32 v3, 0x40880000, v3
	v_max_f32_e32 v3, 0xda24260, v3
	v_mul_f32_e32 v188, 0x3c010204, v3
	v_rcp_f32_e32 v3, v2
	s_add_u32 s9, s9, 0x8000
	v_writelane_b32 v255, s9, 60
	s_addc_u32 s9, s11, 0
	v_fma_f32 v4, -v2, v3, 1.0
	v_fmac_f32_e32 v3, v4, v3
	v_div_scale_f32 v4, vcc, s12, v1, s12
	v_mul_f32_e32 v5, v4, v3
	v_fma_f32 v6, -v2, v5, v4
	v_fmac_f32_e32 v5, v6, v3
	v_fma_f32 v2, -v2, v5, v4
	s_add_u32 s22, s46, 0x1ec00000
	v_writelane_b32 v255, s9, 61
	v_div_fmas_f32 v2, v2, v3, v5
	s_addc_u32 s23, s47, 0
	s_lshl_b32 s11, s10, 6
	v_div_fixup_f32 v190, v2, v1, s12
	v_writelane_b32 v255, s11, 62
	v_and_b32_e32 v1, 48, v0
	v_lshlrev_b32_e32 v2, 6, v0
	s_movk_i32 s11, 0x3c0
	v_lshlrev_b32_e32 v0, 2, v0
	s_and_b32 s9, s1, 3
	s_lshl_b32 s10, s10, 13
	v_and_or_b32 v1, v2, s11, v1
	v_and_b32_e32 v0, 32, v0
	v_bitop3_b32 v2, v1, s10, v0 bitop3:0xde
	s_lshl_b32 s10, s9, 5
	v_writelane_b32 v255, s10, 63
	s_lshl_b32 s10, s9, 12
	v_bitop3_b32 v0, v1, s10, v0 bitop3:0xde
	s_add_u32 s10, s44, 0x80
	s_waitcnt vmcnt(2)
	s_barrier
	s_addc_u32 s11, s45, 0
	s_add_i32 s71, s2, 0x18000
	s_mov_b32 m0, s71
	s_nop 0
	global_load_lds_dwordx4 v185, s[10:11]
	s_add_i32 s72, s2, 0x1a000
	s_mov_b32 m0, s72
	s_nop 0
	global_load_lds_dwordx4 v187, s[10:11]
	s_add_u32 s10, s76, 0x80
	s_addc_u32 s11, s77, 0
	s_add_i32 s90, s2, 0x8000
	s_mov_b32 m0, s90
	s_nop 0
	global_load_lds_dwordx4 v184, s[10:11]
	s_add_i32 s91, s2, 0xa000
	s_mov_b32 m0, s91
	s_nop 0
	global_load_lds_dwordx4 v186, s[10:11]
	s_add_u32 s10, s44, 0x40080
	s_addc_u32 s11, s45, 0
	s_lshl_b32 s9, s9, 3
	s_add_i32 s16, s9, 0
	s_add_i32 s92, s2, 0x1c000
	s_mov_b32 m0, s92
	s_nop 0
	global_load_lds_dwordx4 v185, s[10:11]
	s_add_i32 s94, s2, 0x1e000
	s_add_i32 s31, s2, 0xc000
	s_add_i32 s16, s16, 0x20000
	s_mov_b32 m0, s94
	s_nop 0
	global_load_lds_dwordx4 v187, s[10:11]
	s_cmpk_lt_u32 s0, 0x100
	s_waitcnt vmcnt(6)
	s_cselect_b64 s[50:51], -1, 0
	s_lshl_b32 s17, s1, 5
	s_cmp_lt_u32 s0, 64
	s_cselect_b64 s[62:63], -1, 0
	v_cmp_eq_f32_e64 s[40:41], 0, v190
	s_mov_b32 s55, s54
	s_mov_b32 s30, 0
	v_add_u32_e32 v191, 0, v0
	v_add_u32_e32 v192, 0, v2
	v_readlane_b32 s0, v253, 10
	s_barrier
	s_branch .LBB0_924

.LBB0_929:
	s_cmp_gt_u32 s66, 13
	s_cselect_b64 s[82:83], -1, 0
	s_and_b64 vcc, s[82:83], exec
	s_cselect_b32 s68, -14, 2
	s_add_i32 s82, s68, s66
	s_ashr_i32 s83, s82, 31
	s_lshl_b64 s[82:83], s[82:83], 7
	s_add_u32 s68, s76, s82
	s_addc_u32 s69, s77, s83
	s_add_u32 s84, s44, s82
	s_addc_u32 s85, s45, s83
	s_cmp_gt_u32 s66, 12
	s_cselect_b32 s82, -13, 3
	s_add_i32 s82, s82, s66
	s_ashr_i32 s83, s82, 31
	s_lshl_b64 s[82:83], s[82:83], 7
	s_add_u32 s37, s76, s82
	s_addc_u32 s13, s77, s83
	s_add_u32 s67, s44, s82
	s_addc_u32 s35, s45, s83
	s_cmp_eq_u32 s66, 14
	s_cselect_b32 s86, s27, s68
	s_mov_b32 s68, s66
	v_add_u32_e32 v140, 0x10000, v191
	v_add_u32_e32 v156, 0x14000, v191
	ds_read_b128 v[128:131], v140
	ds_read_b128 v[132:135], v140 offset:1024
	ds_read_b128 v[136:139], v140 offset:2048
	ds_read_b128 v[140:143], v140 offset:3072
	ds_read_b128 v[144:147], v156
	ds_read_b128 v[148:151], v156 offset:1024
	ds_read_b128 v[152:155], v156 offset:2048
	ds_read_b128 v[156:159], v156 offset:3072
	s_cselect_b32 s87, s1, s69
	s_cselect_b32 s89, s75, s85
	s_cselect_b32 s88, s9, s84
	s_cselect_b32 s83, s11, s13
	s_cselect_b32 s82, s10, s37
	s_cselect_b32 s85, s65, s35
	s_cselect_b32 s84, s12, s67
	ds_read_b128 v[160:163], v192
	ds_read_b128 v[164:167], v192 offset:1024
	ds_read_b128 v[168:171], v192 offset:2048
	ds_read_b128 v[172:175], v192 offset:3072
	ds_read_b128 v[176:179], v192 offset:4096
	ds_read_b128 v[180:183], v192 offset:5120
	ds_read_b128 v[194:197], v192 offset:6144
	ds_read_b128 v[198:201], v192 offset:7168
	s_add_u32 s68, s42, 0x40080
	s_addc_u32 s69, s43, 0
	s_mov_b32 m0, s31
	s_nop 0
	global_load_lds_dwordx4 v184, s[68:69]
	s_add_i32 s13, s2, 0xe000
	s_mov_b32 m0, s13
	s_nop 0
	global_load_lds_dwordx4 v186, s[68:69]
	s_setprio 1
	s_waitcnt vmcnt(8)
	s_waitcnt lgkmcnt(0)
	s_barrier
	v_mfma_i32_16x16x64_i8 v[124:127], v[128:131], v[160:163], v[124:127]
	v_mfma_i32_16x16x64_i8 v[120:123], v[136:139], v[160:163], v[120:123]
	v_mfma_i32_16x16x64_i8 v[116:119], v[128:131], v[168:171], v[116:119]
	v_mfma_i32_16x16x64_i8 v[112:115], v[136:139], v[168:171], v[112:115]
	v_mfma_i32_16x16x64_i8 v[108:111], v[128:131], v[176:179], v[108:111]
	v_mfma_i32_16x16x64_i8 v[104:107], v[136:139], v[176:179], v[104:107]
	v_mfma_i32_16x16x64_i8 v[100:103], v[128:131], v[194:197], v[100:103]
	v_mfma_i32_16x16x64_i8 v[96:99], v[136:139], v[194:197], v[96:99]
	v_mfma_i32_16x16x64_i8 v[124:127], v[132:135], v[164:167], v[124:127]
	v_mfma_i32_16x16x64_i8 v[120:123], v[140:143], v[164:167], v[120:123]
	v_mfma_i32_16x16x64_i8 v[116:119], v[132:135], v[172:175], v[116:119]
	v_mfma_i32_16x16x64_i8 v[112:115], v[140:143], v[172:175], v[112:115]
	v_mfma_i32_16x16x64_i8 v[108:111], v[132:135], v[180:183], v[108:111]
	v_mfma_i32_16x16x64_i8 v[104:107], v[140:143], v[180:183], v[104:107]
	v_mfma_i32_16x16x64_i8 v[100:103], v[132:135], v[198:201], v[100:103]
	v_mfma_i32_16x16x64_i8 v[96:99], v[140:143], v[198:201], v[96:99]
	v_mfma_i32_16x16x64_i8 v[92:95], v[144:147], v[160:163], v[92:95]
	v_mfma_i32_16x16x64_i8 v[88:91], v[152:155], v[160:163], v[88:91]
	v_mfma_i32_16x16x64_i8 v[84:87], v[144:147], v[168:171], v[84:87]
	v_mfma_i32_16x16x64_i8 v[80:83], v[152:155], v[168:171], v[80:83]
	v_mfma_i32_16x16x64_i8 v[76:79], v[144:147], v[176:179], v[76:79]
	v_mfma_i32_16x16x64_i8 v[72:75], v[152:155], v[176:179], v[72:75]
	v_mfma_i32_16x16x64_i8 v[68:71], v[144:147], v[194:197], v[68:71]
	v_mfma_i32_16x16x64_i8 v[64:67], v[152:155], v[194:197], v[64:67]
	v_mfma_i32_16x16x64_i8 v[92:95], v[148:151], v[164:167], v[92:95]
	v_mfma_i32_16x16x64_i8 v[88:91], v[156:159], v[164:167], v[88:91]
	v_mfma_i32_16x16x64_i8 v[84:87], v[148:151], v[172:175], v[84:87]
	v_mfma_i32_16x16x64_i8 v[80:83], v[156:159], v[172:175], v[80:83]
	v_mfma_i32_16x16x64_i8 v[76:79], v[148:151], v[180:183], v[76:79]
	v_mfma_i32_16x16x64_i8 v[72:75], v[156:159], v[180:183], v[72:75]
	v_mfma_i32_16x16x64_i8 v[68:71], v[148:151], v[198:201], v[68:71]
	v_mfma_i32_16x16x64_i8 v[64:67], v[156:159], v[198:201], v[64:67]
	s_barrier
	s_setprio 0
	ds_read_b128 v[160:163], v192 offset:16384
	ds_read_b128 v[164:167], v192 offset:17408
	ds_read_b128 v[168:171], v192 offset:18432
	ds_read_b128 v[172:175], v192 offset:19456
	ds_read_b128 v[176:179], v192 offset:20480
	ds_read_b128 v[180:183], v192 offset:21504
	ds_read_b128 v[194:197], v192 offset:22528
	ds_read_b128 v[198:201], v192 offset:23552
	s_mov_b32 m0, s3
	s_nop 0
	global_load_lds_dwordx4 v185, s[88:89]
	s_add_u32 s68, s88, 0x40000
	s_mov_b32 m0, s18
	s_nop 0
	global_load_lds_dwordx4 v187, s[88:89]
	s_addc_u32 s69, s89, 0
	s_mov_b32 m0, s19
	s_nop 0
	global_load_lds_dwordx4 v185, s[68:69]
	s_nop 0
	s_mov_b32 m0, s28
	s_nop 0
	global_load_lds_dwordx4 v187, s[68:69]
	s_nop 0
	s_mov_b32 m0, s2
	s_nop 0
	global_load_lds_dwordx4 v184, s[86:87]
	s_nop 0
	s_mov_b32 m0, s29
	s_nop 0
	global_load_lds_dwordx4 v186, s[86:87]
	s_setprio 1
	s_waitcnt vmcnt(8)
	s_waitcnt lgkmcnt(0)
	s_barrier
	v_mfma_i32_16x16x64_i8 v[60:63], v[128:131], v[160:163], v[60:63]
	v_mfma_i32_16x16x64_i8 v[56:59], v[136:139], v[160:163], v[56:59]
	v_mfma_i32_16x16x64_i8 v[52:55], v[128:131], v[168:171], v[52:55]
	v_mfma_i32_16x16x64_i8 v[48:51], v[136:139], v[168:171], v[48:51]
	v_mfma_i32_16x16x64_i8 v[44:47], v[128:131], v[176:179], v[44:47]
	v_mfma_i32_16x16x64_i8 v[40:43], v[136:139], v[176:179], v[40:43]
	v_mfma_i32_16x16x64_i8 v[36:39], v[128:131], v[194:197], v[36:39]
	v_mfma_i32_16x16x64_i8 v[32:35], v[136:139], v[194:197], v[32:35]
	v_mfma_i32_16x16x64_i8 v[60:63], v[132:135], v[164:167], v[60:63]
	v_mfma_i32_16x16x64_i8 v[56:59], v[140:143], v[164:167], v[56:59]
	v_mfma_i32_16x16x64_i8 v[52:55], v[132:135], v[172:175], v[52:55]
	v_mfma_i32_16x16x64_i8 v[48:51], v[140:143], v[172:175], v[48:51]
	v_mfma_i32_16x16x64_i8 v[44:47], v[132:135], v[180:183], v[44:47]
	v_mfma_i32_16x16x64_i8 v[40:43], v[140:143], v[180:183], v[40:43]
	v_mfma_i32_16x16x64_i8 v[36:39], v[132:135], v[198:201], v[36:39]
	v_mfma_i32_16x16x64_i8 v[32:35], v[140:143], v[198:201], v[32:35]
	v_mfma_i32_16x16x64_i8 v[28:31], v[144:147], v[160:163], v[28:31]
	v_mfma_i32_16x16x64_i8 v[24:27], v[152:155], v[160:163], v[24:27]
	v_mfma_i32_16x16x64_i8 v[20:23], v[144:147], v[168:171], v[20:23]
	v_mfma_i32_16x16x64_i8 v[16:19], v[152:155], v[168:171], v[16:19]
	v_mfma_i32_16x16x64_i8 v[12:15], v[144:147], v[176:179], v[12:15]
	v_mfma_i32_16x16x64_i8 v[8:11], v[152:155], v[176:179], v[8:11]
	v_mfma_i32_16x16x64_i8 v[4:7], v[144:147], v[194:197], v[4:7]
	v_mfma_i32_16x16x64_i8 v[0:3], v[152:155], v[194:197], v[0:3]
	v_mfma_i32_16x16x64_i8 v[28:31], v[148:151], v[164:167], v[28:31]
	v_mfma_i32_16x16x64_i8 v[24:27], v[156:159], v[164:167], v[24:27]
	v_mfma_i32_16x16x64_i8 v[20:23], v[148:151], v[172:175], v[20:23]
	v_mfma_i32_16x16x64_i8 v[16:19], v[156:159], v[172:175], v[16:19]
	v_mfma_i32_16x16x64_i8 v[12:15], v[148:151], v[180:183], v[12:15]
	v_mfma_i32_16x16x64_i8 v[8:11], v[156:159], v[180:183], v[8:11]
	v_mfma_i32_16x16x64_i8 v[4:7], v[148:151], v[198:201], v[4:7]
	v_mfma_i32_16x16x64_i8 v[0:3], v[156:159], v[198:201], v[0:3]
	s_barrier
	s_setprio 0
	v_add_u32_e32 v140, 0x18000, v191
	v_add_u32_e32 v156, 0x1c000, v191
	ds_read_b128 v[128:131], v140
	ds_read_b128 v[132:135], v140 offset:1024
	ds_read_b128 v[136:139], v140 offset:2048
	ds_read_b128 v[140:143], v140 offset:3072
	ds_read_b128 v[144:147], v156
	ds_read_b128 v[148:151], v156 offset:1024
	ds_read_b128 v[152:155], v156 offset:2048
	ds_read_b128 v[156:159], v156 offset:3072
	ds_read_b128 v[160:163], v192 offset:32768
	ds_read_b128 v[164:167], v192 offset:33792
	ds_read_b128 v[168:171], v192 offset:34816
	ds_read_b128 v[172:175], v192 offset:35840
	ds_read_b128 v[176:179], v192 offset:36864
	ds_read_b128 v[180:183], v192 offset:37888
	ds_read_b128 v[194:197], v192 offset:38912
	ds_read_b128 v[198:201], v192 offset:39936
	s_add_u32 s68, s86, 0x40000
	s_addc_u32 s69, s87, 0
	s_mov_b32 m0, s34
	s_nop 0
	global_load_lds_dwordx4 v184, s[68:69]
	s_nop 0
	s_mov_b32 m0, s36
	s_nop 0
	global_load_lds_dwordx4 v186, s[68:69]
	s_setprio 1
	s_waitcnt vmcnt(8)
	s_waitcnt lgkmcnt(0)
	s_barrier
	v_mfma_i32_16x16x64_i8 v[124:127], v[128:131], v[160:163], v[124:127]
	v_mfma_i32_16x16x64_i8 v[120:123], v[136:139], v[160:163], v[120:123]
	v_mfma_i32_16x16x64_i8 v[116:119], v[128:131], v[168:171], v[116:119]
	v_mfma_i32_16x16x64_i8 v[112:115], v[136:139], v[168:171], v[112:115]
	v_mfma_i32_16x16x64_i8 v[108:111], v[128:131], v[176:179], v[108:111]
	v_mfma_i32_16x16x64_i8 v[104:107], v[136:139], v[176:179], v[104:107]
	v_mfma_i32_16x16x64_i8 v[100:103], v[128:131], v[194:197], v[100:103]
	v_mfma_i32_16x16x64_i8 v[96:99], v[136:139], v[194:197], v[96:99]
	v_mfma_i32_16x16x64_i8 v[124:127], v[132:135], v[164:167], v[124:127]
	v_mfma_i32_16x16x64_i8 v[120:123], v[140:143], v[164:167], v[120:123]
	v_mfma_i32_16x16x64_i8 v[116:119], v[132:135], v[172:175], v[116:119]
	v_mfma_i32_16x16x64_i8 v[112:115], v[140:143], v[172:175], v[112:115]
	v_mfma_i32_16x16x64_i8 v[108:111], v[132:135], v[180:183], v[108:111]
	v_mfma_i32_16x16x64_i8 v[104:107], v[140:143], v[180:183], v[104:107]
	v_mfma_i32_16x16x64_i8 v[100:103], v[132:135], v[198:201], v[100:103]
	v_mfma_i32_16x16x64_i8 v[96:99], v[140:143], v[198:201], v[96:99]
	v_mfma_i32_16x16x64_i8 v[92:95], v[144:147], v[160:163], v[92:95]
	v_mfma_i32_16x16x64_i8 v[88:91], v[152:155], v[160:163], v[88:91]
	v_mfma_i32_16x16x64_i8 v[84:87], v[144:147], v[168:171], v[84:87]
	v_mfma_i32_16x16x64_i8 v[80:83], v[152:155], v[168:171], v[80:83]
	v_mfma_i32_16x16x64_i8 v[76:79], v[144:147], v[176:179], v[76:79]
	v_mfma_i32_16x16x64_i8 v[72:75], v[152:155], v[176:179], v[72:75]
	v_mfma_i32_16x16x64_i8 v[68:71], v[144:147], v[194:197], v[68:71]
	v_mfma_i32_16x16x64_i8 v[64:67], v[152:155], v[194:197], v[64:67]
	v_mfma_i32_16x16x64_i8 v[92:95], v[148:151], v[164:167], v[92:95]
	v_mfma_i32_16x16x64_i8 v[88:91], v[156:159], v[164:167], v[88:91]
	v_mfma_i32_16x16x64_i8 v[84:87], v[148:151], v[172:175], v[84:87]
	v_mfma_i32_16x16x64_i8 v[80:83], v[156:159], v[172:175], v[80:83]
	v_mfma_i32_16x16x64_i8 v[76:79], v[148:151], v[180:183], v[76:79]
	v_mfma_i32_16x16x64_i8 v[72:75], v[156:159], v[180:183], v[72:75]
	v_mfma_i32_16x16x64_i8 v[68:71], v[148:151], v[198:201], v[68:71]
	v_mfma_i32_16x16x64_i8 v[64:67], v[156:159], v[198:201], v[64:67]
	s_barrier
	s_setprio 0
	ds_read_b128 v[160:163], v192 offset:49152
	ds_read_b128 v[164:167], v192 offset:50176
	ds_read_b128 v[168:171], v192 offset:51200
	ds_read_b128 v[172:175], v192 offset:52224
	ds_read_b128 v[176:179], v192 offset:53248
	ds_read_b128 v[180:183], v192 offset:54272
	ds_read_b128 v[194:197], v192 offset:55296
	ds_read_b128 v[198:201], v192 offset:56320
	s_mov_b32 m0, s71
	s_nop 0
	global_load_lds_dwordx4 v185, s[84:85]
	s_add_u32 s68, s84, 0x40000
	s_mov_b32 m0, s72
	s_nop 0
	global_load_lds_dwordx4 v187, s[84:85]
	s_addc_u32 s69, s85, 0
	s_mov_b32 m0, s92
	s_nop 0
	global_load_lds_dwordx4 v185, s[68:69]
	s_nop 0
	s_mov_b32 m0, s94
	s_nop 0
	global_load_lds_dwordx4 v187, s[68:69]
	s_nop 0
	s_mov_b32 m0, s90
	s_nop 0
	global_load_lds_dwordx4 v184, s[82:83]
	s_nop 0
	s_mov_b32 m0, s91
	s_nop 0
	global_load_lds_dwordx4 v186, s[82:83]
	s_setprio 1
	s_waitcnt vmcnt(8)
	s_waitcnt lgkmcnt(0)
	s_barrier
	v_mfma_i32_16x16x64_i8 v[60:63], v[128:131], v[160:163], v[60:63]
	v_mfma_i32_16x16x64_i8 v[56:59], v[136:139], v[160:163], v[56:59]
	v_mfma_i32_16x16x64_i8 v[52:55], v[128:131], v[168:171], v[52:55]
	v_mfma_i32_16x16x64_i8 v[48:51], v[136:139], v[168:171], v[48:51]
	v_mfma_i32_16x16x64_i8 v[44:47], v[128:131], v[176:179], v[44:47]
	v_mfma_i32_16x16x64_i8 v[40:43], v[136:139], v[176:179], v[40:43]
	v_mfma_i32_16x16x64_i8 v[36:39], v[128:131], v[194:197], v[36:39]
	v_mfma_i32_16x16x64_i8 v[32:35], v[136:139], v[194:197], v[32:35]
	v_mfma_i32_16x16x64_i8 v[60:63], v[132:135], v[164:167], v[60:63]
	v_mfma_i32_16x16x64_i8 v[56:59], v[140:143], v[164:167], v[56:59]
	v_mfma_i32_16x16x64_i8 v[52:55], v[132:135], v[172:175], v[52:55]
	v_mfma_i32_16x16x64_i8 v[48:51], v[140:143], v[172:175], v[48:51]
	v_mfma_i32_16x16x64_i8 v[44:47], v[132:135], v[180:183], v[44:47]
	v_mfma_i32_16x16x64_i8 v[40:43], v[140:143], v[180:183], v[40:43]
	v_mfma_i32_16x16x64_i8 v[36:39], v[132:135], v[198:201], v[36:39]
	v_mfma_i32_16x16x64_i8 v[32:35], v[140:143], v[198:201], v[32:35]
	v_mfma_i32_16x16x64_i8 v[28:31], v[144:147], v[160:163], v[28:31]
	v_mfma_i32_16x16x64_i8 v[24:27], v[152:155], v[160:163], v[24:27]
	v_mfma_i32_16x16x64_i8 v[20:23], v[144:147], v[168:171], v[20:23]
	v_mfma_i32_16x16x64_i8 v[16:19], v[152:155], v[168:171], v[16:19]
	v_mfma_i32_16x16x64_i8 v[12:15], v[144:147], v[176:179], v[12:15]
	v_mfma_i32_16x16x64_i8 v[8:11], v[152:155], v[176:179], v[8:11]
	v_mfma_i32_16x16x64_i8 v[4:7], v[144:147], v[194:197], v[4:7]
	v_mfma_i32_16x16x64_i8 v[0:3], v[152:155], v[194:197], v[0:3]
	v_mfma_i32_16x16x64_i8 v[28:31], v[148:151], v[164:167], v[28:31]
	v_mfma_i32_16x16x64_i8 v[24:27], v[156:159], v[164:167], v[24:27]
	v_mfma_i32_16x16x64_i8 v[20:23], v[148:151], v[172:175], v[20:23]
	v_mfma_i32_16x16x64_i8 v[16:19], v[156:159], v[172:175], v[16:19]
	v_mfma_i32_16x16x64_i8 v[12:15], v[148:151], v[180:183], v[12:15]
	v_mfma_i32_16x16x64_i8 v[8:11], v[156:159], v[180:183], v[8:11]
	v_mfma_i32_16x16x64_i8 v[4:7], v[148:151], v[198:201], v[4:7]
	v_mfma_i32_16x16x64_i8 v[0:3], v[156:159], v[198:201], v[0:3]
	s_barrier
	s_setprio 0
	s_add_i32 s66, s66, 2
	s_add_u32 s42, s42, 0x100
	s_addc_u32 s43, s43, 0
	s_cbranch_vccz .LBB0_929
	s_and_b64 vcc, exec, s[50:51]
	s_cbranch_vccz .LBB0_932
	s_barrier

.LBB0_970:
	s_or_b64 exec, exec, s[44:45]
	v_lshlrev_b32_e32 v147, 2, v195
	s_waitcnt lgkmcnt(0)
	s_barrier
	v_lshl_add_u32 v144, v194, 3, 0
	v_add_u32_e32 v4, 16, v147
	global_load_dwordx4 v[8:11], v147, s[58:59]
	global_load_dwordx4 v[12:15], v147, s[60:61]
	global_load_dwordx4 v[0:3], v4, s[58:59]
	s_nop 0
	global_load_dwordx4 v[4:7], v4, s[60:61]
	v_add_u32_e32 v146, 0x22000, v144
	ds_read_b64 v[144:145], v146
	s_and_b64 vcc, exec, s[40:41]
	s_waitcnt lgkmcnt(0)
	v_sub_f32_e32 v85, v85, v144
	v_sub_f32_e32 v84, v84, v144
	v_sub_f32_e32 v81, v81, v144
	v_sub_f32_e32 v80, v80, v144
	v_sub_f32_e32 v87, v87, v144
	v_sub_f32_e32 v86, v86, v144
	v_sub_f32_e32 v83, v83, v144
	v_sub_f32_e32 v82, v82, v144
	v_pk_mul_f32 v[80:81], v[144:145], v[80:81] op_sel:[1,0]
	v_pk_mul_f32 v[84:85], v[144:145], v[84:85] op_sel:[1,0]
	v_pk_mul_f32 v[82:83], v[144:145], v[82:83] op_sel:[1,0]
	v_pk_mul_f32 v[86:87], v[144:145], v[86:87] op_sel:[1,0]
	s_waitcnt vmcnt(2)
	v_pk_fma_f32 v[84:85], v[10:11], v[84:85], v[14:15]
	v_pk_fma_f32 v[144:145], v[8:9], v[80:81], v[12:13]
	s_waitcnt vmcnt(0)
	v_pk_fma_f32 v[80:81], v[2:3], v[86:87], v[6:7]
	v_pk_fma_f32 v[82:83], v[0:1], v[82:83], v[4:5]
	v_cvt_pk_bf16_f32 v148, v144, v145
	v_cvt_pk_bf16_f32 v149, v84, v85
	s_nop 0
	v_cvt_pk_bf16_f32 v150, v82, v83
	v_cvt_pk_bf16_f32 v151, v80, v81
	global_store_dwordx4 v193, v[148:151], s[52:53]
	s_cbranch_vccz .LBB0_1021
	v_cvt_pk_fp8_f32 v86, v144, v145
	v_cvt_pk_fp8_f32 v87, v82, v83
	v_cvt_pk_fp8_f32 v86, v84, v85 op_sel:[0,0,1]
	v_cvt_pk_fp8_f32 v87, v80, v81 op_sel:[0,0,1]
	s_cbranch_execnz .LBB0_973

.LBB0_973:
	ds_read_b64 v[82:83], v146 offset:128
	v_lshrrev_b32_e32 v80, 1, v193
	global_store_dwordx2 v80, v[86:87], s[56:57]
	v_add_u32_e32 v144, 0x10000, v193
	s_andn2_b64 vcc, exec, s[40:41]
	s_waitcnt lgkmcnt(0)
	v_sub_f32_e32 v80, v89, v82
	v_sub_f32_e32 v85, v92, v82
	v_sub_f32_e32 v84, v88, v82
	v_sub_f32_e32 v89, v94, v82
	v_sub_f32_e32 v88, v90, v82
	v_sub_f32_e32 v81, v93, v82
	v_pk_mul_f32 v[84:85], v[82:83], v[84:85] op_sel:[1,0]
	v_sub_f32_e32 v87, v95, v82
	v_sub_f32_e32 v86, v91, v82
	v_pk_mul_f32 v[88:89], v[82:83], v[88:89] op_sel:[1,0]
	v_pk_mul_f32 v[80:81], v[82:83], v[80:81] op_sel:[1,0]
	v_pk_fma_f32 v[84:85], v[8:9], v[84:85], v[12:13]
	v_pk_mul_f32 v[82:83], v[82:83], v[86:87] op_sel:[1,0]
	v_pk_fma_f32 v[86:87], v[0:1], v[88:89], v[4:5]
	v_cvt_pk_bf16_f32 v88, v84, v85
	v_pk_fma_f32 v[80:81], v[10:11], v[80:81], v[14:15]
	v_pk_fma_f32 v[82:83], v[2:3], v[82:83], v[6:7]
	v_cvt_pk_bf16_f32 v89, v80, v81
	v_cvt_pk_bf16_f32 v90, v86, v87
	s_nop 0
	v_cvt_pk_bf16_f32 v91, v82, v83
	global_store_dwordx4 v144, v[88:91], s[52:53]
	s_nop 1
	v_cndmask_b32_e64 v88, 0, 1, s[40:41]
	v_cmp_ne_u32_e64 s[42:43], 1, v88
	s_cbranch_vccnz .LBB0_1022
	v_cvt_pk_fp8_f32 v88, v84, v85
	v_cvt_pk_fp8_f32 v89, v86, v87
	v_cvt_pk_fp8_f32 v88, v80, v81 op_sel:[0,0,1]
	v_cvt_pk_fp8_f32 v89, v82, v83 op_sel:[0,0,1]
	s_cbranch_execnz .LBB0_976

.LBB0_976:
	ds_read_b64 v[82:83], v146 offset:256
	v_lshrrev_b32_e32 v80, 1, v144
	global_store_dwordx2 v80, v[88:89], s[56:57]
	v_add_u32_e32 v90, 0x20000, v193
	s_and_b64 vcc, exec, s[42:43]
	s_waitcnt lgkmcnt(0)
	v_sub_f32_e32 v81, v101, v82
	v_sub_f32_e32 v80, v97, v82
	v_sub_f32_e32 v85, v100, v82
	v_sub_f32_e32 v84, v96, v82
	v_sub_f32_e32 v87, v103, v82
	v_sub_f32_e32 v86, v99, v82
	v_sub_f32_e32 v89, v102, v82
	v_sub_f32_e32 v88, v98, v82
	v_pk_mul_f32 v[84:85], v[82:83], v[84:85] op_sel:[1,0]
	v_pk_mul_f32 v[80:81], v[82:83], v[80:81] op_sel:[1,0]
	v_pk_mul_f32 v[88:89], v[82:83], v[88:89] op_sel:[1,0]
	v_pk_mul_f32 v[82:83], v[82:83], v[86:87] op_sel:[1,0]
	v_pk_fma_f32 v[80:81], v[10:11], v[80:81], v[14:15]
	v_pk_fma_f32 v[84:85], v[8:9], v[84:85], v[12:13]
	v_pk_fma_f32 v[82:83], v[2:3], v[82:83], v[6:7]
	v_pk_fma_f32 v[86:87], v[0:1], v[88:89], v[4:5]
	v_cvt_pk_bf16_f32 v92, v84, v85
	v_cvt_pk_bf16_f32 v93, v80, v81
	s_nop 0
	v_cvt_pk_bf16_f32 v94, v86, v87
	v_cvt_pk_bf16_f32 v95, v82, v83
	global_store_dwordx4 v90, v[92:95], s[52:53]
	s_cbranch_vccnz .LBB0_1023
	v_cvt_pk_fp8_f32 v88, v84, v85
	v_cvt_pk_fp8_f32 v89, v86, v87
	v_cvt_pk_fp8_f32 v88, v80, v81 op_sel:[0,0,1]
	v_cvt_pk_fp8_f32 v89, v82, v83 op_sel:[0,0,1]
	s_cbranch_execnz .LBB0_979

.LBB0_979:
	ds_read_b64 v[82:83], v146 offset:384
	v_lshrrev_b32_e32 v80, 1, v90
	global_store_dwordx2 v80, v[88:89], s[56:57]
	v_add_u32_e32 v90, 0x30000, v193
	s_and_b64 vcc, exec, s[42:43]
	s_waitcnt lgkmcnt(0)
	v_sub_f32_e32 v81, v109, v82
	v_sub_f32_e32 v80, v105, v82
	v_sub_f32_e32 v85, v108, v82
	v_sub_f32_e32 v84, v104, v82
	v_sub_f32_e32 v87, v111, v82
	v_sub_f32_e32 v86, v107, v82
	v_sub_f32_e32 v89, v110, v82
	v_sub_f32_e32 v88, v106, v82
	v_pk_mul_f32 v[84:85], v[82:83], v[84:85] op_sel:[1,0]
	v_pk_mul_f32 v[80:81], v[82:83], v[80:81] op_sel:[1,0]
	v_pk_mul_f32 v[88:89], v[82:83], v[88:89] op_sel:[1,0]
	v_pk_mul_f32 v[82:83], v[82:83], v[86:87] op_sel:[1,0]
	v_pk_fma_f32 v[80:81], v[10:11], v[80:81], v[14:15]
	v_pk_fma_f32 v[84:85], v[8:9], v[84:85], v[12:13]
	v_pk_fma_f32 v[82:83], v[2:3], v[82:83], v[6:7]
	v_pk_fma_f32 v[86:87], v[0:1], v[88:89], v[4:5]
	v_cvt_pk_bf16_f32 v92, v84, v85
	v_cvt_pk_bf16_f32 v93, v80, v81
	s_nop 0
	v_cvt_pk_bf16_f32 v94, v86, v87
	v_cvt_pk_bf16_f32 v95, v82, v83
	global_store_dwordx4 v90, v[92:95], s[52:53]
	s_cbranch_vccnz .LBB0_1024
	v_cvt_pk_fp8_f32 v88, v84, v85
	v_cvt_pk_fp8_f32 v89, v86, v87
	v_cvt_pk_fp8_f32 v88, v80, v81 op_sel:[0,0,1]
	v_cvt_pk_fp8_f32 v89, v82, v83 op_sel:[0,0,1]
	s_cbranch_execnz .LBB0_982

.LBB0_982:
	ds_read_b64 v[82:83], v146 offset:1024
	v_lshrrev_b32_e32 v80, 1, v90
	global_store_dwordx2 v80, v[88:89], s[56:57]
	v_add_u32_e32 v90, 0x80000, v193
	s_and_b64 vcc, exec, s[42:43]
	s_waitcnt lgkmcnt(0)
	v_sub_f32_e32 v81, v117, v82
	v_sub_f32_e32 v80, v113, v82
	v_sub_f32_e32 v85, v116, v82
	v_sub_f32_e32 v84, v112, v82
	v_sub_f32_e32 v87, v119, v82
	v_sub_f32_e32 v86, v115, v82
	v_sub_f32_e32 v89, v118, v82
	v_sub_f32_e32 v88, v114, v82
	v_pk_mul_f32 v[84:85], v[82:83], v[84:85] op_sel:[1,0]
	v_pk_mul_f32 v[80:81], v[82:83], v[80:81] op_sel:[1,0]
	v_pk_mul_f32 v[88:89], v[82:83], v[88:89] op_sel:[1,0]
	v_pk_mul_f32 v[82:83], v[82:83], v[86:87] op_sel:[1,0]
	v_pk_fma_f32 v[80:81], v[10:11], v[80:81], v[14:15]
	v_pk_fma_f32 v[84:85], v[8:9], v[84:85], v[12:13]
	v_pk_fma_f32 v[82:83], v[2:3], v[82:83], v[6:7]
	v_pk_fma_f32 v[86:87], v[0:1], v[88:89], v[4:5]
	v_cvt_pk_bf16_f32 v92, v84, v85
	v_cvt_pk_bf16_f32 v93, v80, v81
	s_nop 0
	v_cvt_pk_bf16_f32 v94, v86, v87
	v_cvt_pk_bf16_f32 v95, v82, v83
	global_store_dwordx4 v90, v[92:95], s[52:53]
	s_cbranch_vccnz .LBB0_1025
	v_cvt_pk_fp8_f32 v88, v84, v85
	v_cvt_pk_fp8_f32 v89, v86, v87
	v_cvt_pk_fp8_f32 v88, v80, v81 op_sel:[0,0,1]
	v_cvt_pk_fp8_f32 v89, v82, v83 op_sel:[0,0,1]
	s_cbranch_execnz .LBB0_985

.LBB0_985:
	ds_read_b64 v[82:83], v146 offset:1152
	v_lshrrev_b32_e32 v80, 1, v90
	global_store_dwordx2 v80, v[88:89], s[56:57]
	v_add_u32_e32 v90, 0x90000, v193
	s_and_b64 vcc, exec, s[42:43]
	s_waitcnt lgkmcnt(0)
	v_sub_f32_e32 v81, v125, v82
	v_sub_f32_e32 v80, v121, v82
	v_sub_f32_e32 v85, v124, v82
	v_sub_f32_e32 v84, v120, v82
	v_sub_f32_e32 v87, v127, v82
	v_sub_f32_e32 v86, v123, v82
	v_sub_f32_e32 v89, v126, v82
	v_sub_f32_e32 v88, v122, v82
	v_pk_mul_f32 v[84:85], v[82:83], v[84:85] op_sel:[1,0]
	v_pk_mul_f32 v[80:81], v[82:83], v[80:81] op_sel:[1,0]
	v_pk_mul_f32 v[88:89], v[82:83], v[88:89] op_sel:[1,0]
	v_pk_mul_f32 v[82:83], v[82:83], v[86:87] op_sel:[1,0]
	v_pk_fma_f32 v[80:81], v[10:11], v[80:81], v[14:15]
	v_pk_fma_f32 v[84:85], v[8:9], v[84:85], v[12:13]
	v_pk_fma_f32 v[82:83], v[2:3], v[82:83], v[6:7]
	v_pk_fma_f32 v[86:87], v[0:1], v[88:89], v[4:5]
	v_cvt_pk_bf16_f32 v92, v84, v85
	v_cvt_pk_bf16_f32 v93, v80, v81
	s_nop 0
	v_cvt_pk_bf16_f32 v94, v86, v87
	v_cvt_pk_bf16_f32 v95, v82, v83
	global_store_dwordx4 v90, v[92:95], s[52:53]
	s_cbranch_vccnz .LBB0_1026
	v_cvt_pk_fp8_f32 v88, v84, v85
	v_cvt_pk_fp8_f32 v89, v86, v87
	v_cvt_pk_fp8_f32 v88, v80, v81 op_sel:[0,0,1]
	v_cvt_pk_fp8_f32 v89, v82, v83 op_sel:[0,0,1]
	s_cbranch_execnz .LBB0_988

.LBB0_988:
	ds_read_b64 v[82:83], v146 offset:1280
	v_lshrrev_b32_e32 v80, 1, v90
	global_store_dwordx2 v80, v[88:89], s[56:57]
	v_add_u32_e32 v90, 0xa0000, v193
	s_and_b64 vcc, exec, s[42:43]
	s_waitcnt lgkmcnt(0)
	v_sub_f32_e32 v81, v133, v82
	v_sub_f32_e32 v80, v129, v82
	v_sub_f32_e32 v85, v132, v82
	v_sub_f32_e32 v84, v128, v82
	v_sub_f32_e32 v87, v135, v82
	v_sub_f32_e32 v86, v131, v82
	v_sub_f32_e32 v89, v134, v82
	v_sub_f32_e32 v88, v130, v82
	v_pk_mul_f32 v[84:85], v[82:83], v[84:85] op_sel:[1,0]
	v_pk_mul_f32 v[80:81], v[82:83], v[80:81] op_sel:[1,0]
	v_pk_mul_f32 v[88:89], v[82:83], v[88:89] op_sel:[1,0]
	v_pk_mul_f32 v[82:83], v[82:83], v[86:87] op_sel:[1,0]
	v_pk_fma_f32 v[80:81], v[10:11], v[80:81], v[14:15]
	v_pk_fma_f32 v[84:85], v[8:9], v[84:85], v[12:13]
	v_pk_fma_f32 v[82:83], v[2:3], v[82:83], v[6:7]
	v_pk_fma_f32 v[86:87], v[0:1], v[88:89], v[4:5]
	v_cvt_pk_bf16_f32 v92, v84, v85
	v_cvt_pk_bf16_f32 v93, v80, v81
	s_nop 0
	v_cvt_pk_bf16_f32 v94, v86, v87
	v_cvt_pk_bf16_f32 v95, v82, v83
	global_store_dwordx4 v90, v[92:95], s[52:53]
	s_cbranch_vccnz .LBB0_1027
	v_cvt_pk_fp8_f32 v88, v84, v85
	v_cvt_pk_fp8_f32 v89, v86, v87
	v_cvt_pk_fp8_f32 v88, v80, v81 op_sel:[0,0,1]
	v_cvt_pk_fp8_f32 v89, v82, v83 op_sel:[0,0,1]
	s_cbranch_execnz .LBB0_991

.LBB0_991:
	ds_read_b64 v[82:83], v146 offset:1408
	v_lshrrev_b32_e32 v80, 1, v90
	global_store_dwordx2 v80, v[88:89], s[56:57]
	v_add_u32_e32 v80, 0xb0000, v193
	s_and_b64 vcc, exec, s[42:43]
	s_waitcnt lgkmcnt(0)
	v_sub_f32_e32 v85, v141, v82
	v_sub_f32_e32 v84, v137, v82
	v_sub_f32_e32 v87, v140, v82
	v_sub_f32_e32 v86, v136, v82
	v_pk_mul_f32 v[86:87], v[82:83], v[86:87] op_sel:[1,0]
	v_pk_mul_f32 v[84:85], v[82:83], v[84:85] op_sel:[1,0]
	v_pk_fma_f32 v[8:9], v[8:9], v[86:87], v[12:13]
	v_pk_fma_f32 v[10:11], v[10:11], v[84:85], v[14:15]
	v_sub_f32_e32 v13, v143, v82
	v_sub_f32_e32 v12, v139, v82
	v_sub_f32_e32 v15, v142, v82
	v_sub_f32_e32 v14, v138, v82
	v_pk_mul_f32 v[14:15], v[82:83], v[14:15] op_sel:[1,0]
	v_pk_mul_f32 v[12:13], v[82:83], v[12:13] op_sel:[1,0]
	v_pk_fma_f32 v[0:1], v[0:1], v[14:15], v[4:5]
	v_pk_fma_f32 v[2:3], v[2:3], v[12:13], v[6:7]
	v_cvt_pk_bf16_f32 v4, v8, v9
	v_cvt_pk_bf16_f32 v5, v10, v11
	v_cvt_pk_bf16_f32 v6, v0, v1
	s_nop 0
	v_cvt_pk_bf16_f32 v7, v2, v3
	global_store_dwordx4 v80, v[4:7], s[52:53]
	s_cbranch_vccnz .LBB0_1028
	s_nop 0
	v_cvt_pk_fp8_f32 v4, v8, v9
	v_cvt_pk_fp8_f32 v5, v0, v1
	v_cvt_pk_fp8_f32 v4, v10, v11 op_sel:[0,0,1]
	v_cvt_pk_fp8_f32 v5, v2, v3 op_sel:[0,0,1]
	s_cbranch_execnz .LBB0_994

.LBB0_994:
	v_lshrrev_b32_e32 v0, 1, v80
	global_store_dwordx2 v0, v[4:5], s[56:57]
	v_add_u32_e32 v0, 0x200, v147
	v_add_u32_e32 v4, 0x210, v147
	global_load_dwordx4 v[8:11], v0, s[58:59]
	global_load_dwordx4 v[12:15], v0, s[60:61]
	s_nop 0
	global_load_dwordx4 v[0:3], v4, s[58:59]
	s_nop 0
	global_load_dwordx4 v[4:7], v4, s[60:61]
	ds_read_b64 v[80:81], v146
	v_add_u32_e32 v82, 0x100, v193
	s_and_b64 vcc, exec, s[42:43]
	s_waitcnt lgkmcnt(0)
	v_sub_f32_e32 v63, v63, v80
	v_sub_f32_e32 v62, v62, v80
	v_sub_f32_e32 v61, v61, v80
	v_sub_f32_e32 v60, v60, v80
	v_sub_f32_e32 v59, v59, v80
	v_sub_f32_e32 v58, v58, v80
	v_sub_f32_e32 v57, v57, v80
	v_sub_f32_e32 v56, v56, v80
	v_pk_mul_f32 v[84:85], v[80:81], v[60:61] op_sel:[1,0]
	v_pk_mul_f32 v[60:61], v[80:81], v[62:63] op_sel:[1,0]
	v_pk_mul_f32 v[86:87], v[80:81], v[56:57] op_sel:[1,0]
	v_pk_mul_f32 v[56:57], v[80:81], v[58:59] op_sel:[1,0]
	s_waitcnt vmcnt(2)
	v_pk_fma_f32 v[60:61], v[10:11], v[60:61], v[14:15]
	v_pk_fma_f32 v[62:63], v[8:9], v[84:85], v[12:13]
	s_waitcnt vmcnt(0)
	v_pk_fma_f32 v[56:57], v[2:3], v[56:57], v[6:7]
	v_pk_fma_f32 v[58:59], v[0:1], v[86:87], v[4:5]
	v_cvt_pk_bf16_f32 v84, v62, v63
	v_cvt_pk_bf16_f32 v85, v60, v61
	s_nop 0
	v_cvt_pk_bf16_f32 v86, v58, v59
	v_cvt_pk_bf16_f32 v87, v56, v57
	global_store_dwordx4 v82, v[84:87], s[52:53]
	s_cbranch_vccnz .LBB0_1029
	v_cvt_pk_fp8_f32 v80, v62, v63
	v_cvt_pk_fp8_f32 v81, v58, v59
	v_cvt_pk_fp8_f32 v80, v60, v61 op_sel:[0,0,1]
	v_cvt_pk_fp8_f32 v81, v56, v57 op_sel:[0,0,1]
	s_cbranch_execnz .LBB0_997

.LBB0_997:
	v_lshrrev_b32_e32 v56, 1, v82
	global_store_dwordx2 v56, v[80:81], s[56:57]
	ds_read_b64 v[56:57], v146 offset:128
	v_add_u32_e32 v58, 0x10100, v193
	s_and_b64 vcc, exec, s[42:43]
	s_waitcnt lgkmcnt(0)
	v_sub_f32_e32 v49, v49, v56
	v_sub_f32_e32 v48, v48, v56
	v_sub_f32_e32 v53, v53, v56
	v_sub_f32_e32 v52, v52, v56
	v_pk_mul_f32 v[60:61], v[56:57], v[48:49] op_sel:[1,0]
	v_sub_f32_e32 v55, v55, v56
	v_sub_f32_e32 v54, v54, v56
	v_sub_f32_e32 v51, v51, v56
	v_sub_f32_e32 v50, v50, v56
	v_pk_mul_f32 v[48:49], v[56:57], v[52:53] op_sel:[1,0]
	v_pk_fma_f32 v[52:53], v[8:9], v[60:61], v[12:13]
	v_pk_mul_f32 v[60:61], v[56:57], v[50:51] op_sel:[1,0]
	v_pk_mul_f32 v[50:51], v[56:57], v[54:55] op_sel:[1,0]
	v_pk_fma_f32 v[48:49], v[10:11], v[48:49], v[14:15]
	v_pk_fma_f32 v[50:51], v[2:3], v[50:51], v[6:7]
	v_pk_fma_f32 v[54:55], v[0:1], v[60:61], v[4:5]
	v_cvt_pk_bf16_f32 v60, v52, v53
	v_cvt_pk_bf16_f32 v61, v48, v49
	s_nop 0
	v_cvt_pk_bf16_f32 v62, v54, v55
	v_cvt_pk_bf16_f32 v63, v50, v51
	global_store_dwordx4 v58, v[60:63], s[52:53]
	s_cbranch_vccnz .LBB0_1030
	v_cvt_pk_fp8_f32 v56, v52, v53
	v_cvt_pk_fp8_f32 v57, v54, v55
	v_cvt_pk_fp8_f32 v56, v48, v49 op_sel:[0,0,1]
	v_cvt_pk_fp8_f32 v57, v50, v51 op_sel:[0,0,1]
	s_cbranch_execnz .LBB0_1000

.LBB0_1000:
	v_lshrrev_b32_e32 v48, 1, v58
	global_store_dwordx2 v48, v[56:57], s[56:57]
	ds_read_b64 v[48:49], v146 offset:256
	v_add_u32_e32 v50, 0x20100, v193
	s_and_b64 vcc, exec, s[42:43]
	s_waitcnt lgkmcnt(0)
	v_sub_f32_e32 v45, v45, v48
	v_sub_f32_e32 v44, v44, v48
	v_sub_f32_e32 v47, v47, v48
	v_sub_f32_e32 v46, v46, v48
	v_pk_mul_f32 v[52:53], v[48:49], v[44:45] op_sel:[1,0]
	v_sub_f32_e32 v43, v43, v48
	v_sub_f32_e32 v42, v42, v48
	v_sub_f32_e32 v41, v41, v48
	v_sub_f32_e32 v40, v40, v48
	v_pk_mul_f32 v[44:45], v[48:49], v[46:47] op_sel:[1,0]
	v_pk_fma_f32 v[46:47], v[8:9], v[52:53], v[12:13]
	v_pk_mul_f32 v[52:53], v[48:49], v[40:41] op_sel:[1,0]
	v_pk_mul_f32 v[40:41], v[48:49], v[42:43] op_sel:[1,0]
	v_pk_fma_f32 v[44:45], v[10:11], v[44:45], v[14:15]
	v_pk_fma_f32 v[40:41], v[2:3], v[40:41], v[6:7]
	v_pk_fma_f32 v[42:43], v[0:1], v[52:53], v[4:5]
	v_cvt_pk_bf16_f32 v52, v46, v47
	v_cvt_pk_bf16_f32 v53, v44, v45
	s_nop 0
	v_cvt_pk_bf16_f32 v54, v42, v43
	v_cvt_pk_bf16_f32 v55, v40, v41
	global_store_dwordx4 v50, v[52:55], s[52:53]
	s_cbranch_vccnz .LBB0_1031
	v_cvt_pk_fp8_f32 v48, v46, v47
	v_cvt_pk_fp8_f32 v49, v42, v43
	v_cvt_pk_fp8_f32 v48, v44, v45 op_sel:[0,0,1]
	v_cvt_pk_fp8_f32 v49, v40, v41 op_sel:[0,0,1]
	s_cbranch_execnz .LBB0_1003

.LBB0_1003:
	v_lshrrev_b32_e32 v40, 1, v50
	global_store_dwordx2 v40, v[48:49], s[56:57]
	ds_read_b64 v[40:41], v146 offset:384
	v_add_u32_e32 v42, 0x30100, v193
	s_and_b64 vcc, exec, s[42:43]
	s_waitcnt lgkmcnt(0)
	v_sub_f32_e32 v37, v37, v40
	v_sub_f32_e32 v36, v36, v40
	v_sub_f32_e32 v39, v39, v40
	v_sub_f32_e32 v38, v38, v40
	v_pk_mul_f32 v[44:45], v[40:41], v[36:37] op_sel:[1,0]
	v_sub_f32_e32 v35, v35, v40
	v_sub_f32_e32 v34, v34, v40
	v_sub_f32_e32 v33, v33, v40
	v_sub_f32_e32 v32, v32, v40
	v_pk_mul_f32 v[36:37], v[40:41], v[38:39] op_sel:[1,0]
	v_pk_fma_f32 v[38:39], v[8:9], v[44:45], v[12:13]
	v_pk_mul_f32 v[44:45], v[40:41], v[32:33] op_sel:[1,0]
	v_pk_mul_f32 v[32:33], v[40:41], v[34:35] op_sel:[1,0]
	v_pk_fma_f32 v[36:37], v[10:11], v[36:37], v[14:15]
	v_pk_fma_f32 v[32:33], v[2:3], v[32:33], v[6:7]
	v_pk_fma_f32 v[34:35], v[0:1], v[44:45], v[4:5]
	v_cvt_pk_bf16_f32 v44, v38, v39
	v_cvt_pk_bf16_f32 v45, v36, v37
	s_nop 0
	v_cvt_pk_bf16_f32 v46, v34, v35
	v_cvt_pk_bf16_f32 v47, v32, v33
	global_store_dwordx4 v42, v[44:47], s[52:53]
	s_cbranch_vccnz .LBB0_1032
	v_cvt_pk_fp8_f32 v40, v38, v39
	v_cvt_pk_fp8_f32 v41, v34, v35
	v_cvt_pk_fp8_f32 v40, v36, v37 op_sel:[0,0,1]
	v_cvt_pk_fp8_f32 v41, v32, v33 op_sel:[0,0,1]
	s_cbranch_execnz .LBB0_1006

.LBB0_1006:
	v_lshrrev_b32_e32 v32, 1, v42
	global_store_dwordx2 v32, v[40:41], s[56:57]
	ds_read_b64 v[32:33], v146 offset:1024
	v_add_u32_e32 v34, 0x80100, v193
	s_and_b64 vcc, exec, s[42:43]
	s_waitcnt lgkmcnt(0)
	v_sub_f32_e32 v29, v29, v32
	v_sub_f32_e32 v28, v28, v32
	v_sub_f32_e32 v31, v31, v32
	v_sub_f32_e32 v30, v30, v32
	v_pk_mul_f32 v[36:37], v[32:33], v[28:29] op_sel:[1,0]
	v_sub_f32_e32 v27, v27, v32
	v_sub_f32_e32 v26, v26, v32
	v_sub_f32_e32 v25, v25, v32
	v_sub_f32_e32 v24, v24, v32
	v_pk_mul_f32 v[28:29], v[32:33], v[30:31] op_sel:[1,0]
	v_pk_fma_f32 v[30:31], v[8:9], v[36:37], v[12:13]
	v_pk_mul_f32 v[36:37], v[32:33], v[24:25] op_sel:[1,0]
	v_pk_mul_f32 v[24:25], v[32:33], v[26:27] op_sel:[1,0]
	v_pk_fma_f32 v[28:29], v[10:11], v[28:29], v[14:15]
	v_pk_fma_f32 v[24:25], v[2:3], v[24:25], v[6:7]
	v_pk_fma_f32 v[26:27], v[0:1], v[36:37], v[4:5]
	v_cvt_pk_bf16_f32 v36, v30, v31
	v_cvt_pk_bf16_f32 v37, v28, v29
	s_nop 0
	v_cvt_pk_bf16_f32 v38, v26, v27
	v_cvt_pk_bf16_f32 v39, v24, v25
	global_store_dwordx4 v34, v[36:39], s[52:53]
	s_cbranch_vccnz .LBB0_1033
	v_cvt_pk_fp8_f32 v32, v30, v31
	v_cvt_pk_fp8_f32 v33, v26, v27
	v_cvt_pk_fp8_f32 v32, v28, v29 op_sel:[0,0,1]
	v_cvt_pk_fp8_f32 v33, v24, v25 op_sel:[0,0,1]
	s_cbranch_execnz .LBB0_1009

.LBB0_1009:
	ds_read_b64 v[26:27], v146 offset:1152
	v_lshrrev_b32_e32 v24, 1, v34
	global_store_dwordx2 v24, v[32:33], s[56:57]
	v_add_u32_e32 v30, 0x90100, v193
	s_and_b64 vcc, exec, s[42:43]
	s_waitcnt lgkmcnt(0)
	v_sub_f32_e32 v21, v21, v26
	v_sub_f32_e32 v20, v20, v26
	v_sub_f32_e32 v25, v65, v26
	v_sub_f32_e32 v24, v64, v26
	v_pk_mul_f32 v[28:29], v[26:27], v[20:21] op_sel:[1,0]
	v_pk_mul_f32 v[20:21], v[26:27], v[24:25] op_sel:[1,0]
	v_pk_fma_f32 v[24:25], v[8:9], v[28:29], v[12:13]
	v_sub_f32_e32 v29, v67, v26
	v_sub_f32_e32 v28, v66, v26
	v_sub_f32_e32 v17, v17, v26
	v_sub_f32_e32 v16, v16, v26
	v_pk_mul_f32 v[32:33], v[26:27], v[16:17] op_sel:[1,0]
	v_pk_mul_f32 v[16:17], v[26:27], v[28:29] op_sel:[1,0]
	v_pk_fma_f32 v[20:21], v[10:11], v[20:21], v[14:15]
	v_pk_fma_f32 v[16:17], v[2:3], v[16:17], v[6:7]
	v_pk_fma_f32 v[26:27], v[0:1], v[32:33], v[4:5]
	v_cvt_pk_bf16_f32 v32, v24, v25
	v_cvt_pk_bf16_f32 v33, v20, v21
	s_nop 0
	v_cvt_pk_bf16_f32 v34, v26, v27
	v_cvt_pk_bf16_f32 v35, v16, v17
	global_store_dwordx4 v30, v[32:35], s[52:53]
	s_cbranch_vccnz .LBB0_1034
	v_cvt_pk_fp8_f32 v28, v24, v25
	v_cvt_pk_fp8_f32 v29, v26, v27
	v_cvt_pk_fp8_f32 v28, v20, v21 op_sel:[0,0,1]
	v_cvt_pk_fp8_f32 v29, v16, v17 op_sel:[0,0,1]
	s_cbranch_execnz .LBB0_1012

.LBB0_1012:
	ds_read_b64 v[24:25], v146 offset:1280
	v_lshrrev_b32_e32 v16, 1, v30
	global_store_dwordx2 v16, v[28:29], s[56:57]
	v_add_u32_e32 v26, 0xa0100, v193
	s_and_b64 vcc, exec, s[42:43]
	s_waitcnt lgkmcnt(0)
	v_sub_f32_e32 v19, v19, v24
	v_sub_f32_e32 v18, v18, v24
	v_pk_mul_f32 v[18:19], v[24:25], v[18:19] op_sel:[1,0]
	v_sub_f32_e32 v17, v73, v24
	v_sub_f32_e32 v16, v72, v24
	v_pk_fma_f32 v[20:21], v[8:9], v[18:19], v[12:13]
	v_sub_f32_e32 v19, v75, v24
	v_sub_f32_e32 v18, v74, v24
	v_sub_f32_e32 v23, v23, v24
	v_sub_f32_e32 v22, v22, v24
	v_pk_mul_f32 v[16:17], v[24:25], v[16:17] op_sel:[1,0]
	v_pk_mul_f32 v[22:23], v[24:25], v[22:23] op_sel:[1,0]
	v_pk_mul_f32 v[18:19], v[24:25], v[18:19] op_sel:[1,0]
	v_pk_fma_f32 v[16:17], v[10:11], v[16:17], v[14:15]
	v_pk_fma_f32 v[18:19], v[2:3], v[18:19], v[6:7]
	v_pk_fma_f32 v[22:23], v[0:1], v[22:23], v[4:5]
	v_cvt_pk_bf16_f32 v28, v20, v21
	v_cvt_pk_bf16_f32 v29, v16, v17
	s_nop 0
	v_cvt_pk_bf16_f32 v30, v22, v23
	v_cvt_pk_bf16_f32 v31, v18, v19
	global_store_dwordx4 v26, v[28:31], s[52:53]
	s_cbranch_vccnz .LBB0_1035
	v_cvt_pk_fp8_f32 v24, v20, v21
	v_cvt_pk_fp8_f32 v25, v22, v23
	v_cvt_pk_fp8_f32 v24, v16, v17 op_sel:[0,0,1]
	v_cvt_pk_fp8_f32 v25, v18, v19 op_sel:[0,0,1]
	s_cbranch_execnz .LBB0_1015

.LBB0_1015:
	ds_read_b64 v[18:19], v146 offset:1408
	v_lshrrev_b32_e32 v16, 1, v26
	global_store_dwordx2 v16, v[24:25], s[56:57]
	v_add_u32_e32 v16, 0xb0100, v193
	s_and_b64 vcc, exec, s[42:43]
	s_waitcnt lgkmcnt(0)
	v_sub_f32_e32 v21, v77, v18
	v_sub_f32_e32 v20, v76, v18
	v_sub_f32_e32 v23, v69, v18
	v_sub_f32_e32 v22, v68, v18
	v_pk_mul_f32 v[22:23], v[18:19], v[22:23] op_sel:[1,0]
	v_pk_mul_f32 v[20:21], v[18:19], v[20:21] op_sel:[1,0]
	v_pk_fma_f32 v[8:9], v[8:9], v[22:23], v[12:13]
	v_pk_fma_f32 v[10:11], v[10:11], v[20:21], v[14:15]
	v_sub_f32_e32 v13, v79, v18
	v_sub_f32_e32 v12, v78, v18
	v_sub_f32_e32 v15, v71, v18
	v_sub_f32_e32 v14, v70, v18
	v_pk_mul_f32 v[14:15], v[18:19], v[14:15] op_sel:[1,0]
	v_pk_mul_f32 v[12:13], v[18:19], v[12:13] op_sel:[1,0]
	v_pk_fma_f32 v[0:1], v[0:1], v[14:15], v[4:5]
	v_pk_fma_f32 v[2:3], v[2:3], v[12:13], v[6:7]
	v_cvt_pk_bf16_f32 v4, v8, v9
	v_cvt_pk_bf16_f32 v5, v10, v11
	v_cvt_pk_bf16_f32 v6, v0, v1
	s_nop 0
	v_cvt_pk_bf16_f32 v7, v2, v3
	global_store_dwordx4 v16, v[4:7], s[52:53]
	s_cbranch_vccnz .LBB0_1036
	s_nop 0
	v_cvt_pk_fp8_f32 v4, v8, v9
	v_cvt_pk_fp8_f32 v5, v0, v1
	v_cvt_pk_fp8_f32 v4, v10, v11 op_sel:[0,0,1]
	v_cvt_pk_fp8_f32 v5, v2, v3 op_sel:[0,0,1]
	s_cbranch_execnz .LBB0_1018

.LBB0_1296:
	v_readlane_b32 s0, v253, 2
	v_readlane_b32 s1, v253, 3
	s_load_dwordx2 s[0:1], s[0:1], 0xf8
	v_readlane_b32 s20, v253, 6
	v_readlane_b32 s22, v253, 8
	v_readlane_b32 s23, v253, 9
	s_mov_b64 s[10:11], s[22:23]
	s_waitcnt lgkmcnt(0)
	global_load_dword v0, v189, s[0:1] offset:512 sc1
	v_readlane_b32 s0, v255, 47
	s_add_i32 s2, s0, 10
	s_cmp_lt_i32 s2, s11
	v_mov_b32_e32 v1, 0x108
	s_cselect_b64 s[0:1], -1, 0
	s_cmp_gt_i32 s10, s3
	v_readlane_b32 s21, v253, 7
	s_waitcnt vmcnt(0)
	v_readfirstlane_b32 s3, v0
	v_med3_i32 v0, v0, 0, v1
	s_nop 0
	v_readfirstlane_b32 s27, v0
	s_cbranch_scc1 .LBB0_1372
	s_cmp_gt_i32 s3, 0
	s_cselect_b64 s[10:11], -1, 0
	s_and_b64 s[10:11], s[16:17], s[10:11]
	s_andn2_b64 vcc, exec, s[10:11]
	s_cbranch_vccnz .LBB0_1316
	v_readlane_b32 s10, v253, 2
	v_readlane_b32 s11, v253, 3
	s_load_dwordx2 s[16:17], s[10:11], 0xf8
	v_mov_b32_e32 v0, 0x1000
	s_mul_i32 s13, s27, 56
	v_readlane_b32 s10, v255, 14
	s_waitcnt lgkmcnt(0)
	global_load_dword v1, v0, s[16:17] offset:24 sc1
	global_load_dword v2, v0, s[16:17] offset:28 sc1
	global_load_dwordx2 v[4:5], v0, s[16:17] offset:80 sc1
	v_mbcnt_lo_u32_b32 v0, -1, 0
	v_mbcnt_hi_u32_b32 v0, -1, v0
	s_cmp_ge_i32 s10, s13
	v_or_b32_e32 v0, s33, v0
	v_readlane_b32 s11, v255, 15
	v_readfirstlane_b32 s9, v0
	s_waitcnt vmcnt(0)
	v_readfirstlane_b32 s40, v4
	v_readfirstlane_b32 s41, v5
	s_cbranch_scc1 .LBB0_1316
	v_bfe_i32 v5, v0, 27, 1
	v_lshlrev_b32_e32 v3, 4, v0
	v_lshrrev_b32_e32 v5, 22, v5
	v_add_u32_e32 v5, v3, v5
	v_and_b32_e32 v5, 0xfffffc00, v5
	v_sub_u32_e32 v5, v3, v5
	v_ashrrev_i32_e32 v4, 31, v0
	v_lshrrev_b32_e32 v6, 4, v5
	v_lshrrev_b32_e32 v4, 26, v4
	v_bitop3_b32 v6, v6, v5, 32 bitop3:0x6c
	v_ashrrev_i32_e32 v5, 31, v5
	v_add_u32_e32 v4, v0, v4
	v_lshrrev_b32_e32 v5, 26, v5
	v_ashrrev_i32_e32 v4, 6, v4
	v_add_u32_e32 v5, v6, v5
	v_lshlrev_b32_e32 v7, 3, v4
	v_ashrrev_i32_e32 v5, 6, v5
	v_and_b32_e32 v7, -16, v7
	v_mul_i32_i24_e32 v8, 64, v5
	v_add_u32_e32 v7, v5, v7
	v_sub_u32_e32 v6, v6, v8
	v_lshlrev_b32_e32 v4, 5, v4
	v_ashrrev_i16_sdwa v6, v242, sext(v6) dst_sel:DWORD dst_unused:UNUSED_PAD src0_sel:DWORD src1_sel:BYTE_0
	v_lshlrev_b32_e32 v8, 1, v7
	v_lshrrev_b32_e32 v9, 2, v7
	v_and_b32_e32 v5, 3, v5
	s_mov_b32 s11, 0x1fffe0
	v_and_b32_e32 v4, 32, v4
	v_bfe_i32 v6, v6, 0, 16
	v_and_b32_e32 v8, 24, v8
	v_and_b32_e32 v9, 4, v9
	v_and_or_b32 v5, v7, s11, v5
	v_or3_b32 v5, v5, v9, v8
	v_add_lshl_u32 v4, v4, v6, 1
	v_add_u32_e32 v3, 0x2000, v3
	v_lshl_add_u32 v132, v7, 11, v4
	v_lshl_add_u32 v133, v5, 11, v4
	v_ashrrev_i32_e32 v4, 31, v3
	v_lshrrev_b32_e32 v4, 22, v4
	v_add_u32_e32 v4, v3, v4
	v_ashrrev_i32_e32 v4, 10, v4
	v_mul_i32_i24_e32 v5, 0x400, v4
	v_sub_u32_e32 v3, v3, v5
	v_lshrrev_b32_e32 v5, 4, v3
	v_bitop3_b32 v3, v5, v3, 32 bitop3:0x6c
	v_ashrrev_i32_e32 v6, 31, v3
	v_lshrrev_b32_e32 v6, 26, v6
	s_add_u32 s18, s16, 0x45900000
	v_lshlrev_b32_e32 v5, 3, v4
	v_add_u32_e32 v6, v3, v6
	v_writelane_b32 v255, s28, 48
	s_addc_u32 s19, s17, 0
	v_and_b32_e32 v5, -16, v5
	v_ashrrev_i32_e32 v7, 6, v6
	v_writelane_b32 v255, s29, 49
	s_add_u32 s28, s16, 0xb900000
	v_add_u32_e32 v5, v7, v5
	v_and_b32_e32 v7, 3, v7
	s_addc_u32 s29, s17, 0
	v_and_or_b32 v7, v5, s11, v7
	s_ashr_i32 s11, s9, 6
	s_lshr_b32 s30, s13, 3
	v_readlane_b32 s20, v254, 54
	s_ashr_i32 s10, s9, 8
	s_lshl_b32 s12, s11, 10
	s_add_i32 s31, s30, 1
	v_readlane_b32 s21, v254, 55
	s_and_b64 s[20:21], s[20:21], exec
	s_cselect_b32 s20, s31, s30
	v_readlane_b32 s21, v255, 0
	s_mul_i32 s20, s20, s21
	v_readlane_b32 s21, v255, 3
	s_add_i32 s20, s20, s21
	s_mul_hi_i32 s21, s20, 0x92492493
	s_add_i32 s21, s21, s20
	s_lshr_b32 s22, s21, 31
	s_ashr_i32 s21, s21, 8
	s_add_i32 s21, s21, s22
	v_and_b32_e32 v6, 0xc0, v6
	s_lshl_b32 s22, s21, 3
	v_sub_u32_e32 v3, v3, v6
	s_sub_i32 s23, s27, s22
	v_lshlrev_b32_e32 v4, 5, v4
	v_ashrrev_i16_sdwa v3, v242, sext(v3) dst_sel:DWORD dst_unused:UNUSED_PAD src0_sel:DWORD src1_sel:BYTE_0
	s_min_i32 s23, s23, 8
	s_mulk_i32 s21, 0x1c0
	v_and_b32_e32 v4, 32, v4
	v_bfe_i32 v3, v3, 0, 16
	s_sub_i32 s34, s20, s21
	s_sext_i32_i16 s20, s23
	v_add_lshl_u32 v3, v4, v3, 1
	v_cvt_f32_i32_e32 v4, s20
	v_lshlrev_b32_e32 v6, 1, v5
	v_lshrrev_b32_e32 v8, 2, v5
	v_and_b32_e32 v6, 24, v6
	v_and_b32_e32 v8, 4, v8
	v_or3_b32 v6, v7, v8, v6
	v_lshl_add_u32 v134, v5, 11, v3
	v_lshl_add_u32 v135, v6, 11, v3
	v_cvt_f32_i32_e32 v3, s34
	v_rcp_iflag_f32_e32 v5, v4
	s_xor_b32 s21, s34, s20
	s_ashr_i32 s21, s21, 30
	s_or_b32 s35, s21, 1
	v_mul_f32_e32 v5, v3, v5
	v_trunc_f32_e32 v5, v5
	v_fma_f32 v3, -v5, v4, v3
	v_cvt_i32_f32_e32 v5, v5
	v_cmp_ge_f32_e64 s[20:21], |v3|, |v4|
	s_and_b64 s[20:21], s[20:21], exec
	s_cselect_b32 s20, s35, 0
	v_readfirstlane_b32 s21, v5
	s_add_i32 s20, s21, s20
	s_sext_i32_i16 s85, s20
	s_mul_i32 s20, s20, s23
	s_sub_i32 s20, s34, s20
	s_sext_i32_i16 s20, s20
	s_add_i32 s52, s22, s20
	s_ashr_i32 s53, s52, 31
	s_lshl_b64 s[20:21], s[52:53], 2
	s_add_u32 s20, s16, s20
	s_addc_u32 s21, s17, s21
	global_load_dword v3, v189, s[20:21] offset:768
	s_lshl_b64 s[22:23], s[52:53], 19
	s_waitcnt vmcnt(0)
	v_readfirstlane_b32 s20, v3
	s_mul_i32 s20, s20, 56
	s_add_i32 s20, s20, s85
	s_ashr_i32 s21, s20, 31
	s_lshl_b64 s[20:21], s[20:21], 19
	s_add_u32 s54, s28, s20
	s_addc_u32 s55, s29, s21
	s_add_i32 s34, s12, 0
	s_add_i32 s35, s34, 0x10000
	s_mov_b32 m0, s35
	s_nop 0
	global_load_lds_dwordx4 v133, s[54:55]
	s_add_i32 s36, s34, 0x12000
	s_mov_b32 m0, s36
	s_nop 0
	global_load_lds_dwordx4 v135, s[54:55]
	s_add_u32 s20, s54, 0x40000
	s_addc_u32 s21, s55, 0
	s_add_i32 s37, s34, 0x14000
	s_mov_b32 m0, s37
	s_nop 0
	global_load_lds_dwordx4 v133, s[20:21]
	s_add_i32 s65, s34, 0x16000
	s_mov_b32 m0, s65
	s_nop 0
	global_load_lds_dwordx4 v135, s[20:21]
	s_add_u32 s56, s18, s22
	s_addc_u32 s57, s19, s23
	s_mov_b32 m0, s34
	s_nop 0
	global_load_lds_dwordx4 v132, s[56:57]
	s_add_i32 s66, s34, 0x2000
	s_mov_b32 m0, s66
	s_nop 0
	global_load_lds_dwordx4 v134, s[56:57]
	s_add_u32 s20, s56, 0x40000
	s_addc_u32 s21, s57, 0
	s_add_i32 s67, s34, 0x4000
	s_mov_b32 m0, s67
	s_nop 0
	global_load_lds_dwordx4 v132, s[20:21]
	s_add_i32 s68, s34, 0x6000
	s_mov_b32 m0, s68
	s_nop 0
	global_load_lds_dwordx4 v134, s[20:21]
	s_cmp_eq_u32 s10, 1
	s_cselect_b64 s[20:21], -1, 0
	s_cmp_lg_u32 s10, 1
	s_cbranch_scc1 .LBB0_1301
	s_barrier
.LBB0_1301:
	s_add_u32 s22, s16, 0x56100000
	s_flbit_i32_b32 s12, s41
	s_addc_u32 s23, s17, 0
	s_min_u32 s12, s12, 32
	s_lshl_b64 s[40:41], s[40:41], s12
	s_min_u32 s40, s40, 1
	v_fmac_f32_e32 v2, 0x40880000, v1
	s_or_b32 s40, s41, s40
	v_max_f32_e32 v1, 0xda24260, v2
	v_cvt_f32_u32_e32 v2, s40
	s_sub_i32 s12, 32, s12
	v_mul_f32_e32 v1, 0x3c010204, v1
	s_lshl_b32 s69, s10, 6
	v_ldexp_f32 v2, v2, s12
	v_mul_f32_e32 v2, 0x2f800000, v2
	s_mov_b32 s12, 0x4ae00000
	v_div_scale_f32 v3, s[40:41], s12, s12, v2
	v_rcp_f32_e32 v4, v3
	s_lshl_b32 s10, s10, 13
	s_waitcnt vmcnt(2)
	s_barrier
	v_fma_f32 v5, -v3, v4, 1.0
	v_fmac_f32_e32 v4, v5, v4
	v_div_scale_f32 v5, vcc, v2, s12, v2
	v_mul_f32_e32 v6, v5, v4
	v_fma_f32 v7, -v3, v6, v5
	v_fmac_f32_e32 v6, v7, v4
	v_fma_f32 v3, -v3, v6, v5
	v_div_fmas_f32 v3, v3, v4, v6
	v_div_fixup_f32 v2, v3, s12, v2
	s_mov_b32 s12, 0xf800000
	v_cmp_gt_f32_e32 vcc, s12, v2
	v_mul_f32_e32 v3, 0x4f800000, v2
	s_movk_i32 s12, 0x3c0
	v_cndmask_b32_e32 v2, v2, v3, vcc
	v_sqrt_f32_e32 v3, v2
	s_mov_b32 s83, 0
	v_add_u32_e32 v4, -1, v3
	v_fma_f32 v5, -v4, v3, v2
	v_cmp_ge_f32_e64 s[40:41], 0, v5
	v_add_u32_e32 v5, 1, v3
	s_nop 0
	v_cndmask_b32_e64 v4, v3, v4, s[40:41]
	v_fma_f32 v3, -v5, v3, v2
	v_cmp_lt_f32_e64 s[40:41], 0, v3
	s_nop 1
	v_cndmask_b32_e64 v3, v4, v5, s[40:41]
	v_mul_f32_e32 v4, 0x37800000, v3
	v_cndmask_b32_e32 v3, v3, v4, vcc
	v_cmp_class_f32_e32 vcc, v2, v250
	s_nop 1
	v_cndmask_b32_e32 v2, v3, v2, vcc
	v_mul_f32_e32 v2, 0x40880000, v2
	v_max_f32_e32 v2, 0xda24260, v2
	v_mul_f32_e32 v2, 0x3c010204, v2
	v_mul_f32_e32 v1, v1, v2
	v_and_b32_e32 v2, 48, v0
	v_lshlrev_b32_e32 v3, 6, v0
	v_lshlrev_b32_e32 v0, 2, v0
	v_and_or_b32 v2, v3, s12, v2
	v_and_b32_e32 v0, 32, v0
	v_bitop3_b32 v3, v2, s10, v0 bitop3:0xde
	s_lshl_b32 s10, s11, 5
	s_and_b32 s70, s10, 0x60
	s_lshl_b32 s10, s70, 7
	v_bitop3_b32 v0, s10, v2, v0 bitop3:0xf6
	s_add_u32 s10, s54, 0x80
	s_addc_u32 s11, s55, 0
	s_add_i32 s71, s34, 0x18000
	s_mov_b32 m0, s71
	s_nop 0
	global_load_lds_dwordx4 v133, s[10:11]
	s_add_i32 s72, s34, 0x1a000
	s_mov_b32 m0, s72
	s_nop 0
	global_load_lds_dwordx4 v135, s[10:11]
	s_add_u32 s10, s56, 0x80
	s_addc_u32 s11, s57, 0
	s_add_i32 s78, s34, 0x8000
	s_mov_b32 m0, s78
	s_nop 0
	global_load_lds_dwordx4 v132, s[10:11]
	s_add_i32 s79, s34, 0xa000
	s_mov_b32 m0, s79
	s_nop 0
	global_load_lds_dwordx4 v134, s[10:11]
	s_add_u32 s10, s54, 0x40080
	s_addc_u32 s11, s55, 0
	s_add_i32 s80, s34, 0x1c000
	s_mov_b32 m0, s80
	s_nop 0
	global_load_lds_dwordx4 v133, s[10:11]
	s_add_i32 s81, s34, 0x1e000
	s_mov_b32 m0, s81
	s_nop 0
	global_load_lds_dwordx4 v135, s[10:11]
	s_waitcnt vmcnt(6)
	s_add_i32 s82, s34, 0xc000
	s_cmpk_lt_u32 s9, 0x100
	v_mul_f32_e32 v128, 0xbfb8aa3b, v1
	v_mul_f32_e32 v130, v1, v1
	s_cselect_b64 s[40:41], -1, 0
	v_mov_b32_e32 v129, v128
	v_mov_b32_e32 v131, v130
	v_add_u32_e32 v136, 0, v0
	v_add_u32_e32 v137, 0, v3
	s_barrier
	s_branch .LBB0_1304

.LBB0_1309:
	s_cmp_gt_u32 s87, 13
	s_cselect_b64 s[60:61], -1, 0
	s_and_b64 vcc, s[60:61], exec
	s_cselect_b32 s60, -14, 2
	s_add_i32 s60, s60, s87
	s_ashr_i32 s61, s60, 31
	s_lshl_b64 s[60:61], s[60:61], 7
	s_add_u32 s62, s56, s60
	s_addc_u32 s63, s57, s61
	s_add_u32 s76, s54, s60
	s_addc_u32 s77, s55, s61
	s_cmp_gt_u32 s87, 12
	s_cselect_b32 s60, -13, 3
	s_add_i32 s60, s60, s87
	s_ashr_i32 s61, s60, 31
	s_lshl_b64 s[60:61], s[60:61], 7
	s_add_u32 s88, s56, s60
	s_addc_u32 s89, s57, s61
	s_add_u32 s90, s54, s60
	s_mov_b32 s60, s87
	v_add_u32_e32 v150, 0x10000, v136
	v_add_u32_e32 v166, 0x14000, v136
	ds_read_b128 v[138:141], v150
	ds_read_b128 v[142:145], v150 offset:1024
	ds_read_b128 v[146:149], v150 offset:2048
	ds_read_b128 v[150:153], v150 offset:3072
	ds_read_b128 v[154:157], v166
	ds_read_b128 v[158:161], v166 offset:1024
	ds_read_b128 v[162:165], v166 offset:2048
	ds_read_b128 v[166:169], v166 offset:3072
	s_addc_u32 s91, s55, s61
	s_cmp_eq_u32 s87, 14
	s_cselect_b32 s75, s43, s63
	s_cselect_b32 s74, s53, s62
	s_cselect_b32 s77, s47, s77
	s_cselect_b32 s76, s9, s76
	s_cselect_b32 s61, s11, s89
	s_cselect_b32 s60, s10, s88
	s_cselect_b32 s63, s86, s91
	s_cselect_b32 s62, s12, s90
	ds_read_b128 v[170:173], v137
	ds_read_b128 v[174:177], v137 offset:1024
	ds_read_b128 v[178:181], v137 offset:2048
	ds_read_b128 v[182:185], v137 offset:3072
	ds_read_b128 v[190:193], v137 offset:4096
	ds_read_b128 v[194:197], v137 offset:5120
	ds_read_b128 v[198:201], v137 offset:6144
	ds_read_b128 v[202:205], v137 offset:7168
	s_add_u32 s88, s58, 0x40080
	s_addc_u32 s89, s59, 0
	s_mov_b32 m0, s82
	s_nop 0
	global_load_lds_dwordx4 v132, s[88:89]
	s_add_i32 s90, s34, 0xe000
	s_mov_b32 m0, s90
	s_nop 0
	global_load_lds_dwordx4 v134, s[88:89]
	s_setprio 1
	s_waitcnt vmcnt(8)
	s_waitcnt lgkmcnt(0)
	s_barrier
	v_mfma_i32_16x16x64_i8 v[124:127], v[138:141], v[170:173], v[124:127]
	v_mfma_i32_16x16x64_i8 v[120:123], v[146:149], v[170:173], v[120:123]
	v_mfma_i32_16x16x64_i8 v[116:119], v[138:141], v[178:181], v[116:119]
	v_mfma_i32_16x16x64_i8 v[112:115], v[146:149], v[178:181], v[112:115]
	v_mfma_i32_16x16x64_i8 v[108:111], v[138:141], v[190:193], v[108:111]
	v_mfma_i32_16x16x64_i8 v[104:107], v[146:149], v[190:193], v[104:107]
	v_mfma_i32_16x16x64_i8 v[100:103], v[138:141], v[198:201], v[100:103]
	v_mfma_i32_16x16x64_i8 v[96:99], v[146:149], v[198:201], v[96:99]
	v_mfma_i32_16x16x64_i8 v[124:127], v[142:145], v[174:177], v[124:127]
	v_mfma_i32_16x16x64_i8 v[120:123], v[150:153], v[174:177], v[120:123]
	v_mfma_i32_16x16x64_i8 v[116:119], v[142:145], v[182:185], v[116:119]
	v_mfma_i32_16x16x64_i8 v[112:115], v[150:153], v[182:185], v[112:115]
	v_mfma_i32_16x16x64_i8 v[108:111], v[142:145], v[194:197], v[108:111]
	v_mfma_i32_16x16x64_i8 v[104:107], v[150:153], v[194:197], v[104:107]
	v_mfma_i32_16x16x64_i8 v[100:103], v[142:145], v[202:205], v[100:103]
	v_mfma_i32_16x16x64_i8 v[96:99], v[150:153], v[202:205], v[96:99]
	v_mfma_i32_16x16x64_i8 v[92:95], v[154:157], v[170:173], v[92:95]
	v_mfma_i32_16x16x64_i8 v[88:91], v[162:165], v[170:173], v[88:91]
	v_mfma_i32_16x16x64_i8 v[84:87], v[154:157], v[178:181], v[84:87]
	v_mfma_i32_16x16x64_i8 v[80:83], v[162:165], v[178:181], v[80:83]
	v_mfma_i32_16x16x64_i8 v[76:79], v[154:157], v[190:193], v[76:79]
	v_mfma_i32_16x16x64_i8 v[72:75], v[162:165], v[190:193], v[72:75]
	v_mfma_i32_16x16x64_i8 v[68:71], v[154:157], v[198:201], v[68:71]
	v_mfma_i32_16x16x64_i8 v[64:67], v[162:165], v[198:201], v[64:67]
	v_mfma_i32_16x16x64_i8 v[92:95], v[158:161], v[174:177], v[92:95]
	v_mfma_i32_16x16x64_i8 v[88:91], v[166:169], v[174:177], v[88:91]
	v_mfma_i32_16x16x64_i8 v[84:87], v[158:161], v[182:185], v[84:87]
	v_mfma_i32_16x16x64_i8 v[80:83], v[166:169], v[182:185], v[80:83]
	v_mfma_i32_16x16x64_i8 v[76:79], v[158:161], v[194:197], v[76:79]
	v_mfma_i32_16x16x64_i8 v[72:75], v[166:169], v[194:197], v[72:75]
	v_mfma_i32_16x16x64_i8 v[68:71], v[158:161], v[202:205], v[68:71]
	v_mfma_i32_16x16x64_i8 v[64:67], v[166:169], v[202:205], v[64:67]
	s_barrier
	s_setprio 0
	ds_read_b128 v[170:173], v137 offset:16384
	ds_read_b128 v[174:177], v137 offset:17408
	ds_read_b128 v[178:181], v137 offset:18432
	ds_read_b128 v[182:185], v137 offset:19456
	ds_read_b128 v[190:193], v137 offset:20480
	ds_read_b128 v[194:197], v137 offset:21504
	ds_read_b128 v[198:201], v137 offset:22528
	ds_read_b128 v[202:205], v137 offset:23552
	s_mov_b32 m0, s35
	s_nop 0
	global_load_lds_dwordx4 v133, s[76:77]
	s_nop 0
	s_mov_b32 m0, s36
	s_nop 0
	global_load_lds_dwordx4 v135, s[76:77]
	s_add_u32 s76, s76, 0x40000
	s_addc_u32 s77, s77, 0
	s_mov_b32 m0, s37
	s_nop 0
	global_load_lds_dwordx4 v133, s[76:77]
	s_nop 0
	s_mov_b32 m0, s65
	s_nop 0
	global_load_lds_dwordx4 v135, s[76:77]
	s_mov_b32 m0, s34
	s_nop 0
	global_load_lds_dwordx4 v132, s[74:75]
	s_nop 0
	s_mov_b32 m0, s66
	s_nop 0
	global_load_lds_dwordx4 v134, s[74:75]
	s_setprio 1
	s_waitcnt vmcnt(8)
	s_waitcnt lgkmcnt(0)
	s_barrier
	v_mfma_i32_16x16x64_i8 v[60:63], v[138:141], v[170:173], v[60:63]
	v_mfma_i32_16x16x64_i8 v[56:59], v[146:149], v[170:173], v[56:59]
	v_mfma_i32_16x16x64_i8 v[52:55], v[138:141], v[178:181], v[52:55]
	v_mfma_i32_16x16x64_i8 v[48:51], v[146:149], v[178:181], v[48:51]
	v_mfma_i32_16x16x64_i8 v[44:47], v[138:141], v[190:193], v[44:47]
	v_mfma_i32_16x16x64_i8 v[40:43], v[146:149], v[190:193], v[40:43]
	v_mfma_i32_16x16x64_i8 v[36:39], v[138:141], v[198:201], v[36:39]
	v_mfma_i32_16x16x64_i8 v[32:35], v[146:149], v[198:201], v[32:35]
	v_mfma_i32_16x16x64_i8 v[60:63], v[142:145], v[174:177], v[60:63]
	v_mfma_i32_16x16x64_i8 v[56:59], v[150:153], v[174:177], v[56:59]
	v_mfma_i32_16x16x64_i8 v[52:55], v[142:145], v[182:185], v[52:55]
	v_mfma_i32_16x16x64_i8 v[48:51], v[150:153], v[182:185], v[48:51]
	v_mfma_i32_16x16x64_i8 v[44:47], v[142:145], v[194:197], v[44:47]
	v_mfma_i32_16x16x64_i8 v[40:43], v[150:153], v[194:197], v[40:43]
	v_mfma_i32_16x16x64_i8 v[36:39], v[142:145], v[202:205], v[36:39]
	v_mfma_i32_16x16x64_i8 v[32:35], v[150:153], v[202:205], v[32:35]
	v_mfma_i32_16x16x64_i8 v[28:31], v[154:157], v[170:173], v[28:31]
	v_mfma_i32_16x16x64_i8 v[24:27], v[162:165], v[170:173], v[24:27]
	v_mfma_i32_16x16x64_i8 v[20:23], v[154:157], v[178:181], v[20:23]
	v_mfma_i32_16x16x64_i8 v[16:19], v[162:165], v[178:181], v[16:19]
	v_mfma_i32_16x16x64_i8 v[12:15], v[154:157], v[190:193], v[12:15]
	v_mfma_i32_16x16x64_i8 v[8:11], v[162:165], v[190:193], v[8:11]
	v_mfma_i32_16x16x64_i8 v[4:7], v[154:157], v[198:201], v[4:7]
	v_mfma_i32_16x16x64_i8 v[0:3], v[162:165], v[198:201], v[0:3]
	v_mfma_i32_16x16x64_i8 v[28:31], v[158:161], v[174:177], v[28:31]
	v_mfma_i32_16x16x64_i8 v[24:27], v[166:169], v[174:177], v[24:27]
	v_mfma_i32_16x16x64_i8 v[20:23], v[158:161], v[182:185], v[20:23]
	v_mfma_i32_16x16x64_i8 v[16:19], v[166:169], v[182:185], v[16:19]
	v_mfma_i32_16x16x64_i8 v[12:15], v[158:161], v[194:197], v[12:15]
	v_mfma_i32_16x16x64_i8 v[8:11], v[166:169], v[194:197], v[8:11]
	v_mfma_i32_16x16x64_i8 v[4:7], v[158:161], v[202:205], v[4:7]
	v_mfma_i32_16x16x64_i8 v[0:3], v[166:169], v[202:205], v[0:3]
	s_barrier
	s_setprio 0
	v_add_u32_e32 v150, 0x18000, v136
	v_add_u32_e32 v166, 0x1c000, v136
	ds_read_b128 v[138:141], v150
	ds_read_b128 v[142:145], v150 offset:1024
	ds_read_b128 v[146:149], v150 offset:2048
	ds_read_b128 v[150:153], v150 offset:3072
	ds_read_b128 v[154:157], v166
	ds_read_b128 v[158:161], v166 offset:1024
	ds_read_b128 v[162:165], v166 offset:2048
	ds_read_b128 v[166:169], v166 offset:3072
	ds_read_b128 v[170:173], v137 offset:32768
	ds_read_b128 v[174:177], v137 offset:33792
	ds_read_b128 v[178:181], v137 offset:34816
	ds_read_b128 v[182:185], v137 offset:35840
	ds_read_b128 v[190:193], v137 offset:36864
	ds_read_b128 v[194:197], v137 offset:37888
	ds_read_b128 v[198:201], v137 offset:38912
	ds_read_b128 v[202:205], v137 offset:39936
	s_add_u32 s74, s74, 0x40000
	s_addc_u32 s75, s75, 0
	s_mov_b32 m0, s67
	s_nop 0
	global_load_lds_dwordx4 v132, s[74:75]
	s_nop 0
	s_mov_b32 m0, s68
	s_nop 0
	global_load_lds_dwordx4 v134, s[74:75]
	s_setprio 1
	s_waitcnt vmcnt(8)
	s_waitcnt lgkmcnt(0)
	s_barrier
	v_mfma_i32_16x16x64_i8 v[124:127], v[138:141], v[170:173], v[124:127]
	v_mfma_i32_16x16x64_i8 v[120:123], v[146:149], v[170:173], v[120:123]
	v_mfma_i32_16x16x64_i8 v[116:119], v[138:141], v[178:181], v[116:119]
	v_mfma_i32_16x16x64_i8 v[112:115], v[146:149], v[178:181], v[112:115]
	v_mfma_i32_16x16x64_i8 v[108:111], v[138:141], v[190:193], v[108:111]
	v_mfma_i32_16x16x64_i8 v[104:107], v[146:149], v[190:193], v[104:107]
	v_mfma_i32_16x16x64_i8 v[100:103], v[138:141], v[198:201], v[100:103]
	v_mfma_i32_16x16x64_i8 v[96:99], v[146:149], v[198:201], v[96:99]
	v_mfma_i32_16x16x64_i8 v[124:127], v[142:145], v[174:177], v[124:127]
	v_mfma_i32_16x16x64_i8 v[120:123], v[150:153], v[174:177], v[120:123]
	v_mfma_i32_16x16x64_i8 v[116:119], v[142:145], v[182:185], v[116:119]
	v_mfma_i32_16x16x64_i8 v[112:115], v[150:153], v[182:185], v[112:115]
	v_mfma_i32_16x16x64_i8 v[108:111], v[142:145], v[194:197], v[108:111]
	v_mfma_i32_16x16x64_i8 v[104:107], v[150:153], v[194:197], v[104:107]
	v_mfma_i32_16x16x64_i8 v[100:103], v[142:145], v[202:205], v[100:103]
	v_mfma_i32_16x16x64_i8 v[96:99], v[150:153], v[202:205], v[96:99]
	v_mfma_i32_16x16x64_i8 v[92:95], v[154:157], v[170:173], v[92:95]
	v_mfma_i32_16x16x64_i8 v[88:91], v[162:165], v[170:173], v[88:91]
	v_mfma_i32_16x16x64_i8 v[84:87], v[154:157], v[178:181], v[84:87]
	v_mfma_i32_16x16x64_i8 v[80:83], v[162:165], v[178:181], v[80:83]
	v_mfma_i32_16x16x64_i8 v[76:79], v[154:157], v[190:193], v[76:79]
	v_mfma_i32_16x16x64_i8 v[72:75], v[162:165], v[190:193], v[72:75]
	v_mfma_i32_16x16x64_i8 v[68:71], v[154:157], v[198:201], v[68:71]
	v_mfma_i32_16x16x64_i8 v[64:67], v[162:165], v[198:201], v[64:67]
	v_mfma_i32_16x16x64_i8 v[92:95], v[158:161], v[174:177], v[92:95]
	v_mfma_i32_16x16x64_i8 v[88:91], v[166:169], v[174:177], v[88:91]
	v_mfma_i32_16x16x64_i8 v[84:87], v[158:161], v[182:185], v[84:87]
	v_mfma_i32_16x16x64_i8 v[80:83], v[166:169], v[182:185], v[80:83]
	v_mfma_i32_16x16x64_i8 v[76:79], v[158:161], v[194:197], v[76:79]
	v_mfma_i32_16x16x64_i8 v[72:75], v[166:169], v[194:197], v[72:75]
	v_mfma_i32_16x16x64_i8 v[68:71], v[158:161], v[202:205], v[68:71]
	v_mfma_i32_16x16x64_i8 v[64:67], v[166:169], v[202:205], v[64:67]
	s_barrier
	s_setprio 0
	ds_read_b128 v[170:173], v137 offset:49152
	ds_read_b128 v[174:177], v137 offset:50176
	ds_read_b128 v[178:181], v137 offset:51200
	ds_read_b128 v[182:185], v137 offset:52224
	ds_read_b128 v[190:193], v137 offset:53248
	ds_read_b128 v[194:197], v137 offset:54272
	ds_read_b128 v[198:201], v137 offset:55296
	ds_read_b128 v[202:205], v137 offset:56320
	s_mov_b32 m0, s71
	s_nop 0
	global_load_lds_dwordx4 v133, s[62:63]
	s_nop 0
	s_mov_b32 m0, s72
	s_nop 0
	global_load_lds_dwordx4 v135, s[62:63]
	s_add_u32 s62, s62, 0x40000
	s_addc_u32 s63, s63, 0
	s_mov_b32 m0, s80
	s_nop 0
	global_load_lds_dwordx4 v133, s[62:63]
	s_nop 0
	s_mov_b32 m0, s81
	s_nop 0
	global_load_lds_dwordx4 v135, s[62:63]
	s_mov_b32 m0, s78
	s_nop 0
	global_load_lds_dwordx4 v132, s[60:61]
	s_nop 0
	s_mov_b32 m0, s79
	s_nop 0
	global_load_lds_dwordx4 v134, s[60:61]
	s_setprio 1
	s_waitcnt vmcnt(8)
	s_waitcnt lgkmcnt(0)
	s_barrier
	v_mfma_i32_16x16x64_i8 v[60:63], v[138:141], v[170:173], v[60:63]
	v_mfma_i32_16x16x64_i8 v[56:59], v[146:149], v[170:173], v[56:59]
	v_mfma_i32_16x16x64_i8 v[52:55], v[138:141], v[178:181], v[52:55]
	v_mfma_i32_16x16x64_i8 v[48:51], v[146:149], v[178:181], v[48:51]
	v_mfma_i32_16x16x64_i8 v[44:47], v[138:141], v[190:193], v[44:47]
	v_mfma_i32_16x16x64_i8 v[40:43], v[146:149], v[190:193], v[40:43]
	v_mfma_i32_16x16x64_i8 v[36:39], v[138:141], v[198:201], v[36:39]
	v_mfma_i32_16x16x64_i8 v[32:35], v[146:149], v[198:201], v[32:35]
	v_mfma_i32_16x16x64_i8 v[60:63], v[142:145], v[174:177], v[60:63]
	v_mfma_i32_16x16x64_i8 v[56:59], v[150:153], v[174:177], v[56:59]
	v_mfma_i32_16x16x64_i8 v[52:55], v[142:145], v[182:185], v[52:55]
	v_mfma_i32_16x16x64_i8 v[48:51], v[150:153], v[182:185], v[48:51]
	v_mfma_i32_16x16x64_i8 v[44:47], v[142:145], v[194:197], v[44:47]
	v_mfma_i32_16x16x64_i8 v[40:43], v[150:153], v[194:197], v[40:43]
	v_mfma_i32_16x16x64_i8 v[36:39], v[142:145], v[202:205], v[36:39]
	v_mfma_i32_16x16x64_i8 v[32:35], v[150:153], v[202:205], v[32:35]
	v_mfma_i32_16x16x64_i8 v[28:31], v[154:157], v[170:173], v[28:31]
	v_mfma_i32_16x16x64_i8 v[24:27], v[162:165], v[170:173], v[24:27]
	v_mfma_i32_16x16x64_i8 v[20:23], v[154:157], v[178:181], v[20:23]
	v_mfma_i32_16x16x64_i8 v[16:19], v[162:165], v[178:181], v[16:19]
	v_mfma_i32_16x16x64_i8 v[12:15], v[154:157], v[190:193], v[12:15]
	v_mfma_i32_16x16x64_i8 v[8:11], v[162:165], v[190:193], v[8:11]
	v_mfma_i32_16x16x64_i8 v[4:7], v[154:157], v[198:201], v[4:7]
	v_mfma_i32_16x16x64_i8 v[0:3], v[162:165], v[198:201], v[0:3]
	v_mfma_i32_16x16x64_i8 v[28:31], v[158:161], v[174:177], v[28:31]
	v_mfma_i32_16x16x64_i8 v[24:27], v[166:169], v[174:177], v[24:27]
	v_mfma_i32_16x16x64_i8 v[20:23], v[158:161], v[182:185], v[20:23]
	v_mfma_i32_16x16x64_i8 v[16:19], v[166:169], v[182:185], v[16:19]
	v_mfma_i32_16x16x64_i8 v[12:15], v[158:161], v[194:197], v[12:15]
	v_mfma_i32_16x16x64_i8 v[8:11], v[166:169], v[194:197], v[8:11]
	v_mfma_i32_16x16x64_i8 v[4:7], v[158:161], v[202:205], v[4:7]
	v_mfma_i32_16x16x64_i8 v[0:3], v[166:169], v[202:205], v[0:3]
	s_barrier
	s_setprio 0
	s_add_i32 s87, s87, 2
	s_add_u32 s58, s58, 0x100
	s_addc_u32 s59, s59, 0
	s_cbranch_vccz .LBB0_1309
	s_and_b64 vcc, exec, s[40:41]
	s_cbranch_vccz .LBB0_1312
	s_barrier
.LBB0_1312:
	v_cvt_f32_i32_e32 v124, v124
	v_cvt_f32_i32_e32 v125, v125
	v_cvt_f32_i32_e32 v140, v88
	v_cvt_f32_i32_e32 v88, v86
	v_cvt_f32_i32_e32 v86, v80
	v_cvt_f32_i32_e32 v80, v78
	v_cvt_f32_i32_e32 v78, v72
	v_cvt_f32_i32_e32 v72, v70
	v_cvt_f32_i32_e32 v70, v64
	v_cvt_f32_i32_e32 v64, v60
	v_cvt_f32_i32_e32 v60, v56
	v_cvt_f32_i32_e32 v56, v52
	v_cvt_f32_i32_e32 v52, v48
	v_cvt_f32_i32_e32 v48, v44
	v_cvt_f32_i32_e32 v44, v40
	v_cvt_f32_i32_e32 v40, v36
	v_cvt_f32_i32_e32 v36, v32
	v_cvt_f32_i32_e32 v32, v34
	v_cvt_f32_i32_e32 v34, v30
	v_cvt_f32_i32_e32 v30, v24
	v_cvt_f32_i32_e32 v24, v22
	v_cvt_f32_i32_e32 v22, v16
	v_cvt_f32_i32_e32 v16, v14
	v_cvt_f32_i32_e32 v14, v8
	v_cvt_f32_i32_e32 v8, v4
	v_cvt_f32_i32_e32 v4, v0
	v_mbcnt_lo_u32_b32 v0, -1, 0
	v_mbcnt_hi_u32_b32 v0, -1, v0
	s_lshl_b32 s9, s52, 8
	v_cvt_f32_i32_e32 v141, v89
	v_cvt_f32_i32_e32 v89, v87
	v_cvt_f32_i32_e32 v87, v81
	v_cvt_f32_i32_e32 v81, v79
	v_cvt_f32_i32_e32 v79, v73
	v_cvt_f32_i32_e32 v73, v71
	v_cvt_f32_i32_e32 v71, v65
	v_cvt_f32_i32_e32 v65, v61
	v_cvt_f32_i32_e32 v61, v57
	v_cvt_f32_i32_e32 v57, v53
	v_cvt_f32_i32_e32 v53, v49
	v_cvt_f32_i32_e32 v49, v45
	v_cvt_f32_i32_e32 v45, v41
	v_cvt_f32_i32_e32 v41, v37
	v_cvt_f32_i32_e32 v37, v33
	v_cvt_f32_i32_e32 v33, v35
	v_cvt_f32_i32_e32 v35, v31
	v_cvt_f32_i32_e32 v31, v25
	v_cvt_f32_i32_e32 v25, v23
	v_cvt_f32_i32_e32 v23, v17
	v_cvt_f32_i32_e32 v17, v15
	v_cvt_f32_i32_e32 v15, v9
	v_cvt_f32_i32_e32 v9, v5
	v_cvt_f32_i32_e32 v5, v1
	s_add_i32 s9, s9, s69
	v_ashrrev_i32_e32 v1, 2, v0
	v_cvt_f32_i32_e32 v139, v121
	v_cvt_f32_i32_e32 v121, v117
	v_cvt_f32_i32_e32 v117, v113
	v_cvt_f32_i32_e32 v113, v109
	v_cvt_f32_i32_e32 v109, v105
	v_cvt_f32_i32_e32 v105, v101
	v_cvt_f32_i32_e32 v101, v97
	v_cvt_f32_i32_e32 v97, v99
	v_cvt_f32_i32_e32 v99, v93
	v_cvt_f32_i32_e32 v142, v90
	v_cvt_f32_i32_e32 v90, v84
	v_cvt_f32_i32_e32 v84, v82
	v_cvt_f32_i32_e32 v82, v76
	v_cvt_f32_i32_e32 v76, v74
	v_cvt_f32_i32_e32 v74, v68
	v_cvt_f32_i32_e32 v68, v66
	v_cvt_f32_i32_e32 v66, v28
	v_cvt_f32_i32_e32 v28, v26
	v_cvt_f32_i32_e32 v26, v20
	v_cvt_f32_i32_e32 v20, v18
	v_cvt_f32_i32_e32 v18, v12
	v_cvt_f32_i32_e32 v12, v10
	v_and_b32_e32 v10, 3, v0
	v_and_b32_e32 v0, -4, v0
	v_add_u32_e32 v93, s9, v1
	s_lshl_b32 s9, s85, 7
	v_cvt_f32_i32_e32 v138, v120
	v_cvt_f32_i32_e32 v120, v116
	v_cvt_f32_i32_e32 v116, v112
	v_cvt_f32_i32_e32 v112, v108
	v_cvt_f32_i32_e32 v108, v104
	v_cvt_f32_i32_e32 v104, v100
	v_cvt_f32_i32_e32 v100, v96
	v_cvt_f32_i32_e32 v96, v98
	v_cvt_f32_i32_e32 v98, v92
	v_cvt_f32_i32_e32 v143, v91
	v_cvt_f32_i32_e32 v91, v85
	v_cvt_f32_i32_e32 v85, v83
	v_cvt_f32_i32_e32 v83, v77
	v_cvt_f32_i32_e32 v77, v75
	v_cvt_f32_i32_e32 v75, v69
	v_cvt_f32_i32_e32 v69, v67
	v_cvt_f32_i32_e32 v67, v29
	v_cvt_f32_i32_e32 v29, v27
	v_cvt_f32_i32_e32 v27, v21
	v_cvt_f32_i32_e32 v21, v19
	v_cvt_f32_i32_e32 v19, v13
	v_cvt_f32_i32_e32 v13, v11
	v_lshl_add_u32 v92, v10, 6, v0
	v_lshl_or_b32 v0, v10, 3, s9
	v_pk_mul_f32 v[10:11], v[128:129], v[124:125]
	v_cvt_f32_i32_e32 v126, v126
	v_exp_f32_e32 v10, v10
	v_exp_f32_e32 v11, v11
	v_cvt_f32_i32_e32 v127, v127
	v_pk_mul_f32 v[124:125], v[130:131], v[124:125]
	v_cvt_f32_i32_e32 v94, v94
	v_pk_add_f32 v[10:11], v[10:11], 1.0 op_sel_hi:[1,0]
	v_pk_mul_f32 v[98:99], v[124:125], v[98:99]
	v_rcp_f32_e32 v10, v10
	v_rcp_f32_e32 v11, v11
	v_cvt_f32_i32_e32 v95, v95
	v_pk_mul_f32 v[124:125], v[130:131], v[126:127]
	v_cvt_f32_i32_e32 v122, v122
	v_pk_mul_f32 v[10:11], v[10:11], v[98:99]
	v_pk_mul_f32 v[98:99], v[128:129], v[126:127]
	v_pk_mul_f32 v[94:95], v[124:125], v[94:95]
	v_exp_f32_e32 v98, v98
	v_exp_f32_e32 v99, v99
	v_cvt_f32_i32_e32 v123, v123
	v_pk_mul_f32 v[124:125], v[130:131], v[138:139]
	v_or_b32_e32 v0, s70, v0
	v_pk_add_f32 v[98:99], v[98:99], 1.0 op_sel_hi:[1,0]
	v_pk_mul_f32 v[124:125], v[124:125], v[140:141]
	v_rcp_f32_e32 v98, v98
	v_rcp_f32_e32 v99, v99
	s_movk_i32 s9, 0x1c00
	v_ashrrev_i32_e32 v1, 31, v0
	v_cvt_f32_i32_e32 v118, v118
	v_pk_mul_f32 v[94:95], v[98:99], v[94:95]
	v_pk_mul_f32 v[98:99], v[128:129], v[138:139]
	v_cvt_f32_i32_e32 v119, v119
	v_exp_f32_e32 v98, v98
	v_exp_f32_e32 v99, v99
	v_cvt_f32_i32_e32 v114, v114
	v_cvt_f32_i32_e32 v115, v115
	v_cvt_f32_i32_e32 v110, v110
	v_pk_add_f32 v[98:99], v[98:99], 1.0 op_sel_hi:[1,0]
	v_cvt_f32_i32_e32 v111, v111
	v_rcp_f32_e32 v98, v98
	v_rcp_f32_e32 v99, v99
	v_cvt_f32_i32_e32 v106, v106
	v_cvt_f32_i32_e32 v107, v107
	v_cvt_f32_i32_e32 v102, v102
	v_pk_mul_f32 v[98:99], v[98:99], v[124:125]
	v_pk_mul_f32 v[124:125], v[128:129], v[122:123]
	v_pk_mul_f32 v[122:123], v[130:131], v[122:123]
	v_exp_f32_e32 v124, v124
	v_exp_f32_e32 v125, v125
	v_pk_mul_f32 v[122:123], v[122:123], v[142:143]
	v_cvt_f32_i32_e32 v103, v103
	v_cvt_f32_i32_e32 v62, v62
	v_pk_add_f32 v[124:125], v[124:125], 1.0 op_sel_hi:[1,0]
	v_cvt_f32_i32_e32 v63, v63
	v_rcp_f32_e32 v124, v124
	v_rcp_f32_e32 v125, v125
	v_cvt_f32_i32_e32 v58, v58
	v_cvt_f32_i32_e32 v59, v59
	v_cvt_f32_i32_e32 v54, v54
	v_pk_mul_f32 v[122:123], v[124:125], v[122:123]
	v_cvt_pk_fp8_f32 v124, v10, v11
	v_cvt_pk_fp8_f32 v10, v98, v99
	v_cvt_f32_i32_e32 v55, v55
	v_cvt_pk_fp8_f32 v124, v94, v95 op_sel:[0,0,1]
	v_cvt_f32_i32_e32 v50, v50
	v_cvt_pk_fp8_f32 v10, v122, v123 op_sel:[0,0,1]
	v_cvt_f32_i32_e32 v51, v51
	ds_bpermute_b32 v94, v92, v124
	v_cvt_f32_i32_e32 v46, v46
	ds_bpermute_b32 v95, v92, v10
	v_mov_b64_e32 v[10:11], s[22:23]
	v_mad_i64_i32 v[98:99], s[10:11], v93, s9, v[10:11]
	v_lshl_add_u64 v[98:99], v[98:99], 0, v[0:1]
	s_waitcnt lgkmcnt(0)
	global_store_dwordx2 v[98:99], v[94:95], off
	v_pk_mul_f32 v[94:95], v[128:129], v[120:121]
	v_pk_mul_f32 v[98:99], v[130:131], v[120:121]
	v_exp_f32_e32 v94, v94
	v_exp_f32_e32 v95, v95
	v_pk_mul_f32 v[90:91], v[98:99], v[90:91]
	v_pk_mul_f32 v[98:99], v[130:131], v[118:119]
	v_cvt_f32_i32_e32 v47, v47
	v_pk_add_f32 v[94:95], v[94:95], 1.0 op_sel_hi:[1,0]
	v_pk_mul_f32 v[88:89], v[98:99], v[88:89]
	v_rcp_f32_e32 v94, v94
	v_rcp_f32_e32 v95, v95
	v_pk_mul_f32 v[98:99], v[130:131], v[116:117]
	v_cvt_f32_i32_e32 v42, v42
	v_pk_mul_f32 v[86:87], v[98:99], v[86:87]
	v_pk_mul_f32 v[90:91], v[94:95], v[90:91]
	v_pk_mul_f32 v[94:95], v[128:129], v[118:119]
	v_pk_mul_f32 v[98:99], v[130:131], v[114:115]
	v_exp_f32_e32 v94, v94
	v_exp_f32_e32 v95, v95
	v_pk_mul_f32 v[84:85], v[98:99], v[84:85]
	v_cvt_f32_i32_e32 v43, v43
	v_cvt_f32_i32_e32 v38, v38
	v_pk_add_f32 v[94:95], v[94:95], 1.0 op_sel_hi:[1,0]
	v_cvt_f32_i32_e32 v39, v39
	v_rcp_f32_e32 v94, v94
	v_rcp_f32_e32 v95, v95
	v_cvt_f32_i32_e32 v6, v6
	v_cvt_f32_i32_e32 v7, v7
	v_cvt_f32_i32_e32 v2, v2
	v_pk_mul_f32 v[88:89], v[94:95], v[88:89]
	v_pk_mul_f32 v[94:95], v[128:129], v[116:117]
	v_cvt_f32_i32_e32 v3, v3
	v_exp_f32_e32 v94, v94
	v_exp_f32_e32 v95, v95
	s_mov_b64 s[52:53], -1
	s_andn2_b64 vcc, exec, s[44:45]
	v_readlane_b32 s90, v255, 39
	v_pk_add_f32 v[94:95], v[94:95], 1.0 op_sel_hi:[1,0]
	v_readlane_b32 s91, v255, 40
	v_rcp_f32_e32 v94, v94
	v_rcp_f32_e32 v95, v95
	s_nop 0
	v_pk_mul_f32 v[86:87], v[94:95], v[86:87]
	v_pk_mul_f32 v[94:95], v[128:129], v[114:115]
	s_nop 0
	v_exp_f32_e32 v94, v94
	v_exp_f32_e32 v95, v95
	s_nop 0
	v_pk_add_f32 v[94:95], v[94:95], 1.0 op_sel_hi:[1,0]
	s_nop 0
	v_rcp_f32_e32 v94, v94
	v_rcp_f32_e32 v95, v95
	s_nop 0
	v_pk_mul_f32 v[84:85], v[94:95], v[84:85]
	v_cvt_pk_fp8_f32 v94, v90, v91
	v_cvt_pk_fp8_f32 v94, v88, v89 op_sel:[0,0,1]
	v_cvt_pk_fp8_f32 v89, v86, v87
	v_pk_mul_f32 v[86:87], v[130:131], v[112:113]
	ds_bpermute_b32 v88, v92, v94
	v_pk_mul_f32 v[82:83], v[86:87], v[82:83]
	v_cvt_pk_fp8_f32 v89, v84, v85 op_sel:[0,0,1]
	v_add_u32_e32 v84, 16, v93
	v_mad_i64_i32 v[84:85], s[10:11], v84, s9, v[10:11]
	ds_bpermute_b32 v89, v92, v89
	v_lshl_add_u64 v[84:85], v[84:85], 0, v[0:1]
	v_pk_mul_f32 v[86:87], v[130:131], v[110:111]
	s_waitcnt lgkmcnt(0)
	global_store_dwordx2 v[84:85], v[88:89], off
	v_pk_mul_f32 v[84:85], v[128:129], v[112:113]
	v_pk_mul_f32 v[80:81], v[86:87], v[80:81]
	v_exp_f32_e32 v84, v84
	v_exp_f32_e32 v85, v85
	v_pk_mul_f32 v[86:87], v[130:131], v[108:109]
	v_pk_add_f32 v[84:85], v[84:85], 1.0 op_sel_hi:[1,0]
	s_nop 0
	v_rcp_f32_e32 v84, v84
	v_rcp_f32_e32 v85, v85
	v_pk_mul_f32 v[78:79], v[86:87], v[78:79]
	v_pk_mul_f32 v[86:87], v[130:131], v[106:107]
	v_pk_mul_f32 v[82:83], v[84:85], v[82:83]
	v_pk_mul_f32 v[84:85], v[128:129], v[110:111]
	v_pk_mul_f32 v[76:77], v[86:87], v[76:77]
	v_exp_f32_e32 v84, v84
	v_exp_f32_e32 v85, v85
	s_nop 0
	v_pk_add_f32 v[84:85], v[84:85], 1.0 op_sel_hi:[1,0]
	s_nop 0
	v_rcp_f32_e32 v84, v84
	v_rcp_f32_e32 v85, v85
	s_nop 0
	v_pk_mul_f32 v[80:81], v[84:85], v[80:81]
	v_pk_mul_f32 v[84:85], v[128:129], v[108:109]
	s_nop 0
	v_exp_f32_e32 v84, v84
	v_exp_f32_e32 v85, v85
	s_nop 0
	v_pk_add_f32 v[84:85], v[84:85], 1.0 op_sel_hi:[1,0]
	s_nop 0
	v_rcp_f32_e32 v84, v84
	v_rcp_f32_e32 v85, v85
	s_nop 0
	v_pk_mul_f32 v[78:79], v[84:85], v[78:79]
	v_pk_mul_f32 v[84:85], v[128:129], v[106:107]
	s_nop 0
	v_exp_f32_e32 v84, v84
	v_exp_f32_e32 v85, v85
	s_nop 0
	v_pk_add_f32 v[84:85], v[84:85], 1.0 op_sel_hi:[1,0]
	s_nop 0
	v_rcp_f32_e32 v84, v84
	v_rcp_f32_e32 v85, v85
	s_nop 0
	v_pk_mul_f32 v[76:77], v[84:85], v[76:77]
	v_cvt_pk_fp8_f32 v84, v82, v83
	v_cvt_pk_fp8_f32 v84, v80, v81 op_sel:[0,0,1]
	v_cvt_pk_fp8_f32 v81, v78, v79
	v_pk_mul_f32 v[78:79], v[130:131], v[104:105]
	ds_bpermute_b32 v80, v92, v84
	v_pk_mul_f32 v[74:75], v[78:79], v[74:75]
	v_cvt_pk_fp8_f32 v81, v76, v77 op_sel:[0,0,1]
	v_add_u32_e32 v76, 32, v93
	v_mad_i64_i32 v[76:77], s[10:11], v76, s9, v[10:11]
	ds_bpermute_b32 v81, v92, v81
	v_lshl_add_u64 v[76:77], v[76:77], 0, v[0:1]
	v_pk_mul_f32 v[78:79], v[130:131], v[102:103]
	s_waitcnt lgkmcnt(0)
	global_store_dwordx2 v[76:77], v[80:81], off
	v_pk_mul_f32 v[76:77], v[128:129], v[104:105]
	v_pk_mul_f32 v[72:73], v[78:79], v[72:73]
	v_exp_f32_e32 v76, v76
	v_exp_f32_e32 v77, v77
	v_pk_mul_f32 v[78:79], v[130:131], v[100:101]
	v_pk_add_f32 v[76:77], v[76:77], 1.0 op_sel_hi:[1,0]
	s_nop 0
	v_rcp_f32_e32 v76, v76
	v_rcp_f32_e32 v77, v77
	v_pk_mul_f32 v[70:71], v[78:79], v[70:71]
	v_pk_mul_f32 v[78:79], v[130:131], v[96:97]
	v_pk_mul_f32 v[74:75], v[76:77], v[74:75]
	v_pk_mul_f32 v[76:77], v[128:129], v[102:103]
	v_pk_mul_f32 v[68:69], v[78:79], v[68:69]
	v_exp_f32_e32 v76, v76
	v_exp_f32_e32 v77, v77
	s_nop 0
	v_pk_add_f32 v[76:77], v[76:77], 1.0 op_sel_hi:[1,0]
	s_nop 0
	v_rcp_f32_e32 v76, v76
	v_rcp_f32_e32 v77, v77
	s_nop 0
	v_pk_mul_f32 v[72:73], v[76:77], v[72:73]
	v_pk_mul_f32 v[76:77], v[128:129], v[100:101]
	s_nop 0
	v_exp_f32_e32 v76, v76
	v_exp_f32_e32 v77, v77
	s_nop 0
	v_pk_add_f32 v[76:77], v[76:77], 1.0 op_sel_hi:[1,0]
	s_nop 0
	v_rcp_f32_e32 v76, v76
	v_rcp_f32_e32 v77, v77
	s_nop 0
	v_pk_mul_f32 v[70:71], v[76:77], v[70:71]
	v_pk_mul_f32 v[76:77], v[128:129], v[96:97]
	s_nop 0
	v_exp_f32_e32 v76, v76
	v_exp_f32_e32 v77, v77
	s_nop 0
	v_pk_add_f32 v[76:77], v[76:77], 1.0 op_sel_hi:[1,0]
	s_nop 0
	v_rcp_f32_e32 v76, v76
	v_rcp_f32_e32 v77, v77
	s_nop 0
	v_pk_mul_f32 v[68:69], v[76:77], v[68:69]
	v_cvt_pk_fp8_f32 v76, v74, v75
	v_cvt_pk_fp8_f32 v76, v72, v73 op_sel:[0,0,1]
	v_cvt_pk_fp8_f32 v73, v70, v71
	v_add_u32_e32 v70, 0x80, v93
	ds_bpermute_b32 v72, v92, v76
	v_cvt_pk_fp8_f32 v73, v68, v69 op_sel:[0,0,1]
	v_add_u32_e32 v68, 48, v93
	v_mad_i64_i32 v[68:69], s[10:11], v68, s9, v[10:11]
	ds_bpermute_b32 v73, v92, v73
	v_lshl_add_u64 v[68:69], v[68:69], 0, v[0:1]
	s_waitcnt lgkmcnt(0)
	global_store_dwordx2 v[68:69], v[72:73], off
	v_pk_mul_f32 v[68:69], v[128:129], v[64:65]
	v_pk_mul_f32 v[64:65], v[130:131], v[64:65]
	s_nop 0
	v_pk_mul_f32 v[64:65], v[64:65], v[66:67]
	v_exp_f32_e32 v66, v68
	v_exp_f32_e32 v67, v69
	s_nop 0
	v_pk_add_f32 v[66:67], v[66:67], 1.0 op_sel_hi:[1,0]
	s_nop 0
	v_rcp_f32_e32 v66, v66
	v_rcp_f32_e32 v67, v67
	s_nop 0
	v_pk_mul_f32 v[64:65], v[66:67], v[64:65]
	v_pk_mul_f32 v[66:67], v[128:129], v[62:63]
	v_pk_mul_f32 v[62:63], v[130:131], v[62:63]
	s_nop 0
	v_pk_mul_f32 v[34:35], v[62:63], v[34:35]
	v_exp_f32_e32 v62, v66
	v_exp_f32_e32 v63, v67
	s_nop 0
	v_pk_add_f32 v[62:63], v[62:63], 1.0 op_sel_hi:[1,0]
	s_nop 0
	v_rcp_f32_e32 v62, v62
	v_rcp_f32_e32 v63, v63
	s_nop 0
	v_pk_mul_f32 v[34:35], v[62:63], v[34:35]
	v_pk_mul_f32 v[62:63], v[128:129], v[60:61]
	v_pk_mul_f32 v[60:61], v[130:131], v[60:61]
	s_nop 0
	v_pk_mul_f32 v[30:31], v[60:61], v[30:31]
	v_exp_f32_e32 v60, v62
	v_exp_f32_e32 v61, v63
	s_nop 0
	v_pk_add_f32 v[60:61], v[60:61], 1.0 op_sel_hi:[1,0]
	s_nop 0
	v_rcp_f32_e32 v60, v60
	v_rcp_f32_e32 v61, v61
	s_nop 0
	v_pk_mul_f32 v[30:31], v[60:61], v[30:31]
	v_pk_mul_f32 v[60:61], v[128:129], v[58:59]
	v_pk_mul_f32 v[58:59], v[130:131], v[58:59]
	s_nop 0
	v_pk_mul_f32 v[28:29], v[58:59], v[28:29]
	v_exp_f32_e32 v58, v60
	v_exp_f32_e32 v59, v61
	s_nop 0
	v_pk_add_f32 v[58:59], v[58:59], 1.0 op_sel_hi:[1,0]
	s_nop 0
	v_rcp_f32_e32 v58, v58
	v_rcp_f32_e32 v59, v59
	s_nop 0
	v_pk_mul_f32 v[28:29], v[58:59], v[28:29]
	v_cvt_pk_fp8_f32 v58, v64, v65
	v_cvt_pk_fp8_f32 v58, v34, v35 op_sel:[0,0,1]
	v_cvt_pk_fp8_f32 v35, v30, v31
	v_pk_mul_f32 v[30:31], v[130:131], v[56:57]
	ds_bpermute_b32 v34, v92, v58
	v_pk_mul_f32 v[26:27], v[30:31], v[26:27]
	v_cvt_pk_fp8_f32 v35, v28, v29 op_sel:[0,0,1]
	v_mad_i64_i32 v[28:29], s[10:11], v70, s9, v[10:11]
	v_lshl_add_u64 v[28:29], v[28:29], 0, v[0:1]
	ds_bpermute_b32 v35, v92, v35
	v_pk_mul_f32 v[30:31], v[130:131], v[54:55]
	s_waitcnt lgkmcnt(0)
	global_store_dwordx2 v[28:29], v[34:35], off
	v_pk_mul_f32 v[28:29], v[128:129], v[56:57]
	v_pk_mul_f32 v[24:25], v[30:31], v[24:25]
	v_exp_f32_e32 v28, v28
	v_exp_f32_e32 v29, v29
	v_pk_mul_f32 v[30:31], v[130:131], v[52:53]
	v_pk_add_f32 v[28:29], v[28:29], 1.0 op_sel_hi:[1,0]
	s_nop 0
	v_rcp_f32_e32 v28, v28
	v_rcp_f32_e32 v29, v29
	v_pk_mul_f32 v[22:23], v[30:31], v[22:23]
	v_pk_mul_f32 v[30:31], v[130:131], v[50:51]
	v_pk_mul_f32 v[26:27], v[28:29], v[26:27]
	v_pk_mul_f32 v[28:29], v[128:129], v[54:55]
	v_pk_mul_f32 v[20:21], v[30:31], v[20:21]
	v_exp_f32_e32 v28, v28
	v_exp_f32_e32 v29, v29
	s_nop 0
	v_pk_add_f32 v[28:29], v[28:29], 1.0 op_sel_hi:[1,0]
	s_nop 0
	v_rcp_f32_e32 v28, v28
	v_rcp_f32_e32 v29, v29
	s_nop 0
	v_pk_mul_f32 v[24:25], v[28:29], v[24:25]
	v_pk_mul_f32 v[28:29], v[128:129], v[52:53]
	s_nop 0
	v_exp_f32_e32 v28, v28
	v_exp_f32_e32 v29, v29
	s_nop 0
	v_pk_add_f32 v[28:29], v[28:29], 1.0 op_sel_hi:[1,0]
	s_nop 0
	v_rcp_f32_e32 v28, v28
	v_rcp_f32_e32 v29, v29
	s_nop 0
	v_pk_mul_f32 v[22:23], v[28:29], v[22:23]
	v_pk_mul_f32 v[28:29], v[128:129], v[50:51]
	s_nop 0
	v_exp_f32_e32 v28, v28
	v_exp_f32_e32 v29, v29
	s_nop 0
	v_pk_add_f32 v[28:29], v[28:29], 1.0 op_sel_hi:[1,0]
	s_nop 0
	v_rcp_f32_e32 v28, v28
	v_rcp_f32_e32 v29, v29
	s_nop 0
	v_pk_mul_f32 v[20:21], v[28:29], v[20:21]
	v_cvt_pk_fp8_f32 v28, v26, v27
	v_cvt_pk_fp8_f32 v28, v24, v25 op_sel:[0,0,1]
	v_cvt_pk_fp8_f32 v25, v22, v23
	v_pk_mul_f32 v[22:23], v[130:131], v[48:49]
	ds_bpermute_b32 v24, v92, v28
	v_pk_mul_f32 v[18:19], v[22:23], v[18:19]
	v_cvt_pk_fp8_f32 v25, v20, v21 op_sel:[0,0,1]
	v_add_u32_e32 v20, 0x90, v93
	v_mad_i64_i32 v[20:21], s[10:11], v20, s9, v[10:11]
	ds_bpermute_b32 v25, v92, v25
	v_lshl_add_u64 v[20:21], v[20:21], 0, v[0:1]
	v_pk_mul_f32 v[22:23], v[130:131], v[46:47]
	s_waitcnt lgkmcnt(0)
	global_store_dwordx2 v[20:21], v[24:25], off
	v_pk_mul_f32 v[20:21], v[128:129], v[48:49]
	v_pk_mul_f32 v[16:17], v[22:23], v[16:17]
	v_exp_f32_e32 v20, v20
	v_exp_f32_e32 v21, v21
	v_pk_mul_f32 v[22:23], v[130:131], v[44:45]
	v_pk_add_f32 v[20:21], v[20:21], 1.0 op_sel_hi:[1,0]
	s_nop 0
	v_rcp_f32_e32 v20, v20
	v_rcp_f32_e32 v21, v21
	v_pk_mul_f32 v[14:15], v[22:23], v[14:15]
	v_pk_mul_f32 v[22:23], v[130:131], v[42:43]
	v_pk_mul_f32 v[18:19], v[20:21], v[18:19]
	v_pk_mul_f32 v[20:21], v[128:129], v[46:47]
	v_pk_mul_f32 v[12:13], v[22:23], v[12:13]
	v_exp_f32_e32 v20, v20
	v_exp_f32_e32 v21, v21
	s_nop 0
	v_pk_add_f32 v[20:21], v[20:21], 1.0 op_sel_hi:[1,0]
	s_nop 0
	v_rcp_f32_e32 v20, v20
	v_rcp_f32_e32 v21, v21
	s_nop 0
	v_pk_mul_f32 v[16:17], v[20:21], v[16:17]
	v_pk_mul_f32 v[20:21], v[128:129], v[44:45]
	s_nop 0
	v_exp_f32_e32 v20, v20
	v_exp_f32_e32 v21, v21
	s_nop 0
	v_pk_add_f32 v[20:21], v[20:21], 1.0 op_sel_hi:[1,0]
	s_nop 0
	v_rcp_f32_e32 v20, v20
	v_rcp_f32_e32 v21, v21
	s_nop 0
	v_pk_mul_f32 v[14:15], v[20:21], v[14:15]
	v_pk_mul_f32 v[20:21], v[128:129], v[42:43]
	s_nop 0
	v_exp_f32_e32 v20, v20
	v_exp_f32_e32 v21, v21
	s_nop 0
	v_pk_add_f32 v[20:21], v[20:21], 1.0 op_sel_hi:[1,0]
	s_nop 0
	v_rcp_f32_e32 v20, v20
	v_rcp_f32_e32 v21, v21
	s_nop 0
	v_pk_mul_f32 v[12:13], v[20:21], v[12:13]
	v_cvt_pk_fp8_f32 v20, v18, v19
	v_cvt_pk_fp8_f32 v20, v16, v17 op_sel:[0,0,1]
	v_cvt_pk_fp8_f32 v17, v14, v15
	v_pk_mul_f32 v[14:15], v[130:131], v[40:41]
	ds_bpermute_b32 v16, v92, v20
	v_pk_mul_f32 v[8:9], v[14:15], v[8:9]
	v_cvt_pk_fp8_f32 v17, v12, v13 op_sel:[0,0,1]
	v_add_u32_e32 v12, 0xa0, v93
	v_mad_i64_i32 v[12:13], s[10:11], v12, s9, v[10:11]
	ds_bpermute_b32 v17, v92, v17
	v_lshl_add_u64 v[12:13], v[12:13], 0, v[0:1]
	v_pk_mul_f32 v[14:15], v[130:131], v[38:39]
	s_waitcnt lgkmcnt(0)
	global_store_dwordx2 v[12:13], v[16:17], off
	v_pk_mul_f32 v[12:13], v[128:129], v[40:41]
	v_pk_mul_f32 v[6:7], v[14:15], v[6:7]
	v_exp_f32_e32 v12, v12
	v_exp_f32_e32 v13, v13
	v_pk_mul_f32 v[14:15], v[130:131], v[36:37]
	v_pk_add_f32 v[12:13], v[12:13], 1.0 op_sel_hi:[1,0]
	s_nop 0
	v_rcp_f32_e32 v12, v12
	v_rcp_f32_e32 v13, v13
	v_pk_mul_f32 v[4:5], v[14:15], v[4:5]
	v_pk_mul_f32 v[14:15], v[130:131], v[32:33]
	v_pk_mul_f32 v[8:9], v[12:13], v[8:9]
	v_pk_mul_f32 v[12:13], v[128:129], v[38:39]
	v_pk_mul_f32 v[2:3], v[14:15], v[2:3]
	v_exp_f32_e32 v12, v12
	v_exp_f32_e32 v13, v13
	s_nop 0
	v_pk_add_f32 v[12:13], v[12:13], 1.0 op_sel_hi:[1,0]
	s_nop 0
	v_rcp_f32_e32 v12, v12
	v_rcp_f32_e32 v13, v13
	s_nop 0
	v_pk_mul_f32 v[6:7], v[12:13], v[6:7]
	v_pk_mul_f32 v[12:13], v[128:129], v[36:37]
	s_nop 0
	v_exp_f32_e32 v12, v12
	v_exp_f32_e32 v13, v13
	s_nop 0
	v_pk_add_f32 v[12:13], v[12:13], 1.0 op_sel_hi:[1,0]
	s_nop 0
	v_rcp_f32_e32 v12, v12
	v_rcp_f32_e32 v13, v13
	s_nop 0
	v_pk_mul_f32 v[4:5], v[12:13], v[4:5]
	v_pk_mul_f32 v[12:13], v[128:129], v[32:33]
	s_nop 0
	v_exp_f32_e32 v12, v12
	v_exp_f32_e32 v13, v13
	s_nop 0
	v_pk_add_f32 v[12:13], v[12:13], 1.0 op_sel_hi:[1,0]
	s_nop 0
	v_rcp_f32_e32 v12, v12
	v_rcp_f32_e32 v13, v13
	s_nop 0
	v_pk_mul_f32 v[2:3], v[12:13], v[2:3]
	v_cvt_pk_fp8_f32 v12, v8, v9
	v_cvt_pk_fp8_f32 v12, v6, v7 op_sel:[0,0,1]
	v_cvt_pk_fp8_f32 v7, v4, v5
	ds_bpermute_b32 v6, v92, v12
	v_cvt_pk_fp8_f32 v7, v2, v3 op_sel:[0,0,1]
	v_add_u32_e32 v2, 0xb0, v93
	v_mad_i64_i32 v[2:3], s[10:11], v2, s9, v[10:11]
	ds_bpermute_b32 v7, v92, v7
	v_lshl_add_u64 v[0:1], v[2:3], 0, v[0:1]
	s_waitcnt lgkmcnt(0)
	global_store_dwordx2 v[0:1], v[6:7], off
	s_cbranch_vccnz .LBB0_1303
	s_andn2_b64 vcc, exec, s[20:21]
	s_cbranch_vccnz .LBB0_1302
	s_barrier
	s_branch .LBB0_1302

.LBB0_1372:
	v_readlane_b32 s16, v253, 6
	v_readlane_b32 s18, v253, 8
	v_readlane_b32 s19, v253, 9
	s_mov_b64 s[10:11], s[18:19]
	s_cmp_gt_i32 s10, s2
	v_readlane_b32 s17, v253, 7
	s_cbranch_scc1 .LBB0_1450
	s_cmp_gt_i32 s3, 0
	s_cselect_b64 s[2:3], -1, 0
	s_and_b64 s[0:1], s[0:1], s[2:3]
	s_andn2_b64 vcc, exec, s[0:1]
	s_cbranch_vccnz .LBB0_1394
	v_readlane_b32 s0, v253, 2
	v_readlane_b32 s1, v253, 3
	v_mbcnt_lo_u32_b32 v0, -1, 0
	v_mbcnt_hi_u32_b32 v0, -1, v0
	s_lshl_b32 s2, s27, 3
	v_or_b32_e32 v0, s33, v0
	v_readlane_b32 s10, v255, 14
	s_cmp_ge_i32 s10, s2
	v_readfirstlane_b32 s9, v0
	v_readlane_b32 s11, v255, 15
	s_cbranch_scc1 .LBB0_1394
	v_bfe_i32 v3, v0, 27, 1
	v_lshlrev_b32_e32 v1, 4, v0
	v_lshrrev_b32_e32 v3, 22, v3
	v_add_u32_e32 v3, v1, v3
	v_and_b32_e32 v3, 0xfffffc00, v3
	v_sub_u32_e32 v3, v1, v3
	v_ashrrev_i32_e32 v2, 31, v0
	v_lshrrev_b32_e32 v4, 4, v3
	v_lshrrev_b32_e32 v2, 26, v2
	v_bitop3_b32 v4, v4, v3, 32 bitop3:0x6c
	v_ashrrev_i32_e32 v3, 31, v3
	v_add_u32_e32 v2, v0, v2
	v_lshrrev_b32_e32 v3, 26, v3
	v_ashrrev_i32_e32 v2, 6, v2
	v_add_u32_e32 v3, v4, v3
	v_lshlrev_b32_e32 v5, 3, v2
	v_ashrrev_i32_e32 v3, 6, v3
	v_and_b32_e32 v5, -16, v5
	v_mul_i32_i24_e32 v6, 64, v3
	v_add_u32_e32 v5, v3, v5
	v_sub_u32_e32 v4, v4, v6
	v_lshlrev_b32_e32 v2, 5, v2
	v_ashrrev_i16_sdwa v4, v242, sext(v4) dst_sel:DWORD dst_unused:UNUSED_PAD src0_sel:DWORD src1_sel:BYTE_0
	v_lshlrev_b32_e32 v6, 1, v5
	v_lshrrev_b32_e32 v7, 2, v5
	v_and_b32_e32 v3, 3, v3
	s_mov_b32 s12, 0x3fffe0
	v_and_b32_e32 v2, 32, v2
	v_bfe_i32 v4, v4, 0, 16
	v_and_b32_e32 v6, 24, v6
	v_and_b32_e32 v7, 4, v7
	v_and_or_b32 v3, v5, s12, v3
	v_or3_b32 v3, v3, v7, v6
	v_add_lshl_u32 v2, v2, v4, 1
	s_movk_i32 s11, 0x1c00
	v_mad_u64_u32 v[128:129], s[16:17], v5, s11, v[2:3]
	v_add_u32_e32 v1, 0x2000, v1
	v_mad_u32_u24 v129, v3, s11, v2
	v_ashrrev_i32_e32 v2, 31, v1
	v_lshrrev_b32_e32 v2, 22, v2
	v_add_u32_e32 v2, v1, v2
	v_ashrrev_i32_e32 v2, 10, v2
	v_mul_i32_i24_e32 v3, 0x400, v2
	v_sub_u32_e32 v1, v1, v3
	v_lshrrev_b32_e32 v3, 4, v1
	v_bitop3_b32 v1, v3, v1, 32 bitop3:0x6c
	v_ashrrev_i32_e32 v4, 31, v1
	s_load_dwordx2 s[0:1], s[0:1], 0xf8
	v_lshrrev_b32_e32 v4, 26, v4
	v_add_u32_e32 v4, v1, v4
	v_lshlrev_b32_e32 v3, 3, v2
	v_ashrrev_i32_e32 v5, 6, v4
	v_and_b32_e32 v4, 0xc0, v4
	v_and_b32_e32 v3, -16, v3
	v_sub_u32_e32 v1, v1, v4
	v_add_u32_e32 v3, v5, v3
	v_lshlrev_b32_e32 v2, 5, v2
	v_ashrrev_i16_sdwa v1, v242, sext(v1) dst_sel:DWORD dst_unused:UNUSED_PAD src0_sel:DWORD src1_sel:BYTE_0
	s_waitcnt lgkmcnt(0)
	s_add_u32 s3, s0, 0x56100000
	v_and_b32_e32 v2, 32, v2
	v_bfe_i32 v1, v1, 0, 16
	v_lshlrev_b32_e32 v4, 1, v3
	v_lshrrev_b32_e32 v6, 2, v3
	v_and_b32_e32 v5, 3, v5
	s_addc_u32 s13, s1, 0
	v_and_b32_e32 v4, 24, v4
	v_and_b32_e32 v6, 4, v6
	v_and_or_b32 v5, v3, s12, v5
	v_add_lshl_u32 v2, v2, v1, 1
	s_add_u32 s18, s0, 0x27900000
	v_or3_b32 v4, v5, v6, v4
	v_mad_u64_u32 v[130:131], s[16:17], v3, s11, v[2:3]
	s_addc_u32 s19, s1, 0
	v_mad_u32_u24 v131, v4, s11, v2
	s_ashr_i32 s11, s9, 6
	v_readlane_b32 s16, v254, 54
	s_mov_b64 s[84:85], s[28:29]
	s_ashr_i32 s10, s9, 8
	s_lshl_b32 s12, s11, 10
	s_add_i32 s28, s27, 1
	v_readlane_b32 s17, v254, 55
	s_and_b64 s[16:17], s[16:17], exec
	s_cselect_b32 s16, s28, s27
	v_readlane_b32 s17, v255, 0
	s_mul_i32 s16, s16, s17
	v_readlane_b32 s17, v255, 3
	s_add_i32 s16, s16, s17
	s_ashr_i32 s17, s16, 31
	s_lshr_b32 s17, s17, 26
	s_add_i32 s17, s16, s17
	s_ashr_i32 s20, s17, 6
	s_lshl_b32 s20, s20, 3
	s_sub_i32 s21, s27, s20
	s_min_i32 s21, s21, 8
	s_abs_i32 s23, s21
	v_cvt_f32_u32_e32 v1, s23
	s_sub_i32 s29, 0, s23
	s_andn2_b32 s17, s17, 63
	s_sub_i32 s16, s16, s17
	v_rcp_iflag_f32_e32 v1, v1
	s_abs_i32 s22, s16
	s_xor_b32 s17, s16, s21
	s_ashr_i32 s17, s17, 31
	v_mul_f32_e32 v1, 0x4f7ffffe, v1
	v_cvt_u32_f32_e32 v1, v1
	s_nop 0
	v_readfirstlane_b32 s30, v1
	s_mul_i32 s29, s29, s30
	s_mul_hi_u32 s29, s30, s29
	s_add_i32 s30, s30, s29
	s_mul_hi_u32 s29, s22, s30
	s_mul_i32 s30, s29, s23
	s_sub_i32 s22, s22, s30
	s_add_i32 s30, s29, 1
	s_sub_i32 s31, s22, s23
	s_cmp_ge_u32 s22, s23
	s_cselect_b32 s29, s30, s29
	s_cselect_b32 s22, s31, s22
	s_add_i32 s30, s29, 1
	s_cmp_ge_u32 s22, s23
	s_cselect_b32 s22, s30, s29
	s_xor_b32 s22, s22, s17
	s_sub_i32 s78, s22, s17
	s_mul_i32 s17, s78, s21
	s_sub_i32 s16, s16, s17
	s_add_i32 s48, s20, s16
	s_ashr_i32 s49, s48, 31
	s_lshl_b64 s[16:17], s[48:49], 2
	s_add_u32 s16, s0, s16
	s_addc_u32 s17, s1, s17
	global_load_dword v1, v189, s[16:17] offset:768
	s_mul_i32 s21, s48, 0x1c0000
	s_mul_hi_i32 s20, s48, 0x1c0000
	s_waitcnt vmcnt(0)
	v_readfirstlane_b32 s16, v1
	s_lshl_b32 s16, s16, 3
	s_add_i32 s17, s16, s78
	s_mul_hi_i32 s16, s17, 0x1c0000
	s_mul_i32 s17, s17, 0x1c0000
	s_add_u32 s50, s18, s17
	s_addc_u32 s51, s19, s16
	s_add_i32 s29, s12, 0
	s_add_i32 s30, s29, 0x10000
	s_mov_b32 m0, s30
	s_nop 0
	global_load_lds_dwordx4 v129, s[50:51]
	s_add_i32 s31, s29, 0x12000
	s_mov_b32 m0, s31
	s_nop 0
	global_load_lds_dwordx4 v131, s[50:51]
	s_add_u32 s16, s50, 0xe0000
	s_addc_u32 s17, s51, 0
	s_add_i32 s34, s29, 0x14000
	s_mov_b32 m0, s34
	s_nop 0
	global_load_lds_dwordx4 v129, s[16:17]
	s_add_i32 s35, s29, 0x16000
	s_mov_b32 m0, s35
	s_nop 0
	global_load_lds_dwordx4 v131, s[16:17]
	s_add_u32 s52, s3, s21
	s_addc_u32 s53, s13, s20
	s_mov_b32 m0, s29
	s_nop 0
	global_load_lds_dwordx4 v128, s[52:53]
	s_add_i32 s36, s29, 0x2000
	s_mov_b32 m0, s36
	s_nop 0
	global_load_lds_dwordx4 v130, s[52:53]
	s_add_u32 s16, s52, 0xe0000
	s_addc_u32 s17, s53, 0
	s_add_i32 s37, s29, 0x4000
	s_mov_b32 m0, s37
	s_nop 0
	global_load_lds_dwordx4 v128, s[16:17]
	s_add_i32 s65, s29, 0x6000
	s_mov_b32 m0, s65
	s_nop 0
	global_load_lds_dwordx4 v130, s[16:17]
	s_cmp_eq_u32 s10, 1
	s_cselect_b64 s[16:17], -1, 0
	s_cmp_lg_u32 s10, 1
	s_cbranch_scc1 .LBB0_1377
	s_barrier
.LBB0_1377:
	s_add_u32 s20, s0, 0x45900000
	v_and_b32_e32 v1, 48, v0
	v_lshlrev_b32_e32 v2, 6, v0
	s_movk_i32 s12, 0x3c0
	v_lshlrev_b32_e32 v0, 2, v0
	s_addc_u32 s21, s1, 0
	s_lshl_b32 s66, s10, 6
	s_lshl_b32 s10, s10, 13
	v_and_or_b32 v1, v2, s12, v1
	v_and_b32_e32 v0, 32, v0
	v_bitop3_b32 v2, v1, s10, v0 bitop3:0xde
	s_lshl_b32 s10, s11, 5
	s_and_b32 s67, s10, 0x60
	s_lshl_b32 s10, s67, 7
	v_bitop3_b32 v0, s10, v1, v0 bitop3:0xf6
	s_add_u32 s10, s50, 0x80
	s_waitcnt vmcnt(2)
	s_barrier
	s_addc_u32 s11, s51, 0
	s_add_i32 s68, s29, 0x18000
	s_mov_b32 m0, s68
	s_nop 0
	global_load_lds_dwordx4 v129, s[10:11]
	s_add_i32 s69, s29, 0x1a000
	s_mov_b32 m0, s69
	s_nop 0
	global_load_lds_dwordx4 v131, s[10:11]
	s_add_u32 s10, s52, 0x80
	s_addc_u32 s11, s53, 0
	s_add_i32 s70, s29, 0x8000
	s_mov_b32 m0, s70
	s_nop 0
	global_load_lds_dwordx4 v128, s[10:11]
	s_add_i32 s71, s29, 0xa000
	s_mov_b32 m0, s71
	s_nop 0
	global_load_lds_dwordx4 v130, s[10:11]
	s_add_u32 s10, s50, 0xe0080
	s_addc_u32 s11, s51, 0
	s_add_i32 s72, s29, 0x1c000
	s_mov_b32 m0, s72
	s_nop 0
	global_load_lds_dwordx4 v129, s[10:11]
	s_add_i32 s74, s29, 0x1e000
	s_mov_b32 m0, s74
	s_nop 0
	global_load_lds_dwordx4 v131, s[10:11]
	s_waitcnt vmcnt(6)
	s_add_i32 s75, s29, 0xc000
	s_cmpk_lt_u32 s9, 0x100
	s_mov_b32 s76, 0
	s_cselect_b64 s[22:23], -1, 0
	v_add_u32_e32 v134, 0, v0
	v_add_u32_e32 v135, 0, v2
	s_barrier
	s_branch .LBB0_1380

.LBB0_1387:
	s_cmp_gt_u32 s12, 53
	s_cselect_b64 s[56:57], -1, 0
	s_and_b64 vcc, s[56:57], exec
	s_cselect_b32 s56, 0xffffffca, 2
	s_add_i32 s56, s56, s12
	s_ashr_i32 s57, s56, 31
	s_lshl_b64 s[56:57], s[56:57], 7
	s_add_u32 s58, s52, s56
	s_addc_u32 s59, s53, s57
	s_add_u32 s62, s50, s56
	s_addc_u32 s63, s51, s57
	s_cmp_gt_u32 s12, 52
	s_cselect_b32 s56, 0xffffffcb, 3
	s_add_i32 s56, s56, s12
	s_ashr_i32 s57, s56, 31
	s_lshl_b64 s[56:57], s[56:57], 7
	s_add_u32 s79, s52, s56
	s_addc_u32 s80, s53, s57
	s_add_u32 s81, s50, s56
	s_mov_b32 s56, s12
	v_add_u32_e32 v132, 0x10000, v134
	ds_read_b128 v[136:139], v132
	ds_read_b128 v[140:143], v132 offset:1024
	ds_read_b128 v[144:147], v132 offset:2048
	ds_read_b128 v[148:151], v132 offset:3072
	v_add_u32_e32 v132, 0x14000, v134
	ds_read_b128 v[152:155], v132
	ds_read_b128 v[156:159], v132 offset:1024
	ds_read_b128 v[160:163], v132 offset:2048
	ds_read_b128 v[164:167], v132 offset:3072
	s_addc_u32 s82, s51, s57
	s_cmp_eq_u32 s12, 54
	s_cselect_b32 s61, s45, s59
	s_cselect_b32 s60, s44, s58
	s_cselect_b32 s63, s47, s63
	s_cselect_b32 s62, s46, s62
	s_cselect_b32 s57, s49, s80
	s_cselect_b32 s56, s9, s79
	s_cselect_b32 s59, s11, s82
	s_cselect_b32 s58, s10, s81
	ds_read_b128 v[168:171], v135
	ds_read_b128 v[172:175], v135 offset:1024
	ds_read_b128 v[176:179], v135 offset:2048
	ds_read_b128 v[180:183], v135 offset:3072
	ds_read_b128 v[190:193], v135 offset:4096
	ds_read_b128 v[194:197], v135 offset:5120
	ds_read_b128 v[198:201], v135 offset:6144
	ds_read_b128 v[202:205], v135 offset:7168
	s_add_u32 s80, s54, 0xe0080
	s_addc_u32 s81, s55, 0
	s_mov_b32 m0, s75
	s_nop 0
	global_load_lds_dwordx4 v128, s[80:81]
	s_add_i32 s79, s29, 0xe000
	s_mov_b32 m0, s79
	s_nop 0
	global_load_lds_dwordx4 v130, s[80:81]
	s_setprio 1
	s_waitcnt vmcnt(8)
	s_waitcnt lgkmcnt(0)
	s_barrier
	v_mfma_f32_16x16x128_f8f6f4 v[124:127], v[136:143], v[168:175], v[124:127]
	v_mfma_f32_16x16x128_f8f6f4 v[120:123], v[144:151], v[168:175], v[120:123]
	v_mfma_f32_16x16x128_f8f6f4 v[108:111], v[136:143], v[176:183], v[108:111]
	v_mfma_f32_16x16x128_f8f6f4 v[104:107], v[144:151], v[176:183], v[104:107]
	v_mfma_f32_16x16x128_f8f6f4 v[184:187], v[136:143], v[190:197], v[92:95]
	v_mfma_f32_16x16x128_f8f6f4 v[206:209], v[144:151], v[190:197], v[88:91]
	v_mfma_f32_16x16x128_f8f6f4 v[210:213], v[136:143], v[198:205], v[76:79]
	v_mfma_f32_16x16x128_f8f6f4 v[214:217], v[144:151], v[198:205], v[72:75]
	v_mfma_f32_16x16x128_f8f6f4 v[116:119], v[152:159], v[168:175], v[116:119]
	v_mfma_f32_16x16x128_f8f6f4 v[112:115], v[160:167], v[168:175], v[112:115]
	v_mfma_f32_16x16x128_f8f6f4 v[100:103], v[152:159], v[176:183], v[100:103]
	v_mfma_f32_16x16x128_f8f6f4 v[96:99], v[160:167], v[176:183], v[96:99]
	v_mfma_f32_16x16x128_f8f6f4 v[168:171], v[152:159], v[190:197], v[84:87]
	v_mfma_f32_16x16x128_f8f6f4 v[172:175], v[160:167], v[190:197], v[80:83]
	v_mfma_f32_16x16x128_f8f6f4 v[176:179], v[152:159], v[198:205], v[68:71]
	v_mfma_f32_16x16x128_f8f6f4 v[180:183], v[160:167], v[198:205], v[64:67]
	s_barrier
	s_setprio 0
	s_nop 4
	ds_read_b128 v[64:67], v135 offset:16384
	ds_read_b128 v[68:71], v135 offset:17408
	ds_read_b128 v[72:75], v135 offset:18432
	ds_read_b128 v[76:79], v135 offset:19456
	ds_read_b128 v[80:83], v135 offset:20480
	ds_read_b128 v[84:87], v135 offset:21504
	ds_read_b128 v[88:91], v135 offset:22528
	ds_read_b128 v[92:95], v135 offset:23552
	s_mov_b32 m0, s30
	s_nop 0
	global_load_lds_dwordx4 v129, s[62:63]
	s_nop 0
	s_mov_b32 m0, s31
	s_nop 0
	global_load_lds_dwordx4 v131, s[62:63]
	s_add_u32 s62, s62, 0xe0000
	s_addc_u32 s63, s63, 0
	s_mov_b32 m0, s34
	s_nop 0
	global_load_lds_dwordx4 v129, s[62:63]
	s_nop 0
	s_mov_b32 m0, s35
	s_nop 0
	global_load_lds_dwordx4 v131, s[62:63]
	s_mov_b32 m0, s29
	s_nop 0
	global_load_lds_dwordx4 v128, s[60:61]
	s_nop 0
	s_mov_b32 m0, s36
	s_nop 0
	global_load_lds_dwordx4 v130, s[60:61]
	s_setprio 1
	s_waitcnt vmcnt(8)
	s_waitcnt lgkmcnt(0)
	s_barrier
	v_mfma_f32_16x16x128_f8f6f4 v[60:63], v[136:143], v[64:71], v[60:63]
	v_mfma_f32_16x16x128_f8f6f4 v[56:59], v[144:151], v[64:71], v[56:59]
	v_mfma_f32_16x16x128_f8f6f4 v[190:193], v[136:143], v[72:79], v[44:47]
	v_mfma_f32_16x16x128_f8f6f4 v[194:197], v[144:151], v[72:79], v[40:43]
	v_mfma_f32_16x16x128_f8f6f4 v[198:201], v[136:143], v[80:87], v[28:31]
	v_mfma_f32_16x16x128_f8f6f4 v[202:205], v[144:151], v[80:87], v[24:27]
	v_mfma_f32_16x16x128_f8f6f4 v[218:221], v[136:143], v[88:95], v[12:15]
	v_mfma_f32_16x16x128_f8f6f4 v[222:225], v[144:151], v[88:95], v[8:11]
	v_mfma_f32_16x16x128_f8f6f4 v[52:55], v[152:159], v[64:71], v[52:55]
	v_mfma_f32_16x16x128_f8f6f4 v[48:51], v[160:167], v[64:71], v[48:51]
	v_mfma_f32_16x16x128_f8f6f4 v[226:229], v[152:159], v[72:79], v[36:39]
	v_mfma_f32_16x16x128_f8f6f4 v[230:233], v[160:167], v[72:79], v[32:35]
	v_mfma_f32_16x16x128_f8f6f4 v[238:241], v[152:159], v[80:87], v[20:23]
	v_mfma_f32_16x16x128_f8f6f4 v[244:247], v[160:167], v[80:87], v[16:19]
	v_mfma_f32_16x16x128_f8f6f4 v[248:251], v[152:159], v[88:95], v[4:7]
	v_mfma_f32_16x16x128_f8f6f4 v[234:237], v[160:167], v[88:95], v[0:3]
	s_barrier
	s_setprio 0
	v_add_u32_e32 v8, 0x18000, v134
	s_nop 3
	ds_read_b128 v[0:3], v8
	ds_read_b128 v[4:7], v8 offset:1024
	ds_read_b128 v[16:19], v8 offset:2048
	ds_read_b128 v[20:23], v8 offset:3072
	v_add_u32_e32 v8, 0x1c000, v134
	ds_read_b128 v[136:139], v8
	ds_read_b128 v[140:143], v8 offset:1024
	ds_read_b128 v[144:147], v8 offset:2048
	ds_read_b128 v[148:151], v8 offset:3072
	ds_read_b128 v[8:11], v135 offset:32768
	ds_read_b128 v[12:15], v135 offset:33792
	ds_read_b128 v[24:27], v135 offset:34816
	ds_read_b128 v[28:31], v135 offset:35840
	ds_read_b128 v[32:35], v135 offset:36864
	ds_read_b128 v[36:39], v135 offset:37888
	ds_read_b128 v[40:43], v135 offset:38912
	ds_read_b128 v[44:47], v135 offset:39936
	s_add_u32 s60, s60, 0xe0000
	s_addc_u32 s61, s61, 0
	s_mov_b32 m0, s37
	s_nop 0
	global_load_lds_dwordx4 v128, s[60:61]
	s_nop 0
	s_mov_b32 m0, s65
	s_nop 0
	global_load_lds_dwordx4 v130, s[60:61]
	s_setprio 1
	s_waitcnt vmcnt(8)
	s_waitcnt lgkmcnt(0)
	s_barrier
	v_mfma_f32_16x16x128_f8f6f4 v[124:127], v[0:7], v[8:15], v[124:127]
	v_mfma_f32_16x16x128_f8f6f4 v[120:123], v[16:23], v[8:15], v[120:123]
	v_mfma_f32_16x16x128_f8f6f4 v[108:111], v[0:7], v[24:31], v[108:111]
	v_mfma_f32_16x16x128_f8f6f4 v[104:107], v[16:23], v[24:31], v[104:107]
	v_mfma_f32_16x16x128_f8f6f4 v[92:95], v[0:7], v[32:39], v[184:187]
	v_mfma_f32_16x16x128_f8f6f4 v[88:91], v[16:23], v[32:39], v[206:209]
	v_mfma_f32_16x16x128_f8f6f4 v[76:79], v[0:7], v[40:47], v[210:213]
	v_mfma_f32_16x16x128_f8f6f4 v[72:75], v[16:23], v[40:47], v[214:217]
	v_mfma_f32_16x16x128_f8f6f4 v[116:119], v[136:143], v[8:15], v[116:119]
	v_mfma_f32_16x16x128_f8f6f4 v[112:115], v[144:151], v[8:15], v[112:115]
	v_mfma_f32_16x16x128_f8f6f4 v[100:103], v[136:143], v[24:31], v[100:103]
	v_mfma_f32_16x16x128_f8f6f4 v[96:99], v[144:151], v[24:31], v[96:99]
	v_mfma_f32_16x16x128_f8f6f4 v[84:87], v[136:143], v[32:39], v[168:171]
	v_mfma_f32_16x16x128_f8f6f4 v[80:83], v[144:151], v[32:39], v[172:175]
	v_mfma_f32_16x16x128_f8f6f4 v[68:71], v[136:143], v[40:47], v[176:179]
	v_mfma_f32_16x16x128_f8f6f4 v[64:67], v[144:151], v[40:47], v[180:183]
	s_barrier
	s_setprio 0
	ds_read_b128 v[32:35], v135 offset:49152
	ds_read_b128 v[36:39], v135 offset:50176
	ds_read_b128 v[152:155], v135 offset:51200
	ds_read_b128 v[156:159], v135 offset:52224
	ds_read_b128 v[160:163], v135 offset:53248
	ds_read_b128 v[164:167], v135 offset:54272
	ds_read_b128 v[168:171], v135 offset:55296
	ds_read_b128 v[172:175], v135 offset:56320
	s_mov_b32 m0, s68
	s_nop 0
	global_load_lds_dwordx4 v129, s[58:59]
	s_nop 0
	s_mov_b32 m0, s69
	s_nop 0
	global_load_lds_dwordx4 v131, s[58:59]
	s_add_u32 s58, s58, 0xe0000
	s_addc_u32 s59, s59, 0
	s_mov_b32 m0, s72
	s_nop 0
	global_load_lds_dwordx4 v129, s[58:59]
	s_nop 0
	s_mov_b32 m0, s74
	s_nop 0
	global_load_lds_dwordx4 v131, s[58:59]
	s_mov_b32 m0, s70
	s_nop 0
	global_load_lds_dwordx4 v128, s[56:57]
	s_nop 0
	s_mov_b32 m0, s71
	s_nop 0
	global_load_lds_dwordx4 v130, s[56:57]
	s_setprio 1
	s_waitcnt vmcnt(8)
	s_waitcnt lgkmcnt(0)
	s_barrier
	v_mfma_f32_16x16x128_f8f6f4 v[60:63], v[0:7], v[32:39], v[60:63]
	v_mfma_f32_16x16x128_f8f6f4 v[56:59], v[16:23], v[32:39], v[56:59]
	v_mfma_f32_16x16x128_f8f6f4 v[44:47], v[0:7], v[152:159], v[190:193]
	v_mfma_f32_16x16x128_f8f6f4 v[40:43], v[16:23], v[152:159], v[194:197]
	v_mfma_f32_16x16x128_f8f6f4 v[28:31], v[0:7], v[160:167], v[198:201]
	v_mfma_f32_16x16x128_f8f6f4 v[24:27], v[16:23], v[160:167], v[202:205]
	v_mfma_f32_16x16x128_f8f6f4 v[12:15], v[0:7], v[168:175], v[218:221]
	v_mfma_f32_16x16x128_f8f6f4 v[8:11], v[16:23], v[168:175], v[222:225]
	v_mfma_f32_16x16x128_f8f6f4 v[52:55], v[136:143], v[32:39], v[52:55]
	v_mfma_f32_16x16x128_f8f6f4 v[48:51], v[144:151], v[32:39], v[48:51]
	v_mfma_f32_16x16x128_f8f6f4 v[36:39], v[136:143], v[152:159], v[226:229]
	v_mfma_f32_16x16x128_f8f6f4 v[32:35], v[144:151], v[152:159], v[230:233]
	v_mfma_f32_16x16x128_f8f6f4 v[20:23], v[136:143], v[160:167], v[238:241]
	v_mfma_f32_16x16x128_f8f6f4 v[16:19], v[144:151], v[160:167], v[244:247]
	v_mfma_f32_16x16x128_f8f6f4 v[4:7], v[136:143], v[168:175], v[248:251]
	v_mfma_f32_16x16x128_f8f6f4 v[0:3], v[144:151], v[168:175], v[234:237]
	s_barrier
	s_setprio 0
	s_add_i32 s12, s12, 2
	s_add_u32 s54, s54, 0x100
	s_addc_u32 s55, s55, 0
	s_cbranch_vccz .LBB0_1387
	s_and_b64 vcc, exec, s[22:23]
	s_cbranch_vccz .LBB0_1390
	s_barrier

.LBB0_1459:
	v_readlane_b32 s0, v254, 44
	v_readlane_b32 s1, v254, 45
	s_andn2_b64 vcc, exec, s[0:1]
	s_cbranch_vccnz .LBB0_1476
	v_readlane_b32 s0, v253, 2
	v_readlane_b32 s1, v253, 3
	s_load_dwordx2 s[16:17], s[0:1], 0xf8
	v_mov_b32_e32 v0, 0x1000
	v_readlane_b32 s0, v254, 46
	v_readlane_b32 s1, v254, 47
	s_waitcnt lgkmcnt(0)
	global_load_dword v1, v0, s[16:17] offset:8 sc1
	global_load_dword v2, v0, s[16:17] offset:12 sc1
	global_load_dwordx2 v[4:5], v0, s[16:17] offset:64 sc1
	v_mbcnt_lo_u32_b32 v0, -1, 0
	v_mbcnt_hi_u32_b32 v0, -1, v0
	s_andn2_b64 vcc, exec, s[0:1]
	v_or_b32_e32 v0, s33, v0
	s_waitcnt vmcnt(0)
	v_readfirstlane_b32 s20, v4
	v_readfirstlane_b32 s21, v5
	v_readfirstlane_b32 s9, v0
	s_cbranch_vccnz .LBB0_1476
	v_bfe_i32 v5, v0, 27, 1
	v_lshlrev_b32_e32 v3, 4, v0
	v_lshrrev_b32_e32 v5, 22, v5
	v_add_u32_e32 v5, v3, v5
	v_and_b32_e32 v5, 0xfffffc00, v5
	v_sub_u32_e32 v5, v3, v5
	v_ashrrev_i32_e32 v4, 31, v0
	v_lshrrev_b32_e32 v6, 4, v5
	v_lshrrev_b32_e32 v4, 26, v4
	v_bitop3_b32 v6, v6, v5, 32 bitop3:0x6c
	v_ashrrev_i32_e32 v5, 31, v5
	v_add_u32_e32 v4, v0, v4
	v_lshrrev_b32_e32 v5, 26, v5
	v_ashrrev_i32_e32 v4, 6, v4
	v_add_u32_e32 v5, v6, v5
	v_lshlrev_b32_e32 v7, 3, v4
	v_ashrrev_i32_e32 v5, 6, v5
	v_and_b32_e32 v7, -16, v7
	v_mul_i32_i24_e32 v8, 64, v5
	v_add_u32_e32 v7, v5, v7
	v_sub_u32_e32 v6, v6, v8
	v_lshlrev_b32_e32 v4, 5, v4
	v_ashrrev_i16_sdwa v6, v242, sext(v6) dst_sel:DWORD dst_unused:UNUSED_PAD src0_sel:DWORD src1_sel:BYTE_0
	v_lshlrev_b32_e32 v8, 1, v7
	v_lshrrev_b32_e32 v9, 2, v7
	v_and_b32_e32 v5, 3, v5
	s_mov_b32 s0, 0x1fffe0
	v_and_b32_e32 v4, 32, v4
	v_bfe_i32 v6, v6, 0, 16
	v_and_b32_e32 v8, 24, v8
	v_and_b32_e32 v9, 4, v9
	v_and_or_b32 v5, v7, s0, v5
	v_or3_b32 v5, v5, v9, v8
	v_add_lshl_u32 v4, v4, v6, 1
	v_add_u32_e32 v3, 0x2000, v3
	v_lshl_add_u32 v132, v7, 11, v4
	v_lshl_add_u32 v133, v5, 11, v4
	v_ashrrev_i32_e32 v4, 31, v3
	v_lshrrev_b32_e32 v4, 22, v4
	v_add_u32_e32 v4, v3, v4
	v_ashrrev_i32_e32 v4, 10, v4
	v_mul_i32_i24_e32 v5, 0x400, v4
	v_sub_u32_e32 v3, v3, v5
	v_lshrrev_b32_e32 v5, 4, v3
	v_bitop3_b32 v3, v5, v3, 32 bitop3:0x6c
	v_ashrrev_i32_e32 v6, 31, v3
	s_add_u32 s2, s16, 0x19900000
	v_lshrrev_b32_e32 v6, 26, v6
	s_addc_u32 s3, s17, 0
	v_lshlrev_b32_e32 v5, 3, v4
	v_add_u32_e32 v6, v3, v6
	s_add_u32 s13, s16, 0x7700000
	v_and_b32_e32 v5, -16, v5
	v_ashrrev_i32_e32 v7, 6, v6
	s_addc_u32 s18, s17, 0
	v_add_u32_e32 v5, v7, v5
	v_and_b32_e32 v6, 0xc0, v6
	v_and_b32_e32 v7, 3, v7
	s_ashr_i32 s11, s9, 6
	s_ashr_i32 s10, s9, 8
	v_sub_u32_e32 v3, v3, v6
	v_and_or_b32 v7, v5, s0, v7
	s_lshl_b32 s0, s11, 10
	v_readlane_b32 s22, v255, 5
	v_lshlrev_b32_e32 v4, 5, v4
	v_ashrrev_i16_sdwa v3, v242, sext(v3) dst_sel:DWORD dst_unused:UNUSED_PAD src0_sel:DWORD src1_sel:BYTE_0
	v_lshlrev_b32_e32 v6, 1, v5
	v_lshrrev_b32_e32 v8, 2, v5
	v_readlane_b32 s23, v255, 6
	s_add_u32 s48, s13, s22
	v_and_b32_e32 v4, 32, v4
	v_bfe_i32 v3, v3, 0, 16
	v_and_b32_e32 v6, 24, v6
	v_and_b32_e32 v8, 4, v8
	s_addc_u32 s49, s18, s23
	s_add_i32 s19, s0, 0
	v_or3_b32 v6, v7, v8, v6
	v_add_lshl_u32 v3, v4, v3, 1
	s_add_i32 s27, s19, 0x10000
	s_mov_b32 m0, s27
	s_nop 0
	global_load_lds_dwordx4 v133, s[48:49]
	s_mov_b64 s[84:85], s[28:29]
	v_lshl_add_u32 v135, v6, 11, v3
	s_add_i32 s28, s19, 0x12000
	s_mov_b32 m0, s28
	s_nop 0
	global_load_lds_dwordx4 v135, s[48:49]
	s_add_u32 s0, s48, 0x40000
	s_addc_u32 s1, s49, 0
	s_add_i32 s29, s19, 0x14000
	s_mov_b32 m0, s29
	s_nop 0
	global_load_lds_dwordx4 v133, s[0:1]
	s_add_i32 s30, s19, 0x16000
	s_mov_b32 m0, s30
	s_nop 0
	global_load_lds_dwordx4 v135, s[0:1]
	v_readlane_b32 s0, v255, 12
	v_readlane_b32 s1, v255, 13
	s_add_u32 s50, s2, s0
	s_addc_u32 s51, s3, s1
	s_mov_b32 m0, s19
	s_nop 0
	global_load_lds_dwordx4 v132, s[50:51]
	v_lshl_add_u32 v134, v5, 11, v3
	s_add_i32 s31, s19, 0x2000
	s_mov_b32 m0, s31
	s_nop 0
	global_load_lds_dwordx4 v134, s[50:51]
	s_add_u32 s0, s50, 0x40000
	s_addc_u32 s1, s51, 0
	s_add_i32 s34, s19, 0x4000
	s_mov_b32 m0, s34
	s_nop 0
	global_load_lds_dwordx4 v132, s[0:1]
	s_add_i32 s35, s19, 0x6000
	s_mov_b32 m0, s35
	s_nop 0
	global_load_lds_dwordx4 v134, s[0:1]
	s_cmp_eq_u32 s10, 1
	s_cselect_b64 s[0:1], -1, 0
	s_cmp_lg_u32 s10, 1
	s_cbranch_scc1 .LBB0_1463
	s_barrier
.LBB0_1463:
	s_flbit_i32_b32 s12, s21
	s_min_u32 s12, s12, 32
	s_lshl_b64 s[20:21], s[20:21], s12
	s_min_u32 s20, s20, 1
	v_fmac_f32_e32 v2, 0x40880000, v1
	s_or_b32 s20, s21, s20
	v_max_f32_e32 v1, 0xda24260, v2
	v_cvt_f32_u32_e32 v2, s20
	s_sub_i32 s12, 32, s12
	v_mul_f32_e32 v1, 0x3c010204, v1
	s_add_u32 s16, s16, 0x45900000
	v_ldexp_f32 v2, v2, s12
	v_mul_f32_e32 v2, 0x2f800000, v2
	s_mov_b32 s12, 0x4a300000
	v_div_scale_f32 v3, s[20:21], s12, s12, v2
	v_rcp_f32_e32 v4, v3
	s_addc_u32 s17, s17, 0
	s_lshl_b32 s36, s10, 6
	s_lshl_b32 s10, s10, 13
	v_fma_f32 v5, -v3, v4, 1.0
	v_fmac_f32_e32 v4, v5, v4
	v_div_scale_f32 v5, vcc, v2, s12, v2
	v_mul_f32_e32 v6, v5, v4
	v_fma_f32 v7, -v3, v6, v5
	v_fmac_f32_e32 v6, v7, v4
	v_fma_f32 v3, -v3, v6, v5
	v_div_fmas_f32 v3, v3, v4, v6
	v_div_fixup_f32 v2, v3, s12, v2
	s_mov_b32 s12, 0xf800000
	v_cmp_gt_f32_e32 vcc, s12, v2
	v_mul_f32_e32 v3, 0x4f800000, v2
	s_movk_i32 s12, 0x3c0
	v_cndmask_b32_e32 v2, v2, v3, vcc
	v_sqrt_f32_e32 v3, v2
	s_waitcnt vmcnt(2)
	s_barrier
	s_mov_b32 s70, 0
	v_add_u32_e32 v4, -1, v3
	v_fma_f32 v5, -v4, v3, v2
	v_cmp_ge_f32_e64 s[40:41], 0, v5
	v_add_u32_e32 v5, 1, v3
	v_readlane_b32 s71, v255, 4
	v_cndmask_b32_e64 v4, v3, v4, s[40:41]
	v_fma_f32 v3, -v5, v3, v2
	v_cmp_lt_f32_e64 s[40:41], 0, v3
	s_nop 1
	v_cndmask_b32_e64 v3, v4, v5, s[40:41]
	v_mul_f32_e32 v4, 0x37800000, v3
	v_cndmask_b32_e32 v3, v3, v4, vcc
	v_cmp_class_f32_e32 vcc, v2, v250
	s_nop 1
	v_cndmask_b32_e32 v2, v3, v2, vcc
	v_mul_f32_e32 v2, 0x40880000, v2
	v_max_f32_e32 v2, 0xda24260, v2
	v_mul_f32_e32 v2, 0x3c010204, v2
	v_mul_f32_e32 v1, v1, v2
	v_and_b32_e32 v2, 48, v0
	v_lshlrev_b32_e32 v3, 6, v0
	v_lshlrev_b32_e32 v0, 2, v0
	v_and_or_b32 v2, v3, s12, v2
	v_and_b32_e32 v0, 32, v0
	v_bitop3_b32 v3, v2, s10, v0 bitop3:0xde
	s_lshl_b32 s10, s11, 5
	s_and_b32 s37, s10, 0x60
	s_lshl_b32 s10, s37, 7
	v_bitop3_b32 v0, s10, v2, v0 bitop3:0xf6
	s_add_u32 s10, s48, 0x80
	s_addc_u32 s11, s49, 0
	s_add_i32 s62, s19, 0x18000
	s_mov_b32 m0, s62
	s_nop 0
	global_load_lds_dwordx4 v133, s[10:11]
	s_add_i32 s63, s19, 0x1a000
	s_mov_b32 m0, s63
	s_nop 0
	global_load_lds_dwordx4 v135, s[10:11]
	s_add_u32 s10, s50, 0x80
	s_addc_u32 s11, s51, 0
	s_add_i32 s65, s19, 0x8000
	s_mov_b32 m0, s65
	s_nop 0
	global_load_lds_dwordx4 v132, s[10:11]
	s_add_i32 s66, s19, 0xa000
	s_mov_b32 m0, s66
	s_nop 0
	global_load_lds_dwordx4 v134, s[10:11]
	s_add_u32 s10, s48, 0x40080
	s_addc_u32 s11, s49, 0
	s_add_i32 s67, s19, 0x1c000
	s_mov_b32 m0, s67
	s_nop 0
	global_load_lds_dwordx4 v133, s[10:11]
	s_add_i32 s68, s19, 0x1e000
	s_mov_b32 m0, s68
	s_nop 0
	global_load_lds_dwordx4 v135, s[10:11]
	s_waitcnt vmcnt(6)
	s_add_i32 s69, s19, 0xc000
	s_cmpk_lt_u32 s9, 0x100
	v_mul_f32_e32 v128, 0xbfb8aa3b, v1
	v_mul_f32_e32 v130, v1, v1
	v_readlane_b32 s10, v255, 10
	s_cselect_b64 s[20:21], -1, 0
	v_mov_b32_e32 v129, v128
	v_mov_b32_e32 v131, v130
	v_add_u32_e32 v136, 0, v0
	v_add_u32_e32 v137, 0, v3
	s_mov_b32 s72, s10
	s_barrier
	v_readlane_b32 s11, v255, 11
	s_branch .LBB0_1466

.LBB0_1469:
	s_cmp_gt_u32 s76, 13
	s_cselect_b64 s[54:55], -1, 0
	s_and_b64 vcc, s[54:55], exec
	s_cselect_b32 s54, -14, 2
	s_add_i32 s54, s54, s76
	s_ashr_i32 s55, s54, 31
	s_lshl_b64 s[54:55], s[54:55], 7
	s_add_u32 s56, s50, s54
	s_addc_u32 s57, s51, s55
	s_add_u32 s60, s48, s54
	s_addc_u32 s61, s49, s55
	s_cmp_gt_u32 s76, 12
	s_cselect_b32 s54, -13, 3
	s_add_i32 s54, s54, s76
	s_ashr_i32 s55, s54, 31
	s_lshl_b64 s[54:55], s[54:55], 7
	s_add_u32 s77, s50, s54
	s_addc_u32 s78, s51, s55
	s_add_u32 s79, s48, s54
	s_mov_b32 s54, s76
	v_add_u32_e32 v150, 0x10000, v136
	v_add_u32_e32 v166, 0x14000, v136
	ds_read_b128 v[138:141], v150
	ds_read_b128 v[142:145], v150 offset:1024
	ds_read_b128 v[146:149], v150 offset:2048
	ds_read_b128 v[150:153], v150 offset:3072
	ds_read_b128 v[154:157], v166
	ds_read_b128 v[158:161], v166 offset:1024
	ds_read_b128 v[162:165], v166 offset:2048
	ds_read_b128 v[166:169], v166 offset:3072
	s_addc_u32 s80, s49, s55
	s_cmp_eq_u32 s76, 14
	s_cselect_b32 s59, s23, s57
	s_cselect_b32 s58, s74, s56
	s_cselect_b32 s61, s41, s61
	s_cselect_b32 s60, s9, s60
	s_cselect_b32 s55, s11, s78
	s_cselect_b32 s54, s10, s77
	s_cselect_b32 s57, s75, s80
	s_cselect_b32 s56, s12, s79
	ds_read_b128 v[170:173], v137
	ds_read_b128 v[174:177], v137 offset:1024
	ds_read_b128 v[178:181], v137 offset:2048
	ds_read_b128 v[182:185], v137 offset:3072
	ds_read_b128 v[190:193], v137 offset:4096
	ds_read_b128 v[194:197], v137 offset:5120
	ds_read_b128 v[198:201], v137 offset:6144
	ds_read_b128 v[202:205], v137 offset:7168
	s_add_u32 s78, s52, 0x40080
	s_addc_u32 s79, s53, 0
	s_mov_b32 m0, s69
	s_nop 0
	global_load_lds_dwordx4 v132, s[78:79]
	s_add_i32 s77, s19, 0xe000
	s_mov_b32 m0, s77
	s_nop 0
	global_load_lds_dwordx4 v134, s[78:79]
	s_setprio 1
	s_waitcnt vmcnt(8)
	s_waitcnt lgkmcnt(0)
	s_barrier
	v_mfma_i32_16x16x64_i8 v[124:127], v[138:141], v[170:173], v[124:127]
	v_mfma_i32_16x16x64_i8 v[120:123], v[146:149], v[170:173], v[120:123]
	v_mfma_i32_16x16x64_i8 v[116:119], v[138:141], v[178:181], v[116:119]
	v_mfma_i32_16x16x64_i8 v[112:115], v[146:149], v[178:181], v[112:115]
	v_mfma_i32_16x16x64_i8 v[108:111], v[138:141], v[190:193], v[108:111]
	v_mfma_i32_16x16x64_i8 v[104:107], v[146:149], v[190:193], v[104:107]
	v_mfma_i32_16x16x64_i8 v[100:103], v[138:141], v[198:201], v[100:103]
	v_mfma_i32_16x16x64_i8 v[96:99], v[146:149], v[198:201], v[96:99]
	v_mfma_i32_16x16x64_i8 v[124:127], v[142:145], v[174:177], v[124:127]
	v_mfma_i32_16x16x64_i8 v[120:123], v[150:153], v[174:177], v[120:123]
	v_mfma_i32_16x16x64_i8 v[116:119], v[142:145], v[182:185], v[116:119]
	v_mfma_i32_16x16x64_i8 v[112:115], v[150:153], v[182:185], v[112:115]
	v_mfma_i32_16x16x64_i8 v[108:111], v[142:145], v[194:197], v[108:111]
	v_mfma_i32_16x16x64_i8 v[104:107], v[150:153], v[194:197], v[104:107]
	v_mfma_i32_16x16x64_i8 v[100:103], v[142:145], v[202:205], v[100:103]
	v_mfma_i32_16x16x64_i8 v[96:99], v[150:153], v[202:205], v[96:99]
	v_mfma_i32_16x16x64_i8 v[92:95], v[154:157], v[170:173], v[92:95]
	v_mfma_i32_16x16x64_i8 v[88:91], v[162:165], v[170:173], v[88:91]
	v_mfma_i32_16x16x64_i8 v[84:87], v[154:157], v[178:181], v[84:87]
	v_mfma_i32_16x16x64_i8 v[80:83], v[162:165], v[178:181], v[80:83]
	v_mfma_i32_16x16x64_i8 v[76:79], v[154:157], v[190:193], v[76:79]
	v_mfma_i32_16x16x64_i8 v[72:75], v[162:165], v[190:193], v[72:75]
	v_mfma_i32_16x16x64_i8 v[68:71], v[154:157], v[198:201], v[68:71]
	v_mfma_i32_16x16x64_i8 v[64:67], v[162:165], v[198:201], v[64:67]
	v_mfma_i32_16x16x64_i8 v[92:95], v[158:161], v[174:177], v[92:95]
	v_mfma_i32_16x16x64_i8 v[88:91], v[166:169], v[174:177], v[88:91]
	v_mfma_i32_16x16x64_i8 v[84:87], v[158:161], v[182:185], v[84:87]
	v_mfma_i32_16x16x64_i8 v[80:83], v[166:169], v[182:185], v[80:83]
	v_mfma_i32_16x16x64_i8 v[76:79], v[158:161], v[194:197], v[76:79]
	v_mfma_i32_16x16x64_i8 v[72:75], v[166:169], v[194:197], v[72:75]
	v_mfma_i32_16x16x64_i8 v[68:71], v[158:161], v[202:205], v[68:71]
	v_mfma_i32_16x16x64_i8 v[64:67], v[166:169], v[202:205], v[64:67]
	s_barrier
	s_setprio 0
	ds_read_b128 v[170:173], v137 offset:16384
	ds_read_b128 v[174:177], v137 offset:17408
	ds_read_b128 v[178:181], v137 offset:18432
	ds_read_b128 v[182:185], v137 offset:19456
	ds_read_b128 v[190:193], v137 offset:20480
	ds_read_b128 v[194:197], v137 offset:21504
	ds_read_b128 v[198:201], v137 offset:22528
	ds_read_b128 v[202:205], v137 offset:23552
	s_mov_b32 m0, s27
	s_nop 0
	global_load_lds_dwordx4 v133, s[60:61]
	s_nop 0
	s_mov_b32 m0, s28
	s_nop 0
	global_load_lds_dwordx4 v135, s[60:61]
	s_add_u32 s60, s60, 0x40000
	s_addc_u32 s61, s61, 0
	s_mov_b32 m0, s29
	s_nop 0
	global_load_lds_dwordx4 v133, s[60:61]
	s_nop 0
	s_mov_b32 m0, s30
	s_nop 0
	global_load_lds_dwordx4 v135, s[60:61]
	s_mov_b32 m0, s19
	s_nop 0
	global_load_lds_dwordx4 v132, s[58:59]
	s_nop 0
	s_mov_b32 m0, s31
	s_nop 0
	global_load_lds_dwordx4 v134, s[58:59]
	s_setprio 1
	s_waitcnt vmcnt(8)
	s_waitcnt lgkmcnt(0)
	s_barrier
	v_mfma_i32_16x16x64_i8 v[60:63], v[138:141], v[170:173], v[60:63]
	v_mfma_i32_16x16x64_i8 v[56:59], v[146:149], v[170:173], v[56:59]
	v_mfma_i32_16x16x64_i8 v[52:55], v[138:141], v[178:181], v[52:55]
	v_mfma_i32_16x16x64_i8 v[48:51], v[146:149], v[178:181], v[48:51]
	v_mfma_i32_16x16x64_i8 v[44:47], v[138:141], v[190:193], v[44:47]
	v_mfma_i32_16x16x64_i8 v[40:43], v[146:149], v[190:193], v[40:43]
	v_mfma_i32_16x16x64_i8 v[36:39], v[138:141], v[198:201], v[36:39]
	v_mfma_i32_16x16x64_i8 v[32:35], v[146:149], v[198:201], v[32:35]
	v_mfma_i32_16x16x64_i8 v[60:63], v[142:145], v[174:177], v[60:63]
	v_mfma_i32_16x16x64_i8 v[56:59], v[150:153], v[174:177], v[56:59]
	v_mfma_i32_16x16x64_i8 v[52:55], v[142:145], v[182:185], v[52:55]
	v_mfma_i32_16x16x64_i8 v[48:51], v[150:153], v[182:185], v[48:51]
	v_mfma_i32_16x16x64_i8 v[44:47], v[142:145], v[194:197], v[44:47]
	v_mfma_i32_16x16x64_i8 v[40:43], v[150:153], v[194:197], v[40:43]
	v_mfma_i32_16x16x64_i8 v[36:39], v[142:145], v[202:205], v[36:39]
	v_mfma_i32_16x16x64_i8 v[32:35], v[150:153], v[202:205], v[32:35]
	v_mfma_i32_16x16x64_i8 v[28:31], v[154:157], v[170:173], v[28:31]
	v_mfma_i32_16x16x64_i8 v[24:27], v[162:165], v[170:173], v[24:27]
	v_mfma_i32_16x16x64_i8 v[20:23], v[154:157], v[178:181], v[20:23]
	v_mfma_i32_16x16x64_i8 v[16:19], v[162:165], v[178:181], v[16:19]
	v_mfma_i32_16x16x64_i8 v[12:15], v[154:157], v[190:193], v[12:15]
	v_mfma_i32_16x16x64_i8 v[8:11], v[162:165], v[190:193], v[8:11]
	v_mfma_i32_16x16x64_i8 v[4:7], v[154:157], v[198:201], v[4:7]
	v_mfma_i32_16x16x64_i8 v[0:3], v[162:165], v[198:201], v[0:3]
	v_mfma_i32_16x16x64_i8 v[28:31], v[158:161], v[174:177], v[28:31]
	v_mfma_i32_16x16x64_i8 v[24:27], v[166:169], v[174:177], v[24:27]
	v_mfma_i32_16x16x64_i8 v[20:23], v[158:161], v[182:185], v[20:23]
	v_mfma_i32_16x16x64_i8 v[16:19], v[166:169], v[182:185], v[16:19]
	v_mfma_i32_16x16x64_i8 v[12:15], v[158:161], v[194:197], v[12:15]
	v_mfma_i32_16x16x64_i8 v[8:11], v[166:169], v[194:197], v[8:11]
	v_mfma_i32_16x16x64_i8 v[4:7], v[158:161], v[202:205], v[4:7]
	v_mfma_i32_16x16x64_i8 v[0:3], v[166:169], v[202:205], v[0:3]
	s_barrier
	s_setprio 0
	v_add_u32_e32 v150, 0x18000, v136
	v_add_u32_e32 v166, 0x1c000, v136
	ds_read_b128 v[138:141], v150
	ds_read_b128 v[142:145], v150 offset:1024
	ds_read_b128 v[146:149], v150 offset:2048
	ds_read_b128 v[150:153], v150 offset:3072
	ds_read_b128 v[154:157], v166
	ds_read_b128 v[158:161], v166 offset:1024
	ds_read_b128 v[162:165], v166 offset:2048
	ds_read_b128 v[166:169], v166 offset:3072
	ds_read_b128 v[170:173], v137 offset:32768
	ds_read_b128 v[174:177], v137 offset:33792
	ds_read_b128 v[178:181], v137 offset:34816
	ds_read_b128 v[182:185], v137 offset:35840
	ds_read_b128 v[190:193], v137 offset:36864
	ds_read_b128 v[194:197], v137 offset:37888
	ds_read_b128 v[198:201], v137 offset:38912
	ds_read_b128 v[202:205], v137 offset:39936
	s_add_u32 s58, s58, 0x40000
	s_addc_u32 s59, s59, 0
	s_mov_b32 m0, s34
	s_nop 0
	global_load_lds_dwordx4 v132, s[58:59]
	s_nop 0
	s_mov_b32 m0, s35
	s_nop 0
	global_load_lds_dwordx4 v134, s[58:59]
	s_setprio 1
	s_waitcnt vmcnt(8)
	s_waitcnt lgkmcnt(0)
	s_barrier
	v_mfma_i32_16x16x64_i8 v[124:127], v[138:141], v[170:173], v[124:127]
	v_mfma_i32_16x16x64_i8 v[120:123], v[146:149], v[170:173], v[120:123]
	v_mfma_i32_16x16x64_i8 v[116:119], v[138:141], v[178:181], v[116:119]
	v_mfma_i32_16x16x64_i8 v[112:115], v[146:149], v[178:181], v[112:115]
	v_mfma_i32_16x16x64_i8 v[108:111], v[138:141], v[190:193], v[108:111]
	v_mfma_i32_16x16x64_i8 v[104:107], v[146:149], v[190:193], v[104:107]
	v_mfma_i32_16x16x64_i8 v[100:103], v[138:141], v[198:201], v[100:103]
	v_mfma_i32_16x16x64_i8 v[96:99], v[146:149], v[198:201], v[96:99]
	v_mfma_i32_16x16x64_i8 v[124:127], v[142:145], v[174:177], v[124:127]
	v_mfma_i32_16x16x64_i8 v[120:123], v[150:153], v[174:177], v[120:123]
	v_mfma_i32_16x16x64_i8 v[116:119], v[142:145], v[182:185], v[116:119]
	v_mfma_i32_16x16x64_i8 v[112:115], v[150:153], v[182:185], v[112:115]
	v_mfma_i32_16x16x64_i8 v[108:111], v[142:145], v[194:197], v[108:111]
	v_mfma_i32_16x16x64_i8 v[104:107], v[150:153], v[194:197], v[104:107]
	v_mfma_i32_16x16x64_i8 v[100:103], v[142:145], v[202:205], v[100:103]
	v_mfma_i32_16x16x64_i8 v[96:99], v[150:153], v[202:205], v[96:99]
	v_mfma_i32_16x16x64_i8 v[92:95], v[154:157], v[170:173], v[92:95]
	v_mfma_i32_16x16x64_i8 v[88:91], v[162:165], v[170:173], v[88:91]
	v_mfma_i32_16x16x64_i8 v[84:87], v[154:157], v[178:181], v[84:87]
	v_mfma_i32_16x16x64_i8 v[80:83], v[162:165], v[178:181], v[80:83]
	v_mfma_i32_16x16x64_i8 v[76:79], v[154:157], v[190:193], v[76:79]
	v_mfma_i32_16x16x64_i8 v[72:75], v[162:165], v[190:193], v[72:75]
	v_mfma_i32_16x16x64_i8 v[68:71], v[154:157], v[198:201], v[68:71]
	v_mfma_i32_16x16x64_i8 v[64:67], v[162:165], v[198:201], v[64:67]
	v_mfma_i32_16x16x64_i8 v[92:95], v[158:161], v[174:177], v[92:95]
	v_mfma_i32_16x16x64_i8 v[88:91], v[166:169], v[174:177], v[88:91]
	v_mfma_i32_16x16x64_i8 v[84:87], v[158:161], v[182:185], v[84:87]
	v_mfma_i32_16x16x64_i8 v[80:83], v[166:169], v[182:185], v[80:83]
	v_mfma_i32_16x16x64_i8 v[76:79], v[158:161], v[194:197], v[76:79]
	v_mfma_i32_16x16x64_i8 v[72:75], v[166:169], v[194:197], v[72:75]
	v_mfma_i32_16x16x64_i8 v[68:71], v[158:161], v[202:205], v[68:71]
	v_mfma_i32_16x16x64_i8 v[64:67], v[166:169], v[202:205], v[64:67]
	s_barrier
	s_setprio 0
	ds_read_b128 v[170:173], v137 offset:49152
	ds_read_b128 v[174:177], v137 offset:50176
	ds_read_b128 v[178:181], v137 offset:51200
	ds_read_b128 v[182:185], v137 offset:52224
	ds_read_b128 v[190:193], v137 offset:53248
	ds_read_b128 v[194:197], v137 offset:54272
	ds_read_b128 v[198:201], v137 offset:55296
	ds_read_b128 v[202:205], v137 offset:56320
	s_mov_b32 m0, s62
	s_nop 0
	global_load_lds_dwordx4 v133, s[56:57]
	s_nop 0
	s_mov_b32 m0, s63
	s_nop 0
	global_load_lds_dwordx4 v135, s[56:57]
	s_add_u32 s56, s56, 0x40000
	s_addc_u32 s57, s57, 0
	s_mov_b32 m0, s67
	s_nop 0
	global_load_lds_dwordx4 v133, s[56:57]
	s_nop 0
	s_mov_b32 m0, s68
	s_nop 0
	global_load_lds_dwordx4 v135, s[56:57]
	s_mov_b32 m0, s65
	s_nop 0
	global_load_lds_dwordx4 v132, s[54:55]
	s_nop 0
	s_mov_b32 m0, s66
	s_nop 0
	global_load_lds_dwordx4 v134, s[54:55]
	s_setprio 1
	s_waitcnt vmcnt(8)
	s_waitcnt lgkmcnt(0)
	s_barrier
	v_mfma_i32_16x16x64_i8 v[60:63], v[138:141], v[170:173], v[60:63]
	v_mfma_i32_16x16x64_i8 v[56:59], v[146:149], v[170:173], v[56:59]
	v_mfma_i32_16x16x64_i8 v[52:55], v[138:141], v[178:181], v[52:55]
	v_mfma_i32_16x16x64_i8 v[48:51], v[146:149], v[178:181], v[48:51]
	v_mfma_i32_16x16x64_i8 v[44:47], v[138:141], v[190:193], v[44:47]
	v_mfma_i32_16x16x64_i8 v[40:43], v[146:149], v[190:193], v[40:43]
	v_mfma_i32_16x16x64_i8 v[36:39], v[138:141], v[198:201], v[36:39]
	v_mfma_i32_16x16x64_i8 v[32:35], v[146:149], v[198:201], v[32:35]
	v_mfma_i32_16x16x64_i8 v[60:63], v[142:145], v[174:177], v[60:63]
	v_mfma_i32_16x16x64_i8 v[56:59], v[150:153], v[174:177], v[56:59]
	v_mfma_i32_16x16x64_i8 v[52:55], v[142:145], v[182:185], v[52:55]
	v_mfma_i32_16x16x64_i8 v[48:51], v[150:153], v[182:185], v[48:51]
	v_mfma_i32_16x16x64_i8 v[44:47], v[142:145], v[194:197], v[44:47]
	v_mfma_i32_16x16x64_i8 v[40:43], v[150:153], v[194:197], v[40:43]
	v_mfma_i32_16x16x64_i8 v[36:39], v[142:145], v[202:205], v[36:39]
	v_mfma_i32_16x16x64_i8 v[32:35], v[150:153], v[202:205], v[32:35]
	v_mfma_i32_16x16x64_i8 v[28:31], v[154:157], v[170:173], v[28:31]
	v_mfma_i32_16x16x64_i8 v[24:27], v[162:165], v[170:173], v[24:27]
	v_mfma_i32_16x16x64_i8 v[20:23], v[154:157], v[178:181], v[20:23]
	v_mfma_i32_16x16x64_i8 v[16:19], v[162:165], v[178:181], v[16:19]
	v_mfma_i32_16x16x64_i8 v[12:15], v[154:157], v[190:193], v[12:15]
	v_mfma_i32_16x16x64_i8 v[8:11], v[162:165], v[190:193], v[8:11]
	v_mfma_i32_16x16x64_i8 v[4:7], v[154:157], v[198:201], v[4:7]
	v_mfma_i32_16x16x64_i8 v[0:3], v[162:165], v[198:201], v[0:3]
	v_mfma_i32_16x16x64_i8 v[28:31], v[158:161], v[174:177], v[28:31]
	v_mfma_i32_16x16x64_i8 v[24:27], v[166:169], v[174:177], v[24:27]
	v_mfma_i32_16x16x64_i8 v[20:23], v[158:161], v[182:185], v[20:23]
	v_mfma_i32_16x16x64_i8 v[16:19], v[166:169], v[182:185], v[16:19]
	v_mfma_i32_16x16x64_i8 v[12:15], v[158:161], v[194:197], v[12:15]
	v_mfma_i32_16x16x64_i8 v[8:11], v[166:169], v[194:197], v[8:11]
	v_mfma_i32_16x16x64_i8 v[4:7], v[158:161], v[202:205], v[4:7]
	v_mfma_i32_16x16x64_i8 v[0:3], v[166:169], v[202:205], v[0:3]
	s_barrier
	s_setprio 0
	s_add_i32 s76, s76, 2
	s_add_u32 s52, s52, 0x100
	s_addc_u32 s53, s53, 0
	s_cbranch_vccz .LBB0_1469
	s_and_b64 vcc, exec, s[20:21]
	s_cbranch_vccz .LBB0_1472
	s_barrier
.LBB0_1472:
	v_cvt_f32_i32_e32 v124, v124
	v_cvt_f32_i32_e32 v125, v125
	v_cvt_f32_i32_e32 v140, v88
	v_cvt_f32_i32_e32 v88, v86
	v_cvt_f32_i32_e32 v86, v80
	v_cvt_f32_i32_e32 v80, v78
	v_cvt_f32_i32_e32 v78, v72
	v_cvt_f32_i32_e32 v72, v70
	v_cvt_f32_i32_e32 v70, v64
	v_cvt_f32_i32_e32 v64, v60
	v_cvt_f32_i32_e32 v60, v56
	v_cvt_f32_i32_e32 v56, v52
	v_cvt_f32_i32_e32 v52, v48
	v_cvt_f32_i32_e32 v48, v44
	v_cvt_f32_i32_e32 v44, v40
	v_cvt_f32_i32_e32 v40, v36
	v_cvt_f32_i32_e32 v36, v32
	v_cvt_f32_i32_e32 v32, v34
	v_cvt_f32_i32_e32 v34, v30
	v_cvt_f32_i32_e32 v30, v24
	v_cvt_f32_i32_e32 v24, v22
	v_cvt_f32_i32_e32 v22, v16
	v_cvt_f32_i32_e32 v16, v14
	v_cvt_f32_i32_e32 v14, v8
	v_cvt_f32_i32_e32 v8, v4
	v_cvt_f32_i32_e32 v4, v0
	v_mbcnt_lo_u32_b32 v0, -1, 0
	v_mbcnt_hi_u32_b32 v0, -1, v0
	s_lshl_b32 s9, s72, 8
	v_cvt_f32_i32_e32 v141, v89
	v_cvt_f32_i32_e32 v89, v87
	v_cvt_f32_i32_e32 v87, v81
	v_cvt_f32_i32_e32 v81, v79
	v_cvt_f32_i32_e32 v79, v73
	v_cvt_f32_i32_e32 v73, v71
	v_cvt_f32_i32_e32 v71, v65
	v_cvt_f32_i32_e32 v65, v61
	v_cvt_f32_i32_e32 v61, v57
	v_cvt_f32_i32_e32 v57, v53
	v_cvt_f32_i32_e32 v53, v49
	v_cvt_f32_i32_e32 v49, v45
	v_cvt_f32_i32_e32 v45, v41
	v_cvt_f32_i32_e32 v41, v37
	v_cvt_f32_i32_e32 v37, v33
	v_cvt_f32_i32_e32 v33, v35
	v_cvt_f32_i32_e32 v35, v31
	v_cvt_f32_i32_e32 v31, v25
	v_cvt_f32_i32_e32 v25, v23
	v_cvt_f32_i32_e32 v23, v17
	v_cvt_f32_i32_e32 v17, v15
	v_cvt_f32_i32_e32 v15, v9
	v_cvt_f32_i32_e32 v9, v5
	v_cvt_f32_i32_e32 v5, v1
	s_add_i32 s9, s9, s36
	v_ashrrev_i32_e32 v1, 2, v0
	v_cvt_f32_i32_e32 v139, v121
	v_cvt_f32_i32_e32 v121, v117
	v_cvt_f32_i32_e32 v117, v113
	v_cvt_f32_i32_e32 v113, v109
	v_cvt_f32_i32_e32 v109, v105
	v_cvt_f32_i32_e32 v105, v101
	v_cvt_f32_i32_e32 v101, v97
	v_cvt_f32_i32_e32 v97, v99
	v_cvt_f32_i32_e32 v99, v93
	v_cvt_f32_i32_e32 v142, v90
	v_cvt_f32_i32_e32 v90, v84
	v_cvt_f32_i32_e32 v84, v82
	v_cvt_f32_i32_e32 v82, v76
	v_cvt_f32_i32_e32 v76, v74
	v_cvt_f32_i32_e32 v74, v68
	v_cvt_f32_i32_e32 v68, v66
	v_cvt_f32_i32_e32 v66, v28
	v_cvt_f32_i32_e32 v28, v26
	v_cvt_f32_i32_e32 v26, v20
	v_cvt_f32_i32_e32 v20, v18
	v_cvt_f32_i32_e32 v18, v12
	v_cvt_f32_i32_e32 v12, v10
	v_and_b32_e32 v10, 3, v0
	v_and_b32_e32 v0, -4, v0
	v_add_u32_e32 v93, s9, v1
	s_lshl_b32 s9, s71, 7
	v_cvt_f32_i32_e32 v138, v120
	v_cvt_f32_i32_e32 v120, v116
	v_cvt_f32_i32_e32 v116, v112
	v_cvt_f32_i32_e32 v112, v108
	v_cvt_f32_i32_e32 v108, v104
	v_cvt_f32_i32_e32 v104, v100
	v_cvt_f32_i32_e32 v100, v96
	v_cvt_f32_i32_e32 v96, v98
	v_cvt_f32_i32_e32 v98, v92
	v_cvt_f32_i32_e32 v143, v91
	v_cvt_f32_i32_e32 v91, v85
	v_cvt_f32_i32_e32 v85, v83
	v_cvt_f32_i32_e32 v83, v77
	v_cvt_f32_i32_e32 v77, v75
	v_cvt_f32_i32_e32 v75, v69
	v_cvt_f32_i32_e32 v69, v67
	v_cvt_f32_i32_e32 v67, v29
	v_cvt_f32_i32_e32 v29, v27
	v_cvt_f32_i32_e32 v27, v21
	v_cvt_f32_i32_e32 v21, v19
	v_cvt_f32_i32_e32 v19, v13
	v_cvt_f32_i32_e32 v13, v11
	v_lshl_add_u32 v92, v10, 6, v0
	v_lshl_or_b32 v0, v10, 3, s9
	v_pk_mul_f32 v[10:11], v[128:129], v[124:125]
	v_cvt_f32_i32_e32 v126, v126
	v_exp_f32_e32 v10, v10
	v_exp_f32_e32 v11, v11
	v_cvt_f32_i32_e32 v127, v127
	v_pk_mul_f32 v[124:125], v[130:131], v[124:125]
	v_cvt_f32_i32_e32 v94, v94
	v_pk_add_f32 v[10:11], v[10:11], 1.0 op_sel_hi:[1,0]
	v_pk_mul_f32 v[98:99], v[124:125], v[98:99]
	v_rcp_f32_e32 v10, v10
	v_rcp_f32_e32 v11, v11
	v_cvt_f32_i32_e32 v95, v95
	v_pk_mul_f32 v[124:125], v[130:131], v[126:127]
	v_cvt_f32_i32_e32 v122, v122
	v_pk_mul_f32 v[10:11], v[10:11], v[98:99]
	v_pk_mul_f32 v[98:99], v[128:129], v[126:127]
	v_pk_mul_f32 v[94:95], v[124:125], v[94:95]
	v_exp_f32_e32 v98, v98
	v_exp_f32_e32 v99, v99
	v_cvt_f32_i32_e32 v123, v123
	v_pk_mul_f32 v[124:125], v[130:131], v[138:139]
	v_or_b32_e32 v0, s37, v0
	v_pk_add_f32 v[98:99], v[98:99], 1.0 op_sel_hi:[1,0]
	v_pk_mul_f32 v[124:125], v[124:125], v[140:141]
	v_rcp_f32_e32 v98, v98
	v_rcp_f32_e32 v99, v99
	s_movk_i32 s9, 0x1600
	v_ashrrev_i32_e32 v1, 31, v0
	v_cvt_f32_i32_e32 v118, v118
	v_pk_mul_f32 v[94:95], v[98:99], v[94:95]
	v_pk_mul_f32 v[98:99], v[128:129], v[138:139]
	v_cvt_f32_i32_e32 v119, v119
	v_exp_f32_e32 v98, v98
	v_exp_f32_e32 v99, v99
	v_cvt_f32_i32_e32 v114, v114
	v_cvt_f32_i32_e32 v115, v115
	v_cvt_f32_i32_e32 v110, v110
	v_pk_add_f32 v[98:99], v[98:99], 1.0 op_sel_hi:[1,0]
	v_cvt_f32_i32_e32 v111, v111
	v_rcp_f32_e32 v98, v98
	v_rcp_f32_e32 v99, v99
	v_cvt_f32_i32_e32 v106, v106
	v_cvt_f32_i32_e32 v107, v107
	v_cvt_f32_i32_e32 v102, v102
	v_pk_mul_f32 v[98:99], v[98:99], v[124:125]
	v_pk_mul_f32 v[124:125], v[128:129], v[122:123]
	v_pk_mul_f32 v[122:123], v[130:131], v[122:123]
	v_exp_f32_e32 v124, v124
	v_exp_f32_e32 v125, v125
	v_pk_mul_f32 v[122:123], v[122:123], v[142:143]
	v_cvt_f32_i32_e32 v103, v103
	v_cvt_f32_i32_e32 v62, v62
	v_pk_add_f32 v[124:125], v[124:125], 1.0 op_sel_hi:[1,0]
	v_cvt_f32_i32_e32 v63, v63
	v_rcp_f32_e32 v124, v124
	v_rcp_f32_e32 v125, v125
	v_cvt_f32_i32_e32 v58, v58
	v_cvt_f32_i32_e32 v59, v59
	v_cvt_f32_i32_e32 v54, v54
	v_pk_mul_f32 v[122:123], v[124:125], v[122:123]
	v_cvt_pk_fp8_f32 v124, v10, v11
	v_cvt_pk_fp8_f32 v10, v98, v99
	v_cvt_f32_i32_e32 v55, v55
	v_cvt_pk_fp8_f32 v124, v94, v95 op_sel:[0,0,1]
	v_cvt_f32_i32_e32 v50, v50
	v_cvt_pk_fp8_f32 v10, v122, v123 op_sel:[0,0,1]
	v_cvt_f32_i32_e32 v51, v51
	ds_bpermute_b32 v94, v92, v124
	v_cvt_f32_i32_e32 v46, v46
	ds_bpermute_b32 v95, v92, v10
	v_mov_b64_e32 v[10:11], s[16:17]
	v_mad_i64_i32 v[98:99], s[10:11], v93, s9, v[10:11]
	v_lshl_add_u64 v[98:99], v[98:99], 0, v[0:1]
	s_waitcnt lgkmcnt(0)
	global_store_dwordx2 v[98:99], v[94:95], off
	v_pk_mul_f32 v[94:95], v[128:129], v[120:121]
	v_pk_mul_f32 v[98:99], v[130:131], v[120:121]
	v_exp_f32_e32 v94, v94
	v_exp_f32_e32 v95, v95
	v_pk_mul_f32 v[90:91], v[98:99], v[90:91]
	v_pk_mul_f32 v[98:99], v[130:131], v[118:119]
	v_cvt_f32_i32_e32 v47, v47
	v_pk_add_f32 v[94:95], v[94:95], 1.0 op_sel_hi:[1,0]
	v_pk_mul_f32 v[88:89], v[98:99], v[88:89]
	v_rcp_f32_e32 v94, v94
	v_rcp_f32_e32 v95, v95
	v_pk_mul_f32 v[98:99], v[130:131], v[116:117]
	v_cvt_f32_i32_e32 v42, v42
	v_pk_mul_f32 v[86:87], v[98:99], v[86:87]
	v_pk_mul_f32 v[90:91], v[94:95], v[90:91]
	v_pk_mul_f32 v[94:95], v[128:129], v[118:119]
	v_pk_mul_f32 v[98:99], v[130:131], v[114:115]
	v_exp_f32_e32 v94, v94
	v_exp_f32_e32 v95, v95
	v_pk_mul_f32 v[84:85], v[98:99], v[84:85]
	v_cvt_f32_i32_e32 v43, v43
	v_cvt_f32_i32_e32 v38, v38
	v_pk_add_f32 v[94:95], v[94:95], 1.0 op_sel_hi:[1,0]
	v_cvt_f32_i32_e32 v39, v39
	v_rcp_f32_e32 v94, v94
	v_rcp_f32_e32 v95, v95
	v_cvt_f32_i32_e32 v6, v6
	v_cvt_f32_i32_e32 v7, v7
	v_cvt_f32_i32_e32 v2, v2
	v_pk_mul_f32 v[88:89], v[94:95], v[88:89]
	v_pk_mul_f32 v[94:95], v[128:129], v[116:117]
	v_cvt_f32_i32_e32 v3, v3
	v_exp_f32_e32 v94, v94
	v_exp_f32_e32 v95, v95
	s_mov_b64 s[48:49], -1
	s_andn2_b64 vcc, exec, s[42:43]
	v_pk_add_f32 v[94:95], v[94:95], 1.0 op_sel_hi:[1,0]
	s_nop 0
	v_rcp_f32_e32 v94, v94
	v_rcp_f32_e32 v95, v95
	s_nop 0
	v_pk_mul_f32 v[86:87], v[94:95], v[86:87]
	v_pk_mul_f32 v[94:95], v[128:129], v[114:115]
	s_nop 0
	v_exp_f32_e32 v94, v94
	v_exp_f32_e32 v95, v95
	s_nop 0
	v_pk_add_f32 v[94:95], v[94:95], 1.0 op_sel_hi:[1,0]
	s_nop 0
	v_rcp_f32_e32 v94, v94
	v_rcp_f32_e32 v95, v95
	s_nop 0
	v_pk_mul_f32 v[84:85], v[94:95], v[84:85]
	v_cvt_pk_fp8_f32 v94, v90, v91
	v_cvt_pk_fp8_f32 v94, v88, v89 op_sel:[0,0,1]
	v_cvt_pk_fp8_f32 v89, v86, v87
	v_pk_mul_f32 v[86:87], v[130:131], v[112:113]
	ds_bpermute_b32 v88, v92, v94
	v_pk_mul_f32 v[82:83], v[86:87], v[82:83]
	v_cvt_pk_fp8_f32 v89, v84, v85 op_sel:[0,0,1]
	v_add_u32_e32 v84, 16, v93
	v_mad_i64_i32 v[84:85], s[10:11], v84, s9, v[10:11]
	ds_bpermute_b32 v89, v92, v89
	v_lshl_add_u64 v[84:85], v[84:85], 0, v[0:1]
	v_pk_mul_f32 v[86:87], v[130:131], v[110:111]
	s_waitcnt lgkmcnt(0)
	global_store_dwordx2 v[84:85], v[88:89], off
	v_pk_mul_f32 v[84:85], v[128:129], v[112:113]
	v_pk_mul_f32 v[80:81], v[86:87], v[80:81]
	v_exp_f32_e32 v84, v84
	v_exp_f32_e32 v85, v85
	v_pk_mul_f32 v[86:87], v[130:131], v[108:109]
	v_pk_add_f32 v[84:85], v[84:85], 1.0 op_sel_hi:[1,0]
	s_nop 0
	v_rcp_f32_e32 v84, v84
	v_rcp_f32_e32 v85, v85
	v_pk_mul_f32 v[78:79], v[86:87], v[78:79]
	v_pk_mul_f32 v[86:87], v[130:131], v[106:107]
	v_pk_mul_f32 v[82:83], v[84:85], v[82:83]
	v_pk_mul_f32 v[84:85], v[128:129], v[110:111]
	v_pk_mul_f32 v[76:77], v[86:87], v[76:77]
	v_exp_f32_e32 v84, v84
	v_exp_f32_e32 v85, v85
	s_nop 0
	v_pk_add_f32 v[84:85], v[84:85], 1.0 op_sel_hi:[1,0]
	s_nop 0
	v_rcp_f32_e32 v84, v84
	v_rcp_f32_e32 v85, v85
	s_nop 0
	v_pk_mul_f32 v[80:81], v[84:85], v[80:81]
	v_pk_mul_f32 v[84:85], v[128:129], v[108:109]
	s_nop 0
	v_exp_f32_e32 v84, v84
	v_exp_f32_e32 v85, v85
	s_nop 0
	v_pk_add_f32 v[84:85], v[84:85], 1.0 op_sel_hi:[1,0]
	s_nop 0
	v_rcp_f32_e32 v84, v84
	v_rcp_f32_e32 v85, v85
	s_nop 0
	v_pk_mul_f32 v[78:79], v[84:85], v[78:79]
	v_pk_mul_f32 v[84:85], v[128:129], v[106:107]
	s_nop 0
	v_exp_f32_e32 v84, v84
	v_exp_f32_e32 v85, v85
	s_nop 0
	v_pk_add_f32 v[84:85], v[84:85], 1.0 op_sel_hi:[1,0]
	s_nop 0
	v_rcp_f32_e32 v84, v84
	v_rcp_f32_e32 v85, v85
	s_nop 0
	v_pk_mul_f32 v[76:77], v[84:85], v[76:77]
	v_cvt_pk_fp8_f32 v84, v82, v83
	v_cvt_pk_fp8_f32 v84, v80, v81 op_sel:[0,0,1]
	v_cvt_pk_fp8_f32 v81, v78, v79
	v_pk_mul_f32 v[78:79], v[130:131], v[104:105]
	ds_bpermute_b32 v80, v92, v84
	v_pk_mul_f32 v[74:75], v[78:79], v[74:75]
	v_cvt_pk_fp8_f32 v81, v76, v77 op_sel:[0,0,1]
	v_add_u32_e32 v76, 32, v93
	v_mad_i64_i32 v[76:77], s[10:11], v76, s9, v[10:11]
	ds_bpermute_b32 v81, v92, v81
	v_lshl_add_u64 v[76:77], v[76:77], 0, v[0:1]
	v_pk_mul_f32 v[78:79], v[130:131], v[102:103]
	s_waitcnt lgkmcnt(0)
	global_store_dwordx2 v[76:77], v[80:81], off
	v_pk_mul_f32 v[76:77], v[128:129], v[104:105]
	v_pk_mul_f32 v[72:73], v[78:79], v[72:73]
	v_exp_f32_e32 v76, v76
	v_exp_f32_e32 v77, v77
	v_pk_mul_f32 v[78:79], v[130:131], v[100:101]
	v_pk_add_f32 v[76:77], v[76:77], 1.0 op_sel_hi:[1,0]
	s_nop 0
	v_rcp_f32_e32 v76, v76
	v_rcp_f32_e32 v77, v77
	v_pk_mul_f32 v[70:71], v[78:79], v[70:71]
	v_pk_mul_f32 v[78:79], v[130:131], v[96:97]
	v_pk_mul_f32 v[74:75], v[76:77], v[74:75]
	v_pk_mul_f32 v[76:77], v[128:129], v[102:103]
	v_pk_mul_f32 v[68:69], v[78:79], v[68:69]
	v_exp_f32_e32 v76, v76
	v_exp_f32_e32 v77, v77
	s_nop 0
	v_pk_add_f32 v[76:77], v[76:77], 1.0 op_sel_hi:[1,0]
	s_nop 0
	v_rcp_f32_e32 v76, v76
	v_rcp_f32_e32 v77, v77
	s_nop 0
	v_pk_mul_f32 v[72:73], v[76:77], v[72:73]
	v_pk_mul_f32 v[76:77], v[128:129], v[100:101]
	s_nop 0
	v_exp_f32_e32 v76, v76
	v_exp_f32_e32 v77, v77
	s_nop 0
	v_pk_add_f32 v[76:77], v[76:77], 1.0 op_sel_hi:[1,0]
	s_nop 0
	v_rcp_f32_e32 v76, v76
	v_rcp_f32_e32 v77, v77
	s_nop 0
	v_pk_mul_f32 v[70:71], v[76:77], v[70:71]
	v_pk_mul_f32 v[76:77], v[128:129], v[96:97]
	s_nop 0
	v_exp_f32_e32 v76, v76
	v_exp_f32_e32 v77, v77
	s_nop 0
	v_pk_add_f32 v[76:77], v[76:77], 1.0 op_sel_hi:[1,0]
	s_nop 0
	v_rcp_f32_e32 v76, v76
	v_rcp_f32_e32 v77, v77
	s_nop 0
	v_pk_mul_f32 v[68:69], v[76:77], v[68:69]
	v_cvt_pk_fp8_f32 v76, v74, v75
	v_cvt_pk_fp8_f32 v76, v72, v73 op_sel:[0,0,1]
	v_cvt_pk_fp8_f32 v73, v70, v71
	v_add_u32_e32 v70, 0x80, v93
	ds_bpermute_b32 v72, v92, v76
	v_cvt_pk_fp8_f32 v73, v68, v69 op_sel:[0,0,1]
	v_add_u32_e32 v68, 48, v93
	v_mad_i64_i32 v[68:69], s[10:11], v68, s9, v[10:11]
	ds_bpermute_b32 v73, v92, v73
	v_lshl_add_u64 v[68:69], v[68:69], 0, v[0:1]
	s_waitcnt lgkmcnt(0)
	global_store_dwordx2 v[68:69], v[72:73], off
	v_pk_mul_f32 v[68:69], v[128:129], v[64:65]
	v_pk_mul_f32 v[64:65], v[130:131], v[64:65]
	s_nop 0
	v_pk_mul_f32 v[64:65], v[64:65], v[66:67]
	v_exp_f32_e32 v66, v68
	v_exp_f32_e32 v67, v69
	s_nop 0
	v_pk_add_f32 v[66:67], v[66:67], 1.0 op_sel_hi:[1,0]
	s_nop 0
	v_rcp_f32_e32 v66, v66
	v_rcp_f32_e32 v67, v67
	s_nop 0
	v_pk_mul_f32 v[64:65], v[66:67], v[64:65]
	v_pk_mul_f32 v[66:67], v[128:129], v[62:63]
	v_pk_mul_f32 v[62:63], v[130:131], v[62:63]
	s_nop 0
	v_pk_mul_f32 v[34:35], v[62:63], v[34:35]
	v_exp_f32_e32 v62, v66
	v_exp_f32_e32 v63, v67
	s_nop 0
	v_pk_add_f32 v[62:63], v[62:63], 1.0 op_sel_hi:[1,0]
	s_nop 0
	v_rcp_f32_e32 v62, v62
	v_rcp_f32_e32 v63, v63
	s_nop 0
	v_pk_mul_f32 v[34:35], v[62:63], v[34:35]
	v_pk_mul_f32 v[62:63], v[128:129], v[60:61]
	v_pk_mul_f32 v[60:61], v[130:131], v[60:61]
	s_nop 0
	v_pk_mul_f32 v[30:31], v[60:61], v[30:31]
	v_exp_f32_e32 v60, v62
	v_exp_f32_e32 v61, v63
	s_nop 0
	v_pk_add_f32 v[60:61], v[60:61], 1.0 op_sel_hi:[1,0]
	s_nop 0
	v_rcp_f32_e32 v60, v60
	v_rcp_f32_e32 v61, v61
	s_nop 0
	v_pk_mul_f32 v[30:31], v[60:61], v[30:31]
	v_pk_mul_f32 v[60:61], v[128:129], v[58:59]
	v_pk_mul_f32 v[58:59], v[130:131], v[58:59]
	s_nop 0
	v_pk_mul_f32 v[28:29], v[58:59], v[28:29]
	v_exp_f32_e32 v58, v60
	v_exp_f32_e32 v59, v61
	s_nop 0
	v_pk_add_f32 v[58:59], v[58:59], 1.0 op_sel_hi:[1,0]
	s_nop 0
	v_rcp_f32_e32 v58, v58
	v_rcp_f32_e32 v59, v59
	s_nop 0
	v_pk_mul_f32 v[28:29], v[58:59], v[28:29]
	v_cvt_pk_fp8_f32 v58, v64, v65
	v_cvt_pk_fp8_f32 v58, v34, v35 op_sel:[0,0,1]
	v_cvt_pk_fp8_f32 v35, v30, v31
	v_pk_mul_f32 v[30:31], v[130:131], v[56:57]
	ds_bpermute_b32 v34, v92, v58
	v_pk_mul_f32 v[26:27], v[30:31], v[26:27]
	v_cvt_pk_fp8_f32 v35, v28, v29 op_sel:[0,0,1]
	v_mad_i64_i32 v[28:29], s[10:11], v70, s9, v[10:11]
	v_lshl_add_u64 v[28:29], v[28:29], 0, v[0:1]
	ds_bpermute_b32 v35, v92, v35
	v_pk_mul_f32 v[30:31], v[130:131], v[54:55]
	s_waitcnt lgkmcnt(0)
	global_store_dwordx2 v[28:29], v[34:35], off
	v_pk_mul_f32 v[28:29], v[128:129], v[56:57]
	v_pk_mul_f32 v[24:25], v[30:31], v[24:25]
	v_exp_f32_e32 v28, v28
	v_exp_f32_e32 v29, v29
	v_pk_mul_f32 v[30:31], v[130:131], v[52:53]
	v_pk_add_f32 v[28:29], v[28:29], 1.0 op_sel_hi:[1,0]
	s_nop 0
	v_rcp_f32_e32 v28, v28
	v_rcp_f32_e32 v29, v29
	v_pk_mul_f32 v[22:23], v[30:31], v[22:23]
	v_pk_mul_f32 v[30:31], v[130:131], v[50:51]
	v_pk_mul_f32 v[26:27], v[28:29], v[26:27]
	v_pk_mul_f32 v[28:29], v[128:129], v[54:55]
	v_pk_mul_f32 v[20:21], v[30:31], v[20:21]
	v_exp_f32_e32 v28, v28
	v_exp_f32_e32 v29, v29
	s_nop 0
	v_pk_add_f32 v[28:29], v[28:29], 1.0 op_sel_hi:[1,0]
	s_nop 0
	v_rcp_f32_e32 v28, v28
	v_rcp_f32_e32 v29, v29
	s_nop 0
	v_pk_mul_f32 v[24:25], v[28:29], v[24:25]
	v_pk_mul_f32 v[28:29], v[128:129], v[52:53]
	s_nop 0
	v_exp_f32_e32 v28, v28
	v_exp_f32_e32 v29, v29
	s_nop 0
	v_pk_add_f32 v[28:29], v[28:29], 1.0 op_sel_hi:[1,0]
	s_nop 0
	v_rcp_f32_e32 v28, v28
	v_rcp_f32_e32 v29, v29
	s_nop 0
	v_pk_mul_f32 v[22:23], v[28:29], v[22:23]
	v_pk_mul_f32 v[28:29], v[128:129], v[50:51]
	s_nop 0
	v_exp_f32_e32 v28, v28
	v_exp_f32_e32 v29, v29
	s_nop 0
	v_pk_add_f32 v[28:29], v[28:29], 1.0 op_sel_hi:[1,0]
	s_nop 0
	v_rcp_f32_e32 v28, v28
	v_rcp_f32_e32 v29, v29
	s_nop 0
	v_pk_mul_f32 v[20:21], v[28:29], v[20:21]
	v_cvt_pk_fp8_f32 v28, v26, v27
	v_cvt_pk_fp8_f32 v28, v24, v25 op_sel:[0,0,1]
	v_cvt_pk_fp8_f32 v25, v22, v23
	v_pk_mul_f32 v[22:23], v[130:131], v[48:49]
	ds_bpermute_b32 v24, v92, v28
	v_pk_mul_f32 v[18:19], v[22:23], v[18:19]
	v_cvt_pk_fp8_f32 v25, v20, v21 op_sel:[0,0,1]
	v_add_u32_e32 v20, 0x90, v93
	v_mad_i64_i32 v[20:21], s[10:11], v20, s9, v[10:11]
	ds_bpermute_b32 v25, v92, v25
	v_lshl_add_u64 v[20:21], v[20:21], 0, v[0:1]
	v_pk_mul_f32 v[22:23], v[130:131], v[46:47]
	s_waitcnt lgkmcnt(0)
	global_store_dwordx2 v[20:21], v[24:25], off
	v_pk_mul_f32 v[20:21], v[128:129], v[48:49]
	v_pk_mul_f32 v[16:17], v[22:23], v[16:17]
	v_exp_f32_e32 v20, v20
	v_exp_f32_e32 v21, v21
	v_pk_mul_f32 v[22:23], v[130:131], v[44:45]
	v_pk_add_f32 v[20:21], v[20:21], 1.0 op_sel_hi:[1,0]
	s_nop 0
	v_rcp_f32_e32 v20, v20
	v_rcp_f32_e32 v21, v21
	v_pk_mul_f32 v[14:15], v[22:23], v[14:15]
	v_pk_mul_f32 v[22:23], v[130:131], v[42:43]
	v_pk_mul_f32 v[18:19], v[20:21], v[18:19]
	v_pk_mul_f32 v[20:21], v[128:129], v[46:47]
	v_pk_mul_f32 v[12:13], v[22:23], v[12:13]
	v_exp_f32_e32 v20, v20
	v_exp_f32_e32 v21, v21
	s_nop 0
	v_pk_add_f32 v[20:21], v[20:21], 1.0 op_sel_hi:[1,0]
	s_nop 0
	v_rcp_f32_e32 v20, v20
	v_rcp_f32_e32 v21, v21
	s_nop 0
	v_pk_mul_f32 v[16:17], v[20:21], v[16:17]
	v_pk_mul_f32 v[20:21], v[128:129], v[44:45]
	s_nop 0
	v_exp_f32_e32 v20, v20
	v_exp_f32_e32 v21, v21
	s_nop 0
	v_pk_add_f32 v[20:21], v[20:21], 1.0 op_sel_hi:[1,0]
	s_nop 0
	v_rcp_f32_e32 v20, v20
	v_rcp_f32_e32 v21, v21
	s_nop 0
	v_pk_mul_f32 v[14:15], v[20:21], v[14:15]
	v_pk_mul_f32 v[20:21], v[128:129], v[42:43]
	s_nop 0
	v_exp_f32_e32 v20, v20
	v_exp_f32_e32 v21, v21
	s_nop 0
	v_pk_add_f32 v[20:21], v[20:21], 1.0 op_sel_hi:[1,0]
	s_nop 0
	v_rcp_f32_e32 v20, v20
	v_rcp_f32_e32 v21, v21
	s_nop 0
	v_pk_mul_f32 v[12:13], v[20:21], v[12:13]
	v_cvt_pk_fp8_f32 v20, v18, v19
	v_cvt_pk_fp8_f32 v20, v16, v17 op_sel:[0,0,1]
	v_cvt_pk_fp8_f32 v17, v14, v15
	v_pk_mul_f32 v[14:15], v[130:131], v[40:41]
	ds_bpermute_b32 v16, v92, v20
	v_pk_mul_f32 v[8:9], v[14:15], v[8:9]
	v_cvt_pk_fp8_f32 v17, v12, v13 op_sel:[0,0,1]
	v_add_u32_e32 v12, 0xa0, v93
	v_mad_i64_i32 v[12:13], s[10:11], v12, s9, v[10:11]
	ds_bpermute_b32 v17, v92, v17
	v_lshl_add_u64 v[12:13], v[12:13], 0, v[0:1]
	v_pk_mul_f32 v[14:15], v[130:131], v[38:39]
	s_waitcnt lgkmcnt(0)
	global_store_dwordx2 v[12:13], v[16:17], off
	v_pk_mul_f32 v[12:13], v[128:129], v[40:41]
	v_pk_mul_f32 v[6:7], v[14:15], v[6:7]
	v_exp_f32_e32 v12, v12
	v_exp_f32_e32 v13, v13
	v_pk_mul_f32 v[14:15], v[130:131], v[36:37]
	v_pk_add_f32 v[12:13], v[12:13], 1.0 op_sel_hi:[1,0]
	s_nop 0
	v_rcp_f32_e32 v12, v12
	v_rcp_f32_e32 v13, v13
	v_pk_mul_f32 v[4:5], v[14:15], v[4:5]
	v_pk_mul_f32 v[14:15], v[130:131], v[32:33]
	v_pk_mul_f32 v[8:9], v[12:13], v[8:9]
	v_pk_mul_f32 v[12:13], v[128:129], v[38:39]
	v_pk_mul_f32 v[2:3], v[14:15], v[2:3]
	v_exp_f32_e32 v12, v12
	v_exp_f32_e32 v13, v13
	s_nop 0
	v_pk_add_f32 v[12:13], v[12:13], 1.0 op_sel_hi:[1,0]
	s_nop 0
	v_rcp_f32_e32 v12, v12
	v_rcp_f32_e32 v13, v13
	s_nop 0
	v_pk_mul_f32 v[6:7], v[12:13], v[6:7]
	v_pk_mul_f32 v[12:13], v[128:129], v[36:37]
	s_nop 0
	v_exp_f32_e32 v12, v12
	v_exp_f32_e32 v13, v13
	s_nop 0
	v_pk_add_f32 v[12:13], v[12:13], 1.0 op_sel_hi:[1,0]
	s_nop 0
	v_rcp_f32_e32 v12, v12
	v_rcp_f32_e32 v13, v13
	s_nop 0
	v_pk_mul_f32 v[4:5], v[12:13], v[4:5]
	v_pk_mul_f32 v[12:13], v[128:129], v[32:33]
	s_nop 0
	v_exp_f32_e32 v12, v12
	v_exp_f32_e32 v13, v13
	s_nop 0
	v_pk_add_f32 v[12:13], v[12:13], 1.0 op_sel_hi:[1,0]
	s_nop 0
	v_rcp_f32_e32 v12, v12
	v_rcp_f32_e32 v13, v13
	s_nop 0
	v_pk_mul_f32 v[2:3], v[12:13], v[2:3]
	v_cvt_pk_fp8_f32 v12, v8, v9
	v_cvt_pk_fp8_f32 v12, v6, v7 op_sel:[0,0,1]
	v_cvt_pk_fp8_f32 v7, v4, v5
	ds_bpermute_b32 v6, v92, v12
	v_cvt_pk_fp8_f32 v7, v2, v3 op_sel:[0,0,1]
	v_add_u32_e32 v2, 0xb0, v93
	v_mad_i64_i32 v[2:3], s[10:11], v2, s9, v[10:11]
	ds_bpermute_b32 v7, v92, v7
	v_lshl_add_u64 v[0:1], v[2:3], 0, v[0:1]
	s_waitcnt lgkmcnt(0)
	global_store_dwordx2 v[0:1], v[6:7], off
	s_cbranch_vccnz .LBB0_1465
	s_andn2_b64 vcc, exec, s[0:1]
	s_cbranch_vccnz .LBB0_1464
	s_barrier
	s_branch .LBB0_1464

.LBB0_1532:
	v_readlane_b32 s0, v254, 50
	v_readlane_b32 s1, v254, 51
	s_andn2_b64 vcc, exec, s[0:1]
	s_cbranch_vccnz .LBB0_1654
	v_readlane_b32 s0, v253, 2
	v_readlane_b32 s1, v253, 3
	s_load_dwordx4 s[48:51], s[0:1], 0xe0
	s_load_dwordx2 s[46:47], s[0:1], 0xf8
	s_mov_b32 s52, 0x3fb504f3
	v_mov_b32_e32 v0, 0x1000
	s_mov_b32 s3, 0x7fffe0
	s_waitcnt lgkmcnt(0)
	global_load_dword v1, v0, s[46:47] offset:16 sc1
	global_load_dword v2, v0, s[46:47] offset:20 sc1
	v_mbcnt_lo_u32_b32 v0, -1, 0
	v_mbcnt_hi_u32_b32 v0, -1, v0
	s_movk_i32 s2, 0x1600
	v_or_b32_e32 v0, s33, v0
	s_add_u32 s11, s46, 0x45900000
	v_bfe_i32 v5, v0, 27, 1
	s_waitcnt vmcnt(2)
	v_lshlrev_b32_e32 v3, 4, v0
	v_lshrrev_b32_e32 v5, 22, v5
	v_add_u32_e32 v5, v3, v5
	v_and_b32_e32 v5, 0xfffffc00, v5
	v_sub_u32_e32 v5, v3, v5
	v_ashrrev_i32_e32 v4, 31, v0
	v_lshrrev_b32_e32 v6, 4, v5
	v_lshrrev_b32_e32 v4, 26, v4
	v_bitop3_b32 v6, v6, v5, 32 bitop3:0x6c
	v_ashrrev_i32_e32 v5, 31, v5
	v_add_u32_e32 v4, v0, v4
	v_lshrrev_b32_e32 v5, 26, v5
	v_ashrrev_i32_e32 v4, 6, v4
	v_add_u32_e32 v5, v6, v5
	v_lshlrev_b32_e32 v7, 3, v4
	v_ashrrev_i32_e32 v5, 6, v5
	v_and_b32_e32 v7, -16, v7
	v_mul_i32_i24_e32 v8, 64, v5
	v_add_u32_e32 v7, v5, v7
	v_sub_u32_e32 v6, v6, v8
	v_lshlrev_b32_e32 v4, 5, v4
	v_ashrrev_i16_sdwa v6, v242, sext(v6) dst_sel:DWORD dst_unused:UNUSED_PAD src0_sel:DWORD src1_sel:BYTE_0
	v_lshlrev_b32_e32 v8, 1, v7
	v_lshrrev_b32_e32 v9, 2, v7
	v_and_b32_e32 v5, 3, v5
	v_and_b32_e32 v4, 32, v4
	v_bfe_i32 v6, v6, 0, 16
	v_and_b32_e32 v8, 24, v8
	v_and_b32_e32 v9, 4, v9
	v_and_or_b32 v5, v7, s3, v5
	v_or3_b32 v5, v5, v9, v8
	v_add_lshl_u32 v4, v4, v6, 1
	v_mad_u64_u32 v[128:129], s[0:1], v7, s2, v[4:5]
	v_add_u32_e32 v3, 0x2000, v3
	v_mad_u32_u24 v129, v5, s2, v4
	v_ashrrev_i32_e32 v4, 31, v3
	v_lshrrev_b32_e32 v4, 22, v4
	v_add_u32_e32 v4, v3, v4
	v_ashrrev_i32_e32 v4, 10, v4
	v_mul_i32_i24_e32 v5, 0x400, v4
	v_sub_u32_e32 v3, v3, v5
	v_lshrrev_b32_e32 v5, 4, v3
	v_bitop3_b32 v3, v5, v3, 32 bitop3:0x6c
	v_ashrrev_i32_e32 v6, 31, v3
	v_lshrrev_b32_e32 v6, 26, v6
	v_add_u32_e32 v6, v3, v6
	v_ashrrev_i32_e32 v7, 6, v6
	v_and_b32_e32 v6, 0xc0, v6
	v_sub_u32_e32 v3, v3, v6
	v_lshlrev_b32_e32 v5, 3, v4
	v_lshlrev_b32_e32 v4, 5, v4
	v_ashrrev_i16_sdwa v3, v242, sext(v3) dst_sel:DWORD dst_unused:UNUSED_PAD src0_sel:DWORD src1_sel:BYTE_0
	s_addc_u32 s12, s47, 0
	v_and_b32_e32 v5, -16, v5
	v_and_b32_e32 v4, 32, v4
	v_bfe_i32 v3, v3, 0, 16
	v_writelane_b32 v255, s28, 48
	s_add_u32 s37, s46, 0xa300000
	v_readfirstlane_b32 s9, v0
	v_add_u32_e32 v5, v7, v5
	v_add_lshl_u32 v4, v4, v3, 1
	v_writelane_b32 v255, s29, 49
	s_addc_u32 s71, s47, 0
	s_ashr_i32 s10, s9, 6
	v_mad_u64_u32 v[130:131], s[0:1], v5, s2, v[4:5]
	s_ashr_i32 s0, s9, 8
	s_lshl_b32 s72, s10, 10
	v_readlane_b32 s1, v255, 19
	v_lshlrev_b32_e32 v6, 1, v5
	v_lshrrev_b32_e32 v8, 2, v5
	v_and_b32_e32 v7, 3, v7
	s_add_u32 s22, s37, s1
	v_readlane_b32 s1, v255, 18
	v_and_b32_e32 v6, 24, v6
	v_and_b32_e32 v8, 4, v8
	v_and_or_b32 v7, v5, s3, v7
	s_addc_u32 s23, s71, s1
	s_add_i32 s72, s72, 0
	v_or3_b32 v6, v7, v8, v6
	s_add_i32 s84, s72, 0x10000
	s_mov_b32 m0, s84
	s_nop 0
	global_load_lds_dwordx4 v129, s[22:23]
	s_add_i32 s85, s72, 0x12000
	v_mad_u32_u24 v131, v6, s2, v4
	s_mov_b32 m0, s85
	s_nop 0
	global_load_lds_dwordx4 v131, s[22:23]
	s_add_u32 s2, s22, 0xb0000
	s_addc_u32 s3, s23, 0
	s_add_i32 s86, s72, 0x14000
	s_mov_b32 m0, s86
	s_nop 0
	global_load_lds_dwordx4 v129, s[2:3]
	s_add_i32 s87, s72, 0x16000
	s_mov_b32 m0, s87
	s_nop 0
	global_load_lds_dwordx4 v131, s[2:3]
	v_writelane_b32 v255, s11, 52
	v_readlane_b32 s1, v253, 10
	s_mul_i32 s1, s1, 0x160000
	s_add_u32 s44, s11, s1
	s_addc_u32 s45, s12, 0
	s_add_i32 s88, s72, 0x2000
	s_mov_b32 m0, s72
	s_nop 0
	global_load_lds_dwordx4 v128, s[44:45]
	s_add_u32 s2, s44, 0xb0000
	s_mov_b32 m0, s88
	s_nop 0
	global_load_lds_dwordx4 v130, s[44:45]
	s_addc_u32 s3, s45, 0
	s_add_i32 s89, s72, 0x4000
	s_add_i32 s13, s72, 0x6000
	s_mov_b32 m0, s89
	s_nop 0
	global_load_lds_dwordx4 v128, s[2:3]
	s_cmp_eq_u32 s0, 1
	v_writelane_b32 v255, s12, 54
	s_mov_b32 m0, s13
	s_nop 0
	global_load_lds_dwordx4 v130, s[2:3]
	s_cselect_b64 s[2:3], -1, 0
	v_writelane_b32 v255, s2, 50
	s_cmp_lg_u32 s0, 1
	s_nop 0
	v_writelane_b32 v255, s3, 51
	s_cbranch_scc1 .LBB0_1535
	s_barrier
.LBB0_1535:
	s_waitcnt vmcnt(0)
	v_fmac_f32_e32 v2, 0x40880000, v1
	v_max_f32_e32 v1, 0xda24260, v2
	s_mov_b32 s1, 0x42fe0000
	v_div_scale_f32 v2, s[2:3], v1, v1, s1
	v_rcp_f32_e32 v3, v2
	s_add_u32 s56, s46, 0x3d900000
	s_addc_u32 s57, s47, 0
	s_add_u32 s58, s46, 0x35900000
	v_fma_f32 v4, -v2, v3, 1.0
	v_fmac_f32_e32 v3, v4, v3
	v_div_scale_f32 v4, vcc, s1, v1, s1
	s_addc_u32 s59, s47, 0
	v_mul_f32_e32 v5, v4, v3
	s_add_u32 s60, s46, 0x19900000
	v_fma_f32 v6, -v2, v5, v4
	s_addc_u32 s61, s47, 0
	v_fmac_f32_e32 v5, v6, v3
	s_add_u32 s62, s46, 0x1e200000
	v_fma_f32 v2, -v2, v5, v4
	s_addc_u32 s63, s47, 0
	v_div_fmas_f32 v2, v2, v3, v5
	s_add_u32 s69, s46, 0x10000
	v_div_fixup_f32 v188, v2, v1, s1
	v_and_b32_e32 v1, 48, v0
	v_lshlrev_b32_e32 v2, 6, v0
	s_movk_i32 s1, 0x3c0
	v_lshlrev_b32_e32 v0, 2, v0
	s_addc_u32 s66, s47, 0
	s_and_b32 s11, s10, 3
	s_lshl_b32 s67, s0, 6
	s_lshl_b32 s0, s0, 13
	v_and_or_b32 v1, v2, s1, v1
	v_and_b32_e32 v0, 32, v0
	v_bitop3_b32 v2, v1, s0, v0 bitop3:0xde
	s_lshl_b32 s3, s11, 5
	s_lshl_b32 s0, s11, 12
	v_bitop3_b32 v0, v1, s0, v0 bitop3:0xde
	s_add_u32 s0, s22, 0x80
	s_waitcnt vmcnt(2)
	s_barrier
	s_addc_u32 s1, s23, 0
	s_add_i32 s2, s72, 0x18000
	s_mov_b32 m0, s2
	s_nop 0
	global_load_lds_dwordx4 v129, s[0:1]
	s_add_i32 s94, s72, 0x1a000
	s_mov_b32 m0, s94
	s_nop 0
	global_load_lds_dwordx4 v131, s[0:1]
	s_add_u32 s0, s44, 0x80
	s_addc_u32 s1, s45, 0
	s_add_i32 s28, s72, 0x8000
	s_mov_b32 m0, s28
	s_nop 0
	global_load_lds_dwordx4 v128, s[0:1]
	s_add_i32 s29, s72, 0xa000
	s_mov_b32 m0, s29
	s_nop 0
	global_load_lds_dwordx4 v130, s[0:1]
	s_add_u32 s0, s22, 0xb0080
	s_addc_u32 s1, s23, 0
	s_add_i32 s90, s72, 0x1c000
	s_mov_b32 m0, s90
	s_nop 0
	global_load_lds_dwordx4 v129, s[0:1]
	s_add_i32 s91, s72, 0x1e000
	s_mov_b32 m0, s91
	s_nop 0
	global_load_lds_dwordx4 v131, s[0:1]
	s_lshl_b32 s0, s11, 3
	s_add_i32 s92, s0, 0
	s_add_i32 s36, s72, 0xc000
	s_add_i32 s92, s92, 0x20000
	s_cmpk_lt_u32 s9, 0x100
	s_waitcnt vmcnt(6)
	s_cselect_b64 s[0:1], -1, 0
	s_lshl_b32 s68, s10, 5
	s_cmp_lt_u32 s9, 64
	s_cselect_b64 s[20:21], -1, 0
	v_cmp_eq_f32_e64 s[40:41], 0, v188
	s_mov_b32 s53, s52
	s_mov_b32 s65, 0
	v_add_u32_e32 v244, 0, v0
	v_add_u32_e32 v245, 0, v2
	v_readlane_b32 s19, v253, 10
	s_barrier
	s_branch .LBB0_1538

.LBB0_1545:
	s_cmp_gt_u32 s12, 41
	s_cselect_b64 s[76:77], -1, 0
	s_and_b64 vcc, s[76:77], exec
	s_cselect_b32 s30, 0xffffffd6, 2
	s_add_i32 s76, s30, s12
	s_ashr_i32 s77, s76, 31
	s_lshl_b64 s[76:77], s[76:77], 7
	s_add_u32 s30, s44, s76
	s_addc_u32 s54, s45, s77
	s_add_u32 s55, s22, s76
	s_addc_u32 s70, s23, s77
	s_cmp_gt_u32 s12, 40
	s_cselect_b32 s76, 0xffffffd7, 3
	s_add_i32 s76, s76, s12
	s_ashr_i32 s77, s76, 31
	s_lshl_b64 s[76:77], s[76:77], 7
	s_add_u32 s78, s44, s76
	s_addc_u32 s79, s45, s77
	s_add_u32 s31, s22, s76
	s_addc_u32 s35, s23, s77
	s_cmp_eq_u32 s12, 42
	s_cselect_b32 s80, s16, s30
	s_mov_b32 s30, s12
	v_add_u32_e32 v144, 0x10000, v244
	v_add_u32_e32 v160, 0x14000, v244
	ds_read_b128 v[132:135], v144
	ds_read_b128 v[136:139], v144 offset:1024
	ds_read_b128 v[140:143], v144 offset:2048
	ds_read_b128 v[144:147], v144 offset:3072
	ds_read_b128 v[148:151], v160
	ds_read_b128 v[152:155], v160 offset:1024
	ds_read_b128 v[156:159], v160 offset:2048
	ds_read_b128 v[160:163], v160 offset:3072
	s_cselect_b32 s81, s17, s54
	s_cselect_b32 s83, s75, s70
	s_cselect_b32 s82, s74, s55
	s_cselect_b32 s77, s27, s79
	s_cselect_b32 s76, s9, s78
	s_cselect_b32 s79, s11, s35
	s_cselect_b32 s78, s10, s31
	ds_read_b128 v[164:167], v245
	ds_read_b128 v[168:171], v245 offset:1024
	ds_read_b128 v[172:175], v245 offset:2048
	ds_read_b128 v[176:179], v245 offset:3072
	ds_read_b128 v[180:183], v245 offset:4096
	ds_read_b128 v[184:187], v245 offset:5120
	ds_read_b128 v[190:193], v245 offset:6144
	ds_read_b128 v[194:197], v245 offset:7168
	s_add_u32 s54, s42, 0xb0080
	s_addc_u32 s55, s43, 0
	s_mov_b32 m0, s36
	s_nop 0
	global_load_lds_dwordx4 v128, s[54:55]
	s_add_i32 s30, s72, 0xe000
	s_mov_b32 m0, s30
	s_nop 0
	global_load_lds_dwordx4 v130, s[54:55]
	s_setprio 1
	s_waitcnt vmcnt(8)
	s_waitcnt lgkmcnt(0)
	s_barrier
	v_mfma_f32_16x16x128_f8f6f4 v[124:127], v[132:139], v[164:171], v[124:127]
	v_mfma_f32_16x16x128_f8f6f4 v[120:123], v[140:147], v[164:171], v[120:123]
	v_mfma_f32_16x16x128_f8f6f4 v[112:115], v[132:139], v[172:179], v[112:115]
	v_mfma_f32_16x16x128_f8f6f4 v[108:111], v[132:139], v[180:187], v[108:111]
	v_mfma_f32_16x16x128_f8f6f4 v[198:201], v[140:147], v[172:179], v[100:103]
	v_mfma_f32_16x16x128_f8f6f4 v[202:205], v[140:147], v[180:187], v[104:107]
	v_mfma_f32_16x16x128_f8f6f4 v[206:209], v[132:139], v[190:197], v[96:99]
	v_mfma_f32_16x16x128_f8f6f4 v[210:213], v[140:147], v[190:197], v[92:95]
	v_mfma_f32_16x16x128_f8f6f4 v[116:119], v[148:155], v[164:171], v[116:119]
	v_mfma_f32_16x16x128_f8f6f4 v[76:79], v[148:155], v[172:179], v[76:79]
	v_mfma_f32_16x16x128_f8f6f4 v[64:67], v[156:163], v[172:179], v[64:67]
	v_mfma_f32_16x16x128_f8f6f4 v[44:47], v[148:155], v[180:187], v[44:47]
	v_mfma_f32_16x16x128_f8f6f4 v[164:167], v[156:163], v[164:171], v[84:87]
	v_mfma_f32_16x16x128_f8f6f4 v[168:171], v[156:163], v[180:187], v[40:43]
	v_mfma_f32_16x16x128_f8f6f4 v[172:175], v[148:155], v[190:197], v[88:91]
	v_mfma_f32_16x16x128_f8f6f4 v[176:179], v[156:163], v[190:197], v[36:39]
	s_barrier
	s_setprio 0
	s_nop 4
	ds_read_b128 v[36:39], v245 offset:16384
	ds_read_b128 v[40:43], v245 offset:17408
	ds_read_b128 v[84:87], v245 offset:18432
	ds_read_b128 v[88:91], v245 offset:19456
	ds_read_b128 v[92:95], v245 offset:20480
	ds_read_b128 v[96:99], v245 offset:21504
	ds_read_b128 v[100:103], v245 offset:22528
	ds_read_b128 v[104:107], v245 offset:23552
	s_mov_b32 m0, s84
	s_nop 0
	global_load_lds_dwordx4 v129, s[82:83]
	s_add_u32 s54, s82, 0xb0000
	s_mov_b32 m0, s85
	s_nop 0
	global_load_lds_dwordx4 v131, s[82:83]
	s_addc_u32 s55, s83, 0
	s_mov_b32 m0, s86
	s_nop 0
	global_load_lds_dwordx4 v129, s[54:55]
	s_nop 0
	s_mov_b32 m0, s87
	s_nop 0
	global_load_lds_dwordx4 v131, s[54:55]
	s_nop 0
	s_mov_b32 m0, s72
	s_nop 0
	global_load_lds_dwordx4 v128, s[80:81]
	s_nop 0
	s_mov_b32 m0, s88
	s_nop 0
	global_load_lds_dwordx4 v130, s[80:81]
	s_setprio 1
	s_waitcnt vmcnt(8)
	s_waitcnt lgkmcnt(0)
	s_barrier
	v_mfma_f32_16x16x128_f8f6f4 v[80:83], v[132:139], v[36:43], v[80:83]
	v_mfma_f32_16x16x128_f8f6f4 v[72:75], v[132:139], v[84:91], v[72:75]
	v_mfma_f32_16x16x128_f8f6f4 v[68:71], v[140:147], v[84:91], v[68:71]
	v_mfma_f32_16x16x128_f8f6f4 v[60:63], v[132:139], v[92:99], v[60:63]
	v_mfma_f32_16x16x128_f8f6f4 v[56:59], v[140:147], v[92:99], v[56:59]
	v_mfma_f32_16x16x128_f8f6f4 v[180:183], v[140:147], v[36:43], v[32:35]
	v_mfma_f32_16x16x128_f8f6f4 v[184:187], v[132:139], v[100:107], v[52:55]
	v_mfma_f32_16x16x128_f8f6f4 v[190:193], v[140:147], v[100:107], v[48:51]
	v_mfma_f32_16x16x128_f8f6f4 v[194:197], v[148:155], v[36:43], v[24:27]
	v_mfma_f32_16x16x128_f8f6f4 v[214:217], v[156:163], v[36:43], v[20:23]
	v_mfma_f32_16x16x128_f8f6f4 v[218:221], v[148:155], v[84:91], v[8:11]
	v_mfma_f32_16x16x128_f8f6f4 v[222:225], v[156:163], v[84:91], v[4:7]
	v_mfma_f32_16x16x128_f8f6f4 v[246:249], v[148:155], v[92:99], v[28:31]
	v_mfma_f32_16x16x128_f8f6f4 v[238:241], v[156:163], v[92:99], v[0:3]
	v_mfma_f32_16x16x128_f8f6f4 v[230:233], v[148:155], v[100:107], v[16:19]
	v_mfma_f32_16x16x128_f8f6f4 v[226:229], v[156:163], v[100:107], v[12:15]
	s_barrier
	s_setprio 0
	s_nop 4
	v_add_u32_e32 v12, 0x18000, v244
	v_add_u32_e32 v16, 0x1c000, v244
	ds_read_b128 v[0:3], v12
	ds_read_b128 v[4:7], v12 offset:1024
	ds_read_b128 v[8:11], v12 offset:2048
	ds_read_b128 v[12:15], v12 offset:3072
	ds_read_b128 v[132:135], v16
	ds_read_b128 v[136:139], v16 offset:1024
	ds_read_b128 v[140:143], v16 offset:2048
	ds_read_b128 v[144:147], v16 offset:3072
	ds_read_b128 v[16:19], v245 offset:32768
	ds_read_b128 v[20:23], v245 offset:33792
	ds_read_b128 v[24:27], v245 offset:34816
	ds_read_b128 v[28:31], v245 offset:35840
	ds_read_b128 v[32:35], v245 offset:36864
	ds_read_b128 v[36:39], v245 offset:37888
	ds_read_b128 v[48:51], v245 offset:38912
	ds_read_b128 v[52:55], v245 offset:39936
	s_add_u32 s54, s80, 0xb0000
	s_addc_u32 s55, s81, 0
	s_mov_b32 m0, s89
	s_nop 0
	global_load_lds_dwordx4 v128, s[54:55]
	s_nop 0
	s_mov_b32 m0, s13
	s_nop 0
	global_load_lds_dwordx4 v130, s[54:55]
	s_setprio 1
	s_waitcnt vmcnt(8)
	s_waitcnt lgkmcnt(0)
	s_barrier
	v_mfma_f32_16x16x128_f8f6f4 v[124:127], v[0:7], v[16:23], v[124:127]
	v_mfma_f32_16x16x128_f8f6f4 v[120:123], v[8:15], v[16:23], v[120:123]
	v_mfma_f32_16x16x128_f8f6f4 v[112:115], v[0:7], v[24:31], v[112:115]
	v_mfma_f32_16x16x128_f8f6f4 v[100:103], v[8:15], v[24:31], v[198:201]
	v_mfma_f32_16x16x128_f8f6f4 v[108:111], v[0:7], v[32:39], v[108:111]
	v_mfma_f32_16x16x128_f8f6f4 v[104:107], v[8:15], v[32:39], v[202:205]
	v_mfma_f32_16x16x128_f8f6f4 v[96:99], v[0:7], v[48:55], v[206:209]
	v_mfma_f32_16x16x128_f8f6f4 v[92:95], v[8:15], v[48:55], v[210:213]
	v_mfma_f32_16x16x128_f8f6f4 v[116:119], v[132:139], v[16:23], v[116:119]
	v_mfma_f32_16x16x128_f8f6f4 v[84:87], v[140:147], v[16:23], v[164:167]
	v_mfma_f32_16x16x128_f8f6f4 v[76:79], v[132:139], v[24:31], v[76:79]
	v_mfma_f32_16x16x128_f8f6f4 v[64:67], v[140:147], v[24:31], v[64:67]
	v_mfma_f32_16x16x128_f8f6f4 v[44:47], v[132:139], v[32:39], v[44:47]
	v_mfma_f32_16x16x128_f8f6f4 v[40:43], v[140:147], v[32:39], v[168:171]
	v_mfma_f32_16x16x128_f8f6f4 v[88:91], v[132:139], v[48:55], v[172:175]
	v_mfma_f32_16x16x128_f8f6f4 v[36:39], v[140:147], v[48:55], v[176:179]
	s_barrier
	s_setprio 0
	ds_read_b128 v[16:19], v245 offset:49152
	ds_read_b128 v[20:23], v245 offset:50176
	ds_read_b128 v[148:151], v245 offset:51200
	ds_read_b128 v[152:155], v245 offset:52224
	ds_read_b128 v[156:159], v245 offset:53248
	ds_read_b128 v[160:163], v245 offset:54272
	ds_read_b128 v[164:167], v245 offset:55296
	ds_read_b128 v[168:171], v245 offset:56320
	s_mov_b32 m0, s2
	s_nop 0
	global_load_lds_dwordx4 v129, s[78:79]
	s_add_u32 s54, s78, 0xb0000
	s_mov_b32 m0, s94
	s_nop 0
	global_load_lds_dwordx4 v131, s[78:79]
	s_addc_u32 s55, s79, 0
	s_mov_b32 m0, s90
	s_nop 0
	global_load_lds_dwordx4 v129, s[54:55]
	s_nop 0
	s_mov_b32 m0, s91
	s_nop 0
	global_load_lds_dwordx4 v131, s[54:55]
	s_nop 0
	s_mov_b32 m0, s28
	s_nop 0
	global_load_lds_dwordx4 v128, s[76:77]
	s_nop 0
	s_mov_b32 m0, s29
	s_nop 0
	global_load_lds_dwordx4 v130, s[76:77]
	s_setprio 1
	s_waitcnt vmcnt(8)
	s_waitcnt lgkmcnt(0)
	s_barrier
	v_mfma_f32_16x16x128_f8f6f4 v[80:83], v[0:7], v[16:23], v[80:83]
	v_mfma_f32_16x16x128_f8f6f4 v[32:35], v[8:15], v[16:23], v[180:183]
	v_mfma_f32_16x16x128_f8f6f4 v[72:75], v[0:7], v[148:155], v[72:75]
	v_mfma_f32_16x16x128_f8f6f4 v[68:71], v[8:15], v[148:155], v[68:71]
	v_mfma_f32_16x16x128_f8f6f4 v[60:63], v[0:7], v[156:163], v[60:63]
	v_mfma_f32_16x16x128_f8f6f4 v[56:59], v[8:15], v[156:163], v[56:59]
	v_mfma_f32_16x16x128_f8f6f4 v[52:55], v[0:7], v[164:171], v[184:187]
	v_mfma_f32_16x16x128_f8f6f4 v[48:51], v[8:15], v[164:171], v[190:193]
	v_mfma_f32_16x16x128_f8f6f4 v[24:27], v[132:139], v[16:23], v[194:197]
	v_mfma_f32_16x16x128_f8f6f4 v[20:23], v[140:147], v[16:23], v[214:217]
	v_mfma_f32_16x16x128_f8f6f4 v[8:11], v[132:139], v[148:155], v[218:221]
	v_mfma_f32_16x16x128_f8f6f4 v[4:7], v[140:147], v[148:155], v[222:225]
	v_mfma_f32_16x16x128_f8f6f4 v[28:31], v[132:139], v[156:163], v[246:249]
	v_mfma_f32_16x16x128_f8f6f4 v[0:3], v[140:147], v[156:163], v[238:241]
	v_mfma_f32_16x16x128_f8f6f4 v[16:19], v[132:139], v[164:171], v[230:233]
	v_mfma_f32_16x16x128_f8f6f4 v[12:15], v[140:147], v[164:171], v[226:229]
	s_barrier
	s_setprio 0
	s_add_i32 s12, s12, 2
	s_add_u32 s42, s42, 0x100
	s_addc_u32 s43, s43, 0
	s_cbranch_vccz .LBB0_1545
	s_nop 0
	v_mov_b32_e32 v227, 0x7f800000
	v_mov_b32_e32 v226, 0x260
	s_and_b64 vcc, exec, s[0:1]
	s_cbranch_vccz .LBB0_1548
	s_barrier

.LBB0_1586:
	s_or_b64 exec, exec, s[22:23]
	v_lshlrev_b32_e32 v151, 2, v248
	s_waitcnt lgkmcnt(0)
	s_barrier
	v_lshl_add_u32 v148, v247, 3, 0
	v_add_u32_e32 v4, 16, v151
	global_load_dwordx4 v[8:11], v151, s[48:49]
	global_load_dwordx4 v[12:15], v151, s[50:51]
	global_load_dwordx4 v[0:3], v4, s[48:49]
	s_nop 0
	global_load_dwordx4 v[4:7], v4, s[50:51]
	v_add_u32_e32 v150, 0x22000, v148
	ds_read_b64 v[148:149], v150
	s_and_b64 vcc, exec, s[40:41]
	s_waitcnt lgkmcnt(0)
	v_sub_f32_e32 v133, v133, v148
	v_sub_f32_e32 v132, v132, v148
	v_sub_f32_e32 v125, v125, v148
	v_sub_f32_e32 v124, v124, v148
	v_sub_f32_e32 v135, v135, v148
	v_sub_f32_e32 v134, v134, v148
	v_sub_f32_e32 v127, v127, v148
	v_sub_f32_e32 v126, v126, v148
	v_pk_mul_f32 v[124:125], v[148:149], v[124:125] op_sel:[1,0]
	v_pk_mul_f32 v[132:133], v[148:149], v[132:133] op_sel:[1,0]
	v_pk_mul_f32 v[126:127], v[148:149], v[126:127] op_sel:[1,0]
	v_pk_mul_f32 v[134:135], v[148:149], v[134:135] op_sel:[1,0]
	s_waitcnt vmcnt(2)
	v_pk_fma_f32 v[132:133], v[10:11], v[132:133], v[14:15]
	v_pk_fma_f32 v[148:149], v[8:9], v[124:125], v[12:13]
	s_waitcnt vmcnt(0)
	v_pk_fma_f32 v[124:125], v[2:3], v[134:135], v[6:7]
	v_pk_fma_f32 v[126:127], v[0:1], v[126:127], v[4:5]
	v_cvt_pk_bf16_f32 v152, v148, v149
	v_cvt_pk_bf16_f32 v153, v132, v133
	s_nop 0
	v_cvt_pk_bf16_f32 v154, v126, v127
	v_cvt_pk_bf16_f32 v155, v124, v125
	global_store_dwordx4 v246, v[152:155], s[58:59]
	s_cbranch_vccz .LBB0_1637
	v_cvt_pk_fp8_f32 v134, v148, v149
	v_cvt_pk_fp8_f32 v135, v126, v127
	v_cvt_pk_fp8_f32 v134, v132, v133 op_sel:[0,0,1]
	v_cvt_pk_fp8_f32 v135, v124, v125 op_sel:[0,0,1]
	s_cbranch_execnz .LBB0_1589

.LBB0_1589:
	v_lshrrev_b32_e32 v124, 1, v246
	global_store_dwordx2 v124, v[134:135], s[60:61]
	ds_read_b64 v[124:125], v150 offset:128
	v_add_u32_e32 v126, 0x10000, v246
	s_andn2_b64 vcc, exec, s[40:41]
	s_waitcnt lgkmcnt(0)
	v_sub_f32_e32 v133, v83, v124
	v_sub_f32_e32 v132, v73, v124
	v_sub_f32_e32 v73, v82, v124
	v_sub_f32_e32 v72, v72, v124
	v_pk_mul_f32 v[82:83], v[124:125], v[72:73] op_sel:[1,0]
	v_pk_mul_f32 v[72:73], v[124:125], v[132:133] op_sel:[1,0]
	v_sub_f32_e32 v133, v85, v124
	v_sub_f32_e32 v132, v75, v124
	v_sub_f32_e32 v75, v84, v124
	v_sub_f32_e32 v74, v74, v124
	v_pk_mul_f32 v[84:85], v[124:125], v[74:75] op_sel:[1,0]
	v_pk_mul_f32 v[74:75], v[124:125], v[132:133] op_sel:[1,0]
	v_cndmask_b32_e64 v124, 0, 1, s[40:41]
	v_pk_fma_f32 v[72:73], v[10:11], v[72:73], v[14:15]
	v_pk_fma_f32 v[82:83], v[8:9], v[82:83], v[12:13]
	v_pk_fma_f32 v[74:75], v[2:3], v[74:75], v[6:7]
	v_pk_fma_f32 v[84:85], v[0:1], v[84:85], v[4:5]
	v_cmp_ne_u32_e64 s[42:43], 1, v124
	v_cvt_pk_bf16_f32 v132, v82, v83
	v_cvt_pk_bf16_f32 v133, v72, v73
	v_cvt_pk_bf16_f32 v134, v84, v85
	v_cvt_pk_bf16_f32 v135, v74, v75
	global_store_dwordx4 v126, v[132:135], s[58:59]
	s_cbranch_vccnz .LBB0_1638
	v_cvt_pk_fp8_f32 v124, v82, v83
	v_cvt_pk_fp8_f32 v125, v84, v85
	v_cvt_pk_fp8_f32 v124, v72, v73 op_sel:[0,0,1]
	v_cvt_pk_fp8_f32 v125, v74, v75 op_sel:[0,0,1]
	s_cbranch_execnz .LBB0_1592

.LBB0_1592:
	ds_read_b64 v[74:75], v150 offset:256
	v_lshrrev_b32_e32 v72, 1, v126
	global_store_dwordx2 v72, v[124:125], s[60:61]
	v_add_u32_e32 v82, 0x20000, v246
	s_and_b64 vcc, exec, s[42:43]
	s_waitcnt lgkmcnt(0)
	v_sub_f32_e32 v73, v87, v74
	v_sub_f32_e32 v72, v81, v74
	v_sub_f32_e32 v81, v86, v74
	v_sub_f32_e32 v80, v80, v74
	v_sub_f32_e32 v85, v79, v74
	v_sub_f32_e32 v84, v77, v74
	v_sub_f32_e32 v77, v78, v74
	v_sub_f32_e32 v76, v76, v74
	v_pk_mul_f32 v[80:81], v[74:75], v[80:81] op_sel:[1,0]
	v_pk_mul_f32 v[72:73], v[74:75], v[72:73] op_sel:[1,0]
	v_pk_mul_f32 v[76:77], v[74:75], v[76:77] op_sel:[1,0]
	v_pk_mul_f32 v[74:75], v[74:75], v[84:85] op_sel:[1,0]
	v_pk_fma_f32 v[72:73], v[10:11], v[72:73], v[14:15]
	v_pk_fma_f32 v[80:81], v[8:9], v[80:81], v[12:13]
	v_pk_fma_f32 v[74:75], v[2:3], v[74:75], v[6:7]
	v_pk_fma_f32 v[76:77], v[0:1], v[76:77], v[4:5]
	v_cvt_pk_bf16_f32 v84, v80, v81
	v_cvt_pk_bf16_f32 v85, v72, v73
	s_nop 0
	v_cvt_pk_bf16_f32 v86, v76, v77
	v_cvt_pk_bf16_f32 v87, v74, v75
	global_store_dwordx4 v82, v[84:87], s[58:59]
	s_cbranch_vccnz .LBB0_1639
	v_cvt_pk_fp8_f32 v78, v80, v81
	v_cvt_pk_fp8_f32 v79, v76, v77
	v_cvt_pk_fp8_f32 v78, v72, v73 op_sel:[0,0,1]
	v_cvt_pk_fp8_f32 v79, v74, v75 op_sel:[0,0,1]
	s_cbranch_execnz .LBB0_1595

.LBB0_1595:
	ds_read_b64 v[74:75], v150 offset:384
	v_lshrrev_b32_e32 v72, 1, v82
	global_store_dwordx2 v72, v[78:79], s[60:61]
	v_add_u32_e32 v82, 0x30000, v246
	s_and_b64 vcc, exec, s[42:43]
	s_waitcnt lgkmcnt(0)
	v_sub_f32_e32 v73, v93, v74
	v_sub_f32_e32 v72, v89, v74
	v_sub_f32_e32 v77, v92, v74
	v_sub_f32_e32 v76, v88, v74
	v_sub_f32_e32 v79, v95, v74
	v_sub_f32_e32 v78, v91, v74
	v_sub_f32_e32 v81, v94, v74
	v_sub_f32_e32 v80, v90, v74
	v_pk_mul_f32 v[76:77], v[74:75], v[76:77] op_sel:[1,0]
	v_pk_mul_f32 v[72:73], v[74:75], v[72:73] op_sel:[1,0]
	v_pk_mul_f32 v[80:81], v[74:75], v[80:81] op_sel:[1,0]
	v_pk_mul_f32 v[74:75], v[74:75], v[78:79] op_sel:[1,0]
	v_pk_fma_f32 v[72:73], v[10:11], v[72:73], v[14:15]
	v_pk_fma_f32 v[76:77], v[8:9], v[76:77], v[12:13]
	v_pk_fma_f32 v[74:75], v[2:3], v[74:75], v[6:7]
	v_pk_fma_f32 v[78:79], v[0:1], v[80:81], v[4:5]
	v_cvt_pk_bf16_f32 v84, v76, v77
	v_cvt_pk_bf16_f32 v85, v72, v73
	s_nop 0
	v_cvt_pk_bf16_f32 v86, v78, v79
	v_cvt_pk_bf16_f32 v87, v74, v75
	global_store_dwordx4 v82, v[84:87], s[58:59]
	s_cbranch_vccnz .LBB0_1640
	v_cvt_pk_fp8_f32 v80, v76, v77
	v_cvt_pk_fp8_f32 v81, v78, v79
	v_cvt_pk_fp8_f32 v80, v72, v73 op_sel:[0,0,1]
	v_cvt_pk_fp8_f32 v81, v74, v75 op_sel:[0,0,1]
	s_cbranch_execnz .LBB0_1598

.LBB0_1598:
	ds_read_b64 v[74:75], v150 offset:1024
	v_lshrrev_b32_e32 v72, 1, v82
	global_store_dwordx2 v72, v[80:81], s[60:61]
	v_add_u32_e32 v82, 0x80000, v246
	s_and_b64 vcc, exec, s[42:43]
	s_waitcnt lgkmcnt(0)
	v_sub_f32_e32 v73, v101, v74
	v_sub_f32_e32 v72, v97, v74
	v_sub_f32_e32 v77, v100, v74
	v_sub_f32_e32 v76, v96, v74
	v_sub_f32_e32 v79, v103, v74
	v_sub_f32_e32 v78, v99, v74
	v_sub_f32_e32 v81, v102, v74
	v_sub_f32_e32 v80, v98, v74
	v_pk_mul_f32 v[76:77], v[74:75], v[76:77] op_sel:[1,0]
	v_pk_mul_f32 v[72:73], v[74:75], v[72:73] op_sel:[1,0]
	v_pk_mul_f32 v[80:81], v[74:75], v[80:81] op_sel:[1,0]
	v_pk_mul_f32 v[74:75], v[74:75], v[78:79] op_sel:[1,0]
	v_pk_fma_f32 v[72:73], v[10:11], v[72:73], v[14:15]
	v_pk_fma_f32 v[76:77], v[8:9], v[76:77], v[12:13]
	v_pk_fma_f32 v[74:75], v[2:3], v[74:75], v[6:7]
	v_pk_fma_f32 v[78:79], v[0:1], v[80:81], v[4:5]
	v_cvt_pk_bf16_f32 v84, v76, v77
	v_cvt_pk_bf16_f32 v85, v72, v73
	s_nop 0
	v_cvt_pk_bf16_f32 v86, v78, v79
	v_cvt_pk_bf16_f32 v87, v74, v75
	global_store_dwordx4 v82, v[84:87], s[58:59]
	s_cbranch_vccnz .LBB0_1641
	v_cvt_pk_fp8_f32 v80, v76, v77
	v_cvt_pk_fp8_f32 v81, v78, v79
	v_cvt_pk_fp8_f32 v80, v72, v73 op_sel:[0,0,1]
	v_cvt_pk_fp8_f32 v81, v74, v75 op_sel:[0,0,1]
	s_cbranch_execnz .LBB0_1601

.LBB0_1601:
	ds_read_b64 v[74:75], v150 offset:1152
	v_lshrrev_b32_e32 v72, 1, v82
	global_store_dwordx2 v72, v[80:81], s[60:61]
	v_add_u32_e32 v82, 0x90000, v246
	s_and_b64 vcc, exec, s[42:43]
	s_waitcnt lgkmcnt(0)
	v_sub_f32_e32 v73, v109, v74
	v_sub_f32_e32 v72, v105, v74
	v_sub_f32_e32 v77, v108, v74
	v_sub_f32_e32 v76, v104, v74
	v_sub_f32_e32 v79, v111, v74
	v_sub_f32_e32 v78, v107, v74
	v_sub_f32_e32 v81, v110, v74
	v_sub_f32_e32 v80, v106, v74
	v_pk_mul_f32 v[76:77], v[74:75], v[76:77] op_sel:[1,0]
	v_pk_mul_f32 v[72:73], v[74:75], v[72:73] op_sel:[1,0]
	v_pk_mul_f32 v[80:81], v[74:75], v[80:81] op_sel:[1,0]
	v_pk_mul_f32 v[74:75], v[74:75], v[78:79] op_sel:[1,0]
	v_pk_fma_f32 v[72:73], v[10:11], v[72:73], v[14:15]
	v_pk_fma_f32 v[76:77], v[8:9], v[76:77], v[12:13]
	v_pk_fma_f32 v[74:75], v[2:3], v[74:75], v[6:7]
	v_pk_fma_f32 v[78:79], v[0:1], v[80:81], v[4:5]
	v_cvt_pk_bf16_f32 v84, v76, v77
	v_cvt_pk_bf16_f32 v85, v72, v73
	s_nop 0
	v_cvt_pk_bf16_f32 v86, v78, v79
	v_cvt_pk_bf16_f32 v87, v74, v75
	global_store_dwordx4 v82, v[84:87], s[58:59]
	s_cbranch_vccnz .LBB0_1642
	v_cvt_pk_fp8_f32 v80, v76, v77
	v_cvt_pk_fp8_f32 v81, v78, v79
	v_cvt_pk_fp8_f32 v80, v72, v73 op_sel:[0,0,1]
	v_cvt_pk_fp8_f32 v81, v74, v75 op_sel:[0,0,1]
	s_cbranch_execnz .LBB0_1604

.LBB0_1604:
	ds_read_b64 v[74:75], v150 offset:1280
	v_lshrrev_b32_e32 v72, 1, v82
	global_store_dwordx2 v72, v[80:81], s[60:61]
	v_add_u32_e32 v82, 0xa0000, v246
	s_and_b64 vcc, exec, s[42:43]
	s_waitcnt lgkmcnt(0)
	v_sub_f32_e32 v73, v137, v74
	v_sub_f32_e32 v72, v113, v74
	v_sub_f32_e32 v77, v136, v74
	v_sub_f32_e32 v76, v112, v74
	v_sub_f32_e32 v79, v139, v74
	v_sub_f32_e32 v78, v115, v74
	v_sub_f32_e32 v81, v138, v74
	v_sub_f32_e32 v80, v114, v74
	v_pk_mul_f32 v[76:77], v[74:75], v[76:77] op_sel:[1,0]
	v_pk_mul_f32 v[72:73], v[74:75], v[72:73] op_sel:[1,0]
	v_pk_mul_f32 v[80:81], v[74:75], v[80:81] op_sel:[1,0]
	v_pk_mul_f32 v[74:75], v[74:75], v[78:79] op_sel:[1,0]
	v_pk_fma_f32 v[72:73], v[10:11], v[72:73], v[14:15]
	v_pk_fma_f32 v[76:77], v[8:9], v[76:77], v[12:13]
	v_pk_fma_f32 v[74:75], v[2:3], v[74:75], v[6:7]
	v_pk_fma_f32 v[78:79], v[0:1], v[80:81], v[4:5]
	v_cvt_pk_bf16_f32 v84, v76, v77
	v_cvt_pk_bf16_f32 v85, v72, v73
	s_nop 0
	v_cvt_pk_bf16_f32 v86, v78, v79
	v_cvt_pk_bf16_f32 v87, v74, v75
	global_store_dwordx4 v82, v[84:87], s[58:59]
	s_cbranch_vccnz .LBB0_1643
	v_cvt_pk_fp8_f32 v80, v76, v77
	v_cvt_pk_fp8_f32 v81, v78, v79
	v_cvt_pk_fp8_f32 v80, v72, v73 op_sel:[0,0,1]
	v_cvt_pk_fp8_f32 v81, v74, v75 op_sel:[0,0,1]
	s_cbranch_execnz .LBB0_1607

.LBB0_1607:
	ds_read_b64 v[74:75], v150 offset:1408
	v_lshrrev_b32_e32 v72, 1, v82
	global_store_dwordx2 v72, v[80:81], s[60:61]
	v_add_u32_e32 v72, 0xb0000, v246
	s_and_b64 vcc, exec, s[42:43]
	s_waitcnt lgkmcnt(0)
	v_sub_f32_e32 v77, v145, v74
	v_sub_f32_e32 v76, v141, v74
	v_sub_f32_e32 v79, v144, v74
	v_sub_f32_e32 v78, v140, v74
	v_pk_mul_f32 v[78:79], v[74:75], v[78:79] op_sel:[1,0]
	v_pk_mul_f32 v[76:77], v[74:75], v[76:77] op_sel:[1,0]
	v_pk_fma_f32 v[8:9], v[8:9], v[78:79], v[12:13]
	v_pk_fma_f32 v[10:11], v[10:11], v[76:77], v[14:15]
	v_sub_f32_e32 v13, v147, v74
	v_sub_f32_e32 v12, v143, v74
	v_sub_f32_e32 v15, v146, v74
	v_sub_f32_e32 v14, v142, v74
	v_pk_mul_f32 v[14:15], v[74:75], v[14:15] op_sel:[1,0]
	v_pk_mul_f32 v[12:13], v[74:75], v[12:13] op_sel:[1,0]
	v_pk_fma_f32 v[0:1], v[0:1], v[14:15], v[4:5]
	v_pk_fma_f32 v[2:3], v[2:3], v[12:13], v[6:7]
	v_cvt_pk_bf16_f32 v4, v8, v9
	v_cvt_pk_bf16_f32 v5, v10, v11
	v_cvt_pk_bf16_f32 v6, v0, v1
	s_nop 0
	v_cvt_pk_bf16_f32 v7, v2, v3
	global_store_dwordx4 v72, v[4:7], s[58:59]
	s_cbranch_vccnz .LBB0_1644
	s_nop 0
	v_cvt_pk_fp8_f32 v4, v8, v9
	v_cvt_pk_fp8_f32 v5, v0, v1
	v_cvt_pk_fp8_f32 v4, v10, v11 op_sel:[0,0,1]
	v_cvt_pk_fp8_f32 v5, v2, v3 op_sel:[0,0,1]
	s_cbranch_execnz .LBB0_1610

.LBB0_1610:
	v_lshrrev_b32_e32 v0, 1, v72
	global_store_dwordx2 v0, v[4:5], s[60:61]
	v_add_u32_e32 v0, 0x200, v151
	v_add_u32_e32 v4, 0x210, v151
	global_load_dwordx4 v[8:11], v0, s[48:49]
	global_load_dwordx4 v[12:15], v0, s[50:51]
	s_nop 0
	global_load_dwordx4 v[0:3], v4, s[48:49]
	s_nop 0
	global_load_dwordx4 v[4:7], v4, s[50:51]
	ds_read_b64 v[72:73], v150
	v_add_u32_e32 v82, 0x100, v246
	s_and_b64 vcc, exec, s[42:43]
	s_waitcnt lgkmcnt(0)
	v_sub_f32_e32 v75, v123, v72
	v_sub_f32_e32 v74, v122, v72
	v_sub_f32_e32 v77, v121, v72
	v_sub_f32_e32 v76, v120, v72
	v_sub_f32_e32 v79, v119, v72
	v_sub_f32_e32 v78, v118, v72
	v_sub_f32_e32 v81, v117, v72
	v_sub_f32_e32 v80, v116, v72
	v_pk_mul_f32 v[84:85], v[72:73], v[76:77] op_sel:[1,0]
	v_pk_mul_f32 v[74:75], v[72:73], v[74:75] op_sel:[1,0]
	v_pk_mul_f32 v[80:81], v[72:73], v[80:81] op_sel:[1,0]
	v_pk_mul_f32 v[72:73], v[72:73], v[78:79] op_sel:[1,0]
	s_waitcnt vmcnt(2)
	v_pk_fma_f32 v[76:77], v[10:11], v[74:75], v[14:15]
	v_pk_fma_f32 v[78:79], v[8:9], v[84:85], v[12:13]
	s_waitcnt vmcnt(0)
	v_pk_fma_f32 v[72:73], v[2:3], v[72:73], v[6:7]
	v_pk_fma_f32 v[74:75], v[0:1], v[80:81], v[4:5]
	v_cvt_pk_bf16_f32 v84, v78, v79
	v_cvt_pk_bf16_f32 v85, v76, v77
	s_nop 0
	v_cvt_pk_bf16_f32 v86, v74, v75
	v_cvt_pk_bf16_f32 v87, v72, v73
	global_store_dwordx4 v82, v[84:87], s[58:59]
	s_cbranch_vccnz .LBB0_1645
	v_cvt_pk_fp8_f32 v80, v78, v79
	v_cvt_pk_fp8_f32 v81, v74, v75
	v_cvt_pk_fp8_f32 v80, v76, v77 op_sel:[0,0,1]
	v_cvt_pk_fp8_f32 v81, v72, v73 op_sel:[0,0,1]
	s_cbranch_execnz .LBB0_1613

.LBB0_1613:
	v_lshrrev_b32_e32 v72, 1, v82
	global_store_dwordx2 v72, v[80:81], s[60:61]
	ds_read_b64 v[72:73], v150 offset:128
	v_add_u32_e32 v74, 0x10100, v246
	s_and_b64 vcc, exec, s[42:43]
	s_waitcnt lgkmcnt(0)
	v_sub_f32_e32 v17, v17, v72
	v_sub_f32_e32 v16, v16, v72
	v_sub_f32_e32 v53, v53, v72
	v_sub_f32_e32 v52, v52, v72
	v_pk_mul_f32 v[76:77], v[72:73], v[16:17] op_sel:[1,0]
	v_sub_f32_e32 v55, v55, v72
	v_sub_f32_e32 v54, v54, v72
	v_sub_f32_e32 v19, v19, v72
	v_sub_f32_e32 v18, v18, v72
	v_pk_mul_f32 v[16:17], v[72:73], v[52:53] op_sel:[1,0]
	v_pk_fma_f32 v[52:53], v[8:9], v[76:77], v[12:13]
	v_pk_mul_f32 v[76:77], v[72:73], v[18:19] op_sel:[1,0]
	v_pk_mul_f32 v[18:19], v[72:73], v[54:55] op_sel:[1,0]
	v_pk_fma_f32 v[16:17], v[10:11], v[16:17], v[14:15]
	v_pk_fma_f32 v[18:19], v[2:3], v[18:19], v[6:7]
	v_pk_fma_f32 v[54:55], v[0:1], v[76:77], v[4:5]
	v_cvt_pk_bf16_f32 v76, v52, v53
	v_cvt_pk_bf16_f32 v77, v16, v17
	s_nop 0
	v_cvt_pk_bf16_f32 v78, v54, v55
	v_cvt_pk_bf16_f32 v79, v18, v19
	global_store_dwordx4 v74, v[76:79], s[58:59]
	s_cbranch_vccnz .LBB0_1646
	v_cvt_pk_fp8_f32 v72, v52, v53
	v_cvt_pk_fp8_f32 v73, v54, v55
	v_cvt_pk_fp8_f32 v72, v16, v17 op_sel:[0,0,1]
	v_cvt_pk_fp8_f32 v73, v18, v19 op_sel:[0,0,1]
	s_cbranch_execnz .LBB0_1616

.LBB0_1616:
	ds_read_b64 v[18:19], v150 offset:256
	v_lshrrev_b32_e32 v16, 1, v74
	global_store_dwordx2 v16, v[72:73], s[60:61]
	v_add_u32_e32 v54, 0x20100, v246
	s_and_b64 vcc, exec, s[42:43]
	s_waitcnt lgkmcnt(0)
	v_sub_f32_e32 v17, v57, v18
	v_sub_f32_e32 v16, v56, v18
	v_sub_f32_e32 v49, v49, v18
	v_sub_f32_e32 v48, v48, v18
	v_sub_f32_e32 v53, v59, v18
	v_sub_f32_e32 v52, v58, v18
	v_sub_f32_e32 v51, v51, v18
	v_sub_f32_e32 v50, v50, v18
	v_pk_mul_f32 v[48:49], v[18:19], v[48:49] op_sel:[1,0]
	v_pk_mul_f32 v[16:17], v[18:19], v[16:17] op_sel:[1,0]
	v_pk_mul_f32 v[50:51], v[18:19], v[50:51] op_sel:[1,0]
	v_pk_mul_f32 v[18:19], v[18:19], v[52:53] op_sel:[1,0]
	v_pk_fma_f32 v[16:17], v[10:11], v[16:17], v[14:15]
	v_pk_fma_f32 v[48:49], v[8:9], v[48:49], v[12:13]
	v_pk_fma_f32 v[18:19], v[2:3], v[18:19], v[6:7]
	v_pk_fma_f32 v[50:51], v[0:1], v[50:51], v[4:5]
	v_cvt_pk_bf16_f32 v56, v48, v49
	v_cvt_pk_bf16_f32 v57, v16, v17
	s_nop 0
	v_cvt_pk_bf16_f32 v58, v50, v51
	v_cvt_pk_bf16_f32 v59, v18, v19
	global_store_dwordx4 v54, v[56:59], s[58:59]
	s_cbranch_vccnz .LBB0_1647
	v_cvt_pk_fp8_f32 v52, v48, v49
	v_cvt_pk_fp8_f32 v53, v50, v51
	v_cvt_pk_fp8_f32 v52, v16, v17 op_sel:[0,0,1]
	v_cvt_pk_fp8_f32 v53, v18, v19 op_sel:[0,0,1]
	s_cbranch_execnz .LBB0_1619

.LBB0_1619:
	ds_read_b64 v[18:19], v150 offset:384
	v_lshrrev_b32_e32 v16, 1, v54
	global_store_dwordx2 v16, v[52:53], s[60:61]
	v_add_u32_e32 v48, 0x30100, v246
	s_and_b64 vcc, exec, s[42:43]
	s_waitcnt lgkmcnt(0)
	v_sub_f32_e32 v17, v47, v18
	v_sub_f32_e32 v16, v46, v18
	v_sub_f32_e32 v45, v45, v18
	v_sub_f32_e32 v44, v44, v18
	v_sub_f32_e32 v43, v43, v18
	v_sub_f32_e32 v42, v42, v18
	v_sub_f32_e32 v41, v41, v18
	v_sub_f32_e32 v40, v40, v18
	v_pk_mul_f32 v[44:45], v[18:19], v[44:45] op_sel:[1,0]
	v_pk_mul_f32 v[16:17], v[18:19], v[16:17] op_sel:[1,0]
	v_pk_mul_f32 v[40:41], v[18:19], v[40:41] op_sel:[1,0]
	v_pk_mul_f32 v[18:19], v[18:19], v[42:43] op_sel:[1,0]
	v_pk_fma_f32 v[16:17], v[10:11], v[16:17], v[14:15]
	v_pk_fma_f32 v[44:45], v[8:9], v[44:45], v[12:13]
	v_pk_fma_f32 v[18:19], v[2:3], v[18:19], v[6:7]
	v_pk_fma_f32 v[40:41], v[0:1], v[40:41], v[4:5]
	v_cvt_pk_bf16_f32 v50, v44, v45
	v_cvt_pk_bf16_f32 v51, v16, v17
	s_nop 0
	v_cvt_pk_bf16_f32 v52, v40, v41
	v_cvt_pk_bf16_f32 v53, v18, v19
	global_store_dwordx4 v48, v[50:53], s[58:59]
	s_cbranch_vccnz .LBB0_1648
	v_cvt_pk_fp8_f32 v42, v44, v45
	v_cvt_pk_fp8_f32 v43, v40, v41
	v_cvt_pk_fp8_f32 v42, v16, v17 op_sel:[0,0,1]
	v_cvt_pk_fp8_f32 v43, v18, v19 op_sel:[0,0,1]
	s_cbranch_execnz .LBB0_1622

.LBB0_1622:
	ds_read_b64 v[18:19], v150 offset:1024
	v_lshrrev_b32_e32 v16, 1, v48
	global_store_dwordx2 v16, v[42:43], s[60:61]
	v_add_u32_e32 v40, 0x80100, v246
	s_and_b64 vcc, exec, s[42:43]
	s_waitcnt lgkmcnt(0)
	v_sub_f32_e32 v17, v39, v18
	v_sub_f32_e32 v16, v38, v18
	v_sub_f32_e32 v37, v37, v18
	v_sub_f32_e32 v36, v36, v18
	v_sub_f32_e32 v35, v35, v18
	v_sub_f32_e32 v34, v34, v18
	v_sub_f32_e32 v33, v33, v18
	v_sub_f32_e32 v32, v32, v18
	v_pk_mul_f32 v[36:37], v[18:19], v[36:37] op_sel:[1,0]
	v_pk_mul_f32 v[16:17], v[18:19], v[16:17] op_sel:[1,0]
	v_pk_mul_f32 v[32:33], v[18:19], v[32:33] op_sel:[1,0]
	v_pk_mul_f32 v[18:19], v[18:19], v[34:35] op_sel:[1,0]
	v_pk_fma_f32 v[16:17], v[10:11], v[16:17], v[14:15]
	v_pk_fma_f32 v[36:37], v[8:9], v[36:37], v[12:13]
	v_pk_fma_f32 v[18:19], v[2:3], v[18:19], v[6:7]
	v_pk_fma_f32 v[32:33], v[0:1], v[32:33], v[4:5]
	v_cvt_pk_bf16_f32 v42, v36, v37
	v_cvt_pk_bf16_f32 v43, v16, v17
	s_nop 0
	v_cvt_pk_bf16_f32 v44, v32, v33
	v_cvt_pk_bf16_f32 v45, v18, v19
	global_store_dwordx4 v40, v[42:45], s[58:59]
	s_cbranch_vccnz .LBB0_1649
	v_cvt_pk_fp8_f32 v34, v36, v37
	v_cvt_pk_fp8_f32 v35, v32, v33
	v_cvt_pk_fp8_f32 v34, v16, v17 op_sel:[0,0,1]
	v_cvt_pk_fp8_f32 v35, v18, v19 op_sel:[0,0,1]
	s_cbranch_execnz .LBB0_1625

.LBB0_1625:
	ds_read_b64 v[18:19], v150 offset:1152
	v_lshrrev_b32_e32 v16, 1, v40
	global_store_dwordx2 v16, v[34:35], s[60:61]
	v_add_u32_e32 v34, 0x90100, v246
	s_and_b64 vcc, exec, s[42:43]
	s_waitcnt lgkmcnt(0)
	v_sub_f32_e32 v17, v61, v18
	v_sub_f32_e32 v16, v60, v18
	v_sub_f32_e32 v25, v25, v18
	v_sub_f32_e32 v24, v24, v18
	v_sub_f32_e32 v33, v63, v18
	v_sub_f32_e32 v32, v62, v18
	v_sub_f32_e32 v21, v21, v18
	v_sub_f32_e32 v20, v20, v18
	v_pk_mul_f32 v[24:25], v[18:19], v[24:25] op_sel:[1,0]
	v_pk_mul_f32 v[16:17], v[18:19], v[16:17] op_sel:[1,0]
	v_pk_mul_f32 v[20:21], v[18:19], v[20:21] op_sel:[1,0]
	v_pk_mul_f32 v[18:19], v[18:19], v[32:33] op_sel:[1,0]
	v_pk_fma_f32 v[16:17], v[10:11], v[16:17], v[14:15]
	v_pk_fma_f32 v[24:25], v[8:9], v[24:25], v[12:13]
	v_pk_fma_f32 v[18:19], v[2:3], v[18:19], v[6:7]
	v_pk_fma_f32 v[20:21], v[0:1], v[20:21], v[4:5]
	v_cvt_pk_bf16_f32 v36, v24, v25
	v_cvt_pk_bf16_f32 v37, v16, v17
	s_nop 0
	v_cvt_pk_bf16_f32 v38, v20, v21
	v_cvt_pk_bf16_f32 v39, v18, v19
	global_store_dwordx4 v34, v[36:39], s[58:59]
	s_cbranch_vccnz .LBB0_1650
	v_cvt_pk_fp8_f32 v32, v24, v25
	v_cvt_pk_fp8_f32 v33, v20, v21
	v_cvt_pk_fp8_f32 v32, v16, v17 op_sel:[0,0,1]
	v_cvt_pk_fp8_f32 v33, v18, v19 op_sel:[0,0,1]
	s_cbranch_execnz .LBB0_1628

.LBB0_1628:
	ds_read_b64 v[18:19], v150 offset:1280
	v_lshrrev_b32_e32 v16, 1, v34
	global_store_dwordx2 v16, v[32:33], s[60:61]
	v_add_u32_e32 v32, 0xa0100, v246
	s_and_b64 vcc, exec, s[42:43]
	s_waitcnt lgkmcnt(0)
	v_sub_f32_e32 v17, v67, v18
	v_sub_f32_e32 v16, v66, v18
	v_sub_f32_e32 v21, v23, v18
	v_sub_f32_e32 v20, v22, v18
	v_sub_f32_e32 v23, v69, v18
	v_sub_f32_e32 v22, v68, v18
	v_sub_f32_e32 v25, v27, v18
	v_sub_f32_e32 v24, v26, v18
	v_pk_mul_f32 v[20:21], v[18:19], v[20:21] op_sel:[1,0]
	v_pk_mul_f32 v[16:17], v[18:19], v[16:17] op_sel:[1,0]
	v_pk_mul_f32 v[24:25], v[18:19], v[24:25] op_sel:[1,0]
	v_pk_mul_f32 v[18:19], v[18:19], v[22:23] op_sel:[1,0]
	v_pk_fma_f32 v[16:17], v[10:11], v[16:17], v[14:15]
	v_pk_fma_f32 v[20:21], v[8:9], v[20:21], v[12:13]
	v_pk_fma_f32 v[18:19], v[2:3], v[18:19], v[6:7]
	v_pk_fma_f32 v[22:23], v[0:1], v[24:25], v[4:5]
	v_cvt_pk_bf16_f32 v24, v20, v21
	v_cvt_pk_bf16_f32 v25, v16, v17
	s_nop 0
	v_cvt_pk_bf16_f32 v26, v22, v23
	v_cvt_pk_bf16_f32 v27, v18, v19
	global_store_dwordx4 v32, v[24:27], s[58:59]
	s_cbranch_vccnz .LBB0_1651
	s_nop 0
	v_cvt_pk_fp8_f32 v24, v20, v21
	v_cvt_pk_fp8_f32 v25, v22, v23
	v_cvt_pk_fp8_f32 v24, v16, v17 op_sel:[0,0,1]
	v_cvt_pk_fp8_f32 v25, v18, v19 op_sel:[0,0,1]
	s_cbranch_execnz .LBB0_1631

.LBB0_1631:
	ds_read_b64 v[18:19], v150 offset:1408
	v_lshrrev_b32_e32 v16, 1, v32
	global_store_dwordx2 v16, v[24:25], s[60:61]
	v_add_u32_e32 v16, 0xb0100, v246
	s_and_b64 vcc, exec, s[42:43]
	s_waitcnt lgkmcnt(0)
	v_sub_f32_e32 v21, v71, v18
	v_sub_f32_e32 v20, v70, v18
	v_sub_f32_e32 v23, v65, v18
	v_sub_f32_e32 v22, v64, v18
	v_pk_mul_f32 v[22:23], v[18:19], v[22:23] op_sel:[1,0]
	v_pk_mul_f32 v[20:21], v[18:19], v[20:21] op_sel:[1,0]
	v_pk_fma_f32 v[8:9], v[8:9], v[22:23], v[12:13]
	v_pk_fma_f32 v[10:11], v[10:11], v[20:21], v[14:15]
	v_sub_f32_e32 v13, v31, v18
	v_sub_f32_e32 v12, v30, v18
	v_sub_f32_e32 v15, v29, v18
	v_sub_f32_e32 v14, v28, v18
	v_pk_mul_f32 v[14:15], v[18:19], v[14:15] op_sel:[1,0]
	v_pk_mul_f32 v[12:13], v[18:19], v[12:13] op_sel:[1,0]
	v_pk_fma_f32 v[0:1], v[0:1], v[14:15], v[4:5]
	v_pk_fma_f32 v[2:3], v[2:3], v[12:13], v[6:7]
	v_cvt_pk_bf16_f32 v4, v8, v9
	v_cvt_pk_bf16_f32 v5, v10, v11
	v_cvt_pk_bf16_f32 v6, v0, v1
	s_nop 0
	v_cvt_pk_bf16_f32 v7, v2, v3
	global_store_dwordx4 v16, v[4:7], s[58:59]
	s_cbranch_vccnz .LBB0_1652
	s_nop 0
	v_cvt_pk_fp8_f32 v4, v8, v9
	v_cvt_pk_fp8_f32 v5, v0, v1
	v_cvt_pk_fp8_f32 v4, v10, v11 op_sel:[0,0,1]
	v_cvt_pk_fp8_f32 v5, v2, v3 op_sel:[0,0,1]
	s_cbranch_execnz .LBB0_1634
